# v36 + write-through (sc1) on the plain row stores of P0 (bf16 weight copies, SSM tables), h1, in-proj u tiles, h2 and final, so the grid barriers' L2 write-back and the end-of-kernel flush find nothin
# baseline (speedup 1.0000x reference)
.LBB0_25:
	s_or_b64 exec, exec, s[0:1]
	v_add_u32_e32 v76, s33, v82
	v_ashrrev_i32_e32 v77, 31, v76
	v_add_u32_e32 v78, s41, v82
	s_waitcnt vmcnt(6)
	v_cvt_pk_bf16_f32 v84, v10, v11
	v_cvt_pk_bf16_f32 v85, v12, v13
	s_waitcnt vmcnt(6)
	v_cvt_pk_bf16_f32 v86, v6, v7
	v_cvt_pk_bf16_f32 v87, v8, v9
	v_lshl_add_u64 v[76:77], v[76:77], 4, s[6:7]
	v_cmp_gt_i32_e64 s[0:1], s39, v78
	global_store_dwordx4 v[76:77], v[84:87], off sc1
	s_and_saveexec_b64 s[28:29], s[0:1]
	s_cbranch_execz .LBB0_27
	v_ashrrev_i32_e32 v79, 31, v78
	s_waitcnt vmcnt(5)
	v_cvt_pk_bf16_f32 v84, v18, v19
	v_cvt_pk_bf16_f32 v85, v20, v21
	s_waitcnt vmcnt(5)
	v_cvt_pk_bf16_f32 v86, v14, v15
	v_cvt_pk_bf16_f32 v87, v16, v17
	v_lshl_add_u64 v[78:79], v[78:79], 4, s[6:7]
	global_store_dwordx4 v[78:79], v[84:87], off sc1
.LBB0_27:
	s_or_b64 exec, exec, s[28:29]
	v_add_u32_e32 v78, s42, v82
	v_cmp_gt_i32_e64 s[0:1], s39, v78
	s_and_saveexec_b64 s[28:29], s[0:1]
	s_cbranch_execz .LBB0_29
	v_ashrrev_i32_e32 v79, 31, v78
	s_waitcnt vmcnt(3)
	v_cvt_pk_bf16_f32 v84, v26, v27
	v_cvt_pk_bf16_f32 v85, v28, v29
	s_waitcnt vmcnt(3)
	v_cvt_pk_bf16_f32 v86, v22, v23
	v_cvt_pk_bf16_f32 v87, v24, v25
	v_lshl_add_u64 v[78:79], v[78:79], 4, s[6:7]
	global_store_dwordx4 v[78:79], v[84:87], off sc1
.LBB0_29:
	s_or_b64 exec, exec, s[28:29]
	v_add_u32_e32 v78, s43, v82
	v_cmp_gt_i32_e64 s[0:1], s39, v78
	s_and_saveexec_b64 s[28:29], s[0:1]
	s_cbranch_execz .LBB0_31
	v_ashrrev_i32_e32 v79, 31, v78
	s_waitcnt vmcnt(1)
	v_cvt_pk_bf16_f32 v84, v42, v43
	v_cvt_pk_bf16_f32 v85, v44, v45
	s_waitcnt vmcnt(1)
	v_cvt_pk_bf16_f32 v86, v38, v39
	v_cvt_pk_bf16_f32 v87, v40, v41
	v_lshl_add_u64 v[78:79], v[78:79], 4, s[6:7]
	global_store_dwordx4 v[78:79], v[84:87], off sc1

.LBB0_33:
	s_or_b64 exec, exec, s[28:29]
	s_and_saveexec_b64 s[0:1], vcc
	s_cbranch_execz .LBB0_22
	v_cvt_pk_bf16_f32 v84, v30, v31
	v_cvt_pk_bf16_f32 v85, v32, v33
	v_cvt_pk_bf16_f32 v86, v34, v35
	v_cvt_pk_bf16_f32 v87, v36, v37
	v_lshl_add_u64 v[76:77], s[8:9], 4, v[76:77]
	v_cmp_gt_i32_e32 vcc, s39, v73
	global_store_dwordx4 v[76:77], v[84:87], off sc1
	s_and_saveexec_b64 s[28:29], vcc
	s_cbranch_execz .LBB0_37
	s_waitcnt vmcnt(6)
	v_cvt_pk_bf16_f32 v84, v46, v47
	v_cvt_pk_bf16_f32 v85, v48, v49
	v_cvt_pk_bf16_f32 v86, v50, v51
	v_cvt_pk_bf16_f32 v87, v52, v53
	v_lshl_add_u64 v[76:77], s[2:3], 4, v[76:77]
	global_store_dwordx4 v[76:77], v[84:87], off sc1
	s_or_b64 exec, exec, s[28:29]
	v_cmp_gt_i32_e32 vcc, s39, v74
	s_and_saveexec_b64 s[28:29], vcc
	s_cbranch_execnz .LBB0_38

.LBB0_38:
	v_ashrrev_i32_e32 v75, 31, v74
	s_waitcnt vmcnt(4)
	v_cvt_pk_bf16_f32 v76, v54, v55
	v_cvt_pk_bf16_f32 v77, v56, v57
	v_cvt_pk_bf16_f32 v78, v58, v59
	v_cvt_pk_bf16_f32 v79, v60, v61
	v_lshl_add_u64 v[74:75], v[74:75], 4, s[6:7]
	global_store_dwordx4 v[74:75], v[76:79], off sc1
	s_or_b64 exec, exec, s[28:29]
	v_cmp_gt_i32_e32 vcc, s39, v72
	s_and_b64 exec, exec, vcc
	s_cbranch_execz .LBB0_22
.LBB0_39:
	v_ashrrev_i32_e32 v73, 31, v72
	s_waitcnt vmcnt(2)
	v_cvt_pk_bf16_f32 v74, v62, v63
	v_cvt_pk_bf16_f32 v75, v64, v65
	v_cvt_pk_bf16_f32 v76, v66, v67
	v_cvt_pk_bf16_f32 v77, v68, v69
	v_lshl_add_u64 v[72:73], v[72:73], 4, s[6:7]
	global_store_dwordx4 v[72:73], v[74:77], off sc1
	s_branch .LBB0_22

.LBB0_65:
	s_or_b64 exec, exec, s[30:31]
	v_add_u32_e32 v84, s33, v77
	s_waitcnt vmcnt(6)
	v_pk_mul_f32 v[86:87], v[72:73], v[6:7] op_sel_hi:[0,1]
	v_pk_mul_f32 v[88:89], v[72:73], v[8:9] op_sel_hi:[0,1]
	v_cvt_pk_bf16_f32 v86, v86, v87
	v_cvt_pk_bf16_f32 v87, v88, v89
	v_pk_mul_f32 v[88:89], v[72:73], v[10:11] op_sel_hi:[0,1]
	v_pk_mul_f32 v[90:91], v[72:73], v[12:13] op_sel_hi:[0,1]
	v_ashrrev_i32_e32 v85, 31, v84
	v_cvt_pk_bf16_f32 v88, v88, v89
	v_cvt_pk_bf16_f32 v89, v90, v91
	v_lshl_add_u64 v[84:85], v[84:85], 4, s[8:9]
	global_store_dwordx4 v[84:85], v[86:89], off sc1
	s_nop 1
	v_add_u32_e32 v86, s42, v77
	v_cmp_gt_i32_e64 s[0:1], s39, v86
	s_and_saveexec_b64 s[30:31], s[0:1]
	s_cbranch_execz .LBB0_67
	v_pk_mul_f32 v[88:89], v[72:73], v[14:15] op_sel:[1,0]
	v_pk_mul_f32 v[90:91], v[72:73], v[16:17] op_sel:[1,0]
	v_cvt_pk_bf16_f32 v88, v88, v89
	v_cvt_pk_bf16_f32 v89, v90, v91
	v_pk_mul_f32 v[90:91], v[72:73], v[18:19] op_sel:[1,0]
	v_pk_mul_f32 v[92:93], v[72:73], v[20:21] op_sel:[1,0]
	v_ashrrev_i32_e32 v87, 31, v86
	v_cvt_pk_bf16_f32 v90, v90, v91
	v_cvt_pk_bf16_f32 v91, v92, v93
	v_lshl_add_u64 v[86:87], v[86:87], 4, s[8:9]
	global_store_dwordx4 v[86:87], v[88:91], off sc1
.LBB0_67:
	s_or_b64 exec, exec, s[30:31]
	v_add_u32_e32 v86, s43, v77
	v_cmp_gt_i32_e64 s[0:1], s39, v86
	s_and_saveexec_b64 s[30:31], s[0:1]
	s_cbranch_execz .LBB0_69
	s_waitcnt vmcnt(4)
	v_pk_mul_f32 v[88:89], v[70:71], v[22:23] op_sel_hi:[0,1]
	v_pk_mul_f32 v[90:91], v[70:71], v[24:25] op_sel_hi:[0,1]
	v_cvt_pk_bf16_f32 v88, v88, v89
	v_cvt_pk_bf16_f32 v89, v90, v91
	v_pk_mul_f32 v[90:91], v[70:71], v[26:27] op_sel_hi:[0,1]
	v_pk_mul_f32 v[92:93], v[70:71], v[28:29] op_sel_hi:[0,1]
	v_ashrrev_i32_e32 v87, 31, v86
	v_cvt_pk_bf16_f32 v90, v90, v91
	v_cvt_pk_bf16_f32 v91, v92, v93
	v_lshl_add_u64 v[86:87], v[86:87], 4, s[8:9]
	global_store_dwordx4 v[86:87], v[88:91], off sc1
.LBB0_69:
	s_or_b64 exec, exec, s[30:31]
	v_add_u32_e32 v86, s38, v77
	v_cmp_gt_i32_e64 s[0:1], s39, v86
	s_and_saveexec_b64 s[30:31], s[0:1]
	s_cbranch_execz .LBB0_71
	s_waitcnt vmcnt(1)
	v_pk_mul_f32 v[88:89], v[76:77], v[46:47] op_sel_hi:[0,1]
	v_pk_mul_f32 v[90:91], v[76:77], v[48:49] op_sel_hi:[0,1]
	v_cvt_pk_bf16_f32 v88, v88, v89
	v_cvt_pk_bf16_f32 v89, v90, v91
	v_pk_mul_f32 v[90:91], v[76:77], v[50:51] op_sel_hi:[0,1]
	v_pk_mul_f32 v[92:93], v[76:77], v[52:53] op_sel_hi:[0,1]
	v_ashrrev_i32_e32 v87, 31, v86
	v_cvt_pk_bf16_f32 v90, v90, v91
	v_cvt_pk_bf16_f32 v91, v92, v93
	v_lshl_add_u64 v[86:87], v[86:87], 4, s[8:9]
	global_store_dwordx4 v[86:87], v[88:91], off sc1

.LBB0_73:
	s_or_b64 exec, exec, s[30:31]
	s_and_saveexec_b64 s[0:1], vcc
	s_cbranch_execz .LBB0_62
	v_pk_mul_f32 v[86:87], v[34:35], v[74:75] op_sel_hi:[1,0]
	v_pk_mul_f32 v[88:89], v[36:37], v[74:75] op_sel_hi:[1,0]
	v_cvt_pk_bf16_f32 v86, v86, v87
	v_cvt_pk_bf16_f32 v87, v88, v89
	v_pk_mul_f32 v[88:89], v[30:31], v[74:75] op_sel_hi:[1,0]
	v_pk_mul_f32 v[90:91], v[32:33], v[74:75] op_sel_hi:[1,0]
	v_cvt_pk_bf16_f32 v88, v88, v89
	v_cvt_pk_bf16_f32 v89, v90, v91
	v_lshl_add_u64 v[84:85], s[10:11], 4, v[84:85]
	v_cmp_gt_i32_e32 vcc, s39, v81
	global_store_dwordx4 v[84:85], v[86:89], off sc1
	s_and_saveexec_b64 s[30:31], vcc
	s_cbranch_execz .LBB0_77
	v_pk_mul_f32 v[86:87], v[42:43], v[74:75] op_sel:[0,1]
	v_pk_mul_f32 v[88:89], v[44:45], v[74:75] op_sel:[0,1]
	v_cvt_pk_bf16_f32 v86, v86, v87
	v_cvt_pk_bf16_f32 v87, v88, v89
	v_pk_mul_f32 v[88:89], v[38:39], v[74:75] op_sel:[0,1]
	v_pk_mul_f32 v[90:91], v[40:41], v[74:75] op_sel:[0,1]
	v_cvt_pk_bf16_f32 v88, v88, v89
	v_cvt_pk_bf16_f32 v89, v90, v91
	v_lshl_add_u64 v[84:85], s[2:3], 4, v[84:85]
	global_store_dwordx4 v[84:85], v[86:89], off sc1
	s_or_b64 exec, exec, s[30:31]
	v_cmp_gt_i32_e32 vcc, s39, v82
	s_and_saveexec_b64 s[30:31], vcc
	s_cbranch_execnz .LBB0_78

.LBB0_78:
	s_waitcnt vmcnt(2)
	v_pk_mul_f32 v[84:85], v[58:59], v[78:79] op_sel_hi:[1,0]
	v_pk_mul_f32 v[86:87], v[60:61], v[78:79] op_sel_hi:[1,0]
	v_cvt_pk_bf16_f32 v84, v84, v85
	v_cvt_pk_bf16_f32 v85, v86, v87
	v_pk_mul_f32 v[86:87], v[54:55], v[78:79] op_sel_hi:[1,0]
	v_pk_mul_f32 v[88:89], v[56:57], v[78:79] op_sel_hi:[1,0]
	v_ashrrev_i32_e32 v83, 31, v82
	v_cvt_pk_bf16_f32 v86, v86, v87
	v_cvt_pk_bf16_f32 v87, v88, v89
	v_lshl_add_u64 v[82:83], v[82:83], 4, s[8:9]
	global_store_dwordx4 v[82:83], v[84:87], off sc1
	s_or_b64 exec, exec, s[30:31]
	v_cmp_gt_i32_e32 vcc, s39, v80
	s_and_b64 exec, exec, vcc
	s_cbranch_execz .LBB0_62
.LBB0_79:
	s_waitcnt vmcnt(2)
	v_mov_b32_e32 v86, v79
	v_pk_mul_f32 v[82:83], v[66:67], v[86:87] op_sel_hi:[1,0]
	v_pk_mul_f32 v[84:85], v[68:69], v[86:87] op_sel_hi:[1,0]
	v_cvt_pk_bf16_f32 v82, v82, v83
	v_cvt_pk_bf16_f32 v83, v84, v85
	v_pk_mul_f32 v[84:85], v[62:63], v[86:87] op_sel_hi:[1,0]
	v_pk_mul_f32 v[86:87], v[64:65], v[86:87] op_sel_hi:[1,0]
	v_ashrrev_i32_e32 v81, 31, v80
	v_cvt_pk_bf16_f32 v84, v84, v85
	v_cvt_pk_bf16_f32 v85, v86, v87
	v_lshl_add_u64 v[80:81], v[80:81], 4, s[8:9]
	global_store_dwordx4 v[80:81], v[82:85], off sc1
	s_branch .LBB0_62

.LBB0_92:
	s_or_b64 exec, exec, s[28:29]
	s_waitcnt vmcnt(0)
	v_cvt_f64_f32_e32 v[14:15], v30
	s_mov_b32 s28, 0x652b82fe
	v_mul_f64 v[12:13], v[12:13], v[14:15]
	s_mov_b32 s29, 0x3ff71547
	v_mul_f64 v[24:25], v[12:13], s[28:29]
	s_mov_b32 s28, 0xfefa39ef
	v_rndne_f64_e32 v[24:25], v[24:25]
	s_mov_b32 s29, 0xbfe62e42
	v_fma_f64 v[26:27], s[28:29], v[24:25], v[12:13]
	s_mov_b32 s28, 0x3b39803f
	s_mov_b32 s29, 0xbc7abc9e
	v_fmac_f64_e32 v[26:27], s[28:29], v[24:25]
	s_mov_b32 s28, 0x6a5dcb37
	v_mov_b64_e32 v[28:29], v[44:45]
	s_mov_b32 s29, 0x3e5ade15
	v_fmac_f64_e32 v[28:29], s[28:29], v[26:27]
	v_mov_b64_e32 v[34:35], v[46:47]
	v_fmac_f64_e32 v[34:35], v[26:27], v[28:29]
	v_mov_b64_e32 v[28:29], v[48:49]
	v_fmac_f64_e32 v[28:29], v[26:27], v[34:35]
	v_mov_b64_e32 v[34:35], v[50:51]
	v_fmac_f64_e32 v[34:35], v[26:27], v[28:29]
	v_mov_b64_e32 v[28:29], v[52:53]
	v_fmac_f64_e32 v[28:29], v[26:27], v[34:35]
	v_mov_b64_e32 v[34:35], v[54:55]
	v_fmac_f64_e32 v[34:35], v[26:27], v[28:29]
	v_mov_b64_e32 v[28:29], v[56:57]
	v_fmac_f64_e32 v[28:29], v[26:27], v[34:35]
	v_mov_b64_e32 v[34:35], v[58:59]
	v_fmac_f64_e32 v[34:35], v[26:27], v[28:29]
	v_mov_b64_e32 v[28:29], v[60:61]
	s_mov_b32 s28, 0
	v_fmac_f64_e32 v[28:29], v[26:27], v[34:35]
	s_mov_b32 s29, 0x40900000
	v_fma_f64 v[28:29], v[26:27], v[28:29], 1.0
	v_cmp_nlt_f64_e32 vcc, s[28:29], v[12:13]
	s_mov_b32 s28, 0
	v_fma_f64 v[26:27], v[26:27], v[28:29], 1.0
	v_cvt_i32_f64_e32 v24, v[24:25]
	s_mov_b32 s29, 0xc090cc00
	v_ldexp_f64 v[24:25], v[26:27], v24
	v_cmp_ngt_f64_e64 s[46:47], s[28:29], v[12:13]
	s_mov_b32 s28, 0x9037ab78
	v_cndmask_b32_e32 v25, v85, v25, vcc
	s_and_b64 vcc, s[46:47], vcc
	s_mov_b32 s29, 0x3e21eeb6
	s_mov_b32 s30, 0x46cc5e42
	v_cndmask_b32_e32 v12, 0, v24, vcc
	v_cndmask_b32_e64 v13, 0, v25, s[46:47]
	v_mul_f64 v[24:25], v[16:17], v[16:17]
	v_mov_b64_e32 v[36:37], s[28:29]
	s_mov_b32 s31, 0xbda907db
	s_mov_b32 s46, 0xa17f65f6
	v_mul_f64 v[26:27], v[24:25], 0.5
	v_fma_f64 v[64:65], s[30:31], v[24:25], v[36:37]
	s_mov_b32 s47, 0xbe927e4f
	v_add_f64 v[28:29], -v[26:27], 1.0
	v_fma_f64 v[64:65], v[24:25], v[64:65], s[46:47]
	s_mov_b32 s34, 0x16c16967
	v_add_f64 v[34:35], -v[28:29], 1.0
	v_fma_f64 v[64:65], v[24:25], v[64:65], s[76:77]
	s_mov_b32 s35, 0xbf56c16c
	v_add_f64 v[26:27], v[34:35], -v[26:27]
	v_fma_f64 v[64:65], v[24:25], v[64:65], s[34:35]
	v_mul_f64 v[34:35], v[24:25], v[24:25]
	v_fma_f64 v[64:65], v[24:25], v[64:65], s[38:39]
	v_fma_f64 v[26:27], v[16:17], -v[18:19], v[26:27]
	s_mov_b32 s28, 0xb42fdfa7
	v_fmac_f64_e32 v[26:27], v[34:35], v[64:65]
	s_mov_b32 s29, 0xbe5ae600
	s_mov_b32 s0, 0xf9a43bb8
	v_add_f64 v[26:27], v[28:29], v[26:27]
	v_mov_b64_e32 v[28:29], s[28:29]
	s_mov_b32 s1, 0x3de5e0b2
	v_fma_f64 v[34:35], s[0:1], v[24:25], v[28:29]
	v_fma_f64 v[34:35], v[24:25], v[34:35], s[4:5]
	s_mov_b32 s28, 0x11110bb3
	v_fma_f64 v[34:35], v[24:25], v[34:35], s[6:7]
	s_mov_b32 s29, 0x3f811111
	v_fma_f64 v[34:35], v[24:25], v[34:35], s[28:29]
	v_mul_f64 v[64:65], v[16:17], -v[24:25]
	v_mul_f64 v[66:67], v[18:19], 0.5
	v_fmac_f64_e32 v[66:67], v[64:65], v[34:35]
	v_fma_f64 v[18:19], v[24:25], v[66:67], -v[18:19]
	s_mov_b32 s2, s38
	v_fmac_f64_e32 v[18:19], s[2:3], v[64:65]
	v_add_f64 v[16:17], v[16:17], -v[18:19]
	v_and_b32_e32 v18, 1, v31
	v_xor_b32_e32 v17, 0x80000000, v17
	v_cmp_eq_u32_e32 vcc, 0, v18
	v_mul_f64 v[24:25], v[20:21], v[20:21]
	v_fmac_f64_e32 v[36:37], s[30:31], v[24:25]
	v_cndmask_b32_e32 v16, v16, v26, vcc
	v_cndmask_b32_e32 v17, v17, v27, vcc
	v_mul_f64 v[26:27], v[24:25], 0.5
	v_lshlrev_b32_e32 v18, 30, v31
	v_add_f64 v[30:31], -v[26:27], 1.0
	v_fma_f64 v[36:37], v[24:25], v[36:37], s[46:47]
	v_add_f64 v[34:35], -v[30:31], 1.0
	v_fma_f64 v[36:37], v[24:25], v[36:37], s[76:77]
	v_add_f64 v[26:27], v[34:35], -v[26:27]
	v_fma_f64 v[36:37], v[24:25], v[36:37], s[34:35]
	v_fmac_f64_e32 v[28:29], s[0:1], v[24:25]
	v_mul_f64 v[34:35], v[24:25], v[24:25]
	v_fma_f64 v[36:37], v[24:25], v[36:37], s[38:39]
	v_fma_f64 v[26:27], v[20:21], -v[22:23], v[26:27]
	v_fma_f64 v[28:29], v[24:25], v[28:29], s[4:5]
	v_fmac_f64_e32 v[26:27], v[34:35], v[36:37]
	v_fma_f64 v[28:29], v[24:25], v[28:29], s[6:7]
	v_add_f64 v[26:27], v[30:31], v[26:27]
	v_fma_f64 v[28:29], v[24:25], v[28:29], s[28:29]
	v_mul_f64 v[30:31], v[20:21], -v[24:25]
	v_mul_f64 v[34:35], v[22:23], 0.5
	v_fmac_f64_e32 v[34:35], v[30:31], v[28:29]
	s_movk_i32 s11, 0x1f8
	v_fma_f64 v[22:23], v[24:25], v[34:35], -v[22:23]
	v_cmp_class_f64_e64 vcc, v[10:11], s11
	v_fmac_f64_e32 v[22:23], s[2:3], v[30:31]
	v_and_b32_e32 v10, 1, v32
	v_add_f64 v[20:21], v[20:21], -v[22:23]
	v_cmp_eq_u32_e64 s[46:47], 0, v10
	v_bitop3_b32 v17, v17, v18, s43 bitop3:0x78
	v_cndmask_b32_e32 v16, 0, v16, vcc
	v_cndmask_b32_e64 v10, v26, v20, s[46:47]
	v_cndmask_b32_e64 v20, v27, v21, s[46:47]
	v_lshlrev_b32_e32 v21, 30, v32
	v_xor_b32_e32 v11, v21, v11
	v_bitop3_b32 v11, v20, v11, s43 bitop3:0x78
	v_cndmask_b32_e32 v17, v88, v17, vcc
	v_cndmask_b32_e32 v10, 0, v10, vcc
	v_cndmask_b32_e32 v11, v88, v11, vcc
	v_mul_f64 v[18:19], v[12:13], v[16:17]
	v_mul_f64 v[10:11], v[12:13], v[10:11]
	v_mov_b64_e32 v[20:21], v[18:19]
	v_fma_f64 v[24:25], 0, v[18:19], v[10:11]
	v_fmac_f64_e32 v[20:21], 0x80000000, v[10:11]
	v_mul_f64 v[26:27], v[10:11], v[24:25]
	v_cvt_f32_f64_e32 v28, v[20:21]
	v_mul_f64 v[22:23], v[10:11], v[20:21]
	v_fma_f64 v[20:21], v[18:19], v[20:21], -v[26:27]
	v_cvt_f32_f64_e32 v26, v[20:21]
	v_cvt_f32_f64_e32 v27, v[24:25]
	v_fmac_f64_e32 v[22:23], v[18:19], v[24:25]
	ds_write2_b32 v68, v27, v26 offset0:3 offset1:4
	v_mul_f64 v[26:27], v[10:11], v[20:21]
	v_mul_f64 v[24:25], v[10:11], v[22:23]
	v_fma_f64 v[20:21], v[18:19], v[20:21], -v[24:25]
	v_fmac_f64_e32 v[26:27], v[18:19], v[22:23]
	v_cvt_f32_f64_e32 v24, v[20:21]
	v_cvt_f32_f64_e32 v25, v[22:23]
	v_mul_f64 v[22:23], v[10:11], v[26:27]
	ds_write2_b32 v68, v25, v24 offset0:5 offset1:6
	v_mul_f64 v[24:25], v[10:11], v[20:21]
	v_fma_f64 v[20:21], v[18:19], v[20:21], -v[22:23]
	v_cvt_f32_f64_e32 v22, v[20:21]
	v_cvt_f32_f64_e32 v23, v[26:27]
	v_fmac_f64_e32 v[24:25], v[18:19], v[26:27]
	ds_write2_b32 v68, v23, v22 offset0:7 offset1:8
	v_mul_f64 v[22:23], v[10:11], v[20:21]
	v_mul_f64 v[26:27], v[10:11], v[24:25]
	v_fma_f64 v[20:21], v[18:19], v[20:21], -v[26:27]
	v_fmac_f64_e32 v[22:23], v[18:19], v[24:25]
	v_cvt_f32_f64_e32 v26, v[20:21]
	v_cvt_f32_f64_e32 v27, v[24:25]
	v_mul_f64 v[24:25], v[10:11], v[22:23]
	ds_write2_b32 v68, v27, v26 offset0:9 offset1:10
	v_mul_f64 v[26:27], v[10:11], v[20:21]
	v_fma_f64 v[20:21], v[18:19], v[20:21], -v[24:25]
	v_cvt_f32_f64_e32 v24, v[20:21]
	v_cvt_f32_f64_e32 v25, v[22:23]
	v_fmac_f64_e32 v[26:27], v[18:19], v[22:23]
	ds_write2_b32 v68, v25, v24 offset0:11 offset1:12
	v_mul_f64 v[24:25], v[10:11], v[20:21]
	v_mul_f64 v[22:23], v[10:11], v[26:27]
	v_fma_f64 v[20:21], v[18:19], v[20:21], -v[22:23]
	v_fmac_f64_e32 v[24:25], v[18:19], v[26:27]
	v_cvt_f32_f64_e32 v22, v[20:21]
	v_cvt_f32_f64_e32 v23, v[26:27]
	v_mul_f64 v[26:27], v[10:11], v[24:25]
	ds_write2_b32 v68, v23, v22 offset0:13 offset1:14
	v_mul_f64 v[22:23], v[10:11], v[20:21]
	v_fma_f64 v[20:21], v[18:19], v[20:21], -v[26:27]
	v_cvt_f32_f64_e32 v26, v[20:21]
	v_cvt_f32_f64_e32 v27, v[24:25]
	v_fmac_f64_e32 v[22:23], v[18:19], v[24:25]
	ds_write2_b32 v68, v27, v26 offset0:15 offset1:16
	v_mul_f64 v[26:27], v[10:11], v[20:21]
	v_mul_f64 v[24:25], v[10:11], v[22:23]
	v_fma_f64 v[20:21], v[18:19], v[20:21], -v[24:25]
	v_fmac_f64_e32 v[26:27], v[18:19], v[22:23]
	v_cvt_f32_f64_e32 v24, v[20:21]
	v_cvt_f32_f64_e32 v25, v[22:23]
	v_mul_f64 v[22:23], v[10:11], v[26:27]
	ds_write2_b32 v68, v25, v24 offset0:17 offset1:18
	v_mul_f64 v[24:25], v[10:11], v[20:21]
	v_fma_f64 v[20:21], v[18:19], v[20:21], -v[22:23]
	v_cvt_f32_f64_e32 v22, v[20:21]
	v_cvt_f32_f64_e32 v23, v[26:27]
	v_fmac_f64_e32 v[24:25], v[18:19], v[26:27]
	ds_write2_b32 v68, v23, v22 offset0:19 offset1:20
	v_mul_f64 v[22:23], v[10:11], v[20:21]
	v_mul_f64 v[26:27], v[10:11], v[24:25]
	v_fma_f64 v[20:21], v[18:19], v[20:21], -v[26:27]
	v_fmac_f64_e32 v[22:23], v[18:19], v[24:25]
	v_cvt_f32_f64_e32 v26, v[20:21]
	v_cvt_f32_f64_e32 v27, v[24:25]
	v_mul_f64 v[24:25], v[10:11], v[22:23]
	ds_write2_b32 v68, v27, v26 offset0:21 offset1:22
	v_mul_f64 v[26:27], v[10:11], v[20:21]
	v_fma_f64 v[20:21], v[18:19], v[20:21], -v[24:25]
	v_cvt_f32_f64_e32 v24, v[20:21]
	v_cvt_f32_f64_e32 v25, v[22:23]
	v_fmac_f64_e32 v[26:27], v[18:19], v[22:23]
	ds_write2_b32 v68, v25, v24 offset0:23 offset1:24
	v_mul_f64 v[24:25], v[10:11], v[20:21]
	v_mul_f64 v[22:23], v[10:11], v[26:27]
	v_fma_f64 v[20:21], v[18:19], v[20:21], -v[22:23]
	v_fmac_f64_e32 v[24:25], v[18:19], v[26:27]
	v_cvt_f32_f64_e32 v22, v[20:21]
	v_cvt_f32_f64_e32 v23, v[26:27]
	v_mul_f64 v[26:27], v[10:11], v[24:25]
	ds_write2_b32 v68, v23, v22 offset0:25 offset1:26
	v_mul_f64 v[22:23], v[10:11], v[20:21]
	v_fma_f64 v[20:21], v[18:19], v[20:21], -v[26:27]
	v_cvt_f32_f64_e32 v26, v[20:21]
	v_cvt_f32_f64_e32 v27, v[24:25]
	v_fmac_f64_e32 v[22:23], v[18:19], v[24:25]
	ds_write2_b32 v68, v27, v26 offset0:27 offset1:28
	v_mul_f64 v[26:27], v[10:11], v[20:21]
	v_mul_f64 v[24:25], v[10:11], v[22:23]
	v_fma_f64 v[20:21], v[18:19], v[20:21], -v[24:25]
	v_fmac_f64_e32 v[26:27], v[18:19], v[22:23]
	v_cvt_f32_f64_e32 v24, v[20:21]
	v_cvt_f32_f64_e32 v25, v[22:23]
	v_mul_f64 v[22:23], v[10:11], v[26:27]
	ds_write2_b32 v68, v25, v24 offset0:29 offset1:30
	v_mul_f64 v[24:25], v[10:11], v[20:21]
	v_fma_f64 v[20:21], v[18:19], v[20:21], -v[22:23]
	v_fmac_f64_e32 v[24:25], v[18:19], v[26:27]
	v_cvt_f32_f64_e32 v18, v[20:21]
	v_lshlrev_b32_e32 v20, 1, v6
	v_readlane_b32 s28, v255, 12
	v_cvt_f32_f64_e32 v19, v[26:27]
	v_ashrrev_i32_e32 v21, 31, v20
	v_readlane_b32 s29, v255, 13
	ds_write2_b32 v68, v19, v18 offset0:31 offset1:32
	v_cvt_f32_f64_e32 v19, v[24:25]
	v_lshl_add_u64 v[20:21], v[20:21], 2, s[28:29]
	ds_write2_b32 v68, v28, v19 offset0:2 offset1:33
	global_store_dwordx2 v[20:21], v[18:19], off sc1
	v_mul_f64 v[18:19], v[8:9], v[8:9]
	v_fma_f64 v[12:13], v[12:13], v[16:17], -1.0
	v_mul_f64 v[16:17], v[10:11], v[8:9]
	v_fmac_f64_e32 v[18:19], v[14:15], v[14:15]
	v_fmac_f64_e32 v[16:17], v[12:13], v[14:15]
	v_div_scale_f64 v[20:21], s[28:29], v[18:19], v[18:19], v[16:17]
	v_rcp_f64_e32 v[22:23], v[20:21]
	v_mul_f64 v[8:9], v[12:13], v[8:9]
	v_fma_f64 v[8:9], v[10:11], v[14:15], -v[8:9]
	v_div_scale_f64 v[10:11], s[28:29], v[18:19], v[18:19], v[8:9]
	v_rcp_f64_e32 v[12:13], v[10:11]
	v_fma_f64 v[24:25], -v[20:21], v[22:23], 1.0
	v_fmac_f64_e32 v[22:23], v[22:23], v[24:25]
	v_fma_f64 v[24:25], -v[20:21], v[22:23], 1.0
	v_fmac_f64_e32 v[22:23], v[22:23], v[24:25]
	v_div_scale_f64 v[24:25], vcc, v[16:17], v[18:19], v[16:17]
	v_fma_f64 v[14:15], -v[10:11], v[12:13], 1.0
	v_mul_f64 v[26:27], v[24:25], v[22:23]
	v_fmac_f64_e32 v[12:13], v[12:13], v[14:15]
	v_fma_f64 v[20:21], -v[20:21], v[26:27], v[24:25]
	v_fma_f64 v[14:15], -v[10:11], v[12:13], 1.0
	v_div_fmas_f64 v[20:21], v[20:21], v[22:23], v[26:27]
	v_fmac_f64_e32 v[12:13], v[12:13], v[14:15]
	v_div_scale_f64 v[14:15], vcc, v[8:9], v[18:19], v[8:9]
	v_div_fixup_f64 v[64:65], v[20:21], v[18:19], v[16:17]
	v_mul_f64 v[16:17], v[14:15], v[12:13]
	v_fma_f64 v[10:11], -v[10:11], v[16:17], v[14:15]
	s_nop 0
	v_div_fmas_f64 v[10:11], v[10:11], v[12:13], v[16:17]
	v_lshlrev_b64 v[6:7], 6, v[6:7]
	ds_write_b64 v68, v[62:63]
	v_div_fixup_f64 v[66:67], v[10:11], v[18:19], v[8:9]
	v_lshl_add_u64 v[10:11], s[82:83], 0, v[6:7]
	v_lshl_add_u64 v[34:35], s[84:85], 0, v[6:7]
	global_load_dwordx4 v[6:9], v[10:11], off offset:48
	global_load_dwordx4 v[14:17], v[10:11], off offset:32
	global_load_dwordx4 v[22:25], v[10:11], off offset:16
	global_load_dwordx4 v[30:33], v[10:11], off
	s_nop 0
	global_load_dwordx4 v[10:13], v[34:35], off offset:48
	global_load_dwordx4 v[18:21], v[34:35], off offset:32
	global_load_dwordx4 v[26:29], v[34:35], off offset:16
	s_nop 0
	global_load_dwordx4 v[34:37], v[34:35], off
	s_waitcnt vmcnt(4)
	v_cvt_f64_f32_e32 v[92:93], v30
	v_cvt_f64_f32_e32 v[30:31], v31
	s_waitcnt vmcnt(0)
	v_cvt_f64_f32_e32 v[94:95], v34
	v_mul_f64 v[90:91], v[66:67], v[94:95]
	v_mul_f64 v[94:95], v[64:65], v[94:95]
	v_cvt_f64_f32_e32 v[34:35], v35
	v_fma_f64 v[90:91], v[64:65], v[92:93], -v[90:91]
	v_fmac_f64_e32 v[94:95], v[66:67], v[92:93]
	v_mul_f64 v[92:93], v[66:67], v[34:35]
	v_mul_f64 v[34:35], v[64:65], v[34:35]
	v_fma_f64 v[92:93], v[64:65], v[30:31], -v[92:93]
	v_fmac_f64_e32 v[34:35], v[66:67], v[30:31]
	v_cvt_f32_f64_e32 v90, v[90:91]
	v_cvt_f32_f64_e32 v91, v[94:95]
	v_cvt_f32_f64_e32 v92, v[92:93]
	v_cvt_f32_f64_e32 v93, v[34:35]
	ds_write_b128 v84, v[90:93] offset:17408
	v_cvt_f64_f32_e32 v[90:91], v36
	v_cvt_f64_f32_e32 v[34:35], v32
	v_mul_f64 v[30:31], v[66:67], v[90:91]
	v_mul_f64 v[90:91], v[64:65], v[90:91]
	v_cvt_f64_f32_e32 v[36:37], v37
	v_fma_f64 v[30:31], v[64:65], v[34:35], -v[30:31]
	v_fmac_f64_e32 v[90:91], v[66:67], v[34:35]
	v_cvt_f64_f32_e32 v[34:35], v33
	v_mul_f64 v[32:33], v[66:67], v[36:37]
	v_mul_f64 v[36:37], v[64:65], v[36:37]
	v_fma_f64 v[32:33], v[64:65], v[34:35], -v[32:33]
	v_fmac_f64_e32 v[36:37], v[66:67], v[34:35]
	v_cvt_f32_f64_e32 v30, v[30:31]
	v_cvt_f32_f64_e32 v31, v[90:91]
	v_cvt_f32_f64_e32 v32, v[32:33]
	v_cvt_f32_f64_e32 v33, v[36:37]
	v_cvt_f64_f32_e32 v[34:35], v26
	ds_write_b128 v84, v[30:33] offset:17424
	v_cvt_f64_f32_e32 v[32:33], v22
	v_mul_f64 v[30:31], v[66:67], v[34:35]
	v_mul_f64 v[34:35], v[64:65], v[34:35]
	v_cvt_f64_f32_e32 v[26:27], v27
	v_fma_f64 v[30:31], v[64:65], v[32:33], -v[30:31]
	v_fmac_f64_e32 v[34:35], v[66:67], v[32:33]
	v_cvt_f64_f32_e32 v[22:23], v23
	v_mul_f64 v[32:33], v[66:67], v[26:27]
	v_mul_f64 v[26:27], v[64:65], v[26:27]
	v_fma_f64 v[32:33], v[64:65], v[22:23], -v[32:33]
	v_fmac_f64_e32 v[26:27], v[66:67], v[22:23]
	v_cvt_f32_f64_e32 v30, v[30:31]
	v_cvt_f32_f64_e32 v31, v[34:35]
	v_cvt_f32_f64_e32 v32, v[32:33]
	v_cvt_f32_f64_e32 v33, v[26:27]
	ds_write_b128 v84, v[30:33] offset:17440
	v_cvt_f64_f32_e32 v[30:31], v28
	v_cvt_f64_f32_e32 v[26:27], v24
	v_mul_f64 v[22:23], v[66:67], v[30:31]
	v_mul_f64 v[30:31], v[64:65], v[30:31]
	v_cvt_f64_f32_e32 v[28:29], v29
	v_fma_f64 v[22:23], v[64:65], v[26:27], -v[22:23]
	v_fmac_f64_e32 v[30:31], v[66:67], v[26:27]
	v_cvt_f64_f32_e32 v[26:27], v25
	v_mul_f64 v[24:25], v[66:67], v[28:29]
	v_mul_f64 v[28:29], v[64:65], v[28:29]
	v_fma_f64 v[24:25], v[64:65], v[26:27], -v[24:25]
	v_fmac_f64_e32 v[28:29], v[66:67], v[26:27]
	v_cvt_f32_f64_e32 v22, v[22:23]
	v_cvt_f32_f64_e32 v23, v[30:31]
	v_cvt_f32_f64_e32 v24, v[24:25]
	v_cvt_f32_f64_e32 v25, v[28:29]
	v_cvt_f64_f32_e32 v[26:27], v18
	ds_write_b128 v84, v[22:25] offset:17456
	v_cvt_f64_f32_e32 v[24:25], v14
	v_mul_f64 v[22:23], v[66:67], v[26:27]
	v_mul_f64 v[26:27], v[64:65], v[26:27]
	v_cvt_f64_f32_e32 v[18:19], v19
	v_fma_f64 v[22:23], v[64:65], v[24:25], -v[22:23]
	v_fmac_f64_e32 v[26:27], v[66:67], v[24:25]
	v_cvt_f64_f32_e32 v[14:15], v15
	v_mul_f64 v[24:25], v[66:67], v[18:19]
	v_mul_f64 v[18:19], v[64:65], v[18:19]
	v_fma_f64 v[24:25], v[64:65], v[14:15], -v[24:25]
	v_fmac_f64_e32 v[18:19], v[66:67], v[14:15]
	v_cvt_f32_f64_e32 v22, v[22:23]
	v_cvt_f32_f64_e32 v23, v[26:27]
	v_cvt_f32_f64_e32 v24, v[24:25]
	v_cvt_f32_f64_e32 v25, v[18:19]
	ds_write_b128 v84, v[22:25] offset:17472
	v_cvt_f64_f32_e32 v[22:23], v20
	v_cvt_f64_f32_e32 v[18:19], v16
	v_mul_f64 v[14:15], v[66:67], v[22:23]
	v_mul_f64 v[22:23], v[64:65], v[22:23]
	v_cvt_f64_f32_e32 v[20:21], v21
	v_fma_f64 v[14:15], v[64:65], v[18:19], -v[14:15]
	v_fmac_f64_e32 v[22:23], v[66:67], v[18:19]
	v_cvt_f64_f32_e32 v[18:19], v17
	v_mul_f64 v[16:17], v[66:67], v[20:21]
	v_mul_f64 v[20:21], v[64:65], v[20:21]
	v_fma_f64 v[16:17], v[64:65], v[18:19], -v[16:17]
	v_fmac_f64_e32 v[20:21], v[66:67], v[18:19]
	v_cvt_f32_f64_e32 v14, v[14:15]
	v_cvt_f32_f64_e32 v15, v[22:23]
	v_cvt_f32_f64_e32 v16, v[16:17]
	v_cvt_f32_f64_e32 v17, v[20:21]
	v_cvt_f64_f32_e32 v[18:19], v10
	ds_write_b128 v84, v[14:17] offset:17488
	v_cvt_f64_f32_e32 v[16:17], v6
	v_mul_f64 v[14:15], v[66:67], v[18:19]
	v_mul_f64 v[18:19], v[64:65], v[18:19]
	v_cvt_f64_f32_e32 v[10:11], v11
	v_fma_f64 v[14:15], v[64:65], v[16:17], -v[14:15]
	v_fmac_f64_e32 v[18:19], v[66:67], v[16:17]
	v_cvt_f64_f32_e32 v[6:7], v7
	v_mul_f64 v[16:17], v[66:67], v[10:11]
	v_mul_f64 v[10:11], v[64:65], v[10:11]
	v_fma_f64 v[16:17], v[64:65], v[6:7], -v[16:17]
	v_fmac_f64_e32 v[10:11], v[66:67], v[6:7]
	v_cvt_f32_f64_e32 v14, v[14:15]
	v_cvt_f32_f64_e32 v15, v[18:19]
	v_cvt_f32_f64_e32 v16, v[16:17]
	v_cvt_f32_f64_e32 v17, v[10:11]
	ds_write_b128 v84, v[14:17] offset:17504
	v_cvt_f64_f32_e32 v[14:15], v12
	v_cvt_f64_f32_e32 v[10:11], v8
	v_mul_f64 v[6:7], v[66:67], v[14:15]
	v_mul_f64 v[14:15], v[64:65], v[14:15]
	v_cvt_f64_f32_e32 v[12:13], v13
	v_fma_f64 v[6:7], v[64:65], v[10:11], -v[6:7]
	v_fmac_f64_e32 v[14:15], v[66:67], v[10:11]
	v_cvt_f64_f32_e32 v[10:11], v9
	v_mul_f64 v[8:9], v[66:67], v[12:13]
	v_mul_f64 v[12:13], v[64:65], v[12:13]
	v_fma_f64 v[8:9], v[64:65], v[10:11], -v[8:9]
	v_fmac_f64_e32 v[12:13], v[66:67], v[10:11]
	v_cvt_f32_f64_e32 v6, v[6:7]
	v_cvt_f32_f64_e32 v7, v[14:15]
	v_cvt_f32_f64_e32 v8, v[8:9]
	v_cvt_f32_f64_e32 v9, v[12:13]
	ds_write_b128 v84, v[6:9] offset:17520

.LBB0_136:
	v_cndmask_b32_e64 v13, v10, v11, s[44:45]
	v_and_or_b32 v18, v8, 56, v74
	v_and_b32_e32 v19, 30, v9
	v_mad_u32_u24 v13, v18, 17, v13
	v_lshlrev_b32_e32 v18, 7, v18
	v_lshlrev_b32_e32 v19, 2, v19
	v_add3_u32 v18, 0, v18, v19
	v_and_b32_e32 v14, 8, v12
	v_lshl_add_u32 v13, v13, 3, 0
	v_add_u32_e32 v26, 0x4000, v18
	v_cmp_eq_u32_e32 vcc, 0, v14
	ds_read2_b64 v[14:17], v13 offset1:17
	ds_read2_b64 v[18:21], v26 offset0:128 offset1:144
	s_movk_i32 s11, 0x1dff
	v_add_u32_e32 v11, -1, v11
	v_add_u32_e32 v10, 1, v10
	s_waitcnt lgkmcnt(1)
	v_mov_b32_e32 v23, v16
	s_waitcnt lgkmcnt(0)
	v_mov_b32_e32 v24, v19
	v_mov_b32_e32 v25, v21
	v_mov_b32_e32 v16, v15
	v_mov_b32_e32 v19, v20
	v_mov_b32_e32 v22, v14
	v_pk_mul_f32 v[14:15], v[16:17], v[18:19]
	v_pk_mul_f32 v[16:17], v[16:17], v[24:25]
	v_pk_fma_f32 v[14:15], v[22:23], v[24:25], v[14:15]
	v_pk_fma_f32 v[16:17], v[22:23], v[18:19], v[16:17] neg_lo:[0,0,1] neg_hi:[0,0,1]
	v_add_u32_e32 v9, 32, v9
	v_cndmask_b32_e32 v27, v15, v17, vcc
	v_cndmask_b32_e32 v28, v14, v16, vcc
	ds_read2_b64 v[14:17], v13 offset0:34 offset1:51
	ds_read2_b64 v[18:21], v26 offset0:160 offset1:176
	v_add_u32_e32 v8, 0x1000, v8
	s_waitcnt lgkmcnt(1)
	v_mov_b32_e32 v23, v16
	s_waitcnt lgkmcnt(0)
	v_mov_b32_e32 v24, v19
	v_mov_b32_e32 v25, v21
	v_mov_b32_e32 v16, v15
	v_mov_b32_e32 v19, v20
	v_mov_b32_e32 v22, v14
	v_pk_mul_f32 v[14:15], v[16:17], v[18:19]
	v_pk_mul_f32 v[16:17], v[16:17], v[24:25]
	v_pk_fma_f32 v[14:15], v[22:23], v[24:25], v[14:15]
	v_pk_fma_f32 v[16:17], v[22:23], v[18:19], v[16:17] neg_lo:[0,0,1] neg_hi:[0,0,1]
	s_nop 0
	v_cndmask_b32_e32 v29, v15, v17, vcc
	v_cndmask_b32_e32 v30, v14, v16, vcc
	ds_read2_b64 v[14:17], v13 offset0:68 offset1:85
	ds_read2_b64 v[18:21], v26 offset0:192 offset1:208
	s_waitcnt lgkmcnt(1)
	v_mov_b32_e32 v23, v16
	s_waitcnt lgkmcnt(0)
	v_mov_b32_e32 v24, v19
	v_mov_b32_e32 v25, v21
	v_mov_b32_e32 v16, v15
	v_mov_b32_e32 v19, v20
	v_mov_b32_e32 v22, v14
	v_pk_mul_f32 v[14:15], v[16:17], v[18:19]
	v_pk_mul_f32 v[16:17], v[16:17], v[24:25]
	v_pk_fma_f32 v[14:15], v[22:23], v[24:25], v[14:15]
	v_pk_fma_f32 v[16:17], v[22:23], v[18:19], v[16:17] neg_lo:[0,0,1] neg_hi:[0,0,1]
	s_nop 0
	v_cndmask_b32_e32 v31, v15, v17, vcc
	v_cndmask_b32_e32 v32, v14, v16, vcc
	ds_read2_b64 v[14:17], v13 offset0:102 offset1:119
	ds_read2_b64 v[18:21], v26 offset0:224 offset1:240
	s_waitcnt lgkmcnt(1)
	v_mov_b32_e32 v23, v16
	s_waitcnt lgkmcnt(0)
	v_mov_b32_e32 v24, v19
	v_mov_b32_e32 v25, v21
	v_mov_b32_e32 v16, v15
	v_mov_b32_e32 v19, v20
	v_mov_b32_e32 v22, v14
	v_pk_mul_f32 v[14:15], v[16:17], v[18:19]
	v_pk_mul_f32 v[16:17], v[16:17], v[24:25]
	v_pk_fma_f32 v[14:15], v[22:23], v[24:25], v[14:15]
	v_pk_fma_f32 v[16:17], v[22:23], v[18:19], v[16:17] neg_lo:[0,0,1] neg_hi:[0,0,1]
	s_nop 0
	v_cndmask_b32_e32 v13, v15, v17, vcc
	v_cndmask_b32_e32 v17, v14, v16, vcc
	v_cvt_pk_bf16_f32 v14, v28, v27
	v_cvt_pk_bf16_f32 v15, v30, v29
	v_cvt_pk_bf16_f32 v16, v32, v31
	v_cvt_pk_bf16_f32 v17, v17, v13
	v_add_u32_e32 v13, 0x200, v12
	v_cmp_lt_u32_e32 vcc, s11, v12
	global_store_dwordx4 v[6:7], v[14:17], off sc1
	v_lshl_add_u64 v[6:7], v[6:7], 0, s[36:37]
	s_or_b64 s[8:9], vcc, s[8:9]
	v_mov_b32_e32 v12, v13
	s_andn2_b64 exec, exec, s[8:9]
	s_cbranch_execnz .LBB0_136
	s_or_b64 exec, exec, s[8:9]
	s_mov_b64 s[8:9], 0
	v_mov_b32_e32 v16, v69
	v_mov_b32_e32 v17, v81
	v_mov_b64_e32 v[14:15], v[42:43]
	v_mov_b32_e32 v18, v83
	v_mov_b32_e32 v19, v0
	s_branch .LBB0_139
.LBB0_138:
	s_or_b64 exec, exec, s[28:29]
	s_waitcnt lgkmcnt(1)
	v_cvt_pk_bf16_f32 v6, v6, v7
	v_cvt_pk_bf16_f32 v7, v8, v9
	s_waitcnt lgkmcnt(0)
	v_cvt_pk_bf16_f32 v8, v10, v11
	v_cvt_pk_bf16_f32 v9, v12, v13
	s_movk_i32 s11, 0x3dff
	global_store_dwordx4 v[14:15], v[6:9], off sc1
	v_cmp_lt_u32_e32 vcc, s11, v19
	v_add_u32_e32 v18, 0xfffffbe0, v18
	v_add_u32_e32 v6, 0x200, v19
	v_lshl_add_u64 v[14:15], v[14:15], 0, s[36:37]
	v_add_u32_e32 v17, 16, v17
	v_add_u32_e32 v16, 0x1000, v16
	s_or_b64 s[8:9], vcc, s[8:9]
	v_mov_b32_e32 v19, v6
	s_andn2_b64 exec, exec, s[8:9]
	s_cbranch_execz .LBB0_82

.LBB0_165:
	s_or_b64 exec, exec, s[4:5]
	s_waitcnt vmcnt(6)
	v_cvt_pk_bf16_f32 v84, v10, v11
	v_cvt_pk_bf16_f32 v85, v12, v13
	s_waitcnt vmcnt(6)
	v_cvt_pk_bf16_f32 v86, v6, v7
	v_cvt_pk_bf16_f32 v87, v8, v9
	v_cmp_gt_i32_e32 vcc, s31, v82
	global_store_dwordx4 v[74:75], v[84:87], off sc1
	s_and_saveexec_b64 s[4:5], vcc
	s_cbranch_execz .LBB0_175
	v_add_co_u32_e32 v88, vcc, 0x100000, v74
	s_waitcnt vmcnt(5)
	v_cvt_pk_bf16_f32 v84, v18, v19
	v_cvt_pk_bf16_f32 v85, v20, v21
	s_waitcnt vmcnt(5)
	v_cvt_pk_bf16_f32 v86, v14, v15
	v_cvt_pk_bf16_f32 v87, v16, v17
	v_addc_co_u32_e32 v89, vcc, 0, v75, vcc
	global_store_dwordx4 v[88:89], v[84:87], off sc1
	s_or_b64 exec, exec, s[4:5]
	v_cmp_gt_i32_e32 vcc, s30, v82
	s_and_saveexec_b64 s[4:5], vcc
	s_cbranch_execnz .LBB0_176

.LBB0_168:
	v_add_co_u32_e32 v88, vcc, 0x300000, v74
	s_waitcnt vmcnt(1)
	v_cvt_pk_bf16_f32 v84, v42, v43
	v_cvt_pk_bf16_f32 v85, v44, v45
	s_waitcnt vmcnt(1)
	v_cvt_pk_bf16_f32 v86, v38, v39
	v_cvt_pk_bf16_f32 v87, v40, v41
	v_addc_co_u32_e32 v89, vcc, 0, v75, vcc
	global_store_dwordx4 v[88:89], v[84:87], off sc1

.LBB0_171:
	s_or_b64 exec, exec, s[10:11]
	s_and_saveexec_b64 s[10:11], s[0:1]
	s_cbranch_execz .LBB0_162
	v_add_co_u32_e32 v88, vcc, 0x400000, v74
	v_cvt_pk_bf16_f32 v84, v30, v31
	s_nop 0
	v_addc_co_u32_e32 v89, vcc, 0, v75, vcc
	v_cvt_pk_bf16_f32 v85, v32, v33
	v_cvt_pk_bf16_f32 v86, v34, v35
	v_cvt_pk_bf16_f32 v87, v36, v37
	v_cmp_gt_i32_e32 vcc, s36, v82
	global_store_dwordx4 v[88:89], v[84:87], off sc1
	s_and_saveexec_b64 s[0:1], vcc
	s_cbranch_execz .LBB0_177
	v_add_co_u32_e32 v88, vcc, 0x500000, v74
	s_waitcnt vmcnt(6)
	v_cvt_pk_bf16_f32 v84, v46, v47
	v_cvt_pk_bf16_f32 v85, v48, v49
	v_cvt_pk_bf16_f32 v86, v50, v51
	v_cvt_pk_bf16_f32 v87, v52, v53
	v_addc_co_u32_e32 v89, vcc, 0, v75, vcc
	global_store_dwordx4 v[88:89], v[84:87], off sc1
	s_or_b64 exec, exec, s[0:1]
	v_cmp_gt_i32_e32 vcc, s29, v82
	s_and_saveexec_b64 s[0:1], vcc
	s_cbranch_execnz .LBB0_178

.LBB0_176:
	v_add_co_u32_e32 v88, vcc, 0x200000, v74
	s_waitcnt vmcnt(3)
	v_cvt_pk_bf16_f32 v84, v26, v27
	v_cvt_pk_bf16_f32 v85, v28, v29
	s_waitcnt vmcnt(3)
	v_cvt_pk_bf16_f32 v86, v22, v23
	v_cvt_pk_bf16_f32 v87, v24, v25
	v_addc_co_u32_e32 v89, vcc, 0, v75, vcc
	global_store_dwordx4 v[88:89], v[84:87], off sc1
	s_or_b64 exec, exec, s[4:5]
	v_cmp_gt_i32_e32 vcc, s33, v82
	s_and_saveexec_b64 s[4:5], vcc
	s_cbranch_execnz .LBB0_168
	s_branch .LBB0_169

.LBB0_178:
	v_add_co_u32_e32 v88, vcc, 0x600000, v74
	s_waitcnt vmcnt(4)
	v_cvt_pk_bf16_f32 v84, v54, v55
	v_cvt_pk_bf16_f32 v85, v56, v57
	v_cvt_pk_bf16_f32 v86, v58, v59
	v_cvt_pk_bf16_f32 v87, v60, v61
	v_addc_co_u32_e32 v89, vcc, 0, v75, vcc
	global_store_dwordx4 v[88:89], v[84:87], off sc1
	s_or_b64 exec, exec, s[0:1]
	v_cmp_gt_i32_e32 vcc, s37, v82
	s_and_b64 exec, exec, vcc
	s_cbranch_execz .LBB0_162
.LBB0_179:
	v_add_co_u32_e32 v88, vcc, 0x700000, v74
	s_waitcnt vmcnt(2)
	v_cvt_pk_bf16_f32 v84, v62, v63
	v_cvt_pk_bf16_f32 v85, v64, v65
	v_cvt_pk_bf16_f32 v86, v66, v67
	v_cvt_pk_bf16_f32 v87, v68, v69
	v_addc_co_u32_e32 v89, vcc, 0, v75, vcc
	global_store_dwordx4 v[88:89], v[84:87], off sc1
	s_branch .LBB0_162

.LBB0_185:
	s_or_b64 exec, exec, s[4:5]
	s_waitcnt vmcnt(6)
	v_cvt_pk_bf16_f32 v84, v10, v11
	v_cvt_pk_bf16_f32 v85, v12, v13
	s_waitcnt vmcnt(6)
	v_cvt_pk_bf16_f32 v86, v6, v7
	v_cvt_pk_bf16_f32 v87, v8, v9
	v_cmp_gt_i32_e32 vcc, s23, v82
	global_store_dwordx4 v[74:75], v[84:87], off sc1
	s_and_saveexec_b64 s[4:5], vcc
	s_cbranch_execz .LBB0_195
	v_add_co_u32_e32 v88, vcc, 0x100000, v74
	s_waitcnt vmcnt(5)
	v_cvt_pk_bf16_f32 v84, v18, v19
	v_cvt_pk_bf16_f32 v85, v20, v21
	s_waitcnt vmcnt(5)
	v_cvt_pk_bf16_f32 v86, v14, v15
	v_cvt_pk_bf16_f32 v87, v16, v17
	v_addc_co_u32_e32 v89, vcc, 0, v75, vcc
	global_store_dwordx4 v[88:89], v[84:87], off sc1
	s_or_b64 exec, exec, s[4:5]
	v_cmp_gt_i32_e32 vcc, 0, v82
	s_and_saveexec_b64 s[4:5], vcc
	s_cbranch_execnz .LBB0_196

.LBB0_191:
	s_or_b64 exec, exec, s[10:11]
	s_and_saveexec_b64 s[10:11], s[0:1]
	s_cbranch_execz .LBB0_182
	v_add_co_u32_e32 v88, vcc, 0x400000, v74
	v_cvt_pk_bf16_f32 v84, v30, v31
	s_nop 0
	v_addc_co_u32_e32 v89, vcc, 0, v75, vcc
	v_cvt_pk_bf16_f32 v85, v32, v33
	v_cvt_pk_bf16_f32 v86, v34, v35
	v_cvt_pk_bf16_f32 v87, v36, v37
	v_cmp_gt_u32_e32 vcc, s31, v82
	global_store_dwordx4 v[88:89], v[84:87], off sc1
	s_and_saveexec_b64 s[0:1], vcc
	s_cbranch_execz .LBB0_197
	v_add_co_u32_e32 v88, vcc, 0x500000, v74
	s_waitcnt vmcnt(6)
	v_cvt_pk_bf16_f32 v84, v46, v47
	v_cvt_pk_bf16_f32 v85, v48, v49
	v_cvt_pk_bf16_f32 v86, v50, v51
	v_cvt_pk_bf16_f32 v87, v52, v53
	v_addc_co_u32_e32 v89, vcc, 0, v75, vcc
	global_store_dwordx4 v[88:89], v[84:87], off sc1
	s_or_b64 exec, exec, s[0:1]
	v_cmp_gt_u32_e32 vcc, s33, v82
	s_and_saveexec_b64 s[0:1], vcc
	s_cbranch_execnz .LBB0_198

.LBB0_196:
	v_add_co_u32_e32 v88, vcc, 0x200000, v74
	s_waitcnt vmcnt(3)
	v_cvt_pk_bf16_f32 v84, v26, v27
	v_cvt_pk_bf16_f32 v85, v28, v29
	s_waitcnt vmcnt(3)
	v_cvt_pk_bf16_f32 v86, v22, v23
	v_cvt_pk_bf16_f32 v87, v24, v25
	v_addc_co_u32_e32 v89, vcc, 0, v75, vcc
	global_store_dwordx4 v[88:89], v[84:87], off sc1
	s_or_b64 exec, exec, s[4:5]
	v_cmp_gt_i32_e32 vcc, s28, v82
	s_and_saveexec_b64 s[4:5], vcc
	s_cbranch_execnz .LBB0_188
	s_branch .LBB0_189

.LBB0_198:
	v_add_co_u32_e32 v88, vcc, 0x600000, v74
	s_waitcnt vmcnt(4)
	v_cvt_pk_bf16_f32 v84, v54, v55
	v_cvt_pk_bf16_f32 v85, v56, v57
	v_cvt_pk_bf16_f32 v86, v58, v59
	v_cvt_pk_bf16_f32 v87, v60, v61
	v_addc_co_u32_e32 v89, vcc, 0, v75, vcc
	global_store_dwordx4 v[88:89], v[84:87], off sc1
	s_or_b64 exec, exec, s[0:1]
	v_cmp_gt_u32_e32 vcc, s34, v82
	s_and_b64 exec, exec, vcc
	s_cbranch_execz .LBB0_182

.LBB0_205:
	s_or_b64 exec, exec, s[4:5]
	s_waitcnt vmcnt(6)
	v_pk_mul_f32 v[84:85], v[74:75], v[6:7] op_sel_hi:[0,1]
	v_pk_mul_f32 v[86:87], v[74:75], v[8:9] op_sel_hi:[0,1]
	v_cvt_pk_bf16_f32 v84, v84, v85
	v_cvt_pk_bf16_f32 v85, v86, v87
	v_pk_mul_f32 v[86:87], v[74:75], v[10:11] op_sel_hi:[0,1]
	v_pk_mul_f32 v[88:89], v[74:75], v[12:13] op_sel_hi:[0,1]
	v_cvt_pk_bf16_f32 v86, v86, v87
	v_cvt_pk_bf16_f32 v87, v88, v89
	v_cmp_gt_i32_e32 vcc, s36, v70
	global_store_dwordx4 v[76:77], v[84:87], off sc1
	s_and_saveexec_b64 s[4:5], vcc
	s_cbranch_execz .LBB0_215
	v_pk_mul_f32 v[84:85], v[74:75], v[14:15] op_sel:[1,0]
	v_pk_mul_f32 v[86:87], v[74:75], v[16:17] op_sel:[1,0]
	v_cvt_pk_bf16_f32 v84, v84, v85
	v_cvt_pk_bf16_f32 v85, v86, v87
	v_pk_mul_f32 v[86:87], v[74:75], v[18:19] op_sel:[1,0]
	v_pk_mul_f32 v[88:89], v[74:75], v[20:21] op_sel:[1,0]
	v_cvt_pk_bf16_f32 v86, v86, v87
	v_cvt_pk_bf16_f32 v87, v88, v89
	v_add_co_u32_e32 v88, vcc, 0x100000, v76
	s_nop 1
	v_addc_co_u32_e32 v89, vcc, 0, v77, vcc
	global_store_dwordx4 v[88:89], v[84:87], off sc1
	s_or_b64 exec, exec, s[4:5]
	v_cmp_gt_i32_e32 vcc, s34, v70
	s_and_saveexec_b64 s[4:5], vcc
	s_cbranch_execnz .LBB0_216

.LBB0_208:
	s_waitcnt vmcnt(1)
	v_pk_mul_f32 v[84:85], v[80:81], v[46:47] op_sel_hi:[0,1]
	v_pk_mul_f32 v[86:87], v[80:81], v[48:49] op_sel_hi:[0,1]
	v_cvt_pk_bf16_f32 v84, v84, v85
	v_cvt_pk_bf16_f32 v85, v86, v87
	v_pk_mul_f32 v[86:87], v[80:81], v[50:51] op_sel_hi:[0,1]
	v_pk_mul_f32 v[88:89], v[80:81], v[52:53] op_sel_hi:[0,1]
	v_cvt_pk_bf16_f32 v86, v86, v87
	v_cvt_pk_bf16_f32 v87, v88, v89
	v_add_co_u32_e32 v88, vcc, 0x300000, v76
	s_nop 1
	v_addc_co_u32_e32 v89, vcc, 0, v77, vcc
	global_store_dwordx4 v[88:89], v[84:87], off sc1

.LBB0_211:
	s_or_b64 exec, exec, s[22:23]
	s_and_saveexec_b64 s[22:23], s[0:1]
	s_cbranch_execz .LBB0_202
	v_pk_mul_f32 v[84:85], v[34:35], v[78:79] op_sel_hi:[1,0]
	v_pk_mul_f32 v[86:87], v[36:37], v[78:79] op_sel_hi:[1,0]
	v_cvt_pk_bf16_f32 v84, v84, v85
	v_cvt_pk_bf16_f32 v85, v86, v87
	v_pk_mul_f32 v[86:87], v[30:31], v[78:79] op_sel_hi:[1,0]
	v_pk_mul_f32 v[88:89], v[32:33], v[78:79] op_sel_hi:[1,0]
	v_cvt_pk_bf16_f32 v86, v86, v87
	v_cvt_pk_bf16_f32 v87, v88, v89
	v_add_co_u32_e32 v88, vcc, 0x400000, v76
	s_nop 1
	v_addc_co_u32_e32 v89, vcc, 0, v77, vcc
	v_cmp_gt_i32_e32 vcc, s31, v70
	global_store_dwordx4 v[88:89], v[84:87], off sc1
	s_and_saveexec_b64 s[0:1], vcc
	s_cbranch_execz .LBB0_217
	v_pk_mul_f32 v[84:85], v[42:43], v[78:79] op_sel:[0,1]
	v_pk_mul_f32 v[86:87], v[44:45], v[78:79] op_sel:[0,1]
	v_cvt_pk_bf16_f32 v84, v84, v85
	v_cvt_pk_bf16_f32 v85, v86, v87
	v_pk_mul_f32 v[86:87], v[38:39], v[78:79] op_sel:[0,1]
	v_pk_mul_f32 v[88:89], v[40:41], v[78:79] op_sel:[0,1]
	v_cvt_pk_bf16_f32 v86, v86, v87
	v_cvt_pk_bf16_f32 v87, v88, v89
	v_add_co_u32_e32 v88, vcc, 0x500000, v76
	s_nop 1
	v_addc_co_u32_e32 v89, vcc, 0, v77, vcc
	global_store_dwordx4 v[88:89], v[84:87], off sc1
	s_or_b64 exec, exec, s[0:1]
	v_cmp_gt_i32_e32 vcc, s30, v70
	s_and_saveexec_b64 s[0:1], vcc
	s_cbranch_execnz .LBB0_218

.LBB0_216:
	s_waitcnt vmcnt(4)
	v_pk_mul_f32 v[84:85], v[72:73], v[22:23] op_sel_hi:[0,1]
	v_pk_mul_f32 v[86:87], v[72:73], v[24:25] op_sel_hi:[0,1]
	v_cvt_pk_bf16_f32 v84, v84, v85
	v_cvt_pk_bf16_f32 v85, v86, v87
	v_pk_mul_f32 v[86:87], v[72:73], v[26:27] op_sel_hi:[0,1]
	v_pk_mul_f32 v[88:89], v[72:73], v[28:29] op_sel_hi:[0,1]
	v_cvt_pk_bf16_f32 v86, v86, v87
	v_cvt_pk_bf16_f32 v87, v88, v89
	v_add_co_u32_e32 v88, vcc, 0x200000, v76
	s_nop 1
	v_addc_co_u32_e32 v89, vcc, 0, v77, vcc
	global_store_dwordx4 v[88:89], v[84:87], off sc1
	s_or_b64 exec, exec, s[4:5]
	v_cmp_gt_i32_e32 vcc, s35, v70
	s_and_saveexec_b64 s[4:5], vcc
	s_cbranch_execnz .LBB0_208
	s_branch .LBB0_209

.LBB0_218:
	s_waitcnt vmcnt(2)
	v_pk_mul_f32 v[84:85], v[58:59], v[82:83] op_sel_hi:[1,0]
	v_pk_mul_f32 v[86:87], v[60:61], v[82:83] op_sel_hi:[1,0]
	v_cvt_pk_bf16_f32 v84, v84, v85
	v_cvt_pk_bf16_f32 v85, v86, v87
	v_pk_mul_f32 v[86:87], v[54:55], v[82:83] op_sel_hi:[1,0]
	v_pk_mul_f32 v[88:89], v[56:57], v[82:83] op_sel_hi:[1,0]
	v_cvt_pk_bf16_f32 v86, v86, v87
	v_cvt_pk_bf16_f32 v87, v88, v89
	v_add_co_u32_e32 v88, vcc, 0x600000, v76
	s_nop 1
	v_addc_co_u32_e32 v89, vcc, 0, v77, vcc
	global_store_dwordx4 v[88:89], v[84:87], off sc1
	s_or_b64 exec, exec, s[0:1]
	v_cmp_gt_i32_e32 vcc, s29, v70
	s_and_b64 exec, exec, vcc
	s_cbranch_execz .LBB0_202
.LBB0_219:
	s_waitcnt vmcnt(2)
	v_mov_b32_e32 v70, v83
	v_pk_mul_f32 v[84:85], v[66:67], v[70:71] op_sel_hi:[1,0]
	v_pk_mul_f32 v[86:87], v[68:69], v[70:71] op_sel_hi:[1,0]
	v_cvt_pk_bf16_f32 v84, v84, v85
	v_cvt_pk_bf16_f32 v85, v86, v87
	v_pk_mul_f32 v[86:87], v[62:63], v[70:71] op_sel_hi:[1,0]
	v_pk_mul_f32 v[88:89], v[64:65], v[70:71] op_sel_hi:[1,0]
	v_cvt_pk_bf16_f32 v86, v86, v87
	v_cvt_pk_bf16_f32 v87, v88, v89
	v_add_co_u32_e32 v88, vcc, 0x700000, v76
	s_nop 1
	v_addc_co_u32_e32 v89, vcc, 0, v77, vcc
	global_store_dwordx4 v[88:89], v[84:87], off sc1
	s_branch .LBB0_202

.LBB0_244:
	s_or_b64 exec, exec, s[0:1]
	s_waitcnt vmcnt(0)
	v_cvt_f64_f32_e32 v[12:13], v29
	s_mov_b32 s0, 0x652b82fe
	v_mul_f64 v[18:19], v[18:19], v[12:13]
	s_mov_b32 s1, 0x3ff71547
	v_mul_f64 v[24:25], v[18:19], s[0:1]
	s_mov_b32 s0, 0xfefa39ef
	v_rndne_f64_e32 v[24:25], v[24:25]
	s_mov_b32 s1, 0xbfe62e42
	v_fma_f64 v[26:27], s[0:1], v[24:25], v[18:19]
	s_mov_b32 s0, 0x3b39803f
	s_mov_b32 s1, 0xbc7abc9e
	v_fmac_f64_e32 v[26:27], s[0:1], v[24:25]
	s_mov_b32 s0, 0x6a5dcb37
	v_mov_b32_e32 v32, 0xfca7ab0c
	v_mov_b32_e32 v33, 0x3e928af3
	s_mov_b32 s1, 0x3e5ade15
	v_fmac_f64_e32 v[32:33], s[0:1], v[26:27]
	v_mov_b32_e32 v34, 0x623fde64
	v_mov_b32_e32 v35, 0x3ec71dee
	v_fmac_f64_e32 v[34:35], v[26:27], v[32:33]
	v_mov_b32_e32 v32, 0x7c89e6b0
	v_mov_b32_e32 v33, 0x3efa0199
	v_fmac_f64_e32 v[32:33], v[26:27], v[34:35]
	v_mov_b32_e32 v34, 0x14761f6e
	v_mov_b32_e32 v35, 0x3f2a01a0
	v_fmac_f64_e32 v[34:35], v[26:27], v[32:33]
	v_mov_b32_e32 v32, 0x1852b7b0
	v_mov_b32_e32 v33, 0x3f56c16c
	v_fmac_f64_e32 v[32:33], v[26:27], v[34:35]
	v_mov_b32_e32 v34, 0x11122322
	v_mov_b32_e32 v35, 0x3f811111
	v_fmac_f64_e32 v[34:35], v[26:27], v[32:33]
	v_mov_b32_e32 v32, 0x555502a1
	v_mov_b32_e32 v33, 0x3fa55555
	v_fmac_f64_e32 v[32:33], v[26:27], v[34:35]
	v_mov_b32_e32 v34, 0x55555511
	v_mov_b32_e32 v35, 0x3fc55555
	v_fmac_f64_e32 v[34:35], v[26:27], v[32:33]
	v_mov_b32_e32 v32, 11
	v_mov_b32_e32 v33, 0x3fe00000
	v_fmac_f64_e32 v[32:33], v[26:27], v[34:35]
	s_mov_b32 s0, 0
	v_fma_f64 v[32:33], v[26:27], v[32:33], 1.0
	s_mov_b32 s1, 0x40900000
	v_fma_f64 v[26:27], v[26:27], v[32:33], 1.0
	v_cvt_i32_f64_e32 v24, v[24:25]
	v_cmp_nlt_f64_e32 vcc, s[0:1], v[18:19]
	s_mov_b32 s0, 0
	v_ldexp_f64 v[24:25], v[26:27], v24
	v_mov_b32_e32 v26, 0x7ff00000
	s_mov_b32 s1, 0xc090cc00
	v_cndmask_b32_e32 v25, v26, v25, vcc
	v_cmp_ngt_f64_e64 s[0:1], s[0:1], v[18:19]
	s_mov_b32 s16, 0x9037ab78
	s_and_b64 vcc, s[0:1], vcc
	v_cndmask_b32_e64 v19, 0, v25, s[0:1]
	s_mov_b32 s17, 0x3e21eeb6
	s_mov_b32 s0, 0x46cc5e42
	v_cndmask_b32_e32 v18, 0, v24, vcc
	v_mul_f64 v[24:25], v[14:15], v[14:15]
	s_mov_b32 s1, 0xbda907db
	v_mov_b64_e32 v[36:37], s[16:17]
	s_mov_b32 s16, 0xa17f65f6
	v_mul_f64 v[26:27], v[24:25], 0.5
	v_fma_f64 v[38:39], s[0:1], v[24:25], v[36:37]
	s_mov_b32 s17, 0xbe927e4f
	s_mov_b32 s18, 0x19f4ec90
	v_add_f64 v[32:33], -v[26:27], 1.0
	v_fma_f64 v[38:39], v[24:25], v[38:39], s[16:17]
	s_mov_b32 s19, 0x3efa01a0
	s_mov_b32 s22, 0x16c16967
	s_mov_b32 s10, 0x55555555
	v_add_f64 v[34:35], -v[32:33], 1.0
	v_fma_f64 v[38:39], v[24:25], v[38:39], s[18:19]
	s_mov_b32 s23, 0xbf56c16c
	s_mov_b32 s11, 0x3fa55555
	v_add_f64 v[26:27], v[34:35], -v[26:27]
	v_fma_f64 v[38:39], v[24:25], v[38:39], s[22:23]
	v_mul_f64 v[34:35], v[24:25], v[24:25]
	v_fma_f64 v[38:39], v[24:25], v[38:39], s[10:11]
	v_fma_f64 v[26:27], v[14:15], -v[16:17], v[26:27]
	s_mov_b32 s24, 0xb42fdfa7
	v_fmac_f64_e32 v[26:27], v[34:35], v[38:39]
	s_mov_b32 s25, 0xbe5ae600
	s_mov_b32 s26, 0xf9a43bb8
	v_add_f64 v[26:27], v[32:33], v[26:27]
	s_mov_b32 s27, 0x3de5e0b2
	v_mov_b64_e32 v[32:33], s[24:25]
	s_mov_b32 s24, 0x796cde01
	v_fma_f64 v[34:35], s[26:27], v[24:25], v[32:33]
	s_mov_b32 s25, 0x3ec71de3
	s_mov_b32 s28, 0x19e83e5c
	s_mov_b32 s8, 0x11110bb3
	v_fma_f64 v[34:35], v[24:25], v[34:35], s[24:25]
	s_mov_b32 s29, 0xbf2a01a0
	s_mov_b32 s9, 0x3f811111
	v_fma_f64 v[34:35], v[24:25], v[34:35], s[28:29]
	v_fma_f64 v[34:35], v[24:25], v[34:35], s[8:9]
	v_mul_f64 v[38:39], v[14:15], -v[24:25]
	v_mul_f64 v[40:41], v[16:17], 0.5
	v_fmac_f64_e32 v[40:41], v[38:39], v[34:35]
	v_fma_f64 v[16:17], v[24:25], v[40:41], -v[16:17]
	s_mov_b32 s31, 0xbfc55555
	s_mov_b32 s30, s10
	v_fmac_f64_e32 v[16:17], s[30:31], v[38:39]
	v_add_f64 v[14:15], v[14:15], -v[16:17]
	v_and_b32_e32 v16, 1, v28
	v_xor_b32_e32 v15, 0x80000000, v15
	v_cmp_eq_u32_e32 vcc, 0, v16
	s_brev_b32 s3, 1
	v_lshlrev_b32_e32 v16, 30, v28
	v_cndmask_b32_e32 v15, v15, v27, vcc
	v_bitop3_b32 v15, v15, v16, s3 bitop3:0x78
	v_mul_f64 v[16:17], v[20:21], v[20:21]
	v_mul_f64 v[24:25], v[16:17], 0.5
	v_fmac_f64_e32 v[36:37], s[0:1], v[16:17]
	v_cndmask_b32_e32 v14, v14, v26, vcc
	v_add_f64 v[26:27], -v[24:25], 1.0
	v_fma_f64 v[34:35], v[16:17], v[36:37], s[16:17]
	v_add_f64 v[28:29], -v[26:27], 1.0
	v_fma_f64 v[34:35], v[16:17], v[34:35], s[18:19]
	v_add_f64 v[24:25], v[28:29], -v[24:25]
	v_fma_f64 v[34:35], v[16:17], v[34:35], s[22:23]
	v_mul_f64 v[28:29], v[16:17], v[16:17]
	v_fma_f64 v[34:35], v[16:17], v[34:35], s[10:11]
	v_fma_f64 v[24:25], v[20:21], -v[22:23], v[24:25]
	v_fmac_f64_e32 v[24:25], v[28:29], v[34:35]
	v_fmac_f64_e32 v[32:33], s[26:27], v[16:17]
	v_add_f64 v[24:25], v[26:27], v[24:25]
	v_fma_f64 v[26:27], v[16:17], v[32:33], s[24:25]
	v_fma_f64 v[26:27], v[16:17], v[26:27], s[28:29]
	v_fma_f64 v[26:27], v[16:17], v[26:27], s[8:9]
	v_mul_f64 v[28:29], v[20:21], -v[16:17]
	v_mul_f64 v[32:33], v[22:23], 0.5
	v_fmac_f64_e32 v[32:33], v[28:29], v[26:27]
	s_movk_i32 s33, 0x1f8
	v_fma_f64 v[16:17], v[16:17], v[32:33], -v[22:23]
	v_cmp_class_f64_e64 vcc, v[10:11], s33
	v_fmac_f64_e32 v[16:17], s[30:31], v[28:29]
	v_and_b32_e32 v10, 1, v30
	v_add_f64 v[16:17], v[20:21], -v[16:17]
	v_cmp_eq_u32_e64 s[0:1], 0, v10
	v_mov_b32_e32 v31, 0x7ff80000
	v_cndmask_b32_e32 v14, 0, v14, vcc
	v_cndmask_b32_e64 v10, v24, v16, s[0:1]
	v_cndmask_b32_e64 v16, v25, v17, s[0:1]
	v_lshlrev_b32_e32 v17, 30, v30
	v_xor_b32_e32 v11, v17, v11
	v_bitop3_b32 v11, v16, v11, s3 bitop3:0x78
	v_cndmask_b32_e32 v15, v31, v15, vcc
	v_cndmask_b32_e32 v10, 0, v10, vcc
	v_cndmask_b32_e32 v11, v31, v11, vcc
	v_mul_u32_u24_e32 v16, 34, v0
	v_mul_f64 v[14:15], v[18:19], v[14:15]
	v_mul_f64 v[10:11], v[18:19], v[10:11]
	v_lshl_add_u32 v18, v16, 2, 0
	v_mov_b32_e32 v16, 1.0
	v_mov_b32_e32 v17, 0
	ds_write_b64 v18, v[16:17]
	v_mov_b64_e32 v[16:17], v[14:15]
	v_fma_f64 v[22:23], 0, v[14:15], v[10:11]
	v_fmac_f64_e32 v[16:17], 0x80000000, v[10:11]
	v_mul_f64 v[24:25], v[10:11], v[22:23]
	v_cvt_f32_f64_e32 v19, v[16:17]
	v_mul_f64 v[20:21], v[10:11], v[16:17]
	v_fma_f64 v[16:17], v[14:15], v[16:17], -v[24:25]
	v_cvt_f32_f64_e32 v24, v[16:17]
	v_cvt_f32_f64_e32 v25, v[22:23]
	v_fmac_f64_e32 v[20:21], v[14:15], v[22:23]
	ds_write2_b32 v18, v25, v24 offset0:3 offset1:4
	v_mul_f64 v[24:25], v[10:11], v[16:17]
	v_mul_f64 v[22:23], v[10:11], v[20:21]
	v_fma_f64 v[16:17], v[14:15], v[16:17], -v[22:23]
	v_fmac_f64_e32 v[24:25], v[14:15], v[20:21]
	v_cvt_f32_f64_e32 v22, v[16:17]
	v_cvt_f32_f64_e32 v23, v[20:21]
	v_mul_f64 v[20:21], v[10:11], v[24:25]
	ds_write2_b32 v18, v23, v22 offset0:5 offset1:6
	v_mul_f64 v[22:23], v[10:11], v[16:17]
	v_fma_f64 v[16:17], v[14:15], v[16:17], -v[20:21]
	v_cvt_f32_f64_e32 v20, v[16:17]
	v_cvt_f32_f64_e32 v21, v[24:25]
	v_fmac_f64_e32 v[22:23], v[14:15], v[24:25]
	ds_write2_b32 v18, v21, v20 offset0:7 offset1:8
	v_mul_f64 v[20:21], v[10:11], v[16:17]
	v_mul_f64 v[24:25], v[10:11], v[22:23]
	v_fma_f64 v[16:17], v[14:15], v[16:17], -v[24:25]
	v_fmac_f64_e32 v[20:21], v[14:15], v[22:23]
	v_cvt_f32_f64_e32 v24, v[16:17]
	v_cvt_f32_f64_e32 v25, v[22:23]
	v_mul_f64 v[22:23], v[10:11], v[20:21]
	ds_write2_b32 v18, v25, v24 offset0:9 offset1:10
	v_mul_f64 v[24:25], v[10:11], v[16:17]
	v_fma_f64 v[16:17], v[14:15], v[16:17], -v[22:23]
	v_cvt_f32_f64_e32 v22, v[16:17]
	v_cvt_f32_f64_e32 v23, v[20:21]
	v_fmac_f64_e32 v[24:25], v[14:15], v[20:21]
	ds_write2_b32 v18, v23, v22 offset0:11 offset1:12
	v_mul_f64 v[22:23], v[10:11], v[16:17]
	v_mul_f64 v[20:21], v[10:11], v[24:25]
	v_fma_f64 v[16:17], v[14:15], v[16:17], -v[20:21]
	v_fmac_f64_e32 v[22:23], v[14:15], v[24:25]
	v_cvt_f32_f64_e32 v20, v[16:17]
	v_cvt_f32_f64_e32 v21, v[24:25]
	v_mul_f64 v[24:25], v[10:11], v[22:23]
	ds_write2_b32 v18, v21, v20 offset0:13 offset1:14
	v_mul_f64 v[20:21], v[10:11], v[16:17]
	v_fma_f64 v[16:17], v[14:15], v[16:17], -v[24:25]
	v_cvt_f32_f64_e32 v24, v[16:17]
	v_cvt_f32_f64_e32 v25, v[22:23]
	v_fmac_f64_e32 v[20:21], v[14:15], v[22:23]
	ds_write2_b32 v18, v25, v24 offset0:15 offset1:16
	v_mul_f64 v[24:25], v[10:11], v[16:17]
	v_mul_f64 v[22:23], v[10:11], v[20:21]
	v_fma_f64 v[16:17], v[14:15], v[16:17], -v[22:23]
	v_fmac_f64_e32 v[24:25], v[14:15], v[20:21]
	v_cvt_f32_f64_e32 v22, v[16:17]
	v_cvt_f32_f64_e32 v23, v[20:21]
	v_mul_f64 v[20:21], v[10:11], v[24:25]
	ds_write2_b32 v18, v23, v22 offset0:17 offset1:18
	v_mul_f64 v[22:23], v[10:11], v[16:17]
	v_fma_f64 v[16:17], v[14:15], v[16:17], -v[20:21]
	v_cvt_f32_f64_e32 v20, v[16:17]
	v_cvt_f32_f64_e32 v21, v[24:25]
	v_fmac_f64_e32 v[22:23], v[14:15], v[24:25]
	ds_write2_b32 v18, v21, v20 offset0:19 offset1:20
	v_mul_f64 v[20:21], v[10:11], v[16:17]
	v_mul_f64 v[24:25], v[10:11], v[22:23]
	v_fma_f64 v[16:17], v[14:15], v[16:17], -v[24:25]
	v_fmac_f64_e32 v[20:21], v[14:15], v[22:23]
	v_cvt_f32_f64_e32 v24, v[16:17]
	v_cvt_f32_f64_e32 v25, v[22:23]
	v_mul_f64 v[22:23], v[10:11], v[20:21]
	ds_write2_b32 v18, v25, v24 offset0:21 offset1:22
	v_mul_f64 v[24:25], v[10:11], v[16:17]
	v_fma_f64 v[16:17], v[14:15], v[16:17], -v[22:23]
	v_cvt_f32_f64_e32 v22, v[16:17]
	v_cvt_f32_f64_e32 v23, v[20:21]
	v_fmac_f64_e32 v[24:25], v[14:15], v[20:21]
	ds_write2_b32 v18, v23, v22 offset0:23 offset1:24
	v_mul_f64 v[22:23], v[10:11], v[16:17]
	v_mul_f64 v[20:21], v[10:11], v[24:25]
	v_fma_f64 v[16:17], v[14:15], v[16:17], -v[20:21]
	v_fmac_f64_e32 v[22:23], v[14:15], v[24:25]
	v_cvt_f32_f64_e32 v20, v[16:17]
	v_cvt_f32_f64_e32 v21, v[24:25]
	v_mul_f64 v[24:25], v[10:11], v[22:23]
	ds_write2_b32 v18, v21, v20 offset0:25 offset1:26
	v_mul_f64 v[20:21], v[10:11], v[16:17]
	v_fma_f64 v[16:17], v[14:15], v[16:17], -v[24:25]
	v_cvt_f32_f64_e32 v24, v[16:17]
	v_cvt_f32_f64_e32 v25, v[22:23]
	v_fmac_f64_e32 v[20:21], v[14:15], v[22:23]
	ds_write2_b32 v18, v25, v24 offset0:27 offset1:28
	v_mul_f64 v[24:25], v[10:11], v[16:17]
	v_mul_f64 v[22:23], v[10:11], v[20:21]
	v_fma_f64 v[16:17], v[14:15], v[16:17], -v[22:23]
	v_fmac_f64_e32 v[24:25], v[14:15], v[20:21]
	v_cvt_f32_f64_e32 v22, v[16:17]
	v_cvt_f32_f64_e32 v23, v[20:21]
	v_mul_f64 v[20:21], v[10:11], v[24:25]
	ds_write2_b32 v18, v23, v22 offset0:29 offset1:30
	v_mul_f64 v[22:23], v[10:11], v[16:17]
	v_fma_f64 v[16:17], v[14:15], v[16:17], -v[20:21]
	v_fmac_f64_e32 v[22:23], v[14:15], v[24:25]
	v_cvt_f32_f64_e32 v16, v[16:17]
	v_cvt_f32_f64_e32 v17, v[24:25]
	ds_write2_b32 v18, v17, v16 offset0:31 offset1:32
	v_cvt_f32_f64_e32 v17, v[22:23]
	s_andn2_b64 vcc, exec, s[4:5]
	ds_write2_b32 v18, v19, v17 offset0:2 offset1:33
	s_cbranch_vccnz .LBB0_246
	v_lshlrev_b32_e32 v20, 1, v6
	v_ashrrev_i32_e32 v21, 31, v20
	v_lshl_add_u64 v[20:21], v[20:21], 2, s[70:71]
	v_add_co_u32_e32 v20, vcc, 0x1f158000, v20
	s_nop 1
	v_addc_co_u32_e32 v21, vcc, 0, v21, vcc
	global_store_dwordx2 v[20:21], v[16:17], off sc1

.LBB0_290:
	v_cndmask_b32_e32 v21, v19, v13, vcc
	v_and_or_b32 v22, v15, 56, v12
	v_and_b32_e32 v23, 30, v14
	v_mad_u32_u24 v21, v22, 17, v21
	v_lshlrev_b32_e32 v22, 7, v22
	v_lshlrev_b32_e32 v23, 2, v23
	v_add3_u32 v26, 0, v22, v23
	v_add_u32_e32 v24, 0x400, v20
	v_lshl_add_u32 v21, v21, 3, 0
	v_add_u32_e32 v50, 0x4000, v26
	v_and_b32_e32 v62, 8, v20
	v_cmp_lt_u32_e64 s[0:1], s8, v20
	v_mov_b32_e32 v20, v24
	ds_read2_b64 v[22:25], v21 offset1:17
	ds_read2_b64 v[26:29], v21 offset0:34 offset1:51
	ds_read2_b64 v[30:33], v21 offset0:68 offset1:85
	ds_read2_b64 v[34:37], v21 offset0:102 offset1:119
	ds_read2_b64 v[38:41], v50 offset0:128 offset1:144
	ds_read2_b64 v[42:45], v50 offset0:160 offset1:176
	ds_read2_b64 v[46:49], v50 offset0:192 offset1:208
	ds_read2_b64 v[50:53], v50 offset0:224 offset1:240
	s_or_b64 s[4:5], s[0:1], s[4:5]
	v_cmp_eq_u32_e64 s[0:1], 0, v62
	v_add_u32_e32 v13, -2, v13
	s_waitcnt lgkmcnt(7)
	v_mov_b32_e32 v54, v22
	v_mov_b32_e32 v55, v24
	v_mov_b32_e32 v24, v23
	s_waitcnt lgkmcnt(6)
	v_mov_b32_e32 v22, v26
	v_mov_b32_e32 v23, v28
	v_mov_b32_e32 v28, v27
	s_waitcnt lgkmcnt(5)
	v_mov_b32_e32 v26, v30
	v_mov_b32_e32 v27, v32
	v_mov_b32_e32 v32, v31
	s_waitcnt lgkmcnt(4)
	v_mov_b32_e32 v30, v34
	v_mov_b32_e32 v31, v36
	v_mov_b32_e32 v36, v35
	s_waitcnt lgkmcnt(3)
	v_mov_b32_e32 v34, v39
	v_mov_b32_e32 v35, v41
	v_mov_b32_e32 v39, v40
	s_waitcnt lgkmcnt(2)
	v_mov_b32_e32 v40, v43
	v_mov_b32_e32 v41, v45
	v_mov_b32_e32 v43, v44
	s_waitcnt lgkmcnt(1)
	v_mov_b32_e32 v44, v47
	v_mov_b32_e32 v45, v49
	v_mov_b32_e32 v47, v48
	s_waitcnt lgkmcnt(0)
	v_mov_b32_e32 v48, v51
	v_mov_b32_e32 v49, v53
	v_mov_b32_e32 v51, v52
	v_pk_mul_f32 v[52:53], v[24:25], v[38:39]
	v_pk_mul_f32 v[24:25], v[24:25], v[34:35]
	v_pk_mul_f32 v[56:57], v[28:29], v[42:43]
	v_pk_mul_f32 v[28:29], v[28:29], v[40:41]
	v_pk_mul_f32 v[58:59], v[32:33], v[46:47]
	v_pk_mul_f32 v[32:33], v[32:33], v[44:45]
	v_pk_mul_f32 v[60:61], v[36:37], v[50:51]
	v_pk_mul_f32 v[36:37], v[36:37], v[48:49]
	v_pk_fma_f32 v[34:35], v[54:55], v[34:35], v[52:53]
	v_pk_fma_f32 v[24:25], v[54:55], v[38:39], v[24:25] neg_lo:[0,0,1] neg_hi:[0,0,1]
	v_pk_fma_f32 v[38:39], v[22:23], v[40:41], v[56:57]
	v_pk_fma_f32 v[22:23], v[22:23], v[42:43], v[28:29] neg_lo:[0,0,1] neg_hi:[0,0,1]
	v_pk_fma_f32 v[28:29], v[26:27], v[44:45], v[58:59]
	v_pk_fma_f32 v[26:27], v[26:27], v[46:47], v[32:33] neg_lo:[0,0,1] neg_hi:[0,0,1]
	v_pk_fma_f32 v[32:33], v[30:31], v[48:49], v[60:61]
	v_pk_fma_f32 v[30:31], v[30:31], v[50:51], v[36:37] neg_lo:[0,0,1] neg_hi:[0,0,1]
	v_cndmask_b32_e64 v21, v35, v25, s[0:1]
	v_cndmask_b32_e64 v24, v34, v24, s[0:1]
	v_cndmask_b32_e64 v23, v39, v23, s[0:1]
	v_cndmask_b32_e64 v25, v38, v22, s[0:1]
	v_cndmask_b32_e64 v27, v29, v27, s[0:1]
	v_cndmask_b32_e64 v26, v28, v26, s[0:1]
	v_cndmask_b32_e64 v28, v33, v31, s[0:1]
	v_cndmask_b32_e64 v29, v32, v30, s[0:1]
	v_cvt_pk_bf16_f32 v22, v24, v21
	v_cvt_pk_bf16_f32 v23, v25, v23
	v_cvt_pk_bf16_f32 v24, v26, v27
	v_cvt_pk_bf16_f32 v25, v29, v28
	v_add_u32_e32 v19, 2, v19
	v_add_u32_e32 v14, 64, v14
	v_add_u32_e32 v15, 0x2000, v15
	global_store_dwordx4 v[10:11], v[22:25], off sc1
	v_lshl_add_u64 v[10:11], v[10:11], 0, s[6:7]
	s_andn2_b64 exec, exec, s[4:5]
	s_cbranch_execnz .LBB0_290
	s_or_b64 exec, exec, s[4:5]
	v_lshrrev_b32_e32 v10, 1, v1
	v_lshlrev_b32_e32 v11, 1, v17
	v_lshlrev_b32_e32 v12, 2, v18
	v_sub_u32_e32 v1, 16, v10
	v_add_u32_e32 v19, 1, v10
	v_mul_u32_u24_e32 v10, 0x420, v10
	v_and_b32_e32 v11, 0x3c0, v11
	v_and_b32_e32 v12, 32, v12
	v_add3_u32 v10, v10, v11, v12
	v_mul_u32_u24_e32 v9, 0x420, v9
	v_sub_u32_e32 v9, v10, v9
	s_lshl_b64 s[0:1], s[2:3], 18
	v_add_u32_e32 v9, 0, v9
	v_add_u32_e32 v20, 0x102e0, v9
	v_mov_b32_e32 v9, s1
	v_or_b32_e32 v8, s0, v8
	v_lshl_add_u64 v[6:7], v[8:9], 0, v[6:7]
	v_lshl_add_u64 v[6:7], s[70:71], 0, v[6:7]
	s_mov_b64 s[0:1], 0x1e158000
	v_lshl_add_u64 v[14:15], v[6:7], 0, s[0:1]
	s_mov_b64 s[0:1], 0
	s_movk_i32 s6, 0x1fff
	s_movk_i32 s7, 0x80
	s_movk_i32 s8, 0x41
	s_mov_b64 s[2:3], 0x4000
	s_movk_i32 s9, 0x3bff
	s_branch .LBB0_293
.LBB0_292:
	s_or_b64 exec, exec, s[4:5]
	s_waitcnt lgkmcnt(1)
	v_cvt_pk_bf16_f32 v6, v6, v7
	v_cvt_pk_bf16_f32 v7, v8, v9
	s_waitcnt lgkmcnt(0)
	v_cvt_pk_bf16_f32 v8, v10, v11
	v_cvt_pk_bf16_f32 v9, v12, v13
	global_store_dwordx4 v[14:15], v[6:9], off sc1
	v_cmp_lt_u32_e32 vcc, s9, v17
	v_add_u32_e32 v20, 0xfffff7c0, v20
	v_add_u32_e32 v6, 0x400, v17
	v_lshl_add_u64 v[14:15], v[14:15], 0, s[2:3]
	v_add_u32_e32 v16, 32, v16
	v_add_u32_e32 v18, 0x2000, v18
	s_or_b64 s[0:1], vcc, s[0:1]
	v_mov_b32_e32 v17, v6
	s_andn2_b64 exec, exec, s[0:1]
	s_cbranch_execz .LBB0_297

.LBB0_372:
	s_lshr_b32 s4, s11, 9
	s_ashr_i32 s9, s8, 31
	s_mulk_i32 s4, 0x3000
	s_lshl_b64 s[0:1], s[8:9], 13
	s_ashr_i32 s5, s4, 31
	v_lshl_add_u64 v[2:3], v[160:161], 0, s[0:1]
	s_lshl_b64 s[0:1], s[4:5], 2
	s_add_u32 s6, s22, s0
	s_addc_u32 s7, s23, s1
	global_load_dwordx4 v[150:153], v[162:163], off
	global_load_dwordx4 v[154:157], v[162:163], off offset:1024
	global_load_dwordx4 v[186:189], v[162:163], off offset:2048
	global_load_dwordx4 v[190:193], v[162:163], off offset:3072
	global_load_dwordx4 v[194:197], v[164:165], off
	global_load_dwordx4 v[198:201], v[166:167], off
	global_load_dwordx4 v[202:205], v[168:169], off
	global_load_dwordx4 v[206:209], v[172:173], off
	global_load_dwordx4 v[34:37], v[2:3], off nt
	global_load_dwordx4 v[30:33], v[2:3], off offset:1024 nt
	global_load_dwordx4 v[26:29], v[2:3], off offset:2048 nt
	global_load_dwordx4 v[22:25], v[2:3], off offset:3072 nt
	v_add_co_u32_e32 v2, vcc, 0x1000, v2
	s_add_u32 s0, s6, 0x2000
	s_nop 0
	v_addc_co_u32_e32 v3, vcc, 0, v3, vcc
	s_addc_u32 s1, s7, 0
	global_load_dwordx4 v[50:53], v[2:3], off nt
	global_load_dwordx4 v[46:49], v[2:3], off offset:1024 nt
	global_load_dwordx4 v[42:45], v[2:3], off offset:2048 nt
	global_load_dwordx4 v[38:41], v[2:3], off offset:3072 nt
	global_load_dwordx4 v[10:13], v247, s[6:7]
	global_load_dwordx4 v[6:9], v247, s[6:7] offset:1024
	s_nop 0
	global_load_dwordx4 v[2:5], v247, s[6:7] offset:2048
	global_load_dwordx4 v[14:17], v251, s[6:7]
	global_load_dwordx4 v[18:21], v252, s[6:7]
	s_add_i32 s14, s8, 1
	global_load_dwordx4 v[178:181], v247, s[0:1]
	global_load_dwordx4 v[182:185], v248, s[0:1]
	global_load_dwordx4 v[210:213], v249, s[0:1]
	global_load_dwordx4 v[214:217], v250, s[0:1]
	global_load_dwordx4 v[218:221], v251, s[0:1]
	global_load_dwordx4 v[222:225], v252, s[0:1]
	global_load_dwordx4 v[226:229], v253, s[0:1]
	global_load_dwordx4 v[230:233], v254, s[0:1]
	s_ashr_i32 s15, s14, 31
	s_add_i32 s16, s8, 2
	s_add_i32 s18, s8, 3
	s_lshl_b64 s[0:1], s[14:15], 13
	s_ashr_i32 s17, s16, 31
	s_ashr_i32 s19, s18, 31
	s_waitcnt vmcnt(32)
	v_lshl_add_u64 v[70:71], v[160:161], 0, s[0:1]
	s_lshl_b64 s[4:5], s[16:17], 13
	s_lshl_b64 s[26:27], s[18:19], 13
	global_load_dwordx4 v[130:133], v[70:71], off nt
	global_load_dwordx4 v[126:129], v[70:71], off offset:1024 nt
	global_load_dwordx4 v[118:121], v[70:71], off offset:2048 nt
	global_load_dwordx4 v[110:113], v[70:71], off offset:3072 nt
	v_lshl_add_u64 v[72:73], v[160:161], 0, s[4:5]
	v_lshl_add_u64 v[74:75], v[160:161], 0, s[26:27]
	global_load_dwordx4 v[98:101], v[72:73], off nt
	global_load_dwordx4 v[94:97], v[72:73], off offset:1024 nt
	global_load_dwordx4 v[90:93], v[72:73], off offset:2048 nt
	global_load_dwordx4 v[82:85], v[72:73], off offset:3072 nt
	global_load_dwordx4 v[66:69], v[74:75], off nt
	global_load_dwordx4 v[62:65], v[74:75], off offset:1024 nt
	global_load_dwordx4 v[58:61], v[74:75], off offset:2048 nt
	global_load_dwordx4 v[54:57], v[74:75], off offset:3072 nt
	v_add_co_u32_e32 v70, vcc, s24, v70
	v_add_co_u32_e64 v72, s[0:1], s24, v72
	v_add_co_u32_e64 v234, s[4:5], s24, v74
	v_addc_co_u32_e32 v71, vcc, 0, v71, vcc
	v_addc_co_u32_e64 v73, vcc, 0, v73, s[0:1]
	v_addc_co_u32_e64 v235, vcc, 0, v75, s[4:5]
	global_load_dwordx4 v[146:149], v[70:71], off nt
	global_load_dwordx4 v[142:145], v[70:71], off offset:1024 nt
	global_load_dwordx4 v[138:141], v[70:71], off offset:2048 nt
	global_load_dwordx4 v[134:137], v[70:71], off offset:3072 nt
	global_load_dwordx4 v[122:125], v[72:73], off nt
	global_load_dwordx4 v[114:117], v[72:73], off offset:1024 nt
	global_load_dwordx4 v[106:109], v[72:73], off offset:2048 nt
	global_load_dwordx4 v[102:105], v[72:73], off offset:3072 nt
	global_load_dwordx4 v[86:89], v[234:235], off nt
	global_load_dwordx4 v[78:81], v[234:235], off offset:1024 nt
	global_load_dwordx4 v[74:77], v[234:235], off offset:2048 nt
	s_nop 0
	global_load_dwordx4 v[70:73], v[234:235], off offset:3072 nt
	s_add_i32 s11, s11, s20
	s_lshl_b64 s[0:1], s[8:9], 12
	s_lshl_b64 s[4:5], s[16:17], 12
	s_add_i32 s8, s8, s21
	s_waitcnt vmcnt(44)
	v_mov_b32_e32 v235, v34
	s_waitcnt vmcnt(43)
	v_mov_b32_e32 v239, v31
	v_mov_b32_e32 v237, v36
	s_waitcnt vmcnt(31)
	v_pk_add_f32 v[180:181], v[180:181], 1.0 op_sel_hi:[1,0]
	s_nop 0
	v_pk_mul_f32 v[180:181], v[152:153], v[180:181]
	s_waitcnt vmcnt(30)
	v_pk_add_f32 v[152:153], v[182:183], 1.0 op_sel_hi:[1,0]
	v_pk_add_f32 v[184:185], v[184:185], 1.0 op_sel_hi:[1,0]
	v_pk_mul_f32 v[182:183], v[154:155], v[152:153]
	v_pk_mul_f32 v[184:185], v[156:157], v[184:185]
	s_waitcnt vmcnt(29)
	v_pk_add_f32 v[154:155], v[210:211], 1.0 op_sel_hi:[1,0]
	v_pk_add_f32 v[156:157], v[212:213], 1.0 op_sel_hi:[1,0]
	s_waitcnt vmcnt(28)
	v_pk_add_f32 v[210:211], v[216:217], 1.0 op_sel_hi:[1,0]
	s_waitcnt vmcnt(27)
	v_pk_add_f32 v[212:213], v[220:221], 1.0 op_sel_hi:[1,0]
	v_pk_mul_f32 v[192:193], v[192:193], v[210:211]
	v_pk_add_f32 v[210:211], v[218:219], 1.0 op_sel_hi:[1,0]
	v_pk_mul_f32 v[196:197], v[196:197], v[212:213]
	s_waitcnt vmcnt(26)
	v_pk_add_f32 v[212:213], v[224:225], 1.0 op_sel_hi:[1,0]
	v_pk_mul_f32 v[194:195], v[194:195], v[210:211]
	v_pk_add_f32 v[210:211], v[222:223], 1.0 op_sel_hi:[1,0]
	v_pk_mul_f32 v[200:201], v[200:201], v[212:213]
	s_waitcnt vmcnt(25)
	v_pk_add_f32 v[212:213], v[228:229], 1.0 op_sel_hi:[1,0]
	v_pk_mul_f32 v[198:199], v[198:199], v[210:211]
	v_pk_add_f32 v[210:211], v[226:227], 1.0 op_sel_hi:[1,0]
	v_pk_mul_f32 v[204:205], v[204:205], v[212:213]
	s_waitcnt vmcnt(24)
	v_pk_add_f32 v[212:213], v[230:231], 1.0 op_sel_hi:[1,0]
	v_pk_mul_f32 v[202:203], v[202:203], v[210:211]
	v_mov_b32_e32 v210, v51
	v_mov_b32_e32 v211, v47
	v_pk_mul_f32 v[206:207], v[206:207], v[212:213]
	v_mov_b32_e32 v212, v43
	v_mov_b32_e32 v213, v39
	v_mov_b32_e32 v224, v50
	v_mov_b32_e32 v225, v46
	v_pk_add_f32 v[226:227], v[232:233], 1.0 op_sel_hi:[1,0]
	v_mov_b32_e32 v228, v42
	v_mov_b32_e32 v229, v38
	v_pk_mul_f32 v[210:211], v[210:211], v[210:211]
	v_pk_mul_f32 v[212:213], v[212:213], v[212:213]
	s_waitcnt vmcnt(22)
	v_mov_b32_e32 v238, v127
	v_mov_b32_e32 v153, v30
	v_pk_mul_f32 v[188:189], v[188:189], v[156:157]
	v_pk_add_f32 v[156:157], v[214:215], 1.0 op_sel_hi:[1,0]
	v_pk_mul_f32 v[208:209], v[208:209], v[226:227]
	v_mov_b32_e32 v226, v52
	v_mov_b32_e32 v227, v48
	v_pk_fma_f32 v[210:211], v[224:225], v[224:225], v[210:211]
	v_mov_b32_e32 v224, v44
	v_mov_b32_e32 v225, v40
	v_pk_fma_f32 v[212:213], v[228:229], v[228:229], v[212:213]
	v_mov_b32_e32 v152, v126
	v_pk_mul_f32 v[232:233], v[238:239], v[238:239]
	v_pk_mul_f32 v[190:191], v[190:191], v[156:157]
	v_mov_b32_e32 v157, v27
	v_mov_b32_e32 v221, v23
	v_mov_b32_e32 v228, v53
	v_mov_b32_e32 v229, v49
	v_pk_fma_f32 v[210:211], v[226:227], v[226:227], v[210:211]
	v_mov_b32_e32 v226, v45
	v_mov_b32_e32 v227, v41
	v_pk_fma_f32 v[224:225], v[224:225], v[224:225], v[212:213]
	s_waitcnt vmcnt(21)
	v_mov_b32_e32 v156, v119
	s_waitcnt vmcnt(20)
	v_mov_b32_e32 v220, v111
	v_pk_fma_f32 v[152:153], v[152:153], v[152:153], v[232:233]
	s_waitcnt vmcnt(14)
	v_mov_b32_e32 v232, v63
	v_mov_b32_e32 v233, v95
	v_pk_add_f32 v[178:179], v[178:179], 1.0 op_sel_hi:[1,0]
	v_mov_b32_e32 v215, v26
	v_mov_b32_e32 v219, v22
	v_pk_fma_f32 v[212:213], v[228:229], v[228:229], v[210:211]
	v_pk_fma_f32 v[210:211], v[226:227], v[226:227], v[224:225]
	v_mov_b32_e32 v214, v118
	v_mov_b32_e32 v218, v110
	v_mov_b32_e32 v226, v67
	v_mov_b32_e32 v227, v99
	v_mov_b32_e32 v230, v62
	v_mov_b32_e32 v231, v94
	v_pk_mul_f32 v[156:157], v[156:157], v[156:157]
	v_pk_mul_f32 v[220:221], v[220:221], v[220:221]
	v_pk_mul_f32 v[232:233], v[232:233], v[232:233]
	v_pk_mul_f32 v[178:179], v[150:151], v[178:179]
	v_mov_b32_e32 v151, v35
	v_mov_b32_e32 v217, v28
	v_mov_b32_e32 v150, v131
	v_mov_b32_e32 v216, v120
	v_mov_b32_e32 v224, v66
	v_mov_b32_e32 v225, v98
	v_pk_fma_f32 v[156:157], v[214:215], v[214:215], v[156:157]
	v_pk_fma_f32 v[218:219], v[218:219], v[218:219], v[220:221]
	s_waitcnt vmcnt(13)
	v_mov_b32_e32 v220, v59
	v_mov_b32_e32 v221, v91
	v_pk_mul_f32 v[226:227], v[226:227], v[226:227]
	v_pk_fma_f32 v[230:231], v[230:231], v[230:231], v[232:233]
	s_waitcnt vmcnt(12)
	v_mov_b32_e32 v232, v55
	v_mov_b32_e32 v233, v83
	v_pk_mul_f32 v[186:187], v[186:187], v[154:155]
	v_mov_b32_e32 v155, v32
	v_mov_b32_e32 v234, v130
	v_mov_b32_e32 v154, v128
	v_mov_b32_e32 v228, v68
	v_mov_b32_e32 v229, v100
	v_pk_mul_f32 v[150:151], v[150:151], v[150:151]
	v_mov_b32_e32 v214, v58
	v_mov_b32_e32 v215, v90
	v_pk_fma_f32 v[224:225], v[224:225], v[224:225], v[226:227]
	v_mov_b32_e32 v226, v54
	v_mov_b32_e32 v227, v82
	v_pk_mul_f32 v[220:221], v[220:221], v[220:221]
	v_pk_mul_f32 v[232:233], v[232:233], v[232:233]
	v_pk_fma_f32 v[156:157], v[216:217], v[216:217], v[156:157]
	s_waitcnt vmcnt(11)
	v_mov_b32_e32 v216, v147
	s_waitcnt vmcnt(10)
	v_mov_b32_e32 v217, v143
	v_mov_b32_e32 v223, v24
	v_mov_b32_e32 v236, v132
	v_mov_b32_e32 v222, v112
	v_pk_fma_f32 v[150:151], v[234:235], v[234:235], v[150:151]
	v_pk_fma_f32 v[214:215], v[214:215], v[214:215], v[220:221]
	v_pk_fma_f32 v[226:227], v[226:227], v[226:227], v[232:233]
	v_mov_b32_e32 v232, v60
	v_mov_b32_e32 v233, v92
	v_pk_fma_f32 v[152:153], v[154:155], v[154:155], v[152:153]
	v_mov_b32_e32 v154, v146
	v_mov_b32_e32 v155, v142
	v_pk_fma_f32 v[224:225], v[228:229], v[228:229], v[224:225]
	s_waitcnt vmcnt(9)
	v_mov_b32_e32 v228, v139
	s_waitcnt vmcnt(8)
	v_mov_b32_e32 v229, v135
	v_pk_mul_f32 v[216:217], v[216:217], v[216:217]
	v_mov_b32_e32 v220, v64
	v_mov_b32_e32 v221, v96
	v_pk_fma_f32 v[150:151], v[236:237], v[236:237], v[150:151]
	v_pk_fma_f32 v[218:219], v[222:223], v[222:223], v[218:219]
	v_mov_b32_e32 v222, v138
	v_mov_b32_e32 v223, v134
	v_pk_fma_f32 v[214:215], v[232:233], v[232:233], v[214:215]
	s_waitcnt vmcnt(7)
	v_mov_b32_e32 v232, v123
	s_waitcnt vmcnt(6)
	v_mov_b32_e32 v233, v115
	v_pk_fma_f32 v[236:237], v[154:155], v[154:155], v[216:217]
	v_pk_mul_f32 v[216:217], v[228:229], v[228:229]
	v_pk_fma_f32 v[220:221], v[220:221], v[220:221], v[230:231]
	v_mov_b32_e32 v230, v122
	v_mov_b32_e32 v231, v114
	v_pk_fma_f32 v[228:229], v[222:223], v[222:223], v[216:217]
	v_pk_mul_f32 v[222:223], v[232:233], v[232:233]
	v_mov_b32_e32 v234, v56
	v_mov_b32_e32 v235, v84
	s_waitcnt vmcnt(5)
	v_mov_b32_e32 v154, v107
	s_waitcnt vmcnt(4)
	v_mov_b32_e32 v155, v103
	v_pk_fma_f32 v[230:231], v[230:231], v[230:231], v[222:223]
	s_waitcnt vmcnt(3)
	v_mov_b32_e32 v222, v87
	s_waitcnt vmcnt(2)
	v_mov_b32_e32 v223, v79
	v_pk_fma_f32 v[226:227], v[234:235], v[234:235], v[226:227]
	v_mov_b32_e32 v234, v106
	v_mov_b32_e32 v235, v102
	v_mov_b32_e32 v216, v86
	v_mov_b32_e32 v217, v78
	v_pk_mul_f32 v[154:155], v[154:155], v[154:155]
	v_pk_mul_f32 v[222:223], v[222:223], v[222:223]
	v_pk_fma_f32 v[232:233], v[234:235], v[234:235], v[154:155]
	v_pk_fma_f32 v[234:235], v[216:217], v[216:217], v[222:223]
	s_waitcnt vmcnt(1)
	v_mov_b32_e32 v216, v75
	s_waitcnt vmcnt(0)
	v_mov_b32_e32 v217, v71
	v_mov_b32_e32 v154, v74
	v_mov_b32_e32 v155, v70
	v_pk_mul_f32 v[216:217], v[216:217], v[216:217]
	v_mov_b32_e32 v222, v148
	v_pk_fma_f32 v[238:239], v[154:155], v[154:155], v[216:217]
	v_mov_b32_e32 v155, v37
	v_mov_b32_e32 v154, v133
	v_pk_fma_f32 v[150:151], v[154:155], v[154:155], v[150:151]
	v_mov_b32_e32 v155, v33
	v_mov_b32_e32 v154, v129
	v_pk_fma_f32 v[152:153], v[154:155], v[154:155], v[152:153]
	v_mov_b32_e32 v155, v29
	v_mov_b32_e32 v154, v121
	v_pk_fma_f32 v[154:155], v[154:155], v[154:155], v[156:157]
	v_mov_b32_e32 v157, v25
	v_mov_b32_e32 v156, v113
	v_pk_fma_f32 v[216:217], v[156:157], v[156:157], v[218:219]
	v_mov_b32_e32 v218, v65
	v_mov_b32_e32 v219, v97
	v_mov_b32_e32 v156, v69
	v_mov_b32_e32 v157, v101
	v_pk_fma_f32 v[220:221], v[218:219], v[218:219], v[220:221]
	v_mov_b32_e32 v218, v61
	v_mov_b32_e32 v219, v93
	v_pk_fma_f32 v[156:157], v[156:157], v[156:157], v[224:225]
	v_pk_fma_f32 v[218:219], v[218:219], v[218:219], v[214:215]
	v_mov_b32_e32 v214, v57
	v_mov_b32_e32 v215, v85
	v_mov_b32_e32 v224, v140
	v_mov_b32_e32 v225, v136
	v_pk_fma_f32 v[214:215], v[214:215], v[214:215], v[226:227]
	v_pk_fma_f32 v[226:227], v[224:225], v[224:225], v[228:229]
	v_mov_b32_e32 v224, v124
	v_mov_b32_e32 v225, v116
	v_mov_b32_e32 v223, v144
	v_pk_fma_f32 v[228:229], v[224:225], v[224:225], v[230:231]
	v_mov_b32_e32 v224, v108
	v_mov_b32_e32 v225, v104
	v_pk_fma_f32 v[222:223], v[222:223], v[222:223], v[236:237]
	v_pk_fma_f32 v[230:231], v[224:225], v[224:225], v[232:233]
	v_mov_b32_e32 v224, v88
	v_mov_b32_e32 v225, v80
	v_pk_add_f32 v[240:241], v[156:157], v[220:221]
	v_mov_b32_e32 v156, v149
	v_mov_b32_e32 v157, v145
	v_pk_fma_f32 v[232:233], v[224:225], v[224:225], v[234:235]
	v_mov_b32_e32 v224, v76
	v_mov_b32_e32 v225, v72
	v_pk_fma_f32 v[236:237], v[156:157], v[156:157], v[222:223]
	v_mov_b32_e32 v156, v141
	v_mov_b32_e32 v157, v137
	v_pk_fma_f32 v[234:235], v[224:225], v[224:225], v[238:239]
	v_pk_fma_f32 v[238:239], v[156:157], v[156:157], v[226:227]
	v_mov_b32_e32 v156, v125
	v_mov_b32_e32 v157, v117
	v_pk_fma_f32 v[222:223], v[156:157], v[156:157], v[228:229]
	v_mov_b32_e32 v156, v109
	v_mov_b32_e32 v157, v105
	v_pk_fma_f32 v[220:221], v[156:157], v[156:157], v[230:231]
	v_mov_b32_e32 v156, v89
	v_mov_b32_e32 v157, v81
	v_pk_fma_f32 v[242:243], v[156:157], v[156:157], v[232:233]
	v_mov_b32_e32 v156, v77
	v_mov_b32_e32 v157, v73
	v_pk_add_f32 v[224:225], v[150:151], v[152:153]
	v_pk_fma_f32 v[234:235], v[156:157], v[156:157], v[234:235]
	global_load_dwordx4 v[150:153], v253, s[6:7]
	v_pk_add_f32 v[230:231], v[224:225], v[154:155]
	global_load_dwordx4 v[154:157], v254, s[6:7]
	v_mov_b32_e32 v227, v212
	v_mov_b32_e32 v226, v236
	v_mov_b32_e32 v212, v237
	v_mov_b32_e32 v224, v234
	v_mov_b32_e32 v225, v220
	v_mov_b32_e32 v220, v235
	global_load_dwordx4 v[234:237], v247, s[6:7] offset:3072
	v_pk_add_f32 v[232:233], v[240:241], v[218:219]
	v_pk_add_f32 v[230:231], v[230:231], v[216:217]
	v_mov_b32_e32 v228, v242
	v_mov_b32_e32 v229, v222
	v_pk_add_f32 v[232:233], v[232:233], v[214:215]
	v_pk_add_f32 v[230:231], v[230:231], v[226:227]
	v_mov_b32_e32 v219, v210
	v_mov_b32_e32 v218, v238
	v_mov_b32_e32 v222, v243
	v_pk_add_f32 v[228:229], v[232:233], v[228:229]
	v_pk_add_f32 v[230:231], v[230:231], v[212:213]
	v_mov_b32_e32 v210, v239
	v_pk_add_f32 v[222:223], v[228:229], v[222:223]
	v_pk_add_f32 v[218:219], v[230:231], v[218:219]
	v_pk_add_f32 v[222:223], v[222:223], v[224:225]
	v_pk_add_f32 v[210:211], v[218:219], v[210:211]
	v_pk_add_f32 v[218:219], v[222:223], v[220:221]
	ds_bpermute_b32 v221, v1, v211
	ds_bpermute_b32 v220, v1, v210
	ds_bpermute_b32 v223, v1, v219
	ds_bpermute_b32 v222, v1, v218
	s_lshl_b64 s[6:7], s[18:19], 12
	v_lshl_add_u64 v[216:217], v[174:175], 0, s[0:1]
	s_waitcnt lgkmcnt(2)
	v_pk_add_f32 v[210:211], v[210:211], v[220:221]
	ds_bpermute_b32 v221, v159, v211
	s_waitcnt lgkmcnt(1)
	v_pk_add_f32 v[218:219], v[218:219], v[222:223]
	ds_bpermute_b32 v220, v159, v210
	ds_bpermute_b32 v223, v159, v219
	ds_bpermute_b32 v222, v159, v218
	s_lshl_b64 s[0:1], s[14:15], 12
	v_lshl_add_u64 v[212:213], v[174:175], 0, s[6:7]
	s_waitcnt lgkmcnt(2)
	v_pk_add_f32 v[210:211], v[210:211], v[220:221]
	ds_bpermute_b32 v221, v171, v211
	s_waitcnt lgkmcnt(1)
	v_pk_add_f32 v[218:219], v[218:219], v[222:223]
	ds_bpermute_b32 v220, v171, v210
	ds_bpermute_b32 v223, v171, v219
	ds_bpermute_b32 v222, v171, v218
	v_lshl_add_u64 v[214:215], v[174:175], 0, s[0:1]
	v_lshl_add_u64 v[226:227], v[174:175], 0, s[4:5]
	s_waitcnt lgkmcnt(2)
	v_pk_add_f32 v[210:211], v[210:211], v[220:221]
	ds_bpermute_b32 v221, v244, v211
	s_waitcnt lgkmcnt(1)
	v_pk_add_f32 v[218:219], v[218:219], v[222:223]
	ds_bpermute_b32 v220, v244, v210
	ds_bpermute_b32 v223, v244, v219
	ds_bpermute_b32 v222, v244, v218
	s_cmpk_lt_i32 s11, 0x800
	s_waitcnt lgkmcnt(2)
	v_pk_add_f32 v[210:211], v[210:211], v[220:221]
	ds_bpermute_b32 v221, v245, v211
	s_waitcnt lgkmcnt(1)
	v_pk_add_f32 v[218:219], v[218:219], v[222:223]
	ds_bpermute_b32 v220, v245, v210
	ds_bpermute_b32 v223, v245, v219
	ds_bpermute_b32 v222, v245, v218
	s_waitcnt lgkmcnt(2)
	v_pk_add_f32 v[210:211], v[210:211], v[220:221]
	ds_bpermute_b32 v221, v246, v211
	s_waitcnt lgkmcnt(1)
	v_pk_add_f32 v[218:219], v[218:219], v[222:223]
	ds_bpermute_b32 v220, v246, v210
	ds_bpermute_b32 v223, v246, v219
	ds_bpermute_b32 v222, v246, v218
	s_waitcnt lgkmcnt(2)
	v_pk_add_f32 v[210:211], v[210:211], v[220:221]
	s_nop 0
	v_pk_fma_f32 v[210:211], v[210:211], s[10:11], v[176:177] op_sel_hi:[1,0,0]
	s_waitcnt lgkmcnt(0)
	v_pk_add_f32 v[218:219], v[218:219], v[222:223]
	v_mul_f32_e32 v220, 0x4b800000, v211
	v_pk_fma_f32 v[218:219], v[218:219], s[10:11], v[176:177] op_sel_hi:[1,0,0]
	v_cmp_gt_f32_e64 s[6:7], s25, v211
	v_mul_f32_e32 v221, 0x4b800000, v210
	v_cmp_gt_f32_e32 vcc, s25, v210
	v_mul_f32_e32 v222, 0x4b800000, v219
	v_mul_f32_e32 v223, 0x4b800000, v218
	v_cmp_gt_f32_e64 s[0:1], s25, v218
	v_cmp_gt_f32_e64 s[4:5], s25, v219
	v_cndmask_b32_e64 v211, v211, v220, s[6:7]
	v_cndmask_b32_e32 v210, v210, v221, vcc
	v_cndmask_b32_e64 v219, v219, v222, s[4:5]
	v_cndmask_b32_e64 v218, v218, v223, s[0:1]
	v_rsq_f32_e32 v211, v211
	v_rsq_f32_e32 v220, v210
	v_rsq_f32_e32 v219, v219
	v_rsq_f32_e32 v221, v218
	v_mul_f32_e32 v210, 0x45800000, v211
	v_mul_f32_e32 v218, 0x45800000, v220
	v_mul_f32_e32 v222, 0x45800000, v219
	v_mul_f32_e32 v223, 0x45800000, v221
	v_cndmask_b32_e64 v210, v211, v210, s[6:7]
	v_cndmask_b32_e32 v218, v220, v218, vcc
	v_cndmask_b32_e64 v220, v219, v222, s[4:5]
	v_cndmask_b32_e64 v222, v221, v223, s[0:1]
	v_pk_mul_f32 v[34:35], v[34:35], v[210:211] op_sel_hi:[1,0]
	v_pk_mul_f32 v[36:37], v[36:37], v[210:211] op_sel_hi:[1,0]
	v_pk_mul_f32 v[30:31], v[30:31], v[210:211] op_sel_hi:[1,0]
	v_pk_mul_f32 v[32:33], v[32:33], v[210:211] op_sel_hi:[1,0]
	v_pk_mul_f32 v[26:27], v[26:27], v[210:211] op_sel_hi:[1,0]
	v_pk_mul_f32 v[28:29], v[28:29], v[210:211] op_sel_hi:[1,0]
	v_pk_mul_f32 v[22:23], v[22:23], v[210:211] op_sel_hi:[1,0]
	v_pk_mul_f32 v[24:25], v[24:25], v[210:211] op_sel_hi:[1,0]
	v_pk_mul_f32 v[50:51], v[50:51], v[210:211] op_sel_hi:[1,0]
	v_pk_mul_f32 v[52:53], v[52:53], v[210:211] op_sel_hi:[1,0]
	v_pk_mul_f32 v[46:47], v[46:47], v[210:211] op_sel_hi:[1,0]
	v_pk_mul_f32 v[48:49], v[48:49], v[210:211] op_sel_hi:[1,0]
	v_pk_mul_f32 v[42:43], v[42:43], v[210:211] op_sel_hi:[1,0]
	v_pk_mul_f32 v[44:45], v[44:45], v[210:211] op_sel_hi:[1,0]
	v_pk_mul_f32 v[38:39], v[38:39], v[210:211] op_sel_hi:[1,0]
	v_pk_mul_f32 v[40:41], v[40:41], v[210:211] op_sel_hi:[1,0]
	v_pk_mul_f32 v[130:131], v[130:131], v[218:219] op_sel_hi:[1,0]
	v_pk_mul_f32 v[132:133], v[132:133], v[218:219] op_sel_hi:[1,0]
	v_pk_mul_f32 v[126:127], v[126:127], v[218:219] op_sel_hi:[1,0]
	v_pk_mul_f32 v[128:129], v[128:129], v[218:219] op_sel_hi:[1,0]
	v_pk_mul_f32 v[118:119], v[118:119], v[218:219] op_sel_hi:[1,0]
	v_pk_mul_f32 v[120:121], v[120:121], v[218:219] op_sel_hi:[1,0]
	v_pk_mul_f32 v[110:111], v[110:111], v[218:219] op_sel_hi:[1,0]
	v_pk_mul_f32 v[112:113], v[112:113], v[218:219] op_sel_hi:[1,0]
	v_pk_mul_f32 v[146:147], v[146:147], v[218:219] op_sel_hi:[1,0]
	v_pk_mul_f32 v[148:149], v[148:149], v[218:219] op_sel_hi:[1,0]
	v_pk_mul_f32 v[142:143], v[142:143], v[218:219] op_sel_hi:[1,0]
	v_pk_mul_f32 v[144:145], v[144:145], v[218:219] op_sel_hi:[1,0]
	v_pk_mul_f32 v[138:139], v[138:139], v[218:219] op_sel_hi:[1,0]
	v_pk_mul_f32 v[140:141], v[140:141], v[218:219] op_sel_hi:[1,0]
	v_pk_mul_f32 v[134:135], v[134:135], v[218:219] op_sel_hi:[1,0]
	v_pk_mul_f32 v[136:137], v[136:137], v[218:219] op_sel_hi:[1,0]
	v_pk_mul_f32 v[98:99], v[98:99], v[220:221] op_sel_hi:[1,0]
	v_pk_mul_f32 v[100:101], v[100:101], v[220:221] op_sel_hi:[1,0]
	v_pk_mul_f32 v[94:95], v[94:95], v[220:221] op_sel_hi:[1,0]
	v_pk_mul_f32 v[96:97], v[96:97], v[220:221] op_sel_hi:[1,0]
	v_pk_mul_f32 v[90:91], v[90:91], v[220:221] op_sel_hi:[1,0]
	v_pk_mul_f32 v[92:93], v[92:93], v[220:221] op_sel_hi:[1,0]
	v_pk_mul_f32 v[82:83], v[82:83], v[220:221] op_sel_hi:[1,0]
	v_pk_mul_f32 v[84:85], v[84:85], v[220:221] op_sel_hi:[1,0]
	v_pk_mul_f32 v[122:123], v[122:123], v[220:221] op_sel_hi:[1,0]
	v_pk_mul_f32 v[124:125], v[124:125], v[220:221] op_sel_hi:[1,0]
	v_pk_mul_f32 v[114:115], v[114:115], v[220:221] op_sel_hi:[1,0]
	v_pk_mul_f32 v[116:117], v[116:117], v[220:221] op_sel_hi:[1,0]
	v_pk_mul_f32 v[106:107], v[106:107], v[220:221] op_sel_hi:[1,0]
	v_pk_mul_f32 v[108:109], v[108:109], v[220:221] op_sel_hi:[1,0]
	v_pk_mul_f32 v[102:103], v[102:103], v[220:221] op_sel_hi:[1,0]
	v_pk_mul_f32 v[104:105], v[104:105], v[220:221] op_sel_hi:[1,0]
	v_pk_mul_f32 v[66:67], v[66:67], v[222:223] op_sel_hi:[1,0]
	v_pk_mul_f32 v[68:69], v[68:69], v[222:223] op_sel_hi:[1,0]
	v_pk_mul_f32 v[62:63], v[62:63], v[222:223] op_sel_hi:[1,0]
	v_pk_mul_f32 v[64:65], v[64:65], v[222:223] op_sel_hi:[1,0]
	v_pk_mul_f32 v[58:59], v[58:59], v[222:223] op_sel_hi:[1,0]
	v_pk_mul_f32 v[60:61], v[60:61], v[222:223] op_sel_hi:[1,0]
	v_pk_mul_f32 v[54:55], v[54:55], v[222:223] op_sel_hi:[1,0]
	v_pk_mul_f32 v[56:57], v[56:57], v[222:223] op_sel_hi:[1,0]
	v_pk_mul_f32 v[86:87], v[86:87], v[222:223] op_sel_hi:[1,0]
	v_pk_mul_f32 v[88:89], v[88:89], v[222:223] op_sel_hi:[1,0]
	v_pk_mul_f32 v[78:79], v[78:79], v[222:223] op_sel_hi:[1,0]
	v_pk_mul_f32 v[80:81], v[80:81], v[222:223] op_sel_hi:[1,0]
	v_pk_mul_f32 v[74:75], v[74:75], v[222:223] op_sel_hi:[1,0]
	v_pk_mul_f32 v[76:77], v[76:77], v[222:223] op_sel_hi:[1,0]
	v_pk_mul_f32 v[70:71], v[70:71], v[222:223] op_sel_hi:[1,0]
	v_pk_mul_f32 v[72:73], v[72:73], v[222:223] op_sel_hi:[1,0]
	v_pk_fma_f32 v[34:35], v[178:179], v[34:35], v[10:11]
	v_pk_fma_f32 v[36:37], v[180:181], v[36:37], v[12:13]
	v_pk_fma_f32 v[30:31], v[182:183], v[30:31], v[6:7]
	v_pk_fma_f32 v[32:33], v[184:185], v[32:33], v[8:9]
	v_pk_fma_f32 v[26:27], v[186:187], v[26:27], v[2:3]
	v_pk_fma_f32 v[28:29], v[188:189], v[28:29], v[4:5]
	s_waitcnt vmcnt(0)
	v_pk_fma_f32 v[22:23], v[190:191], v[22:23], v[234:235]
	v_pk_fma_f32 v[24:25], v[192:193], v[24:25], v[236:237]
	v_pk_fma_f32 v[50:51], v[194:195], v[50:51], v[14:15]
	v_pk_fma_f32 v[52:53], v[196:197], v[52:53], v[16:17]
	v_pk_fma_f32 v[46:47], v[198:199], v[46:47], v[18:19]
	v_pk_fma_f32 v[48:49], v[200:201], v[48:49], v[20:21]
	v_pk_fma_f32 v[42:43], v[202:203], v[42:43], v[150:151]
	v_pk_fma_f32 v[44:45], v[204:205], v[44:45], v[152:153]
	v_pk_fma_f32 v[38:39], v[206:207], v[38:39], v[154:155]
	v_pk_fma_f32 v[40:41], v[208:209], v[40:41], v[156:157]
	v_pk_fma_f32 v[130:131], v[178:179], v[130:131], v[10:11]
	v_pk_fma_f32 v[132:133], v[180:181], v[132:133], v[12:13]
	v_pk_fma_f32 v[126:127], v[182:183], v[126:127], v[6:7]
	v_pk_fma_f32 v[128:129], v[184:185], v[128:129], v[8:9]
	v_pk_fma_f32 v[118:119], v[186:187], v[118:119], v[2:3]
	v_pk_fma_f32 v[120:121], v[188:189], v[120:121], v[4:5]
	v_pk_fma_f32 v[110:111], v[190:191], v[110:111], v[234:235]
	v_pk_fma_f32 v[112:113], v[192:193], v[112:113], v[236:237]
	v_pk_fma_f32 v[146:147], v[194:195], v[146:147], v[14:15]
	v_pk_fma_f32 v[148:149], v[196:197], v[148:149], v[16:17]
	v_pk_fma_f32 v[142:143], v[198:199], v[142:143], v[18:19]
	v_pk_fma_f32 v[144:145], v[200:201], v[144:145], v[20:21]
	v_pk_fma_f32 v[138:139], v[202:203], v[138:139], v[150:151]
	v_pk_fma_f32 v[140:141], v[204:205], v[140:141], v[152:153]
	v_pk_fma_f32 v[134:135], v[206:207], v[134:135], v[154:155]
	v_pk_fma_f32 v[136:137], v[208:209], v[136:137], v[156:157]
	v_pk_fma_f32 v[98:99], v[178:179], v[98:99], v[10:11]
	v_pk_fma_f32 v[100:101], v[180:181], v[100:101], v[12:13]
	v_pk_fma_f32 v[94:95], v[182:183], v[94:95], v[6:7]
	v_pk_fma_f32 v[96:97], v[184:185], v[96:97], v[8:9]
	v_pk_fma_f32 v[90:91], v[186:187], v[90:91], v[2:3]
	v_pk_fma_f32 v[92:93], v[188:189], v[92:93], v[4:5]
	v_pk_fma_f32 v[82:83], v[190:191], v[82:83], v[234:235]
	v_pk_fma_f32 v[84:85], v[192:193], v[84:85], v[236:237]
	v_pk_fma_f32 v[122:123], v[194:195], v[122:123], v[14:15]
	v_pk_fma_f32 v[124:125], v[196:197], v[124:125], v[16:17]
	v_pk_fma_f32 v[114:115], v[198:199], v[114:115], v[18:19]
	v_pk_fma_f32 v[116:117], v[200:201], v[116:117], v[20:21]
	v_pk_fma_f32 v[106:107], v[202:203], v[106:107], v[150:151]
	v_pk_fma_f32 v[108:109], v[204:205], v[108:109], v[152:153]
	v_pk_fma_f32 v[102:103], v[206:207], v[102:103], v[154:155]
	v_pk_fma_f32 v[104:105], v[208:209], v[104:105], v[156:157]
	v_pk_fma_f32 v[10:11], v[178:179], v[66:67], v[10:11]
	v_pk_fma_f32 v[12:13], v[180:181], v[68:69], v[12:13]
	v_pk_fma_f32 v[6:7], v[182:183], v[62:63], v[6:7]
	v_pk_fma_f32 v[8:9], v[184:185], v[64:65], v[8:9]
	v_pk_fma_f32 v[2:3], v[186:187], v[58:59], v[2:3]
	v_pk_fma_f32 v[4:5], v[188:189], v[60:61], v[4:5]
	v_pk_fma_f32 v[54:55], v[190:191], v[54:55], v[234:235]
	v_pk_fma_f32 v[56:57], v[192:193], v[56:57], v[236:237]
	v_pk_fma_f32 v[14:15], v[194:195], v[86:87], v[14:15]
	v_pk_fma_f32 v[16:17], v[196:197], v[88:89], v[16:17]
	v_pk_fma_f32 v[18:19], v[198:199], v[78:79], v[18:19]
	v_pk_fma_f32 v[20:21], v[200:201], v[80:81], v[20:21]
	v_pk_fma_f32 v[58:59], v[202:203], v[74:75], v[150:151]
	v_pk_fma_f32 v[60:61], v[204:205], v[76:77], v[152:153]
	v_pk_fma_f32 v[62:63], v[206:207], v[70:71], v[154:155]
	v_pk_fma_f32 v[64:65], v[208:209], v[72:73], v[156:157]
	v_cvt_pk_bf16_f32 v34, v34, v35
	v_cvt_pk_bf16_f32 v35, v36, v37
	v_cvt_pk_bf16_f32 v30, v30, v31
	v_cvt_pk_bf16_f32 v31, v32, v33
	v_cvt_pk_bf16_f32 v26, v26, v27
	v_cvt_pk_bf16_f32 v27, v28, v29
	v_cvt_pk_bf16_f32 v22, v22, v23
	v_cvt_pk_bf16_f32 v23, v24, v25
	v_cvt_pk_bf16_f32 v24, v50, v51
	v_cvt_pk_bf16_f32 v25, v52, v53
	v_cvt_pk_bf16_f32 v28, v46, v47
	v_cvt_pk_bf16_f32 v29, v48, v49
	v_cvt_pk_bf16_f32 v32, v42, v43
	v_cvt_pk_bf16_f32 v33, v44, v45
	v_cvt_pk_bf16_f32 v36, v38, v39
	v_cvt_pk_bf16_f32 v37, v40, v41
	v_cvt_pk_bf16_f32 v38, v130, v131
	v_cvt_pk_bf16_f32 v39, v132, v133
	v_cvt_pk_bf16_f32 v40, v126, v127
	v_cvt_pk_bf16_f32 v41, v128, v129
	v_cvt_pk_bf16_f32 v42, v118, v119
	v_cvt_pk_bf16_f32 v43, v120, v121
	v_cvt_pk_bf16_f32 v44, v110, v111
	v_cvt_pk_bf16_f32 v45, v112, v113
	v_cvt_pk_bf16_f32 v46, v146, v147
	v_cvt_pk_bf16_f32 v47, v148, v149
	v_cvt_pk_bf16_f32 v48, v142, v143
	v_cvt_pk_bf16_f32 v49, v144, v145
	v_cvt_pk_bf16_f32 v50, v138, v139
	v_cvt_pk_bf16_f32 v51, v140, v141
	v_cvt_pk_bf16_f32 v52, v134, v135
	v_cvt_pk_bf16_f32 v53, v136, v137
	v_cvt_pk_bf16_f32 v66, v98, v99
	v_cvt_pk_bf16_f32 v67, v100, v101
	v_cvt_pk_bf16_f32 v68, v94, v95
	v_cvt_pk_bf16_f32 v69, v96, v97
	v_cvt_pk_bf16_f32 v70, v90, v91
	v_cvt_pk_bf16_f32 v71, v92, v93
	v_cvt_pk_bf16_f32 v72, v82, v83
	v_cvt_pk_bf16_f32 v73, v84, v85
	v_cvt_pk_bf16_f32 v74, v122, v123
	v_cvt_pk_bf16_f32 v75, v124, v125
	v_cvt_pk_bf16_f32 v76, v114, v115
	v_cvt_pk_bf16_f32 v77, v116, v117
	v_cvt_pk_bf16_f32 v78, v106, v107
	v_cvt_pk_bf16_f32 v79, v108, v109
	v_cvt_pk_bf16_f32 v80, v102, v103
	v_cvt_pk_bf16_f32 v81, v104, v105
	v_cvt_pk_bf16_f32 v10, v10, v11
	v_cvt_pk_bf16_f32 v11, v12, v13
	v_cvt_pk_bf16_f32 v6, v6, v7
	v_cvt_pk_bf16_f32 v7, v8, v9
	v_cvt_pk_bf16_f32 v2, v2, v3
	v_cvt_pk_bf16_f32 v3, v4, v5
	v_cvt_pk_bf16_f32 v4, v54, v55
	v_cvt_pk_bf16_f32 v5, v56, v57
	v_cvt_pk_bf16_f32 v8, v14, v15
	v_cvt_pk_bf16_f32 v9, v16, v17
	v_cvt_pk_bf16_f32 v12, v18, v19
	v_cvt_pk_bf16_f32 v13, v20, v21
	v_cvt_pk_bf16_f32 v14, v58, v59
	v_cvt_pk_bf16_f32 v15, v60, v61
	v_cvt_pk_bf16_f32 v16, v62, v63
	v_cvt_pk_bf16_f32 v17, v64, v65
	global_store_dwordx2 v[216:217], v[34:35], off sc1
	global_store_dwordx2 v[216:217], v[30:31], off offset:512 sc1
	global_store_dwordx2 v[216:217], v[26:27], off offset:1024 sc1
	global_store_dwordx2 v[216:217], v[22:23], off offset:1536 sc1
	global_store_dwordx2 v[216:217], v[24:25], off offset:2048 sc1
	global_store_dwordx2 v[216:217], v[28:29], off offset:2560 sc1
	global_store_dwordx2 v[216:217], v[32:33], off offset:3072 sc1
	global_store_dwordx2 v[216:217], v[36:37], off offset:3584 sc1
	global_store_dwordx2 v[214:215], v[38:39], off sc1
	global_store_dwordx2 v[214:215], v[40:41], off offset:512 sc1
	global_store_dwordx2 v[214:215], v[42:43], off offset:1024 sc1
	global_store_dwordx2 v[214:215], v[44:45], off offset:1536 sc1
	global_store_dwordx2 v[214:215], v[46:47], off offset:2048 sc1
	global_store_dwordx2 v[214:215], v[48:49], off offset:2560 sc1
	global_store_dwordx2 v[214:215], v[50:51], off offset:3072 sc1
	global_store_dwordx2 v[214:215], v[52:53], off offset:3584 sc1
	global_store_dwordx2 v[226:227], v[66:67], off sc1
	global_store_dwordx2 v[226:227], v[68:69], off offset:512 sc1
	global_store_dwordx2 v[226:227], v[70:71], off offset:1024 sc1
	global_store_dwordx2 v[226:227], v[72:73], off offset:1536 sc1
	global_store_dwordx2 v[226:227], v[74:75], off offset:2048 sc1
	global_store_dwordx2 v[226:227], v[76:77], off offset:2560 sc1
	global_store_dwordx2 v[226:227], v[78:79], off offset:3072 sc1
	global_store_dwordx2 v[226:227], v[80:81], off offset:3584 sc1
	global_store_dwordx2 v[212:213], v[10:11], off sc1
	global_store_dwordx2 v[212:213], v[6:7], off offset:512 sc1
	global_store_dwordx2 v[212:213], v[2:3], off offset:1024 sc1
	global_store_dwordx2 v[212:213], v[4:5], off offset:1536 sc1
	global_store_dwordx2 v[212:213], v[8:9], off offset:2048 sc1
	global_store_dwordx2 v[212:213], v[12:13], off offset:2560 sc1
	global_store_dwordx2 v[212:213], v[14:15], off offset:3072 sc1
	global_store_dwordx2 v[212:213], v[16:17], off offset:3584 sc1
	s_cbranch_scc1 .LBB0_372

.Lrot_ip:
	ds_read_b64_tr_b16 v[174:175], v204
	ds_read_b64_tr_b16 v[176:177], v204 offset:2048
	ds_read_b64_tr_b16 v[178:179], v208
	ds_read_b64_tr_b16 v[180:181], v208 offset:2048
	ds_read_b128 v[182:185], v206
	ds_read_b128 v[186:189], v206 offset:2048
	ds_read_b64_tr_b16 v[190:191], v212
	ds_read_b64_tr_b16 v[192:193], v212 offset:2048
	v_add_u32_e32 v214, s9, v146
	ds_read_b64_tr_b16 v[194:195], v214
	ds_read_b64_tr_b16 v[196:197], v214 offset:2048
	ds_read_b128 v[198:201], v206 offset:4096
	s_waitcnt lgkmcnt(6)
	v_mfma_f32_16x16x32_bf16 v[62:65], v[174:177], v[182:185], v[62:65]
	v_add_u32_e32 v202, 0xfff40000, v173
	s_add_i32 s9, s2, s7
	s_mov_b32 s14, m0
	s_mov_b32 m0, s9
	s_nop 0
	global_load_lds_dwordx4 v202, s[16:17]
	s_mov_b32 m0, s14
	v_mfma_f32_16x16x32_bf16 v[46:49], v[178:181], v[182:185], v[46:49]
	s_waitcnt lgkmcnt(3)
	v_mfma_f32_16x16x32_bf16 v[38:41], v[190:193], v[182:185], v[38:41]
	s_waitcnt lgkmcnt(1)
	v_mfma_f32_16x16x32_bf16 v[34:37], v[194:197], v[182:185], v[34:37]
	v_mfma_f32_16x16x32_bf16 v[30:33], v[174:177], v[186:189], v[30:33]
	ds_read_b128 v[182:185], v206 offset:6144
	v_add_u32_e32 v202, 0xfff80000, v173
	s_add_i32 s14, s9, 0x2000
	v_mfma_f32_16x16x32_bf16 v[26:29], v[178:181], v[186:189], v[26:29]
	s_mov_b32 s30, m0
	s_mov_b32 m0, s14
	s_nop 0
	global_load_lds_dwordx4 v202, s[16:17]
	s_mov_b32 m0, s30
	v_mfma_f32_16x16x32_bf16 v[22:25], v[190:193], v[186:189], v[22:25]
	v_mfma_f32_16x16x32_bf16 v[18:21], v[194:197], v[186:189], v[18:21]
	s_waitcnt lgkmcnt(1)
	v_mfma_f32_16x16x32_bf16 v[66:69], v[174:177], v[198:201], v[66:69]
	ds_read_b128 v[186:189], v206 offset:8192
	v_add_u32_e32 v202, 0xfffc0000, v173
	s_add_i32 s14, s9, 0x4000
	v_mfma_f32_16x16x32_bf16 v[78:81], v[178:181], v[198:201], v[78:81]
	s_mov_b32 s30, m0
	s_mov_b32 m0, s14
	s_nop 0
	global_load_lds_dwordx4 v202, s[16:17]
	s_mov_b32 m0, s30
	v_mfma_f32_16x16x32_bf16 v[90:93], v[190:193], v[198:201], v[90:93]
	v_mfma_f32_16x16x32_bf16 v[94:97], v[194:197], v[198:201], v[94:97]
	s_waitcnt lgkmcnt(1)
	v_mfma_f32_16x16x32_bf16 v[114:117], v[174:177], v[182:185], v[114:117]
	ds_read_b128 v[198:201], v206 offset:10240
	s_addk_i32 s9, 0x6000
	s_mov_b32 s14, m0
	s_mov_b32 m0, s9
	s_nop 0
	global_load_lds_dwordx4 v173, s[16:17]
	s_mov_b32 m0, s14
	v_mfma_f32_16x16x32_bf16 v[122:125], v[178:181], v[182:185], v[122:125]
	v_mfma_f32_16x16x32_bf16 v[138:141], v[190:193], v[182:185], v[138:141]
	v_mfma_f32_16x16x32_bf16 v[142:145], v[194:197], v[182:185], v[142:145]
	ds_read_b128 v[182:185], v206 offset:12288
	ds_read_b64_tr_b16 v[202:203], v204 offset:16384
	ds_read_b64_tr_b16 v[204:205], v204 offset:18432
	s_waitcnt lgkmcnt(4)
	v_mfma_f32_16x16x32_bf16 v[118:121], v[174:177], v[186:189], v[118:121]
	v_mfma_f32_16x16x32_bf16 v[126:129], v[178:181], v[186:189], v[126:129]
	v_mfma_f32_16x16x32_bf16 v[134:137], v[190:193], v[186:189], v[134:137]
	v_mfma_f32_16x16x32_bf16 v[130:133], v[194:197], v[186:189], v[130:133]
	ds_read_b128 v[186:189], v206 offset:14336
	ds_read_b64_tr_b16 v[206:207], v208 offset:16384
	ds_read_b64_tr_b16 v[208:209], v208 offset:18432
	s_waitcnt lgkmcnt(6)
	v_mfma_f32_16x16x32_bf16 v[98:101], v[174:177], v[198:201], v[98:101]
	v_mfma_f32_16x16x32_bf16 v[102:105], v[178:181], v[198:201], v[102:105]
	v_mfma_f32_16x16x32_bf16 v[110:113], v[190:193], v[198:201], v[110:113]
	v_mfma_f32_16x16x32_bf16 v[106:109], v[194:197], v[198:201], v[106:109]
	v_add_u32_e32 v215, s8, v171
	ds_read_b128 v[198:201], v215
	ds_read_b64_tr_b16 v[210:211], v212 offset:16384
	ds_read_b64_tr_b16 v[212:213], v212 offset:18432
	s_waitcnt lgkmcnt(8)
	v_mfma_f32_16x16x32_bf16 v[70:73], v[174:177], v[182:185], v[70:73]
	v_mfma_f32_16x16x32_bf16 v[82:85], v[178:181], v[182:185], v[82:85]
	v_mfma_f32_16x16x32_bf16 v[86:89], v[190:193], v[182:185], v[86:89]
	v_mfma_f32_16x16x32_bf16 v[74:77], v[194:197], v[182:185], v[74:77]
	s_waitcnt lgkmcnt(5)
	v_mfma_f32_16x16x32_bf16 v[42:45], v[174:177], v[186:189], v[42:45]
	ds_read_b128 v[174:177], v215 offset:2048
	s_and_b32 s8, s6, 0x8000
	v_mfma_f32_16x16x32_bf16 v[54:57], v[178:181], v[186:189], v[54:57]
	ds_read_b64_tr_b16 v[178:179], v214 offset:16384
	ds_read_b64_tr_b16 v[180:181], v214 offset:18432
	v_mfma_f32_16x16x32_bf16 v[58:61], v[190:193], v[186:189], v[58:61]
	v_mfma_f32_16x16x32_bf16 v[50:53], v[194:197], v[186:189], v[50:53]
	s_waitcnt lgkmcnt(5)
	v_mfma_f32_16x16x32_bf16 v[62:65], v[202:205], v[198:201], v[62:65]
	ds_read_b128 v[182:185], v215 offset:4096
	s_add_u32 s14, s3, s0
	s_addc_u32 s30, s4, s1
	v_mfma_f32_16x16x32_bf16 v[46:49], v[206:209], v[198:201], v[46:49]
	s_waitcnt vmcnt(7)
	v_add_u32_e32 v190, s8, v172
	s_add_u32 s8, s14, 0x100000
	s_waitcnt lgkmcnt(4)
	v_mfma_f32_16x16x32_bf16 v[38:41], v[210:213], v[198:201], v[38:41]
	ds_write_b128 v190, v[14:17]
	s_addc_u32 s9, s30, 0
	global_load_dwordx4 v[14:17], v162, s[8:9]
	s_waitcnt lgkmcnt(2)
	v_mfma_f32_16x16x32_bf16 v[34:37], v[178:181], v[198:201], v[34:37]
	v_mfma_f32_16x16x32_bf16 v[30:33], v[202:205], v[174:177], v[30:33]
	ds_read_b128 v[186:189], v215 offset:6144
	s_waitcnt vmcnt(7)
	s_add_u32 s8, s14, 0x120000
	v_mfma_f32_16x16x32_bf16 v[26:29], v[206:209], v[174:177], v[26:29]
	ds_write_b128 v190, v[10:13] offset:8192
	s_addc_u32 s9, s30, 0
	global_load_dwordx4 v[10:13], v162, s[8:9]
	v_mfma_f32_16x16x32_bf16 v[22:25], v[210:213], v[174:177], v[22:25]
	v_mfma_f32_16x16x32_bf16 v[18:21], v[178:181], v[174:177], v[18:21]
	s_waitcnt lgkmcnt(3)
	v_mfma_f32_16x16x32_bf16 v[66:69], v[202:205], v[182:185], v[66:69]
	ds_read_b128 v[174:177], v215 offset:8192
	s_waitcnt vmcnt(7)
	s_add_u32 s8, s14, 0x140000
	v_mfma_f32_16x16x32_bf16 v[78:81], v[206:209], v[182:185], v[78:81]
	ds_write_b128 v190, v[6:9] offset:16384
	s_addc_u32 s9, s30, 0
	global_load_dwordx4 v[6:9], v162, s[8:9]
	v_mfma_f32_16x16x32_bf16 v[90:93], v[210:213], v[182:185], v[90:93]
	v_mfma_f32_16x16x32_bf16 v[94:97], v[178:181], v[182:185], v[94:97]
	s_waitcnt lgkmcnt(3)
	v_mfma_f32_16x16x32_bf16 v[114:117], v[202:205], v[186:189], v[114:117]
	ds_read_b128 v[182:185], v215 offset:10240
	s_waitcnt vmcnt(7)
	s_add_u32 s8, s14, 0x160000
	v_mfma_f32_16x16x32_bf16 v[122:125], v[206:209], v[186:189], v[122:125]
	ds_write_b128 v190, v[2:5] offset:24576
	s_addc_u32 s9, s30, 0
	global_load_dwordx4 v[2:5], v162, s[8:9]
	v_mfma_f32_16x16x32_bf16 v[138:141], v[210:213], v[186:189], v[138:141]
	v_mfma_f32_16x16x32_bf16 v[142:145], v[178:181], v[186:189], v[142:145]
	s_waitcnt lgkmcnt(3)
	v_mfma_f32_16x16x32_bf16 v[118:121], v[202:205], v[174:177], v[118:121]
	ds_read_b128 v[186:189], v215 offset:12288
	v_mfma_f32_16x16x32_bf16 v[126:129], v[206:209], v[174:177], v[126:129]
	v_mfma_f32_16x16x32_bf16 v[134:137], v[210:213], v[174:177], v[134:137]
	v_mfma_f32_16x16x32_bf16 v[130:133], v[178:181], v[174:177], v[130:133]
	s_waitcnt lgkmcnt(2)
	v_mfma_f32_16x16x32_bf16 v[98:101], v[202:205], v[182:185], v[98:101]
	ds_read_b128 v[174:177], v215 offset:14336
	v_mfma_f32_16x16x32_bf16 v[102:105], v[206:209], v[182:185], v[102:105]
	v_mfma_f32_16x16x32_bf16 v[110:113], v[210:213], v[182:185], v[110:113]
	v_mfma_f32_16x16x32_bf16 v[106:109], v[178:181], v[182:185], v[106:109]
	s_waitcnt lgkmcnt(1)
	v_mfma_f32_16x16x32_bf16 v[70:73], v[202:205], v[186:189], v[70:73]
	v_mfma_f32_16x16x32_bf16 v[82:85], v[206:209], v[186:189], v[82:85]
	v_mfma_f32_16x16x32_bf16 v[86:89], v[210:213], v[186:189], v[86:89]
	v_mfma_f32_16x16x32_bf16 v[74:77], v[178:181], v[186:189], v[74:77]
	s_waitcnt lgkmcnt(0)
	v_mfma_f32_16x16x32_bf16 v[42:45], v[202:205], v[174:177], v[42:45]
	v_mfma_f32_16x16x32_bf16 v[54:57], v[206:209], v[174:177], v[54:57]
	v_mfma_f32_16x16x32_bf16 v[58:61], v[210:213], v[174:177], v[58:61]
	v_mfma_f32_16x16x32_bf16 v[50:53], v[178:181], v[174:177], v[50:53]
	s_add_i32 s8, s5, 0x8000
	s_cmp_lg_u32 s5, 0x10000
	s_cselect_b32 s5, s8, 0
	s_add_i32 s8, s7, 0x8000
	s_cmp_lg_u32 s7, 0x10000
	s_cselect_b32 s7, s8, 0
	s_add_u32 s0, s0, 0x80000
	s_addc_u32 s1, s1, 0
	s_add_i32 s6, s6, 0x8000
	v_add_u32_e32 v173, 0x80, v173
	s_add_i32 s9, s6, 0xffff8000
	s_and_b32 s9, s9, 0x8000
	s_add_i32 s9, s9, 0
	s_add_i32 s8, s5, 0
	s_add_i32 s9, s9, 0x18000
	v_add_u32_e32 v204, s9, v153
	v_add_u32_e32 v206, s8, v169
	v_add_u32_e32 v212, s9, v151
	v_add_u32_e32 v208, s9, v152
	s_waitcnt lgkmcnt(0)
	s_barrier
	s_cmp_lg_u32 s0, 0xf00000
	s_cbranch_scc1 .Lrot_ip
	s_add_i32 s0, 0, 0x18000
	v_add_u32_e32 v202, s0, v153
	v_add_u32_e32 v169, 0, v169
	v_add_u32_e32 v210, s0, v151
	v_add_u32_e32 v212, s0, v146
	ds_read_b64_tr_b16 v[172:173], v202
	ds_read_b64_tr_b16 v[174:175], v202 offset:2048
	v_add_u32_e32 v206, s0, v152
	ds_read_b128 v[176:179], v169
	ds_read_b64_tr_b16 v[180:181], v206
	ds_read_b64_tr_b16 v[182:183], v206 offset:2048
	ds_read_b128 v[184:187], v169 offset:2048
	ds_read_b64_tr_b16 v[188:189], v210
	ds_read_b64_tr_b16 v[190:191], v210 offset:2048
	ds_read_b64_tr_b16 v[192:193], v212
	ds_read_b64_tr_b16 v[194:195], v212 offset:2048
	s_waitcnt lgkmcnt(7)
	v_mfma_f32_16x16x32_bf16 v[62:65], v[172:175], v[176:179], v[62:65]
	ds_read_b128 v[196:199], v169 offset:4096
	s_waitcnt lgkmcnt(6)
	v_mfma_f32_16x16x32_bf16 v[46:49], v[180:183], v[176:179], v[46:49]
	s_waitcnt lgkmcnt(3)
	v_mfma_f32_16x16x32_bf16 v[38:41], v[188:191], v[176:179], v[38:41]
	s_waitcnt lgkmcnt(1)
	v_mfma_f32_16x16x32_bf16 v[34:37], v[192:195], v[176:179], v[34:37]
	v_mfma_f32_16x16x32_bf16 v[30:33], v[172:175], v[184:187], v[30:33]
	ds_read_b128 v[176:179], v169 offset:6144
	v_mfma_f32_16x16x32_bf16 v[26:29], v[180:183], v[184:187], v[26:29]
	v_mfma_f32_16x16x32_bf16 v[22:25], v[188:191], v[184:187], v[22:25]
	v_mfma_f32_16x16x32_bf16 v[18:21], v[192:195], v[184:187], v[18:21]
	s_waitcnt lgkmcnt(1)
	v_mfma_f32_16x16x32_bf16 v[66:69], v[172:175], v[196:199], v[66:69]
	ds_read_b128 v[184:187], v169 offset:8192
	v_mfma_f32_16x16x32_bf16 v[78:81], v[180:183], v[196:199], v[78:81]
	v_mfma_f32_16x16x32_bf16 v[90:93], v[188:191], v[196:199], v[90:93]
	v_mfma_f32_16x16x32_bf16 v[94:97], v[192:195], v[196:199], v[94:97]
	s_waitcnt lgkmcnt(1)
	v_mfma_f32_16x16x32_bf16 v[114:117], v[172:175], v[176:179], v[114:117]
	ds_read_b128 v[196:199], v169 offset:10240
	v_mfma_f32_16x16x32_bf16 v[122:125], v[180:183], v[176:179], v[122:125]
	v_mfma_f32_16x16x32_bf16 v[138:141], v[188:191], v[176:179], v[138:141]
	v_mfma_f32_16x16x32_bf16 v[142:145], v[192:195], v[176:179], v[142:145]
	ds_read_b128 v[176:179], v169 offset:12288
	ds_read_b64_tr_b16 v[200:201], v202 offset:16384
	ds_read_b64_tr_b16 v[202:203], v202 offset:18432
	s_waitcnt lgkmcnt(4)
	v_mfma_f32_16x16x32_bf16 v[118:121], v[172:175], v[184:187], v[118:121]
	v_mfma_f32_16x16x32_bf16 v[126:129], v[180:183], v[184:187], v[126:129]
	v_mfma_f32_16x16x32_bf16 v[134:137], v[188:191], v[184:187], v[134:137]
	v_mfma_f32_16x16x32_bf16 v[130:133], v[192:195], v[184:187], v[130:133]
	ds_read_b128 v[184:187], v169 offset:14336
	ds_read_b64_tr_b16 v[204:205], v206 offset:16384
	ds_read_b64_tr_b16 v[206:207], v206 offset:18432
	s_waitcnt lgkmcnt(6)
	v_mfma_f32_16x16x32_bf16 v[98:101], v[172:175], v[196:199], v[98:101]
	v_mfma_f32_16x16x32_bf16 v[102:105], v[180:183], v[196:199], v[102:105]
	v_mfma_f32_16x16x32_bf16 v[110:113], v[188:191], v[196:199], v[110:113]
	v_mfma_f32_16x16x32_bf16 v[106:109], v[192:195], v[196:199], v[106:109]
	v_add_u32_e32 v171, 0, v171
	ds_read_b128 v[196:199], v171
	ds_read_b64_tr_b16 v[208:209], v210 offset:16384
	ds_read_b64_tr_b16 v[210:211], v210 offset:18432
	s_waitcnt lgkmcnt(8)
	v_mfma_f32_16x16x32_bf16 v[70:73], v[172:175], v[176:179], v[70:73]
	v_mfma_f32_16x16x32_bf16 v[82:85], v[180:183], v[176:179], v[82:85]
	v_mfma_f32_16x16x32_bf16 v[86:89], v[188:191], v[176:179], v[86:89]
	v_mfma_f32_16x16x32_bf16 v[74:77], v[192:195], v[176:179], v[74:77]
	s_waitcnt lgkmcnt(5)
	v_mfma_f32_16x16x32_bf16 v[42:45], v[172:175], v[184:187], v[42:45]
	ds_read_b128 v[172:175], v171 offset:2048
	ds_read_b64_tr_b16 v[176:177], v212 offset:16384
	ds_read_b64_tr_b16 v[178:179], v212 offset:18432
	v_mfma_f32_16x16x32_bf16 v[54:57], v[180:183], v[184:187], v[54:57]
	v_mfma_f32_16x16x32_bf16 v[58:61], v[188:191], v[184:187], v[58:61]
	v_mfma_f32_16x16x32_bf16 v[50:53], v[192:195], v[184:187], v[50:53]
	ds_read_b128 v[180:183], v171 offset:4096
	s_waitcnt vmcnt(3)
	v_add_u32_e32 v168, s38, v168
	s_waitcnt lgkmcnt(6)
	v_mfma_f32_16x16x32_bf16 v[62:65], v[200:203], v[196:199], v[62:65]
	ds_write_b128 v168, v[14:17]
	v_mfma_f32_16x16x32_bf16 v[46:49], v[204:207], v[196:199], v[46:49]
	s_waitcnt lgkmcnt(5)
	v_mfma_f32_16x16x32_bf16 v[38:41], v[208:211], v[196:199], v[38:41]
	s_waitcnt lgkmcnt(2)
	v_mfma_f32_16x16x32_bf16 v[14:17], v[176:179], v[196:199], v[34:37]
	s_nop 2
	ds_read_b128 v[34:37], v171 offset:6144
	s_waitcnt vmcnt(2)
	v_mfma_f32_16x16x32_bf16 v[30:33], v[200:203], v[172:175], v[30:33]
	ds_write_b128 v168, v[10:13] offset:8192
	v_mfma_f32_16x16x32_bf16 v[26:29], v[204:207], v[172:175], v[26:29]
	v_mfma_f32_16x16x32_bf16 v[22:25], v[208:211], v[172:175], v[22:25]
	v_mfma_f32_16x16x32_bf16 v[10:13], v[176:179], v[172:175], v[18:21]
	s_waitcnt lgkmcnt(3)
	v_mfma_f32_16x16x32_bf16 v[18:21], v[200:203], v[180:183], v[66:69]
	v_mfma_f32_16x16x32_bf16 v[66:69], v[204:207], v[180:183], v[78:81]
	v_mfma_f32_16x16x32_bf16 v[78:81], v[208:211], v[180:183], v[90:93]
	s_nop 2
	ds_read_b128 v[90:93], v171 offset:8192
	s_waitcnt vmcnt(1)
	ds_write_b128 v168, v[6:9] offset:16384
	v_mfma_f32_16x16x32_bf16 v[6:9], v[176:179], v[180:183], v[94:97]
	s_waitcnt lgkmcnt(3)
	v_mfma_f32_16x16x32_bf16 v[94:97], v[200:203], v[34:37], v[114:117]
	v_mfma_f32_16x16x32_bf16 v[114:117], v[204:207], v[34:37], v[122:125]
	v_mfma_f32_16x16x32_bf16 v[122:125], v[208:211], v[34:37], v[138:141]
	s_nop 2
	ds_read_b128 v[138:141], v171 offset:10240
	s_waitcnt vmcnt(0)
	ds_write_b128 v168, v[2:5] offset:24576
	v_mfma_f32_16x16x32_bf16 v[2:5], v[176:179], v[34:37], v[142:145]
	s_waitcnt lgkmcnt(3)
	v_mfma_f32_16x16x32_bf16 v[34:37], v[200:203], v[90:93], v[118:121]
	v_mfma_f32_16x16x32_bf16 v[118:121], v[204:207], v[90:93], v[126:129]
	v_mfma_f32_16x16x32_bf16 v[126:129], v[208:211], v[90:93], v[134:137]
	s_nop 2
	ds_read_b128 v[134:137], v171 offset:12288
	v_mfma_f32_16x16x32_bf16 v[90:93], v[176:179], v[90:93], v[130:133]
	s_waitcnt lgkmcnt(2)
	v_mfma_f32_16x16x32_bf16 v[98:101], v[200:203], v[138:141], v[98:101]
	s_nop 0
	ds_read_b128 v[130:133], v171 offset:14336
	v_mfma_f32_16x16x32_bf16 v[102:105], v[204:207], v[138:141], v[102:105]
	v_mfma_f32_16x16x32_bf16 v[110:113], v[208:211], v[138:141], v[110:113]
	v_mfma_f32_16x16x32_bf16 v[106:109], v[176:179], v[138:141], v[106:109]
	s_waitcnt lgkmcnt(1)
	v_mfma_f32_16x16x32_bf16 v[70:73], v[200:203], v[134:137], v[70:73]
	v_mfma_f32_16x16x32_bf16 v[82:85], v[204:207], v[134:137], v[82:85]
	v_mfma_f32_16x16x32_bf16 v[86:89], v[208:211], v[134:137], v[86:89]
	v_mfma_f32_16x16x32_bf16 v[74:77], v[176:179], v[134:137], v[74:77]
	s_waitcnt lgkmcnt(0)
	v_mfma_f32_16x16x32_bf16 v[42:45], v[200:203], v[130:133], v[42:45]
	v_mfma_f32_16x16x32_bf16 v[54:57], v[204:207], v[130:133], v[54:57]
	v_mfma_f32_16x16x32_bf16 v[58:61], v[208:211], v[130:133], v[58:61]
	v_mfma_f32_16x16x32_bf16 v[50:53], v[176:179], v[130:133], v[50:53]
	s_waitcnt lgkmcnt(0)
	s_barrier
	v_add_u32_e32 v153, s38, v153
	v_add_u32_e32 v152, s38, v152
	v_add_u32_e32 v151, s38, v151
	ds_read_b64_tr_b16 v[130:131], v153
	ds_read_b64_tr_b16 v[132:133], v153 offset:2048
	ds_read_b64_tr_b16 v[134:135], v152
	ds_read_b64_tr_b16 v[136:137], v152 offset:2048
	ds_read_b128 v[138:141], v169 offset:32768
	ds_read_b64_tr_b16 v[142:143], v151
	ds_read_b128 v[172:175], v169 offset:34816
	ds_read_b128 v[176:179], v169 offset:36864
	ds_read_b64_tr_b16 v[144:145], v151 offset:2048
	v_add_u32_e32 v146, s38, v146
	ds_read_b64_tr_b16 v[180:181], v146
	ds_read_b64_tr_b16 v[182:183], v146 offset:2048
	s_waitcnt lgkmcnt(6)
	v_mfma_f32_16x16x32_bf16 v[62:65], v[130:133], v[138:141], v[62:65]
	v_mfma_f32_16x16x32_bf16 v[46:49], v[134:137], v[138:141], v[46:49]
	s_waitcnt lgkmcnt(2)
	v_mfma_f32_16x16x32_bf16 v[38:41], v[142:145], v[138:141], v[38:41]
	s_waitcnt lgkmcnt(0)
	v_mfma_f32_16x16x32_bf16 v[14:17], v[180:183], v[138:141], v[14:17]
	v_mfma_f32_16x16x32_bf16 v[30:33], v[130:133], v[172:175], v[30:33]
	ds_read_b128 v[138:141], v169 offset:38912
	v_mfma_f32_16x16x32_bf16 v[26:29], v[134:137], v[172:175], v[26:29]
	v_mfma_f32_16x16x32_bf16 v[22:25], v[142:145], v[172:175], v[22:25]
	v_mfma_f32_16x16x32_bf16 v[10:13], v[180:183], v[172:175], v[10:13]
	v_mfma_f32_16x16x32_bf16 v[18:21], v[130:133], v[176:179], v[18:21]
	ds_read_b128 v[172:175], v169 offset:40960
	v_mfma_f32_16x16x32_bf16 v[66:69], v[134:137], v[176:179], v[66:69]
	v_mfma_f32_16x16x32_bf16 v[78:81], v[142:145], v[176:179], v[78:81]
	v_mfma_f32_16x16x32_bf16 v[6:9], v[180:183], v[176:179], v[6:9]
	s_waitcnt lgkmcnt(1)
	v_mfma_f32_16x16x32_bf16 v[176:179], v[130:133], v[138:141], v[94:97]
	s_nop 2
	ds_read_b128 v[94:97], v169 offset:43008
	v_mfma_f32_16x16x32_bf16 v[2:5], v[180:183], v[138:141], v[2:5]
	v_mfma_f32_16x16x32_bf16 v[184:187], v[134:137], v[138:141], v[114:117]
	v_mfma_f32_16x16x32_bf16 v[188:191], v[142:145], v[138:141], v[122:125]
	s_nop 1
	ds_read_b128 v[114:117], v169 offset:45056
	ds_read_b64_tr_b16 v[196:197], v153 offset:16384
	ds_read_b64_tr_b16 v[198:199], v153 offset:18432
	s_waitcnt lgkmcnt(4)
	v_mfma_f32_16x16x32_bf16 v[34:37], v[130:133], v[172:175], v[34:37]
	v_mfma_f32_16x16x32_bf16 v[138:141], v[134:137], v[172:175], v[118:121]
	v_mfma_f32_16x16x32_bf16 v[192:195], v[142:145], v[172:175], v[126:129]
	v_mfma_f32_16x16x32_bf16 v[172:175], v[180:183], v[172:175], v[90:93]
	s_nop 2
	ds_read_b128 v[90:93], v169 offset:47104
	ds_read_b64_tr_b16 v[212:213], v152 offset:16384
	ds_read_b64_tr_b16 v[214:215], v152 offset:18432
	s_waitcnt lgkmcnt(6)
	v_mfma_f32_16x16x32_bf16 v[200:203], v[130:133], v[94:97], v[98:101]
	v_mfma_f32_16x16x32_bf16 v[204:207], v[134:137], v[94:97], v[102:105]
	v_mfma_f32_16x16x32_bf16 v[208:211], v[142:145], v[94:97], v[110:113]
	v_mfma_f32_16x16x32_bf16 v[216:219], v[180:183], v[94:97], v[106:109]
	s_waitcnt lgkmcnt(5)
	v_mfma_f32_16x16x32_bf16 v[220:223], v[130:133], v[114:117], v[70:73]
	s_nop 2
	ds_read_b128 v[70:73], v171 offset:32768
	ds_read_b64_tr_b16 v[232:233], v151 offset:16384
	ds_read_b64_tr_b16 v[234:235], v151 offset:18432
	v_mfma_f32_16x16x32_bf16 v[224:227], v[134:137], v[114:117], v[82:85]
	v_mfma_f32_16x16x32_bf16 v[228:231], v[142:145], v[114:117], v[86:89]
	v_mfma_f32_16x16x32_bf16 v[236:239], v[180:183], v[114:117], v[74:77]
	s_waitcnt lgkmcnt(5)
	v_mfma_f32_16x16x32_bf16 v[130:133], v[130:133], v[90:93], v[42:45]
	s_nop 2
	ds_read_b128 v[42:45], v171 offset:34816
	ds_read_b64_tr_b16 v[240:241], v146 offset:16384
	ds_read_b64_tr_b16 v[242:243], v146 offset:18432
	v_mfma_f32_16x16x32_bf16 v[134:137], v[134:137], v[90:93], v[54:57]
	v_mfma_f32_16x16x32_bf16 v[142:145], v[142:145], v[90:93], v[58:61]
	v_mfma_f32_16x16x32_bf16 v[180:183], v[180:183], v[90:93], v[50:53]
	s_waitcnt lgkmcnt(3)
	v_mfma_f32_16x16x32_bf16 v[118:121], v[232:235], v[70:73], v[38:41]
	s_nop 2
	ds_read_b128 v[38:41], v171 offset:36864
	v_mfma_f32_16x16x32_bf16 v[126:129], v[196:199], v[70:73], v[62:65]
	v_mfma_f32_16x16x32_bf16 v[122:125], v[212:215], v[70:73], v[46:49]
	s_waitcnt lgkmcnt(1)
	v_mfma_f32_16x16x32_bf16 v[114:117], v[240:243], v[70:73], v[14:17]
	s_nop 2
	ds_read_b128 v[14:17], v171 offset:38912
	v_mfma_f32_16x16x32_bf16 v[110:113], v[196:199], v[42:45], v[30:33]
	v_mfma_f32_16x16x32_bf16 v[106:109], v[212:215], v[42:45], v[26:29]
	v_mfma_f32_16x16x32_bf16 v[102:105], v[232:235], v[42:45], v[22:25]
	v_mfma_f32_16x16x32_bf16 v[98:101], v[240:243], v[42:45], v[10:13]
	s_nop 2
	ds_read_b128 v[10:13], v171 offset:40960
	s_waitcnt lgkmcnt(2)
	v_mfma_f32_16x16x32_bf16 v[94:97], v[196:199], v[38:41], v[18:21]
	v_mfma_f32_16x16x32_bf16 v[90:93], v[212:215], v[38:41], v[66:69]
	v_mfma_f32_16x16x32_bf16 v[86:89], v[232:235], v[38:41], v[78:81]
	v_mfma_f32_16x16x32_bf16 v[82:85], v[240:243], v[38:41], v[6:9]
	s_nop 2
	ds_read_b128 v[6:9], v171 offset:43008
	s_waitcnt lgkmcnt(2)
	v_mfma_f32_16x16x32_bf16 v[78:81], v[196:199], v[14:17], v[176:179]
	v_mfma_f32_16x16x32_bf16 v[74:77], v[212:215], v[14:17], v[184:187]
	v_mfma_f32_16x16x32_bf16 v[70:73], v[232:235], v[14:17], v[188:191]
	v_mfma_f32_16x16x32_bf16 v[66:69], v[240:243], v[14:17], v[2:5]
	s_nop 2
	ds_read_b128 v[2:5], v171 offset:45056
	s_waitcnt lgkmcnt(2)
	v_mfma_f32_16x16x32_bf16 v[62:65], v[196:199], v[10:13], v[34:37]
	v_mfma_f32_16x16x32_bf16 v[58:61], v[212:215], v[10:13], v[138:141]
	v_mfma_f32_16x16x32_bf16 v[54:57], v[232:235], v[10:13], v[192:195]
	v_mfma_f32_16x16x32_bf16 v[50:53], v[240:243], v[10:13], v[172:175]
	s_waitcnt lgkmcnt(1)
	v_mfma_f32_16x16x32_bf16 v[46:49], v[196:199], v[6:9], v[200:203]
	ds_read_b128 v[138:141], v171 offset:47104
	v_mfma_f32_16x16x32_bf16 v[42:45], v[212:215], v[6:9], v[204:207]
	v_mfma_f32_16x16x32_bf16 v[38:41], v[232:235], v[6:9], v[208:211]
	v_mfma_f32_16x16x32_bf16 v[34:37], v[240:243], v[6:9], v[216:219]
	s_waitcnt lgkmcnt(1)
	v_mfma_f32_16x16x32_bf16 v[30:33], v[196:199], v[2:5], v[220:223]
	v_mfma_f32_16x16x32_bf16 v[26:29], v[212:215], v[2:5], v[224:227]
	v_mfma_f32_16x16x32_bf16 v[22:25], v[232:235], v[2:5], v[228:231]
	v_mfma_f32_16x16x32_bf16 v[18:21], v[240:243], v[2:5], v[236:239]
	s_waitcnt lgkmcnt(0)
	v_mfma_f32_16x16x32_bf16 v[14:17], v[196:199], v[138:141], v[130:133]
	v_mfma_f32_16x16x32_bf16 v[10:13], v[212:215], v[138:141], v[134:137]
	v_mfma_f32_16x16x32_bf16 v[6:9], v[232:235], v[138:141], v[142:145]
	v_mfma_f32_16x16x32_bf16 v[2:5], v[240:243], v[138:141], v[180:183]
	s_waitcnt lgkmcnt(0)
	s_barrier
	v_mov_b32_e32 v151, v155
	v_mov_b32_e32 v168, v1
	s_cmpk_gt_i32 s28, 0x3ff
	s_mov_b64 s[0:1], -1
	s_cbranch_scc1 .LBB0_607
	s_add_i32 s0, s52, s50
	v_add_u32_e32 v140, s0, v168
	s_lshl_b32 s0, s51, 6
	s_or_b32 s0, s0, s28
	v_lshlrev_b32_e32 v132, 2, v151
	v_add_u32_e32 v146, s0, v132
	v_ashrrev_i32_e32 v141, 31, v140
	v_lshlrev_b64 v[142:143], 11, v[140:141]
	v_cmp_lt_i32_e64 s[4:5], s39, v146
	s_and_saveexec_b64 s[0:1], s[4:5]
	s_xor_b64 s[0:1], exec, s[0:1]
	s_cbranch_execz .LBB0_442
	v_cmp_lt_u32_e32 vcc, s41, v146
	s_and_saveexec_b64 s[2:3], vcc
	s_xor_b64 s[2:3], exec, s[2:3]
	s_cbranch_execz .LBB0_439
	v_cmp_lt_u32_e32 vcc, s42, v146
	v_cvt_pk_bf16_f32 v130, v126, v127
	v_cvt_pk_bf16_f32 v131, v128, v129
	s_and_saveexec_b64 s[6:7], vcc
	s_xor_b64 s[6:7], exec, s[6:7]
	s_cbranch_execz .LBB0_436
	v_lshl_add_u64 v[134:135], s[24:25], 0, v[142:143]
	v_lshl_add_u64 v[134:135], v[146:147], 1, v[134:135]
	v_add_co_u32_e32 v134, vcc, 0xfffff000, v134
	s_nop 1
	v_addc_co_u32_e32 v135, vcc, -1, v135, vcc
	global_store_dwordx2 v[134:135], v[130:131], off offset:-2048 sc1
.LBB0_436:
	s_andn2_saveexec_b64 s[6:7], s[6:7]
	s_cbranch_execz .LBB0_438
	v_lshl_add_u64 v[134:135], s[22:23], 0, v[142:143]
	v_lshl_add_u64 v[134:135], v[146:147], 1, v[134:135]
	global_store_dwordx2 v[134:135], v[130:131], off offset:-4096 sc1

.LBB0_439:
	s_andn2_saveexec_b64 s[2:3], s[2:3]
	s_cbranch_execz .LBB0_441
	v_pk_mul_f32 v[130:131], v[126:127], s[26:27] op_sel_hi:[1,0]
	v_pk_mul_f32 v[134:135], v[128:129], s[26:27] op_sel_hi:[1,0]
	v_cvt_pk_bf16_f32 v130, v130, v131
	v_cvt_pk_bf16_f32 v131, v134, v135
	v_lshl_add_u64 v[134:135], s[20:21], 0, v[142:143]
	v_lshl_add_u64 v[134:135], v[146:147], 1, v[134:135]
	global_store_dwordx2 v[134:135], v[130:131], off offset:-2048 sc1

.LBB0_442:
	s_or_saveexec_b64 s[0:1], s[0:1]
	v_ashrrev_i32_e32 v130, 4, v140
	v_lshrrev_b32_e32 v131, 4, v140
	v_bfi_b32 v141, s40, v130, v131
	v_lshlrev_b32_e32 v130, 4, v168
	v_and_b32_e32 v130, 0xf0, v130
	v_and_b32_e32 v131, 12, v132
	v_lshlrev_b32_e32 v132, 5, v146
	v_and_b32_e32 v169, 0xfffffe00, v132
	v_lshlrev_b32_e32 v130, 1, v130
	v_lshlrev_b32_e32 v132, 1, v131
	s_xor_b64 exec, exec, s[0:1]
	s_cbranch_execz .LBB0_444
	v_add_u32_e32 v136, v169, v141
	v_ashrrev_i32_e32 v137, 31, v136
	v_lshlrev_b64 v[136:137], 10, v[136:137]
	v_lshl_add_u64 v[136:137], s[18:19], 0, v[136:137]
	v_mov_b32_e32 v131, v147
	v_lshl_add_u64 v[136:137], v[136:137], 0, v[130:131]
	v_mov_b32_e32 v133, v147
	v_cvt_pk_bf16_f32 v134, v126, v127
	v_cvt_pk_bf16_f32 v135, v128, v129
	v_lshl_add_u64 v[136:137], v[136:137], 0, v[132:133]
	global_store_dwordx2 v[136:137], v[134:135], off sc1
.LBB0_444:
	s_or_b64 exec, exec, s[0:1]
	v_add_u32_e32 v138, 16, v146
	v_cmp_lt_i32_e64 s[8:9], s39, v138
	s_and_saveexec_b64 s[0:1], s[8:9]
	s_xor_b64 s[0:1], exec, s[0:1]
	s_cbranch_execz .LBB0_454
	v_cmp_lt_u32_e32 vcc, s41, v138
	s_and_saveexec_b64 s[2:3], vcc
	s_xor_b64 s[2:3], exec, s[2:3]
	s_cbranch_execz .LBB0_451
	v_cmp_lt_u32_e32 vcc, s42, v138
	v_cvt_pk_bf16_f32 v134, v122, v123
	v_cvt_pk_bf16_f32 v135, v124, v125
	v_mov_b32_e32 v139, v147
	s_and_saveexec_b64 s[6:7], vcc
	s_xor_b64 s[6:7], exec, s[6:7]
	s_cbranch_execz .LBB0_448
	v_lshl_add_u64 v[136:137], s[24:25], 0, v[142:143]
	v_lshl_add_u64 v[136:137], v[138:139], 1, v[136:137]
	v_add_co_u32_e32 v136, vcc, 0xfffff000, v136
	s_nop 1
	v_addc_co_u32_e32 v137, vcc, -1, v137, vcc
	global_store_dwordx2 v[136:137], v[134:135], off offset:-2048 sc1
.LBB0_448:
	s_andn2_saveexec_b64 s[6:7], s[6:7]
	s_cbranch_execz .LBB0_450
	v_lshl_add_u64 v[136:137], s[22:23], 0, v[142:143]
	v_lshl_add_u64 v[136:137], v[138:139], 1, v[136:137]
	global_store_dwordx2 v[136:137], v[134:135], off offset:-4096 sc1

.LBB0_451:
	s_andn2_saveexec_b64 s[2:3], s[2:3]
	s_cbranch_execz .LBB0_453
	v_pk_mul_f32 v[134:135], v[122:123], s[26:27] op_sel_hi:[1,0]
	v_pk_mul_f32 v[136:137], v[124:125], s[26:27] op_sel_hi:[1,0]
	v_cvt_pk_bf16_f32 v134, v134, v135
	v_cvt_pk_bf16_f32 v135, v136, v137
	v_lshl_add_u64 v[136:137], s[20:21], 0, v[142:143]
	v_mov_b32_e32 v139, v147
	v_lshl_add_u64 v[136:137], v[138:139], 1, v[136:137]
	global_store_dwordx2 v[136:137], v[134:135], off offset:-2048 sc1

.LBB0_454:
	s_or_saveexec_b64 s[0:1], s[0:1]
	v_lshlrev_b32_e32 v131, 5, v138
	v_and_b32_e32 v173, 0xfffffe00, v131
	s_xor_b64 exec, exec, s[0:1]
	s_cbranch_execz .LBB0_456
	v_add_u32_e32 v136, v173, v141
	v_ashrrev_i32_e32 v137, 31, v136
	v_lshlrev_b64 v[136:137], 10, v[136:137]
	v_lshl_add_u64 v[136:137], s[18:19], 0, v[136:137]
	v_mov_b32_e32 v131, v147
	v_lshl_add_u64 v[136:137], v[136:137], 0, v[130:131]
	v_mov_b32_e32 v133, v147
	v_cvt_pk_bf16_f32 v134, v122, v123
	v_cvt_pk_bf16_f32 v135, v124, v125
	v_lshl_add_u64 v[136:137], v[136:137], 0, v[132:133]
	global_store_dwordx2 v[136:137], v[134:135], off sc1
.LBB0_456:
	s_or_b64 exec, exec, s[0:1]
	v_add_u32_e32 v136, 32, v146
	v_cmp_lt_i32_e64 s[6:7], s39, v136
	s_and_saveexec_b64 s[0:1], s[6:7]
	s_xor_b64 s[0:1], exec, s[0:1]
	s_cbranch_execz .LBB0_466
	v_cmp_lt_u32_e32 vcc, s41, v136
	s_and_saveexec_b64 s[2:3], vcc
	s_xor_b64 s[2:3], exec, s[2:3]
	s_cbranch_execz .LBB0_463
	v_cmp_lt_u32_e32 vcc, s42, v136
	v_cvt_pk_bf16_f32 v134, v118, v119
	v_cvt_pk_bf16_f32 v135, v120, v121
	v_mov_b32_e32 v137, v147
	s_and_saveexec_b64 s[30:31], vcc
	s_xor_b64 s[30:31], exec, s[30:31]
	s_cbranch_execz .LBB0_460
	v_lshl_add_u64 v[144:145], s[24:25], 0, v[142:143]
	v_lshl_add_u64 v[144:145], v[136:137], 1, v[144:145]
	v_add_co_u32_e32 v144, vcc, 0xfffff000, v144
	s_nop 1
	v_addc_co_u32_e32 v145, vcc, -1, v145, vcc
	global_store_dwordx2 v[144:145], v[134:135], off offset:-2048 sc1
.LBB0_460:
	s_andn2_saveexec_b64 s[30:31], s[30:31]
	s_cbranch_execz .LBB0_462
	v_lshl_add_u64 v[144:145], s[22:23], 0, v[142:143]
	v_lshl_add_u64 v[144:145], v[136:137], 1, v[144:145]
	global_store_dwordx2 v[144:145], v[134:135], off offset:-4096 sc1

.LBB0_463:
	s_andn2_saveexec_b64 s[2:3], s[2:3]
	s_cbranch_execz .LBB0_465
	v_pk_mul_f32 v[134:135], v[118:119], s[26:27] op_sel_hi:[1,0]
	v_pk_mul_f32 v[144:145], v[120:121], s[26:27] op_sel_hi:[1,0]
	v_cvt_pk_bf16_f32 v134, v134, v135
	v_cvt_pk_bf16_f32 v135, v144, v145
	v_lshl_add_u64 v[144:145], s[20:21], 0, v[142:143]
	v_mov_b32_e32 v137, v147
	v_lshl_add_u64 v[144:145], v[136:137], 1, v[144:145]
	global_store_dwordx2 v[144:145], v[134:135], off offset:-2048 sc1

.LBB0_466:
	s_or_saveexec_b64 s[0:1], s[0:1]
	v_lshlrev_b32_e32 v131, 5, v136
	v_and_b32_e32 v172, 0xfffffe00, v131
	s_xor_b64 exec, exec, s[0:1]
	s_cbranch_execz .LBB0_468
	v_add_u32_e32 v144, v172, v141
	v_ashrrev_i32_e32 v145, 31, v144
	v_lshlrev_b64 v[144:145], 10, v[144:145]
	v_lshl_add_u64 v[144:145], s[18:19], 0, v[144:145]
	v_mov_b32_e32 v131, v147
	v_lshl_add_u64 v[144:145], v[144:145], 0, v[130:131]
	v_mov_b32_e32 v133, v147
	v_cvt_pk_bf16_f32 v134, v118, v119
	v_cvt_pk_bf16_f32 v135, v120, v121
	v_lshl_add_u64 v[144:145], v[144:145], 0, v[132:133]
	global_store_dwordx2 v[144:145], v[134:135], off sc1
.LBB0_468:
	s_or_b64 exec, exec, s[0:1]
	v_add_u32_e32 v134, 48, v146
	v_cmp_lt_i32_e64 s[0:1], s39, v134
	s_and_saveexec_b64 s[2:3], s[0:1]
	s_xor_b64 s[2:3], exec, s[2:3]
	s_cbranch_execz .LBB0_478
	v_cmp_lt_u32_e32 vcc, s41, v134
	s_and_saveexec_b64 s[30:31], vcc
	s_xor_b64 s[30:31], exec, s[30:31]
	s_cbranch_execz .LBB0_475
	v_cmp_lt_u32_e32 vcc, s42, v134
	v_cvt_pk_bf16_f32 v144, v114, v115
	v_cvt_pk_bf16_f32 v145, v116, v117
	v_mov_b32_e32 v135, v147
	s_and_saveexec_b64 s[34:35], vcc
	s_xor_b64 s[34:35], exec, s[34:35]
	s_cbranch_execz .LBB0_472
	v_lshl_add_u64 v[142:143], s[24:25], 0, v[142:143]
	v_lshl_add_u64 v[142:143], v[134:135], 1, v[142:143]
	v_add_co_u32_e32 v142, vcc, 0xfffff000, v142
	s_nop 1
	v_addc_co_u32_e32 v143, vcc, -1, v143, vcc
	global_store_dwordx2 v[142:143], v[144:145], off offset:-2048 sc1
.LBB0_472:
	s_andn2_saveexec_b64 s[34:35], s[34:35]
	s_cbranch_execz .LBB0_474
	v_lshl_add_u64 v[142:143], s[22:23], 0, v[142:143]
	v_lshl_add_u64 v[142:143], v[134:135], 1, v[142:143]
	global_store_dwordx2 v[142:143], v[144:145], off offset:-4096 sc1

.LBB0_475:
	s_andn2_saveexec_b64 s[30:31], s[30:31]
	s_cbranch_execz .LBB0_477
	v_pk_mul_f32 v[144:145], v[114:115], s[26:27] op_sel_hi:[1,0]
	v_pk_mul_f32 v[152:153], v[116:117], s[26:27] op_sel_hi:[1,0]
	v_lshl_add_u64 v[142:143], s[20:21], 0, v[142:143]
	v_mov_b32_e32 v135, v147
	v_cvt_pk_bf16_f32 v144, v144, v145
	v_cvt_pk_bf16_f32 v145, v152, v153
	v_lshl_add_u64 v[142:143], v[134:135], 1, v[142:143]
	global_store_dwordx2 v[142:143], v[144:145], off offset:-2048 sc1

.LBB0_478:
	s_or_saveexec_b64 s[2:3], s[2:3]
	v_lshlrev_b32_e32 v131, 5, v134
	v_and_b32_e32 v171, 0xfffffe00, v131
	s_xor_b64 exec, exec, s[2:3]
	s_cbranch_execz .LBB0_480
	v_add_u32_e32 v144, v171, v141
	v_ashrrev_i32_e32 v145, 31, v144
	v_lshlrev_b64 v[144:145], 10, v[144:145]
	v_lshl_add_u64 v[144:145], s[18:19], 0, v[144:145]
	v_mov_b32_e32 v131, v147
	v_lshl_add_u64 v[144:145], v[144:145], 0, v[130:131]
	v_mov_b32_e32 v133, v147
	v_cvt_pk_bf16_f32 v142, v114, v115
	v_cvt_pk_bf16_f32 v143, v116, v117
	v_lshl_add_u64 v[144:145], v[144:145], 0, v[132:133]
	global_store_dwordx2 v[144:145], v[142:143], off sc1
.LBB0_480:
	s_or_b64 exec, exec, s[2:3]
	v_add_u32_e32 v144, 16, v140
	v_ashrrev_i32_e32 v145, 31, v144
	v_lshlrev_b64 v[142:143], 11, v[144:145]
	s_and_saveexec_b64 s[2:3], s[4:5]
	s_xor_b64 s[2:3], exec, s[2:3]
	s_cbranch_execz .LBB0_490
	v_cmp_lt_u32_e32 vcc, s41, v146
	s_and_saveexec_b64 s[30:31], vcc
	s_xor_b64 s[30:31], exec, s[30:31]
	s_cbranch_execz .LBB0_487
	v_cmp_lt_u32_e32 vcc, s42, v146
	v_cvt_pk_bf16_f32 v152, v110, v111
	v_cvt_pk_bf16_f32 v153, v112, v113
	s_and_saveexec_b64 s[34:35], vcc
	s_xor_b64 s[34:35], exec, s[34:35]
	s_cbranch_execz .LBB0_484
	v_lshl_add_u64 v[174:175], s[24:25], 0, v[142:143]
	v_lshl_add_u64 v[174:175], v[146:147], 1, v[174:175]
	v_add_co_u32_e32 v174, vcc, 0xfffff000, v174
	s_nop 1
	v_addc_co_u32_e32 v175, vcc, -1, v175, vcc
	global_store_dwordx2 v[174:175], v[152:153], off offset:-2048 sc1
.LBB0_484:
	s_andn2_saveexec_b64 s[34:35], s[34:35]
	s_cbranch_execz .LBB0_486
	v_lshl_add_u64 v[174:175], s[22:23], 0, v[142:143]
	v_lshl_add_u64 v[174:175], v[146:147], 1, v[174:175]
	global_store_dwordx2 v[174:175], v[152:153], off offset:-4096 sc1

.LBB0_487:
	s_andn2_saveexec_b64 s[30:31], s[30:31]
	s_cbranch_execz .LBB0_489
	v_pk_mul_f32 v[152:153], v[110:111], s[26:27] op_sel_hi:[1,0]
	v_pk_mul_f32 v[174:175], v[112:113], s[26:27] op_sel_hi:[1,0]
	v_cvt_pk_bf16_f32 v152, v152, v153
	v_cvt_pk_bf16_f32 v153, v174, v175
	v_lshl_add_u64 v[174:175], s[20:21], 0, v[142:143]
	v_lshl_add_u64 v[174:175], v[146:147], 1, v[174:175]
	global_store_dwordx2 v[174:175], v[152:153], off offset:-2048 sc1

.LBB0_490:
	s_or_saveexec_b64 s[2:3], s[2:3]
	v_ashrrev_i32_e32 v131, 4, v144
	v_lshrrev_b32_e32 v133, 4, v144
	v_bfi_b32 v135, s40, v131, v133
	s_xor_b64 exec, exec, s[2:3]
	s_cbranch_execz .LBB0_609
	v_add_u32_e32 v152, v135, v169
	v_ashrrev_i32_e32 v153, 31, v152
	v_lshlrev_b64 v[152:153], 10, v[152:153]
	v_lshl_add_u64 v[152:153], s[18:19], 0, v[152:153]
	v_mov_b32_e32 v131, v147
	v_lshl_add_u64 v[152:153], v[152:153], 0, v[130:131]
	v_mov_b32_e32 v133, v147
	v_cvt_pk_bf16_f32 v144, v110, v111
	v_cvt_pk_bf16_f32 v145, v112, v113
	v_lshl_add_u64 v[152:153], v[152:153], 0, v[132:133]
	global_store_dwordx2 v[152:153], v[144:145], off sc1
	s_or_b64 exec, exec, s[2:3]
	s_and_saveexec_b64 s[2:3], s[8:9]
	s_xor_b64 s[2:3], exec, s[2:3]
	s_cbranch_execnz .LBB0_610

.LBB0_493:
	v_add_u32_e32 v152, v173, v135
	v_ashrrev_i32_e32 v153, 31, v152
	v_lshlrev_b64 v[152:153], 10, v[152:153]
	v_lshl_add_u64 v[152:153], s[18:19], 0, v[152:153]
	v_mov_b32_e32 v131, v147
	v_lshl_add_u64 v[152:153], v[152:153], 0, v[130:131]
	v_mov_b32_e32 v133, v147
	v_cvt_pk_bf16_f32 v144, v106, v107
	v_cvt_pk_bf16_f32 v145, v108, v109
	v_lshl_add_u64 v[152:153], v[152:153], 0, v[132:133]
	global_store_dwordx2 v[152:153], v[144:145], off sc1
	s_or_b64 exec, exec, s[2:3]
	s_and_saveexec_b64 s[2:3], s[6:7]
	s_xor_b64 s[2:3], exec, s[2:3]
	s_cbranch_execnz .LBB0_620

.LBB0_495:
	v_add_u32_e32 v152, v172, v135
	v_ashrrev_i32_e32 v153, 31, v152
	v_lshlrev_b64 v[152:153], 10, v[152:153]
	v_lshl_add_u64 v[152:153], s[18:19], 0, v[152:153]
	v_mov_b32_e32 v131, v147
	v_lshl_add_u64 v[152:153], v[152:153], 0, v[130:131]
	v_mov_b32_e32 v133, v147
	v_cvt_pk_bf16_f32 v144, v102, v103
	v_cvt_pk_bf16_f32 v145, v104, v105
	v_lshl_add_u64 v[152:153], v[152:153], 0, v[132:133]
	global_store_dwordx2 v[152:153], v[144:145], off sc1
	s_or_b64 exec, exec, s[2:3]
	s_and_saveexec_b64 s[2:3], s[0:1]
	s_xor_b64 s[2:3], exec, s[2:3]
	s_cbranch_execnz .LBB0_630

.LBB0_497:
	v_add_u32_e32 v144, v171, v135
	v_ashrrev_i32_e32 v145, 31, v144
	v_lshlrev_b64 v[144:145], 10, v[144:145]
	v_lshl_add_u64 v[144:145], s[18:19], 0, v[144:145]
	v_mov_b32_e32 v131, v147
	v_lshl_add_u64 v[144:145], v[144:145], 0, v[130:131]
	v_mov_b32_e32 v133, v147
	v_cvt_pk_bf16_f32 v142, v98, v99
	v_cvt_pk_bf16_f32 v143, v100, v101
	v_lshl_add_u64 v[144:145], v[144:145], 0, v[132:133]
	global_store_dwordx2 v[144:145], v[142:143], off sc1
.LBB0_498:
	s_or_b64 exec, exec, s[2:3]
	v_add_u32_e32 v144, 32, v140
	v_ashrrev_i32_e32 v145, 31, v144
	v_lshlrev_b64 v[142:143], 11, v[144:145]
	s_and_saveexec_b64 s[2:3], s[4:5]
	s_xor_b64 s[2:3], exec, s[2:3]
	s_cbranch_execz .LBB0_508
	v_cmp_lt_u32_e32 vcc, s41, v146
	s_and_saveexec_b64 s[30:31], vcc
	s_xor_b64 s[30:31], exec, s[30:31]
	s_cbranch_execz .LBB0_505
	v_cmp_lt_u32_e32 vcc, s42, v146
	v_cvt_pk_bf16_f32 v152, v94, v95
	v_cvt_pk_bf16_f32 v153, v96, v97
	s_and_saveexec_b64 s[34:35], vcc
	s_xor_b64 s[34:35], exec, s[34:35]
	s_cbranch_execz .LBB0_502
	v_lshl_add_u64 v[174:175], s[24:25], 0, v[142:143]
	v_lshl_add_u64 v[174:175], v[146:147], 1, v[174:175]
	v_add_co_u32_e32 v174, vcc, 0xfffff000, v174
	s_nop 1
	v_addc_co_u32_e32 v175, vcc, -1, v175, vcc
	global_store_dwordx2 v[174:175], v[152:153], off offset:-2048 sc1

.LBB0_505:
	s_andn2_saveexec_b64 s[30:31], s[30:31]
	s_cbranch_execz .LBB0_507
	v_pk_mul_f32 v[152:153], v[94:95], s[26:27] op_sel_hi:[1,0]
	v_pk_mul_f32 v[174:175], v[96:97], s[26:27] op_sel_hi:[1,0]
	v_cvt_pk_bf16_f32 v152, v152, v153
	v_cvt_pk_bf16_f32 v153, v174, v175
	v_lshl_add_u64 v[174:175], s[20:21], 0, v[142:143]
	v_lshl_add_u64 v[174:175], v[146:147], 1, v[174:175]
	global_store_dwordx2 v[174:175], v[152:153], off offset:-2048 sc1

.LBB0_508:
	s_or_saveexec_b64 s[2:3], s[2:3]
	v_ashrrev_i32_e32 v131, 4, v144
	v_lshrrev_b32_e32 v133, 4, v144
	v_bfi_b32 v135, s40, v131, v133
	s_xor_b64 exec, exec, s[2:3]
	s_cbranch_execz .LBB0_639
	v_add_u32_e32 v152, v135, v169
	v_ashrrev_i32_e32 v153, 31, v152
	v_lshlrev_b64 v[152:153], 10, v[152:153]
	v_lshl_add_u64 v[152:153], s[18:19], 0, v[152:153]
	v_mov_b32_e32 v131, v147
	v_lshl_add_u64 v[152:153], v[152:153], 0, v[130:131]
	v_mov_b32_e32 v133, v147
	v_cvt_pk_bf16_f32 v144, v94, v95
	v_cvt_pk_bf16_f32 v145, v96, v97
	v_lshl_add_u64 v[152:153], v[152:153], 0, v[132:133]
	global_store_dwordx2 v[152:153], v[144:145], off sc1
	s_or_b64 exec, exec, s[2:3]
	s_and_saveexec_b64 s[2:3], s[8:9]
	s_xor_b64 s[2:3], exec, s[2:3]
	s_cbranch_execnz .LBB0_640

.LBB0_511:
	v_add_u32_e32 v152, v173, v135
	v_ashrrev_i32_e32 v153, 31, v152
	v_lshlrev_b64 v[152:153], 10, v[152:153]
	v_lshl_add_u64 v[152:153], s[18:19], 0, v[152:153]
	v_mov_b32_e32 v131, v147
	v_lshl_add_u64 v[152:153], v[152:153], 0, v[130:131]
	v_mov_b32_e32 v133, v147
	v_cvt_pk_bf16_f32 v144, v90, v91
	v_cvt_pk_bf16_f32 v145, v92, v93
	v_lshl_add_u64 v[152:153], v[152:153], 0, v[132:133]
	global_store_dwordx2 v[152:153], v[144:145], off sc1
	s_or_b64 exec, exec, s[2:3]
	s_and_saveexec_b64 s[2:3], s[6:7]
	s_xor_b64 s[2:3], exec, s[2:3]
	s_cbranch_execnz .LBB0_650

.LBB0_513:
	v_add_u32_e32 v152, v172, v135
	v_ashrrev_i32_e32 v153, 31, v152
	v_lshlrev_b64 v[152:153], 10, v[152:153]
	v_lshl_add_u64 v[152:153], s[18:19], 0, v[152:153]
	v_mov_b32_e32 v131, v147
	v_lshl_add_u64 v[152:153], v[152:153], 0, v[130:131]
	v_mov_b32_e32 v133, v147
	v_cvt_pk_bf16_f32 v144, v86, v87
	v_cvt_pk_bf16_f32 v145, v88, v89
	v_lshl_add_u64 v[152:153], v[152:153], 0, v[132:133]
	global_store_dwordx2 v[152:153], v[144:145], off sc1
	s_or_b64 exec, exec, s[2:3]
	s_and_saveexec_b64 s[2:3], s[0:1]
	s_xor_b64 s[2:3], exec, s[2:3]
	s_cbranch_execnz .LBB0_660

.LBB0_515:
	v_add_u32_e32 v144, v171, v135
	v_ashrrev_i32_e32 v145, 31, v144
	v_lshlrev_b64 v[144:145], 10, v[144:145]
	v_lshl_add_u64 v[144:145], s[18:19], 0, v[144:145]
	v_mov_b32_e32 v131, v147
	v_lshl_add_u64 v[144:145], v[144:145], 0, v[130:131]
	v_mov_b32_e32 v133, v147
	v_cvt_pk_bf16_f32 v142, v82, v83
	v_cvt_pk_bf16_f32 v143, v84, v85
	v_lshl_add_u64 v[144:145], v[144:145], 0, v[132:133]
	global_store_dwordx2 v[144:145], v[142:143], off sc1
.LBB0_516:
	s_or_b64 exec, exec, s[2:3]
	v_add_u32_e32 v144, 48, v140
	v_ashrrev_i32_e32 v145, 31, v144
	v_lshlrev_b64 v[142:143], 11, v[144:145]
	s_and_saveexec_b64 s[2:3], s[4:5]
	s_xor_b64 s[2:3], exec, s[2:3]
	s_cbranch_execz .LBB0_526
	v_cmp_lt_u32_e32 vcc, s41, v146
	s_and_saveexec_b64 s[30:31], vcc
	s_xor_b64 s[30:31], exec, s[30:31]
	s_cbranch_execz .LBB0_523
	v_cmp_lt_u32_e32 vcc, s42, v146
	v_cvt_pk_bf16_f32 v152, v78, v79
	v_cvt_pk_bf16_f32 v153, v80, v81
	s_and_saveexec_b64 s[34:35], vcc
	s_xor_b64 s[34:35], exec, s[34:35]
	s_cbranch_execz .LBB0_520
	v_lshl_add_u64 v[174:175], s[24:25], 0, v[142:143]
	v_lshl_add_u64 v[174:175], v[146:147], 1, v[174:175]
	v_add_co_u32_e32 v174, vcc, 0xfffff000, v174
	s_nop 1
	v_addc_co_u32_e32 v175, vcc, -1, v175, vcc
	global_store_dwordx2 v[174:175], v[152:153], off offset:-2048 sc1

.LBB0_523:
	s_andn2_saveexec_b64 s[30:31], s[30:31]
	s_cbranch_execz .LBB0_525
	v_pk_mul_f32 v[152:153], v[78:79], s[26:27] op_sel_hi:[1,0]
	v_pk_mul_f32 v[174:175], v[80:81], s[26:27] op_sel_hi:[1,0]
	v_cvt_pk_bf16_f32 v152, v152, v153
	v_cvt_pk_bf16_f32 v153, v174, v175
	v_lshl_add_u64 v[174:175], s[20:21], 0, v[142:143]
	v_lshl_add_u64 v[174:175], v[146:147], 1, v[174:175]
	global_store_dwordx2 v[174:175], v[152:153], off offset:-2048 sc1

.LBB0_526:
	s_or_saveexec_b64 s[2:3], s[2:3]
	v_ashrrev_i32_e32 v131, 4, v144
	v_lshrrev_b32_e32 v133, 4, v144
	v_bfi_b32 v135, s40, v131, v133
	s_xor_b64 exec, exec, s[2:3]
	s_cbranch_execz .LBB0_669
	v_add_u32_e32 v152, v135, v169
	v_ashrrev_i32_e32 v153, 31, v152
	v_lshlrev_b64 v[152:153], 10, v[152:153]
	v_lshl_add_u64 v[152:153], s[18:19], 0, v[152:153]
	v_mov_b32_e32 v131, v147
	v_lshl_add_u64 v[152:153], v[152:153], 0, v[130:131]
	v_mov_b32_e32 v133, v147
	v_cvt_pk_bf16_f32 v144, v78, v79
	v_cvt_pk_bf16_f32 v145, v80, v81
	v_lshl_add_u64 v[152:153], v[152:153], 0, v[132:133]
	global_store_dwordx2 v[152:153], v[144:145], off sc1
	s_or_b64 exec, exec, s[2:3]
	s_and_saveexec_b64 s[2:3], s[8:9]
	s_xor_b64 s[2:3], exec, s[2:3]
	s_cbranch_execnz .LBB0_670

.LBB0_529:
	v_add_u32_e32 v152, v173, v135
	v_ashrrev_i32_e32 v153, 31, v152
	v_lshlrev_b64 v[152:153], 10, v[152:153]
	v_lshl_add_u64 v[152:153], s[18:19], 0, v[152:153]
	v_mov_b32_e32 v131, v147
	v_lshl_add_u64 v[152:153], v[152:153], 0, v[130:131]
	v_mov_b32_e32 v133, v147
	v_cvt_pk_bf16_f32 v144, v74, v75
	v_cvt_pk_bf16_f32 v145, v76, v77
	v_lshl_add_u64 v[152:153], v[152:153], 0, v[132:133]
	global_store_dwordx2 v[152:153], v[144:145], off sc1
	s_or_b64 exec, exec, s[2:3]
	s_and_saveexec_b64 s[2:3], s[6:7]
	s_xor_b64 s[2:3], exec, s[2:3]
	s_cbranch_execnz .LBB0_680

.LBB0_531:
	v_add_u32_e32 v152, v172, v135
	v_ashrrev_i32_e32 v153, 31, v152
	v_lshlrev_b64 v[152:153], 10, v[152:153]
	v_lshl_add_u64 v[152:153], s[18:19], 0, v[152:153]
	v_mov_b32_e32 v131, v147
	v_lshl_add_u64 v[152:153], v[152:153], 0, v[130:131]
	v_mov_b32_e32 v133, v147
	v_cvt_pk_bf16_f32 v144, v70, v71
	v_cvt_pk_bf16_f32 v145, v72, v73
	v_lshl_add_u64 v[152:153], v[152:153], 0, v[132:133]
	global_store_dwordx2 v[152:153], v[144:145], off sc1
	s_or_b64 exec, exec, s[2:3]
	s_and_saveexec_b64 s[2:3], s[0:1]
	s_xor_b64 s[2:3], exec, s[2:3]
	s_cbranch_execnz .LBB0_690

.LBB0_533:
	v_add_u32_e32 v144, v171, v135
	v_ashrrev_i32_e32 v145, 31, v144
	v_lshlrev_b64 v[144:145], 10, v[144:145]
	v_lshl_add_u64 v[144:145], s[18:19], 0, v[144:145]
	v_mov_b32_e32 v131, v147
	v_lshl_add_u64 v[144:145], v[144:145], 0, v[130:131]
	v_mov_b32_e32 v133, v147
	v_cvt_pk_bf16_f32 v142, v66, v67
	v_cvt_pk_bf16_f32 v143, v68, v69
	v_lshl_add_u64 v[144:145], v[144:145], 0, v[132:133]
	global_store_dwordx2 v[144:145], v[142:143], off sc1
.LBB0_534:
	s_or_b64 exec, exec, s[2:3]
	v_add_u32_e32 v144, 64, v140
	v_ashrrev_i32_e32 v145, 31, v144
	v_lshlrev_b64 v[142:143], 11, v[144:145]
	s_and_saveexec_b64 s[2:3], s[4:5]
	s_xor_b64 s[2:3], exec, s[2:3]
	s_cbranch_execz .LBB0_544
	v_cmp_lt_u32_e32 vcc, s41, v146
	s_and_saveexec_b64 s[30:31], vcc
	s_xor_b64 s[30:31], exec, s[30:31]
	s_cbranch_execz .LBB0_541
	v_cmp_lt_u32_e32 vcc, s42, v146
	v_cvt_pk_bf16_f32 v152, v62, v63
	v_cvt_pk_bf16_f32 v153, v64, v65
	s_and_saveexec_b64 s[34:35], vcc
	s_xor_b64 s[34:35], exec, s[34:35]
	s_cbranch_execz .LBB0_538
	v_lshl_add_u64 v[174:175], s[24:25], 0, v[142:143]
	v_lshl_add_u64 v[174:175], v[146:147], 1, v[174:175]
	v_add_co_u32_e32 v174, vcc, 0xfffff000, v174
	s_nop 1
	v_addc_co_u32_e32 v175, vcc, -1, v175, vcc
	global_store_dwordx2 v[174:175], v[152:153], off offset:-2048 sc1

.LBB0_541:
	s_andn2_saveexec_b64 s[30:31], s[30:31]
	s_cbranch_execz .LBB0_543
	v_pk_mul_f32 v[152:153], v[62:63], s[26:27] op_sel_hi:[1,0]
	v_pk_mul_f32 v[174:175], v[64:65], s[26:27] op_sel_hi:[1,0]
	v_cvt_pk_bf16_f32 v152, v152, v153
	v_cvt_pk_bf16_f32 v153, v174, v175
	v_lshl_add_u64 v[174:175], s[20:21], 0, v[142:143]
	v_lshl_add_u64 v[174:175], v[146:147], 1, v[174:175]
	global_store_dwordx2 v[174:175], v[152:153], off offset:-2048 sc1

.LBB0_544:
	s_or_saveexec_b64 s[2:3], s[2:3]
	v_ashrrev_i32_e32 v131, 4, v144
	v_lshrrev_b32_e32 v133, 4, v144
	v_bfi_b32 v135, s40, v131, v133
	s_xor_b64 exec, exec, s[2:3]
	s_cbranch_execz .LBB0_699
	v_add_u32_e32 v152, v135, v169
	v_ashrrev_i32_e32 v153, 31, v152
	v_lshlrev_b64 v[152:153], 10, v[152:153]
	v_lshl_add_u64 v[152:153], s[18:19], 0, v[152:153]
	v_mov_b32_e32 v131, v147
	v_lshl_add_u64 v[152:153], v[152:153], 0, v[130:131]
	v_mov_b32_e32 v133, v147
	v_cvt_pk_bf16_f32 v144, v62, v63
	v_cvt_pk_bf16_f32 v145, v64, v65
	v_lshl_add_u64 v[152:153], v[152:153], 0, v[132:133]
	global_store_dwordx2 v[152:153], v[144:145], off sc1
	s_or_b64 exec, exec, s[2:3]
	s_and_saveexec_b64 s[2:3], s[8:9]
	s_xor_b64 s[2:3], exec, s[2:3]
	s_cbranch_execnz .LBB0_700

.LBB0_547:
	v_add_u32_e32 v152, v173, v135
	v_ashrrev_i32_e32 v153, 31, v152
	v_lshlrev_b64 v[152:153], 10, v[152:153]
	v_lshl_add_u64 v[152:153], s[18:19], 0, v[152:153]
	v_mov_b32_e32 v131, v147
	v_lshl_add_u64 v[152:153], v[152:153], 0, v[130:131]
	v_mov_b32_e32 v133, v147
	v_cvt_pk_bf16_f32 v144, v58, v59
	v_cvt_pk_bf16_f32 v145, v60, v61
	v_lshl_add_u64 v[152:153], v[152:153], 0, v[132:133]
	global_store_dwordx2 v[152:153], v[144:145], off sc1
	s_or_b64 exec, exec, s[2:3]
	s_and_saveexec_b64 s[2:3], s[6:7]
	s_xor_b64 s[2:3], exec, s[2:3]
	s_cbranch_execnz .LBB0_710

.LBB0_549:
	v_add_u32_e32 v152, v172, v135
	v_ashrrev_i32_e32 v153, 31, v152
	v_lshlrev_b64 v[152:153], 10, v[152:153]
	v_lshl_add_u64 v[152:153], s[18:19], 0, v[152:153]
	v_mov_b32_e32 v131, v147
	v_lshl_add_u64 v[152:153], v[152:153], 0, v[130:131]
	v_mov_b32_e32 v133, v147
	v_cvt_pk_bf16_f32 v144, v54, v55
	v_cvt_pk_bf16_f32 v145, v56, v57
	v_lshl_add_u64 v[152:153], v[152:153], 0, v[132:133]
	global_store_dwordx2 v[152:153], v[144:145], off sc1
	s_or_b64 exec, exec, s[2:3]
	s_and_saveexec_b64 s[2:3], s[0:1]
	s_xor_b64 s[2:3], exec, s[2:3]
	s_cbranch_execnz .LBB0_720

.LBB0_551:
	v_add_u32_e32 v144, v171, v135
	v_ashrrev_i32_e32 v145, 31, v144
	v_lshlrev_b64 v[144:145], 10, v[144:145]
	v_lshl_add_u64 v[144:145], s[18:19], 0, v[144:145]
	v_mov_b32_e32 v131, v147
	v_lshl_add_u64 v[144:145], v[144:145], 0, v[130:131]
	v_mov_b32_e32 v133, v147
	v_cvt_pk_bf16_f32 v142, v50, v51
	v_cvt_pk_bf16_f32 v143, v52, v53
	v_lshl_add_u64 v[144:145], v[144:145], 0, v[132:133]
	global_store_dwordx2 v[144:145], v[142:143], off sc1
.LBB0_552:
	s_or_b64 exec, exec, s[2:3]
	v_add_u32_e32 v144, 0x50, v140
	v_ashrrev_i32_e32 v145, 31, v144
	v_lshlrev_b64 v[142:143], 11, v[144:145]
	s_and_saveexec_b64 s[2:3], s[4:5]
	s_xor_b64 s[2:3], exec, s[2:3]
	s_cbranch_execz .LBB0_562
	v_cmp_lt_u32_e32 vcc, s41, v146
	s_and_saveexec_b64 s[30:31], vcc
	s_xor_b64 s[30:31], exec, s[30:31]
	s_cbranch_execz .LBB0_559
	v_cmp_lt_u32_e32 vcc, s42, v146
	v_cvt_pk_bf16_f32 v152, v46, v47
	v_cvt_pk_bf16_f32 v153, v48, v49
	s_and_saveexec_b64 s[34:35], vcc
	s_xor_b64 s[34:35], exec, s[34:35]
	s_cbranch_execz .LBB0_556
	v_lshl_add_u64 v[174:175], s[24:25], 0, v[142:143]
	v_lshl_add_u64 v[174:175], v[146:147], 1, v[174:175]
	v_add_co_u32_e32 v174, vcc, 0xfffff000, v174
	s_nop 1
	v_addc_co_u32_e32 v175, vcc, -1, v175, vcc
	global_store_dwordx2 v[174:175], v[152:153], off offset:-2048 sc1

.LBB0_559:
	s_andn2_saveexec_b64 s[30:31], s[30:31]
	s_cbranch_execz .LBB0_561
	v_pk_mul_f32 v[152:153], v[46:47], s[26:27] op_sel_hi:[1,0]
	v_pk_mul_f32 v[174:175], v[48:49], s[26:27] op_sel_hi:[1,0]
	v_cvt_pk_bf16_f32 v152, v152, v153
	v_cvt_pk_bf16_f32 v153, v174, v175
	v_lshl_add_u64 v[174:175], s[20:21], 0, v[142:143]
	v_lshl_add_u64 v[174:175], v[146:147], 1, v[174:175]
	global_store_dwordx2 v[174:175], v[152:153], off offset:-2048 sc1

.LBB0_562:
	s_or_saveexec_b64 s[2:3], s[2:3]
	v_ashrrev_i32_e32 v131, 4, v144
	v_lshrrev_b32_e32 v133, 4, v144
	v_bfi_b32 v135, s40, v131, v133
	s_xor_b64 exec, exec, s[2:3]
	s_cbranch_execz .LBB0_729
	v_add_u32_e32 v152, v135, v169
	v_ashrrev_i32_e32 v153, 31, v152
	v_lshlrev_b64 v[152:153], 10, v[152:153]
	v_lshl_add_u64 v[152:153], s[18:19], 0, v[152:153]
	v_mov_b32_e32 v131, v147
	v_lshl_add_u64 v[152:153], v[152:153], 0, v[130:131]
	v_mov_b32_e32 v133, v147
	v_cvt_pk_bf16_f32 v144, v46, v47
	v_cvt_pk_bf16_f32 v145, v48, v49
	v_lshl_add_u64 v[152:153], v[152:153], 0, v[132:133]
	global_store_dwordx2 v[152:153], v[144:145], off sc1
	s_or_b64 exec, exec, s[2:3]
	s_and_saveexec_b64 s[2:3], s[8:9]
	s_xor_b64 s[2:3], exec, s[2:3]
	s_cbranch_execnz .LBB0_730

.LBB0_565:
	v_add_u32_e32 v152, v173, v135
	v_ashrrev_i32_e32 v153, 31, v152
	v_lshlrev_b64 v[152:153], 10, v[152:153]
	v_lshl_add_u64 v[152:153], s[18:19], 0, v[152:153]
	v_mov_b32_e32 v131, v147
	v_lshl_add_u64 v[152:153], v[152:153], 0, v[130:131]
	v_mov_b32_e32 v133, v147
	v_cvt_pk_bf16_f32 v144, v42, v43
	v_cvt_pk_bf16_f32 v145, v44, v45
	v_lshl_add_u64 v[152:153], v[152:153], 0, v[132:133]
	global_store_dwordx2 v[152:153], v[144:145], off sc1
	s_or_b64 exec, exec, s[2:3]
	s_and_saveexec_b64 s[2:3], s[6:7]
	s_xor_b64 s[2:3], exec, s[2:3]
	s_cbranch_execnz .LBB0_740

.LBB0_567:
	v_add_u32_e32 v152, v172, v135
	v_ashrrev_i32_e32 v153, 31, v152
	v_lshlrev_b64 v[152:153], 10, v[152:153]
	v_lshl_add_u64 v[152:153], s[18:19], 0, v[152:153]
	v_mov_b32_e32 v131, v147
	v_lshl_add_u64 v[152:153], v[152:153], 0, v[130:131]
	v_mov_b32_e32 v133, v147
	v_cvt_pk_bf16_f32 v144, v38, v39
	v_cvt_pk_bf16_f32 v145, v40, v41
	v_lshl_add_u64 v[152:153], v[152:153], 0, v[132:133]
	global_store_dwordx2 v[152:153], v[144:145], off sc1
	s_or_b64 exec, exec, s[2:3]
	s_and_saveexec_b64 s[2:3], s[0:1]
	s_xor_b64 s[2:3], exec, s[2:3]
	s_cbranch_execnz .LBB0_750

.LBB0_569:
	v_add_u32_e32 v144, v171, v135
	v_ashrrev_i32_e32 v145, 31, v144
	v_lshlrev_b64 v[144:145], 10, v[144:145]
	v_lshl_add_u64 v[144:145], s[18:19], 0, v[144:145]
	v_mov_b32_e32 v131, v147
	v_lshl_add_u64 v[144:145], v[144:145], 0, v[130:131]
	v_mov_b32_e32 v133, v147
	v_cvt_pk_bf16_f32 v142, v34, v35
	v_cvt_pk_bf16_f32 v143, v36, v37
	v_lshl_add_u64 v[144:145], v[144:145], 0, v[132:133]
	global_store_dwordx2 v[144:145], v[142:143], off sc1
.LBB0_570:
	s_or_b64 exec, exec, s[2:3]
	v_add_u32_e32 v144, 0x60, v140
	v_ashrrev_i32_e32 v145, 31, v144
	v_lshlrev_b64 v[142:143], 11, v[144:145]
	s_and_saveexec_b64 s[2:3], s[4:5]
	s_xor_b64 s[2:3], exec, s[2:3]
	s_cbranch_execz .LBB0_580
	v_cmp_lt_u32_e32 vcc, s41, v146
	s_and_saveexec_b64 s[30:31], vcc
	s_xor_b64 s[30:31], exec, s[30:31]
	s_cbranch_execz .LBB0_577
	v_cmp_lt_u32_e32 vcc, s42, v146
	v_cvt_pk_bf16_f32 v152, v30, v31
	v_cvt_pk_bf16_f32 v153, v32, v33
	s_and_saveexec_b64 s[34:35], vcc
	s_xor_b64 s[34:35], exec, s[34:35]
	s_cbranch_execz .LBB0_574
	v_lshl_add_u64 v[174:175], s[24:25], 0, v[142:143]
	v_lshl_add_u64 v[174:175], v[146:147], 1, v[174:175]
	v_add_co_u32_e32 v174, vcc, 0xfffff000, v174
	s_nop 1
	v_addc_co_u32_e32 v175, vcc, -1, v175, vcc
	global_store_dwordx2 v[174:175], v[152:153], off offset:-2048 sc1

.LBB0_577:
	s_andn2_saveexec_b64 s[30:31], s[30:31]
	s_cbranch_execz .LBB0_579
	v_pk_mul_f32 v[152:153], v[30:31], s[26:27] op_sel_hi:[1,0]
	v_pk_mul_f32 v[174:175], v[32:33], s[26:27] op_sel_hi:[1,0]
	v_cvt_pk_bf16_f32 v152, v152, v153
	v_cvt_pk_bf16_f32 v153, v174, v175
	v_lshl_add_u64 v[174:175], s[20:21], 0, v[142:143]
	v_lshl_add_u64 v[174:175], v[146:147], 1, v[174:175]
	global_store_dwordx2 v[174:175], v[152:153], off offset:-2048 sc1

.LBB0_580:
	s_or_saveexec_b64 s[2:3], s[2:3]
	v_ashrrev_i32_e32 v131, 4, v144
	v_lshrrev_b32_e32 v133, 4, v144
	v_bfi_b32 v135, s40, v131, v133
	s_xor_b64 exec, exec, s[2:3]
	s_cbranch_execz .LBB0_759
	v_add_u32_e32 v152, v135, v169
	v_ashrrev_i32_e32 v153, 31, v152
	v_lshlrev_b64 v[152:153], 10, v[152:153]
	v_lshl_add_u64 v[152:153], s[18:19], 0, v[152:153]
	v_mov_b32_e32 v131, v147
	v_lshl_add_u64 v[152:153], v[152:153], 0, v[130:131]
	v_mov_b32_e32 v133, v147
	v_cvt_pk_bf16_f32 v144, v30, v31
	v_cvt_pk_bf16_f32 v145, v32, v33
	v_lshl_add_u64 v[152:153], v[152:153], 0, v[132:133]
	global_store_dwordx2 v[152:153], v[144:145], off sc1
	s_or_b64 exec, exec, s[2:3]
	s_and_saveexec_b64 s[2:3], s[8:9]
	s_xor_b64 s[2:3], exec, s[2:3]
	s_cbranch_execnz .LBB0_760

.LBB0_583:
	v_add_u32_e32 v152, v173, v135
	v_ashrrev_i32_e32 v153, 31, v152
	v_lshlrev_b64 v[152:153], 10, v[152:153]
	v_lshl_add_u64 v[152:153], s[18:19], 0, v[152:153]
	v_mov_b32_e32 v131, v147
	v_lshl_add_u64 v[152:153], v[152:153], 0, v[130:131]
	v_mov_b32_e32 v133, v147
	v_cvt_pk_bf16_f32 v144, v26, v27
	v_cvt_pk_bf16_f32 v145, v28, v29
	v_lshl_add_u64 v[152:153], v[152:153], 0, v[132:133]
	global_store_dwordx2 v[152:153], v[144:145], off sc1
	s_or_b64 exec, exec, s[2:3]
	s_and_saveexec_b64 s[2:3], s[6:7]
	s_xor_b64 s[2:3], exec, s[2:3]
	s_cbranch_execnz .LBB0_770

.LBB0_585:
	v_add_u32_e32 v152, v172, v135
	v_ashrrev_i32_e32 v153, 31, v152
	v_lshlrev_b64 v[152:153], 10, v[152:153]
	v_lshl_add_u64 v[152:153], s[18:19], 0, v[152:153]
	v_mov_b32_e32 v131, v147
	v_lshl_add_u64 v[152:153], v[152:153], 0, v[130:131]
	v_mov_b32_e32 v133, v147
	v_cvt_pk_bf16_f32 v144, v22, v23
	v_cvt_pk_bf16_f32 v145, v24, v25
	v_lshl_add_u64 v[152:153], v[152:153], 0, v[132:133]
	global_store_dwordx2 v[152:153], v[144:145], off sc1
	s_or_b64 exec, exec, s[2:3]
	s_and_saveexec_b64 s[2:3], s[0:1]
	s_xor_b64 s[2:3], exec, s[2:3]
	s_cbranch_execnz .LBB0_780

.LBB0_587:
	v_add_u32_e32 v144, v171, v135
	v_ashrrev_i32_e32 v145, 31, v144
	v_lshlrev_b64 v[144:145], 10, v[144:145]
	v_lshl_add_u64 v[144:145], s[18:19], 0, v[144:145]
	v_mov_b32_e32 v131, v147
	v_lshl_add_u64 v[144:145], v[144:145], 0, v[130:131]
	v_mov_b32_e32 v133, v147
	v_cvt_pk_bf16_f32 v142, v18, v19
	v_cvt_pk_bf16_f32 v143, v20, v21
	v_lshl_add_u64 v[144:145], v[144:145], 0, v[132:133]
	global_store_dwordx2 v[144:145], v[142:143], off sc1
.LBB0_588:
	s_or_b64 exec, exec, s[2:3]
	v_add_u32_e32 v142, 0x70, v140
	v_ashrrev_i32_e32 v143, 31, v142
	v_lshlrev_b64 v[140:141], 11, v[142:143]
	s_and_saveexec_b64 s[2:3], s[4:5]
	s_xor_b64 s[2:3], exec, s[2:3]
	s_cbranch_execz .LBB0_598
	v_cmp_lt_u32_e32 vcc, s41, v146
	s_and_saveexec_b64 s[4:5], vcc
	s_xor_b64 s[4:5], exec, s[4:5]
	s_cbranch_execz .LBB0_595
	v_cmp_lt_u32_e32 vcc, s42, v146
	v_cvt_pk_bf16_f32 v144, v14, v15
	v_cvt_pk_bf16_f32 v145, v16, v17
	s_and_saveexec_b64 s[30:31], vcc
	s_xor_b64 s[30:31], exec, s[30:31]
	s_cbranch_execz .LBB0_592
	v_lshl_add_u64 v[152:153], s[24:25], 0, v[140:141]
	v_lshl_add_u64 v[152:153], v[146:147], 1, v[152:153]
	v_add_co_u32_e32 v152, vcc, 0xfffff000, v152
	s_nop 1
	v_addc_co_u32_e32 v153, vcc, -1, v153, vcc
	global_store_dwordx2 v[152:153], v[144:145], off offset:-2048 sc1
.LBB0_592:
	s_andn2_saveexec_b64 s[30:31], s[30:31]
	s_cbranch_execz .LBB0_594
	v_lshl_add_u64 v[152:153], s[22:23], 0, v[140:141]
	v_lshl_add_u64 v[152:153], v[146:147], 1, v[152:153]
	global_store_dwordx2 v[152:153], v[144:145], off offset:-4096 sc1

.LBB0_595:
	s_andn2_saveexec_b64 s[4:5], s[4:5]
	s_cbranch_execz .LBB0_597
	v_pk_mul_f32 v[144:145], v[14:15], s[26:27] op_sel_hi:[1,0]
	v_pk_mul_f32 v[152:153], v[16:17], s[26:27] op_sel_hi:[1,0]
	v_cvt_pk_bf16_f32 v144, v144, v145
	v_cvt_pk_bf16_f32 v145, v152, v153
	v_lshl_add_u64 v[152:153], s[20:21], 0, v[140:141]
	v_lshl_add_u64 v[152:153], v[146:147], 1, v[152:153]
	global_store_dwordx2 v[152:153], v[144:145], off offset:-2048 sc1

.LBB0_598:
	s_or_saveexec_b64 s[2:3], s[2:3]
	v_ashrrev_i32_e32 v131, 4, v142
	v_lshrrev_b32_e32 v133, 4, v142
	v_bfi_b32 v135, s40, v131, v133
	s_xor_b64 exec, exec, s[2:3]
	s_cbranch_execz .LBB0_789
	v_add_u32_e32 v144, v135, v169
	v_ashrrev_i32_e32 v145, 31, v144
	v_lshlrev_b64 v[144:145], 10, v[144:145]
	v_lshl_add_u64 v[144:145], s[18:19], 0, v[144:145]
	v_mov_b32_e32 v131, v147
	v_lshl_add_u64 v[144:145], v[144:145], 0, v[130:131]
	v_mov_b32_e32 v133, v147
	v_cvt_pk_bf16_f32 v142, v14, v15
	v_cvt_pk_bf16_f32 v143, v16, v17
	v_lshl_add_u64 v[144:145], v[144:145], 0, v[132:133]
	global_store_dwordx2 v[144:145], v[142:143], off sc1
	s_or_b64 exec, exec, s[2:3]
	s_and_saveexec_b64 s[2:3], s[8:9]
	s_xor_b64 s[2:3], exec, s[2:3]
	s_cbranch_execnz .LBB0_790

.LBB0_601:
	v_add_u32_e32 v142, v173, v135
	v_ashrrev_i32_e32 v143, 31, v142
	v_lshlrev_b64 v[142:143], 10, v[142:143]
	v_lshl_add_u64 v[142:143], s[18:19], 0, v[142:143]
	v_mov_b32_e32 v131, v147
	v_lshl_add_u64 v[142:143], v[142:143], 0, v[130:131]
	v_mov_b32_e32 v133, v147
	v_cvt_pk_bf16_f32 v138, v10, v11
	v_cvt_pk_bf16_f32 v139, v12, v13
	v_lshl_add_u64 v[142:143], v[142:143], 0, v[132:133]
	global_store_dwordx2 v[142:143], v[138:139], off sc1
	s_or_b64 exec, exec, s[2:3]
	s_and_saveexec_b64 s[2:3], s[6:7]
	s_xor_b64 s[2:3], exec, s[2:3]
	s_cbranch_execnz .LBB0_800

.LBB0_603:
	v_add_u32_e32 v138, v172, v135
	v_ashrrev_i32_e32 v139, 31, v138
	v_lshlrev_b64 v[138:139], 10, v[138:139]
	v_lshl_add_u64 v[138:139], s[18:19], 0, v[138:139]
	v_mov_b32_e32 v131, v147
	v_lshl_add_u64 v[138:139], v[138:139], 0, v[130:131]
	v_mov_b32_e32 v133, v147
	v_cvt_pk_bf16_f32 v136, v6, v7
	v_cvt_pk_bf16_f32 v137, v8, v9
	v_lshl_add_u64 v[138:139], v[138:139], 0, v[132:133]
	global_store_dwordx2 v[138:139], v[136:137], off sc1
	s_or_b64 exec, exec, s[2:3]
	s_and_saveexec_b64 s[2:3], s[0:1]
	s_xor_b64 s[0:1], exec, s[2:3]
	s_cbranch_execnz .LBB0_810

.LBB0_605:
	v_add_u32_e32 v134, v171, v135
	v_ashrrev_i32_e32 v135, 31, v134
	v_lshlrev_b64 v[134:135], 10, v[134:135]
	v_lshl_add_u64 v[134:135], s[18:19], 0, v[134:135]
	v_mov_b32_e32 v131, v147
	v_lshl_add_u64 v[130:131], v[134:135], 0, v[130:131]
	v_mov_b32_e32 v133, v147
	v_cvt_pk_bf16_f32 v136, v2, v3
	v_cvt_pk_bf16_f32 v137, v4, v5
	v_lshl_add_u64 v[130:131], v[130:131], 0, v[132:133]
	global_store_dwordx2 v[130:131], v[136:137], off sc1

.LBB0_610:
	v_cmp_lt_u32_e32 vcc, s41, v138
	s_and_saveexec_b64 s[30:31], vcc
	s_xor_b64 s[30:31], exec, s[30:31]
	s_cbranch_execz .LBB0_616
	v_cmp_lt_u32_e32 vcc, s42, v138
	v_cvt_pk_bf16_f32 v144, v106, v107
	v_cvt_pk_bf16_f32 v145, v108, v109
	v_mov_b32_e32 v139, v147
	s_and_saveexec_b64 s[34:35], vcc
	s_xor_b64 s[34:35], exec, s[34:35]
	s_cbranch_execz .LBB0_613
	v_lshl_add_u64 v[152:153], s[24:25], 0, v[142:143]
	v_lshl_add_u64 v[152:153], v[138:139], 1, v[152:153]
	v_add_co_u32_e32 v152, vcc, 0xfffff000, v152
	s_nop 1
	v_addc_co_u32_e32 v153, vcc, -1, v153, vcc
	global_store_dwordx2 v[152:153], v[144:145], off offset:-2048 sc1
.LBB0_613:
	s_andn2_saveexec_b64 s[34:35], s[34:35]
	s_cbranch_execz .LBB0_615
	v_lshl_add_u64 v[152:153], s[22:23], 0, v[142:143]
	v_lshl_add_u64 v[152:153], v[138:139], 1, v[152:153]
	global_store_dwordx2 v[152:153], v[144:145], off offset:-4096 sc1

.LBB0_616:
	s_andn2_saveexec_b64 s[30:31], s[30:31]
	s_cbranch_execz .LBB0_618
	v_pk_mul_f32 v[144:145], v[106:107], s[26:27] op_sel_hi:[1,0]
	v_pk_mul_f32 v[152:153], v[108:109], s[26:27] op_sel_hi:[1,0]
	v_cvt_pk_bf16_f32 v144, v144, v145
	v_cvt_pk_bf16_f32 v145, v152, v153
	v_lshl_add_u64 v[152:153], s[20:21], 0, v[142:143]
	v_mov_b32_e32 v139, v147
	v_lshl_add_u64 v[152:153], v[138:139], 1, v[152:153]
	global_store_dwordx2 v[152:153], v[144:145], off offset:-2048 sc1

.LBB0_620:
	v_cmp_lt_u32_e32 vcc, s41, v136
	s_and_saveexec_b64 s[30:31], vcc
	s_xor_b64 s[30:31], exec, s[30:31]
	s_cbranch_execz .LBB0_626
	v_cmp_lt_u32_e32 vcc, s42, v136
	v_cvt_pk_bf16_f32 v144, v102, v103
	v_cvt_pk_bf16_f32 v145, v104, v105
	v_mov_b32_e32 v137, v147
	s_and_saveexec_b64 s[34:35], vcc
	s_xor_b64 s[34:35], exec, s[34:35]
	s_cbranch_execz .LBB0_623
	v_lshl_add_u64 v[152:153], s[24:25], 0, v[142:143]
	v_lshl_add_u64 v[152:153], v[136:137], 1, v[152:153]
	v_add_co_u32_e32 v152, vcc, 0xfffff000, v152
	s_nop 1
	v_addc_co_u32_e32 v153, vcc, -1, v153, vcc
	global_store_dwordx2 v[152:153], v[144:145], off offset:-2048 sc1
.LBB0_623:
	s_andn2_saveexec_b64 s[34:35], s[34:35]
	s_cbranch_execz .LBB0_625
	v_lshl_add_u64 v[152:153], s[22:23], 0, v[142:143]
	v_lshl_add_u64 v[152:153], v[136:137], 1, v[152:153]
	global_store_dwordx2 v[152:153], v[144:145], off offset:-4096 sc1

.LBB0_626:
	s_andn2_saveexec_b64 s[30:31], s[30:31]
	s_cbranch_execz .LBB0_628
	v_pk_mul_f32 v[144:145], v[102:103], s[26:27] op_sel_hi:[1,0]
	v_pk_mul_f32 v[152:153], v[104:105], s[26:27] op_sel_hi:[1,0]
	v_cvt_pk_bf16_f32 v144, v144, v145
	v_cvt_pk_bf16_f32 v145, v152, v153
	v_lshl_add_u64 v[152:153], s[20:21], 0, v[142:143]
	v_mov_b32_e32 v137, v147
	v_lshl_add_u64 v[152:153], v[136:137], 1, v[152:153]
	global_store_dwordx2 v[152:153], v[144:145], off offset:-2048 sc1

.LBB0_630:
	v_cmp_lt_u32_e32 vcc, s41, v134
	s_and_saveexec_b64 s[30:31], vcc
	s_xor_b64 s[30:31], exec, s[30:31]
	s_cbranch_execz .LBB0_636
	v_cmp_lt_u32_e32 vcc, s42, v134
	v_cvt_pk_bf16_f32 v144, v98, v99
	v_cvt_pk_bf16_f32 v145, v100, v101
	v_mov_b32_e32 v135, v147
	s_and_saveexec_b64 s[34:35], vcc
	s_xor_b64 s[34:35], exec, s[34:35]
	s_cbranch_execz .LBB0_633
	v_lshl_add_u64 v[142:143], s[24:25], 0, v[142:143]
	v_lshl_add_u64 v[142:143], v[134:135], 1, v[142:143]
	v_add_co_u32_e32 v142, vcc, 0xfffff000, v142
	s_nop 1
	v_addc_co_u32_e32 v143, vcc, -1, v143, vcc
	global_store_dwordx2 v[142:143], v[144:145], off offset:-2048 sc1

.LBB0_636:
	s_andn2_saveexec_b64 s[30:31], s[30:31]
	s_cbranch_execz .LBB0_638
	v_pk_mul_f32 v[144:145], v[98:99], s[26:27] op_sel_hi:[1,0]
	v_pk_mul_f32 v[152:153], v[100:101], s[26:27] op_sel_hi:[1,0]
	v_lshl_add_u64 v[142:143], s[20:21], 0, v[142:143]
	v_mov_b32_e32 v135, v147
	v_cvt_pk_bf16_f32 v144, v144, v145
	v_cvt_pk_bf16_f32 v145, v152, v153
	v_lshl_add_u64 v[142:143], v[134:135], 1, v[142:143]
	global_store_dwordx2 v[142:143], v[144:145], off offset:-2048 sc1

.LBB0_640:
	v_cmp_lt_u32_e32 vcc, s41, v138
	s_and_saveexec_b64 s[30:31], vcc
	s_xor_b64 s[30:31], exec, s[30:31]
	s_cbranch_execz .LBB0_646
	v_cmp_lt_u32_e32 vcc, s42, v138
	v_cvt_pk_bf16_f32 v144, v90, v91
	v_cvt_pk_bf16_f32 v145, v92, v93
	v_mov_b32_e32 v139, v147
	s_and_saveexec_b64 s[34:35], vcc
	s_xor_b64 s[34:35], exec, s[34:35]
	s_cbranch_execz .LBB0_643
	v_lshl_add_u64 v[152:153], s[24:25], 0, v[142:143]
	v_lshl_add_u64 v[152:153], v[138:139], 1, v[152:153]
	v_add_co_u32_e32 v152, vcc, 0xfffff000, v152
	s_nop 1
	v_addc_co_u32_e32 v153, vcc, -1, v153, vcc
	global_store_dwordx2 v[152:153], v[144:145], off offset:-2048 sc1

.LBB0_646:
	s_andn2_saveexec_b64 s[30:31], s[30:31]
	s_cbranch_execz .LBB0_648
	v_pk_mul_f32 v[144:145], v[90:91], s[26:27] op_sel_hi:[1,0]
	v_pk_mul_f32 v[152:153], v[92:93], s[26:27] op_sel_hi:[1,0]
	v_cvt_pk_bf16_f32 v144, v144, v145
	v_cvt_pk_bf16_f32 v145, v152, v153
	v_lshl_add_u64 v[152:153], s[20:21], 0, v[142:143]
	v_mov_b32_e32 v139, v147
	v_lshl_add_u64 v[152:153], v[138:139], 1, v[152:153]
	global_store_dwordx2 v[152:153], v[144:145], off offset:-2048 sc1

.LBB0_650:
	v_cmp_lt_u32_e32 vcc, s41, v136
	s_and_saveexec_b64 s[30:31], vcc
	s_xor_b64 s[30:31], exec, s[30:31]
	s_cbranch_execz .LBB0_656
	v_cmp_lt_u32_e32 vcc, s42, v136
	v_cvt_pk_bf16_f32 v144, v86, v87
	v_cvt_pk_bf16_f32 v145, v88, v89
	v_mov_b32_e32 v137, v147
	s_and_saveexec_b64 s[34:35], vcc
	s_xor_b64 s[34:35], exec, s[34:35]
	s_cbranch_execz .LBB0_653
	v_lshl_add_u64 v[152:153], s[24:25], 0, v[142:143]
	v_lshl_add_u64 v[152:153], v[136:137], 1, v[152:153]
	v_add_co_u32_e32 v152, vcc, 0xfffff000, v152
	s_nop 1
	v_addc_co_u32_e32 v153, vcc, -1, v153, vcc
	global_store_dwordx2 v[152:153], v[144:145], off offset:-2048 sc1

.LBB0_656:
	s_andn2_saveexec_b64 s[30:31], s[30:31]
	s_cbranch_execz .LBB0_658
	v_pk_mul_f32 v[144:145], v[86:87], s[26:27] op_sel_hi:[1,0]
	v_pk_mul_f32 v[152:153], v[88:89], s[26:27] op_sel_hi:[1,0]
	v_cvt_pk_bf16_f32 v144, v144, v145
	v_cvt_pk_bf16_f32 v145, v152, v153
	v_lshl_add_u64 v[152:153], s[20:21], 0, v[142:143]
	v_mov_b32_e32 v137, v147
	v_lshl_add_u64 v[152:153], v[136:137], 1, v[152:153]
	global_store_dwordx2 v[152:153], v[144:145], off offset:-2048 sc1

.LBB0_660:
	v_cmp_lt_u32_e32 vcc, s41, v134
	s_and_saveexec_b64 s[30:31], vcc
	s_xor_b64 s[30:31], exec, s[30:31]
	s_cbranch_execz .LBB0_666
	v_cmp_lt_u32_e32 vcc, s42, v134
	v_cvt_pk_bf16_f32 v144, v82, v83
	v_cvt_pk_bf16_f32 v145, v84, v85
	v_mov_b32_e32 v135, v147
	s_and_saveexec_b64 s[34:35], vcc
	s_xor_b64 s[34:35], exec, s[34:35]
	s_cbranch_execz .LBB0_663
	v_lshl_add_u64 v[142:143], s[24:25], 0, v[142:143]
	v_lshl_add_u64 v[142:143], v[134:135], 1, v[142:143]
	v_add_co_u32_e32 v142, vcc, 0xfffff000, v142
	s_nop 1
	v_addc_co_u32_e32 v143, vcc, -1, v143, vcc
	global_store_dwordx2 v[142:143], v[144:145], off offset:-2048 sc1

.LBB0_666:
	s_andn2_saveexec_b64 s[30:31], s[30:31]
	s_cbranch_execz .LBB0_668
	v_pk_mul_f32 v[144:145], v[82:83], s[26:27] op_sel_hi:[1,0]
	v_pk_mul_f32 v[152:153], v[84:85], s[26:27] op_sel_hi:[1,0]
	v_lshl_add_u64 v[142:143], s[20:21], 0, v[142:143]
	v_mov_b32_e32 v135, v147
	v_cvt_pk_bf16_f32 v144, v144, v145
	v_cvt_pk_bf16_f32 v145, v152, v153
	v_lshl_add_u64 v[142:143], v[134:135], 1, v[142:143]
	global_store_dwordx2 v[142:143], v[144:145], off offset:-2048 sc1

.LBB0_670:
	v_cmp_lt_u32_e32 vcc, s41, v138
	s_and_saveexec_b64 s[30:31], vcc
	s_xor_b64 s[30:31], exec, s[30:31]
	s_cbranch_execz .LBB0_676
	v_cmp_lt_u32_e32 vcc, s42, v138
	v_cvt_pk_bf16_f32 v144, v74, v75
	v_cvt_pk_bf16_f32 v145, v76, v77
	v_mov_b32_e32 v139, v147
	s_and_saveexec_b64 s[34:35], vcc
	s_xor_b64 s[34:35], exec, s[34:35]
	s_cbranch_execz .LBB0_673
	v_lshl_add_u64 v[152:153], s[24:25], 0, v[142:143]
	v_lshl_add_u64 v[152:153], v[138:139], 1, v[152:153]
	v_add_co_u32_e32 v152, vcc, 0xfffff000, v152
	s_nop 1
	v_addc_co_u32_e32 v153, vcc, -1, v153, vcc
	global_store_dwordx2 v[152:153], v[144:145], off offset:-2048 sc1

.LBB0_676:
	s_andn2_saveexec_b64 s[30:31], s[30:31]
	s_cbranch_execz .LBB0_678
	v_pk_mul_f32 v[144:145], v[74:75], s[26:27] op_sel_hi:[1,0]
	v_pk_mul_f32 v[152:153], v[76:77], s[26:27] op_sel_hi:[1,0]
	v_cvt_pk_bf16_f32 v144, v144, v145
	v_cvt_pk_bf16_f32 v145, v152, v153
	v_lshl_add_u64 v[152:153], s[20:21], 0, v[142:143]
	v_mov_b32_e32 v139, v147
	v_lshl_add_u64 v[152:153], v[138:139], 1, v[152:153]
	global_store_dwordx2 v[152:153], v[144:145], off offset:-2048 sc1

.LBB0_680:
	v_cmp_lt_u32_e32 vcc, s41, v136
	s_and_saveexec_b64 s[30:31], vcc
	s_xor_b64 s[30:31], exec, s[30:31]
	s_cbranch_execz .LBB0_686
	v_cmp_lt_u32_e32 vcc, s42, v136
	v_cvt_pk_bf16_f32 v144, v70, v71
	v_cvt_pk_bf16_f32 v145, v72, v73
	v_mov_b32_e32 v137, v147
	s_and_saveexec_b64 s[34:35], vcc
	s_xor_b64 s[34:35], exec, s[34:35]
	s_cbranch_execz .LBB0_683
	v_lshl_add_u64 v[152:153], s[24:25], 0, v[142:143]
	v_lshl_add_u64 v[152:153], v[136:137], 1, v[152:153]
	v_add_co_u32_e32 v152, vcc, 0xfffff000, v152
	s_nop 1
	v_addc_co_u32_e32 v153, vcc, -1, v153, vcc
	global_store_dwordx2 v[152:153], v[144:145], off offset:-2048 sc1

.LBB0_686:
	s_andn2_saveexec_b64 s[30:31], s[30:31]
	s_cbranch_execz .LBB0_688
	v_pk_mul_f32 v[144:145], v[70:71], s[26:27] op_sel_hi:[1,0]
	v_pk_mul_f32 v[152:153], v[72:73], s[26:27] op_sel_hi:[1,0]
	v_cvt_pk_bf16_f32 v144, v144, v145
	v_cvt_pk_bf16_f32 v145, v152, v153
	v_lshl_add_u64 v[152:153], s[20:21], 0, v[142:143]
	v_mov_b32_e32 v137, v147
	v_lshl_add_u64 v[152:153], v[136:137], 1, v[152:153]
	global_store_dwordx2 v[152:153], v[144:145], off offset:-2048 sc1

.LBB0_690:
	v_cmp_lt_u32_e32 vcc, s41, v134
	s_and_saveexec_b64 s[30:31], vcc
	s_xor_b64 s[30:31], exec, s[30:31]
	s_cbranch_execz .LBB0_696
	v_cmp_lt_u32_e32 vcc, s42, v134
	v_cvt_pk_bf16_f32 v144, v66, v67
	v_cvt_pk_bf16_f32 v145, v68, v69
	v_mov_b32_e32 v135, v147
	s_and_saveexec_b64 s[34:35], vcc
	s_xor_b64 s[34:35], exec, s[34:35]
	s_cbranch_execz .LBB0_693
	v_lshl_add_u64 v[142:143], s[24:25], 0, v[142:143]
	v_lshl_add_u64 v[142:143], v[134:135], 1, v[142:143]
	v_add_co_u32_e32 v142, vcc, 0xfffff000, v142
	s_nop 1
	v_addc_co_u32_e32 v143, vcc, -1, v143, vcc
	global_store_dwordx2 v[142:143], v[144:145], off offset:-2048 sc1

.LBB0_696:
	s_andn2_saveexec_b64 s[30:31], s[30:31]
	s_cbranch_execz .LBB0_698
	v_pk_mul_f32 v[144:145], v[66:67], s[26:27] op_sel_hi:[1,0]
	v_pk_mul_f32 v[152:153], v[68:69], s[26:27] op_sel_hi:[1,0]
	v_lshl_add_u64 v[142:143], s[20:21], 0, v[142:143]
	v_mov_b32_e32 v135, v147
	v_cvt_pk_bf16_f32 v144, v144, v145
	v_cvt_pk_bf16_f32 v145, v152, v153
	v_lshl_add_u64 v[142:143], v[134:135], 1, v[142:143]
	global_store_dwordx2 v[142:143], v[144:145], off offset:-2048 sc1

.LBB0_700:
	v_cmp_lt_u32_e32 vcc, s41, v138
	s_and_saveexec_b64 s[30:31], vcc
	s_xor_b64 s[30:31], exec, s[30:31]
	s_cbranch_execz .LBB0_706
	v_cmp_lt_u32_e32 vcc, s42, v138
	v_cvt_pk_bf16_f32 v144, v58, v59
	v_cvt_pk_bf16_f32 v145, v60, v61
	v_mov_b32_e32 v139, v147
	s_and_saveexec_b64 s[34:35], vcc
	s_xor_b64 s[34:35], exec, s[34:35]
	s_cbranch_execz .LBB0_703
	v_lshl_add_u64 v[152:153], s[24:25], 0, v[142:143]
	v_lshl_add_u64 v[152:153], v[138:139], 1, v[152:153]
	v_add_co_u32_e32 v152, vcc, 0xfffff000, v152
	s_nop 1
	v_addc_co_u32_e32 v153, vcc, -1, v153, vcc
	global_store_dwordx2 v[152:153], v[144:145], off offset:-2048 sc1

.LBB0_706:
	s_andn2_saveexec_b64 s[30:31], s[30:31]
	s_cbranch_execz .LBB0_708
	v_pk_mul_f32 v[144:145], v[58:59], s[26:27] op_sel_hi:[1,0]
	v_pk_mul_f32 v[152:153], v[60:61], s[26:27] op_sel_hi:[1,0]
	v_cvt_pk_bf16_f32 v144, v144, v145
	v_cvt_pk_bf16_f32 v145, v152, v153
	v_lshl_add_u64 v[152:153], s[20:21], 0, v[142:143]
	v_mov_b32_e32 v139, v147
	v_lshl_add_u64 v[152:153], v[138:139], 1, v[152:153]
	global_store_dwordx2 v[152:153], v[144:145], off offset:-2048 sc1

.LBB0_710:
	v_cmp_lt_u32_e32 vcc, s41, v136
	s_and_saveexec_b64 s[30:31], vcc
	s_xor_b64 s[30:31], exec, s[30:31]
	s_cbranch_execz .LBB0_716
	v_cmp_lt_u32_e32 vcc, s42, v136
	v_cvt_pk_bf16_f32 v144, v54, v55
	v_cvt_pk_bf16_f32 v145, v56, v57
	v_mov_b32_e32 v137, v147
	s_and_saveexec_b64 s[34:35], vcc
	s_xor_b64 s[34:35], exec, s[34:35]
	s_cbranch_execz .LBB0_713
	v_lshl_add_u64 v[152:153], s[24:25], 0, v[142:143]
	v_lshl_add_u64 v[152:153], v[136:137], 1, v[152:153]
	v_add_co_u32_e32 v152, vcc, 0xfffff000, v152
	s_nop 1
	v_addc_co_u32_e32 v153, vcc, -1, v153, vcc
	global_store_dwordx2 v[152:153], v[144:145], off offset:-2048 sc1

.LBB0_716:
	s_andn2_saveexec_b64 s[30:31], s[30:31]
	s_cbranch_execz .LBB0_718
	v_pk_mul_f32 v[144:145], v[54:55], s[26:27] op_sel_hi:[1,0]
	v_pk_mul_f32 v[152:153], v[56:57], s[26:27] op_sel_hi:[1,0]
	v_cvt_pk_bf16_f32 v144, v144, v145
	v_cvt_pk_bf16_f32 v145, v152, v153
	v_lshl_add_u64 v[152:153], s[20:21], 0, v[142:143]
	v_mov_b32_e32 v137, v147
	v_lshl_add_u64 v[152:153], v[136:137], 1, v[152:153]
	global_store_dwordx2 v[152:153], v[144:145], off offset:-2048 sc1

.LBB0_720:
	v_cmp_lt_u32_e32 vcc, s41, v134
	s_and_saveexec_b64 s[30:31], vcc
	s_xor_b64 s[30:31], exec, s[30:31]
	s_cbranch_execz .LBB0_726
	v_cmp_lt_u32_e32 vcc, s42, v134
	v_cvt_pk_bf16_f32 v144, v50, v51
	v_cvt_pk_bf16_f32 v145, v52, v53
	v_mov_b32_e32 v135, v147
	s_and_saveexec_b64 s[34:35], vcc
	s_xor_b64 s[34:35], exec, s[34:35]
	s_cbranch_execz .LBB0_723
	v_lshl_add_u64 v[142:143], s[24:25], 0, v[142:143]
	v_lshl_add_u64 v[142:143], v[134:135], 1, v[142:143]
	v_add_co_u32_e32 v142, vcc, 0xfffff000, v142
	s_nop 1
	v_addc_co_u32_e32 v143, vcc, -1, v143, vcc
	global_store_dwordx2 v[142:143], v[144:145], off offset:-2048 sc1

.LBB0_726:
	s_andn2_saveexec_b64 s[30:31], s[30:31]
	s_cbranch_execz .LBB0_728
	v_pk_mul_f32 v[144:145], v[50:51], s[26:27] op_sel_hi:[1,0]
	v_pk_mul_f32 v[152:153], v[52:53], s[26:27] op_sel_hi:[1,0]
	v_lshl_add_u64 v[142:143], s[20:21], 0, v[142:143]
	v_mov_b32_e32 v135, v147
	v_cvt_pk_bf16_f32 v144, v144, v145
	v_cvt_pk_bf16_f32 v145, v152, v153
	v_lshl_add_u64 v[142:143], v[134:135], 1, v[142:143]
	global_store_dwordx2 v[142:143], v[144:145], off offset:-2048 sc1

.LBB0_730:
	v_cmp_lt_u32_e32 vcc, s41, v138
	s_and_saveexec_b64 s[30:31], vcc
	s_xor_b64 s[30:31], exec, s[30:31]
	s_cbranch_execz .LBB0_736
	v_cmp_lt_u32_e32 vcc, s42, v138
	v_cvt_pk_bf16_f32 v144, v42, v43
	v_cvt_pk_bf16_f32 v145, v44, v45
	v_mov_b32_e32 v139, v147
	s_and_saveexec_b64 s[34:35], vcc
	s_xor_b64 s[34:35], exec, s[34:35]
	s_cbranch_execz .LBB0_733
	v_lshl_add_u64 v[152:153], s[24:25], 0, v[142:143]
	v_lshl_add_u64 v[152:153], v[138:139], 1, v[152:153]
	v_add_co_u32_e32 v152, vcc, 0xfffff000, v152
	s_nop 1
	v_addc_co_u32_e32 v153, vcc, -1, v153, vcc
	global_store_dwordx2 v[152:153], v[144:145], off offset:-2048 sc1

.LBB0_736:
	s_andn2_saveexec_b64 s[30:31], s[30:31]
	s_cbranch_execz .LBB0_738
	v_pk_mul_f32 v[144:145], v[42:43], s[26:27] op_sel_hi:[1,0]
	v_pk_mul_f32 v[152:153], v[44:45], s[26:27] op_sel_hi:[1,0]
	v_cvt_pk_bf16_f32 v144, v144, v145
	v_cvt_pk_bf16_f32 v145, v152, v153
	v_lshl_add_u64 v[152:153], s[20:21], 0, v[142:143]
	v_mov_b32_e32 v139, v147
	v_lshl_add_u64 v[152:153], v[138:139], 1, v[152:153]
	global_store_dwordx2 v[152:153], v[144:145], off offset:-2048 sc1

.LBB0_740:
	v_cmp_lt_u32_e32 vcc, s41, v136
	s_and_saveexec_b64 s[30:31], vcc
	s_xor_b64 s[30:31], exec, s[30:31]
	s_cbranch_execz .LBB0_746
	v_cmp_lt_u32_e32 vcc, s42, v136
	v_cvt_pk_bf16_f32 v144, v38, v39
	v_cvt_pk_bf16_f32 v145, v40, v41
	v_mov_b32_e32 v137, v147
	s_and_saveexec_b64 s[34:35], vcc
	s_xor_b64 s[34:35], exec, s[34:35]
	s_cbranch_execz .LBB0_743
	v_lshl_add_u64 v[152:153], s[24:25], 0, v[142:143]
	v_lshl_add_u64 v[152:153], v[136:137], 1, v[152:153]
	v_add_co_u32_e32 v152, vcc, 0xfffff000, v152
	s_nop 1
	v_addc_co_u32_e32 v153, vcc, -1, v153, vcc
	global_store_dwordx2 v[152:153], v[144:145], off offset:-2048 sc1

.LBB0_746:
	s_andn2_saveexec_b64 s[30:31], s[30:31]
	s_cbranch_execz .LBB0_748
	v_pk_mul_f32 v[144:145], v[38:39], s[26:27] op_sel_hi:[1,0]
	v_pk_mul_f32 v[152:153], v[40:41], s[26:27] op_sel_hi:[1,0]
	v_cvt_pk_bf16_f32 v144, v144, v145
	v_cvt_pk_bf16_f32 v145, v152, v153
	v_lshl_add_u64 v[152:153], s[20:21], 0, v[142:143]
	v_mov_b32_e32 v137, v147
	v_lshl_add_u64 v[152:153], v[136:137], 1, v[152:153]
	global_store_dwordx2 v[152:153], v[144:145], off offset:-2048 sc1

.LBB0_750:
	v_cmp_lt_u32_e32 vcc, s41, v134
	s_and_saveexec_b64 s[30:31], vcc
	s_xor_b64 s[30:31], exec, s[30:31]
	s_cbranch_execz .LBB0_756
	v_cmp_lt_u32_e32 vcc, s42, v134
	v_cvt_pk_bf16_f32 v144, v34, v35
	v_cvt_pk_bf16_f32 v145, v36, v37
	v_mov_b32_e32 v135, v147
	s_and_saveexec_b64 s[34:35], vcc
	s_xor_b64 s[34:35], exec, s[34:35]
	s_cbranch_execz .LBB0_753
	v_lshl_add_u64 v[142:143], s[24:25], 0, v[142:143]
	v_lshl_add_u64 v[142:143], v[134:135], 1, v[142:143]
	v_add_co_u32_e32 v142, vcc, 0xfffff000, v142
	s_nop 1
	v_addc_co_u32_e32 v143, vcc, -1, v143, vcc
	global_store_dwordx2 v[142:143], v[144:145], off offset:-2048 sc1

.LBB0_756:
	s_andn2_saveexec_b64 s[30:31], s[30:31]
	s_cbranch_execz .LBB0_758
	v_pk_mul_f32 v[144:145], v[34:35], s[26:27] op_sel_hi:[1,0]
	v_pk_mul_f32 v[152:153], v[36:37], s[26:27] op_sel_hi:[1,0]
	v_lshl_add_u64 v[142:143], s[20:21], 0, v[142:143]
	v_mov_b32_e32 v135, v147
	v_cvt_pk_bf16_f32 v144, v144, v145
	v_cvt_pk_bf16_f32 v145, v152, v153
	v_lshl_add_u64 v[142:143], v[134:135], 1, v[142:143]
	global_store_dwordx2 v[142:143], v[144:145], off offset:-2048 sc1

.LBB0_760:
	v_cmp_lt_u32_e32 vcc, s41, v138
	s_and_saveexec_b64 s[30:31], vcc
	s_xor_b64 s[30:31], exec, s[30:31]
	s_cbranch_execz .LBB0_766
	v_cmp_lt_u32_e32 vcc, s42, v138
	v_cvt_pk_bf16_f32 v144, v26, v27
	v_cvt_pk_bf16_f32 v145, v28, v29
	v_mov_b32_e32 v139, v147
	s_and_saveexec_b64 s[34:35], vcc
	s_xor_b64 s[34:35], exec, s[34:35]
	s_cbranch_execz .LBB0_763
	v_lshl_add_u64 v[152:153], s[24:25], 0, v[142:143]
	v_lshl_add_u64 v[152:153], v[138:139], 1, v[152:153]
	v_add_co_u32_e32 v152, vcc, 0xfffff000, v152
	s_nop 1
	v_addc_co_u32_e32 v153, vcc, -1, v153, vcc
	global_store_dwordx2 v[152:153], v[144:145], off offset:-2048 sc1

.LBB0_766:
	s_andn2_saveexec_b64 s[30:31], s[30:31]
	s_cbranch_execz .LBB0_768
	v_pk_mul_f32 v[144:145], v[26:27], s[26:27] op_sel_hi:[1,0]
	v_pk_mul_f32 v[152:153], v[28:29], s[26:27] op_sel_hi:[1,0]
	v_cvt_pk_bf16_f32 v144, v144, v145
	v_cvt_pk_bf16_f32 v145, v152, v153
	v_lshl_add_u64 v[152:153], s[20:21], 0, v[142:143]
	v_mov_b32_e32 v139, v147
	v_lshl_add_u64 v[152:153], v[138:139], 1, v[152:153]
	global_store_dwordx2 v[152:153], v[144:145], off offset:-2048 sc1

.LBB0_770:
	v_cmp_lt_u32_e32 vcc, s41, v136
	s_and_saveexec_b64 s[30:31], vcc
	s_xor_b64 s[30:31], exec, s[30:31]
	s_cbranch_execz .LBB0_776
	v_cmp_lt_u32_e32 vcc, s42, v136
	v_cvt_pk_bf16_f32 v144, v22, v23
	v_cvt_pk_bf16_f32 v145, v24, v25
	v_mov_b32_e32 v137, v147
	s_and_saveexec_b64 s[34:35], vcc
	s_xor_b64 s[34:35], exec, s[34:35]
	s_cbranch_execz .LBB0_773
	v_lshl_add_u64 v[152:153], s[24:25], 0, v[142:143]
	v_lshl_add_u64 v[152:153], v[136:137], 1, v[152:153]
	v_add_co_u32_e32 v152, vcc, 0xfffff000, v152
	s_nop 1
	v_addc_co_u32_e32 v153, vcc, -1, v153, vcc
	global_store_dwordx2 v[152:153], v[144:145], off offset:-2048 sc1

.LBB0_776:
	s_andn2_saveexec_b64 s[30:31], s[30:31]
	s_cbranch_execz .LBB0_778
	v_pk_mul_f32 v[144:145], v[22:23], s[26:27] op_sel_hi:[1,0]
	v_pk_mul_f32 v[152:153], v[24:25], s[26:27] op_sel_hi:[1,0]
	v_cvt_pk_bf16_f32 v144, v144, v145
	v_cvt_pk_bf16_f32 v145, v152, v153
	v_lshl_add_u64 v[152:153], s[20:21], 0, v[142:143]
	v_mov_b32_e32 v137, v147
	v_lshl_add_u64 v[152:153], v[136:137], 1, v[152:153]
	global_store_dwordx2 v[152:153], v[144:145], off offset:-2048 sc1

.LBB0_780:
	v_cmp_lt_u32_e32 vcc, s41, v134
	s_and_saveexec_b64 s[30:31], vcc
	s_xor_b64 s[30:31], exec, s[30:31]
	s_cbranch_execz .LBB0_786
	v_cmp_lt_u32_e32 vcc, s42, v134
	v_cvt_pk_bf16_f32 v144, v18, v19
	v_cvt_pk_bf16_f32 v145, v20, v21
	v_mov_b32_e32 v135, v147
	s_and_saveexec_b64 s[34:35], vcc
	s_xor_b64 s[34:35], exec, s[34:35]
	s_cbranch_execz .LBB0_783
	v_lshl_add_u64 v[142:143], s[24:25], 0, v[142:143]
	v_lshl_add_u64 v[142:143], v[134:135], 1, v[142:143]
	v_add_co_u32_e32 v142, vcc, 0xfffff000, v142
	s_nop 1
	v_addc_co_u32_e32 v143, vcc, -1, v143, vcc
	global_store_dwordx2 v[142:143], v[144:145], off offset:-2048 sc1

.LBB0_786:
	s_andn2_saveexec_b64 s[30:31], s[30:31]
	s_cbranch_execz .LBB0_788
	v_pk_mul_f32 v[144:145], v[18:19], s[26:27] op_sel_hi:[1,0]
	v_pk_mul_f32 v[152:153], v[20:21], s[26:27] op_sel_hi:[1,0]
	v_lshl_add_u64 v[142:143], s[20:21], 0, v[142:143]
	v_mov_b32_e32 v135, v147
	v_cvt_pk_bf16_f32 v144, v144, v145
	v_cvt_pk_bf16_f32 v145, v152, v153
	v_lshl_add_u64 v[142:143], v[134:135], 1, v[142:143]
	global_store_dwordx2 v[142:143], v[144:145], off offset:-2048 sc1

.LBB0_790:
	v_cmp_lt_u32_e32 vcc, s41, v138
	s_and_saveexec_b64 s[4:5], vcc
	s_xor_b64 s[4:5], exec, s[4:5]
	s_cbranch_execz .LBB0_796
	v_cmp_lt_u32_e32 vcc, s42, v138
	v_cvt_pk_bf16_f32 v142, v10, v11
	v_cvt_pk_bf16_f32 v143, v12, v13
	v_mov_b32_e32 v139, v147
	s_and_saveexec_b64 s[8:9], vcc
	s_xor_b64 s[8:9], exec, s[8:9]
	s_cbranch_execz .LBB0_793
	v_lshl_add_u64 v[144:145], s[24:25], 0, v[140:141]
	v_lshl_add_u64 v[138:139], v[138:139], 1, v[144:145]
	v_add_co_u32_e32 v138, vcc, 0xfffff000, v138
	s_nop 1
	v_addc_co_u32_e32 v139, vcc, -1, v139, vcc
	global_store_dwordx2 v[138:139], v[142:143], off offset:-2048 sc1
.LBB0_793:
	s_andn2_saveexec_b64 s[8:9], s[8:9]
	s_cbranch_execz .LBB0_795
	v_lshl_add_u64 v[144:145], s[22:23], 0, v[140:141]
	v_lshl_add_u64 v[138:139], v[138:139], 1, v[144:145]
	global_store_dwordx2 v[138:139], v[142:143], off offset:-4096 sc1

.LBB0_796:
	s_andn2_saveexec_b64 s[4:5], s[4:5]
	s_cbranch_execz .LBB0_798
	v_pk_mul_f32 v[142:143], v[10:11], s[26:27] op_sel_hi:[1,0]
	v_pk_mul_f32 v[144:145], v[12:13], s[26:27] op_sel_hi:[1,0]
	v_cvt_pk_bf16_f32 v142, v142, v143
	v_cvt_pk_bf16_f32 v143, v144, v145
	v_lshl_add_u64 v[144:145], s[20:21], 0, v[140:141]
	v_mov_b32_e32 v139, v147
	v_lshl_add_u64 v[138:139], v[138:139], 1, v[144:145]
	global_store_dwordx2 v[138:139], v[142:143], off offset:-2048 sc1

.LBB0_800:
	v_cmp_lt_u32_e32 vcc, s41, v136
	s_and_saveexec_b64 s[4:5], vcc
	s_xor_b64 s[4:5], exec, s[4:5]
	s_cbranch_execz .LBB0_806
	v_cmp_lt_u32_e32 vcc, s42, v136
	v_cvt_pk_bf16_f32 v138, v6, v7
	v_cvt_pk_bf16_f32 v139, v8, v9
	v_mov_b32_e32 v137, v147
	s_and_saveexec_b64 s[6:7], vcc
	s_xor_b64 s[6:7], exec, s[6:7]
	s_cbranch_execz .LBB0_803
	v_lshl_add_u64 v[142:143], s[24:25], 0, v[140:141]
	v_lshl_add_u64 v[136:137], v[136:137], 1, v[142:143]
	v_add_co_u32_e32 v136, vcc, 0xfffff000, v136
	s_nop 1
	v_addc_co_u32_e32 v137, vcc, -1, v137, vcc
	global_store_dwordx2 v[136:137], v[138:139], off offset:-2048 sc1
.LBB0_803:
	s_andn2_saveexec_b64 s[6:7], s[6:7]
	s_cbranch_execz .LBB0_805
	v_lshl_add_u64 v[142:143], s[22:23], 0, v[140:141]
	v_lshl_add_u64 v[136:137], v[136:137], 1, v[142:143]
	global_store_dwordx2 v[136:137], v[138:139], off offset:-4096 sc1

.LBB0_806:
	s_andn2_saveexec_b64 s[4:5], s[4:5]
	s_cbranch_execz .LBB0_808
	v_pk_mul_f32 v[138:139], v[6:7], s[26:27] op_sel_hi:[1,0]
	v_pk_mul_f32 v[142:143], v[8:9], s[26:27] op_sel_hi:[1,0]
	v_cvt_pk_bf16_f32 v138, v138, v139
	v_cvt_pk_bf16_f32 v139, v142, v143
	v_lshl_add_u64 v[142:143], s[20:21], 0, v[140:141]
	v_mov_b32_e32 v137, v147
	v_lshl_add_u64 v[136:137], v[136:137], 1, v[142:143]
	global_store_dwordx2 v[136:137], v[138:139], off offset:-2048 sc1

.LBB0_810:
	v_cmp_lt_u32_e32 vcc, s41, v134
	s_and_saveexec_b64 s[2:3], vcc
	s_xor_b64 s[2:3], exec, s[2:3]
	s_cbranch_execz .LBB0_816
	v_cmp_lt_u32_e32 vcc, s42, v134
	v_cvt_pk_bf16_f32 v130, v2, v3
	v_cvt_pk_bf16_f32 v131, v4, v5
	v_mov_b32_e32 v135, v147
	s_and_saveexec_b64 s[4:5], vcc
	s_xor_b64 s[4:5], exec, s[4:5]
	s_cbranch_execz .LBB0_813
	v_lshl_add_u64 v[132:133], s[24:25], 0, v[140:141]
	v_lshl_add_u64 v[132:133], v[134:135], 1, v[132:133]
	v_add_co_u32_e32 v132, vcc, 0xfffff000, v132
	s_nop 1
	v_addc_co_u32_e32 v133, vcc, -1, v133, vcc
	global_store_dwordx2 v[132:133], v[130:131], off offset:-2048 sc1
.LBB0_813:
	s_andn2_saveexec_b64 s[4:5], s[4:5]
	s_cbranch_execz .LBB0_815
	v_lshl_add_u64 v[132:133], s[22:23], 0, v[140:141]
	v_lshl_add_u64 v[132:133], v[134:135], 1, v[132:133]
	global_store_dwordx2 v[132:133], v[130:131], off offset:-4096 sc1

.LBB0_816:
	s_andn2_saveexec_b64 s[2:3], s[2:3]
	s_cbranch_execz .LBB0_818
	v_pk_mul_f32 v[130:131], v[2:3], s[26:27] op_sel_hi:[1,0]
	v_pk_mul_f32 v[132:133], v[4:5], s[26:27] op_sel_hi:[1,0]
	v_cvt_pk_bf16_f32 v130, v130, v131
	v_cvt_pk_bf16_f32 v131, v132, v133
	v_lshl_add_u64 v[132:133], s[20:21], 0, v[140:141]
	v_mov_b32_e32 v135, v147
	v_lshl_add_u64 v[132:133], v[134:135], 1, v[132:133]
	global_store_dwordx2 v[132:133], v[130:131], off offset:-2048 sc1

.LBB0_1201:
	s_ashr_i32 s18, s25, 10
	s_mul_i32 s14, s18, 0x3000
	s_ashr_i32 s21, s20, 31
	s_ashr_i32 s15, s14, 31
	s_lshl_b64 s[26:27], s[20:21], 12
	s_lshl_b64 s[14:15], s[14:15], 2
	s_add_u32 s14, s70, s14
	s_addc_u32 s15, s71, s15
	v_lshl_add_u64 v[14:15], s[14:15], 0, v[66:67]
	v_add_co_u32_e32 v16, vcc, s35, v14
	s_nop 1
	v_addc_co_u32_e32 v17, vcc, 0, v15, vcc
	s_waitcnt lgkmcnt(0)
	global_load_dwordx4 v[2:5], v[16:17], off offset:-4096
	v_add_co_u32_e32 v18, vcc, s34, v14
	s_waitcnt vmcnt(0)
	v_add_f32_e32 v204, 1.0, v2
	v_addc_co_u32_e32 v19, vcc, 0, v15, vcc
	global_load_dwordx4 v[6:9], v[18:19], off offset:1024
	global_load_dwordx4 v[10:13], v[18:19], off offset:2048
	s_nop 0
	global_load_dwordx4 v[18:21], v[18:19], off offset:3072
	s_nop 0
	global_load_dwordx4 v[86:89], v[16:17], off
	global_load_dwordx4 v[90:93], v[16:17], off offset:1024
	global_load_dwordx4 v[94:97], v[16:17], off offset:2048
	global_load_dwordx4 v[98:101], v[16:17], off offset:3072
	v_lshl_add_u64 v[16:17], v[68:69], 0, s[26:27]
	global_load_dwordx2 v[102:103], v[16:17], off offset:2560
	global_load_dwordx2 v[104:105], v[16:17], off offset:3072
	global_load_dwordx2 v[106:107], v[16:17], off offset:3584
	global_load_dwordx2 v[108:109], v[16:17], off offset:2048
	v_add_co_u32_e32 v26, vcc, s30, v16
	v_add_f32_e32 v206, 1.0, v3
	s_nop 0
	v_addc_co_u32_e32 v27, vcc, 0, v17, vcc
	global_load_dwordx2 v[118:119], v[26:27], off offset:2560
	global_load_dwordx2 v[220:221], v[26:27], off offset:3072
	global_load_dwordx2 v[222:223], v[26:27], off offset:3584
	global_load_dwordx2 v[162:163], v[26:27], off offset:2048
	global_load_dwordx4 v[62:65], v[70:71], off
	global_load_dwordx4 v[54:57], v[70:71], off offset:1024
	global_load_dwordx4 v[46:49], v[70:71], off offset:2048
	global_load_dwordx4 v[38:41], v[70:71], off offset:3072
	global_load_dwordx2 v[164:165], v[16:17], off
	global_load_dwordx2 v[166:167], v[26:27], off
	global_load_dwordx4 v[30:33], v[72:73], off
	global_load_dwordx4 v[22:25], v[74:75], off
	global_load_dwordx2 v[168:169], v[16:17], off offset:512
	global_load_dwordx2 v[180:181], v[16:17], off offset:1024
	global_load_dwordx2 v[224:225], v[16:17], off offset:1536
	global_load_dwordx2 v[182:183], v[26:27], off offset:512
	global_load_dwordx2 v[226:227], v[26:27], off offset:1024
	global_load_dwordx2 v[228:229], v[26:27], off offset:1536
	v_add_co_u32_e32 v128, vcc, s36, v14
	v_add_f32_e32 v208, 1.0, v4
	s_nop 0
	v_addc_co_u32_e32 v129, vcc, 0, v15, vcc
	v_lshl_add_u64 v[14:15], v[14:15], 0, s[22:23]
	global_load_dwordx4 v[58:61], v[128:129], off offset:-4096
	global_load_dwordx4 v[50:53], v[14:15], off offset:1024
	global_load_dwordx4 v[42:45], v[14:15], off offset:2048
	global_load_dwordx4 v[34:37], v[14:15], off offset:3072
	global_load_dwordx4 v[26:29], v[128:129], off
	s_nop 0
	global_load_dwordx4 v[14:17], v[128:129], off offset:1024
	v_add_f32_e32 v210, 1.0, v5
	s_waitcnt vmcnt(23)
	v_and_b32_e32 v141, 0xffff0000, v118
	v_lshlrev_b32_e32 v143, 16, v118
	v_lshlrev_b32_e32 v139, 16, v119
	v_add_f32_e32 v194, 1.0, v6
	v_add_f32_e32 v192, 1.0, v7
	v_add_f32_e32 v190, 1.0, v8
	v_add_f32_e32 v188, 1.0, v9
	v_add_f32_e32 v178, 1.0, v10
	v_add_f32_e32 v176, 1.0, v11
	v_add_f32_e32 v174, 1.0, v12
	v_add_f32_e32 v172, 1.0, v13
	v_add_f32_e32 v160, 1.0, v18
	v_add_f32_e32 v156, 1.0, v19
	v_add_f32_e32 v154, 1.0, v20
	v_add_f32_e32 v152, 1.0, v21
	global_load_dwordx4 v[18:21], v[76:77], off
	global_load_dwordx4 v[6:9], v[78:79], off
	global_load_dwordx4 v[10:13], v[128:129], off offset:2048
	global_load_dwordx4 v[2:5], v[128:129], off offset:3072
	v_and_b32_e32 v133, 0xffff0000, v102
	v_and_b32_e32 v132, 0xffff0000, v108
	v_add_f32_e32 v116, 1.0, v94
	v_add_f32_e32 v114, 1.0, v95
	v_lshlrev_b32_e32 v135, 16, v102
	v_lshlrev_b32_e32 v134, 16, v108
	v_pk_mul_f32 v[94:95], v[132:133], v[132:133]
	v_lshlrev_b32_e32 v131, 16, v103
	v_lshlrev_b32_e32 v130, 16, v109
	v_pk_fma_f32 v[94:95], v[134:135], v[134:135], v[94:95]
	v_and_b32_e32 v129, 0xffff0000, v103
	v_and_b32_e32 v128, 0xffff0000, v109
	v_pk_fma_f32 v[94:95], v[130:131], v[130:131], v[94:95]
	s_waitcnt vmcnt(24)
	v_and_b32_e32 v140, 0xffff0000, v162
	v_pk_fma_f32 v[230:231], v[128:129], v[128:129], v[94:95]
	v_lshlrev_b32_e32 v142, 16, v162
	v_pk_mul_f32 v[94:95], v[140:141], v[140:141]
	v_lshlrev_b32_e32 v138, 16, v163
	v_pk_fma_f32 v[94:95], v[142:143], v[142:143], v[94:95]
	v_and_b32_e32 v137, 0xffff0000, v119
	v_and_b32_e32 v136, 0xffff0000, v163
	v_pk_fma_f32 v[94:95], v[138:139], v[138:139], v[94:95]
	s_waitcnt vmcnt(19)
	v_and_b32_e32 v219, 0xffff0000, v164
	s_waitcnt vmcnt(18)
	v_and_b32_e32 v218, 0xffff0000, v166
	s_waitcnt vmcnt(15)
	v_and_b32_e32 v201, 0xffff0000, v168
	s_waitcnt vmcnt(12)
	v_and_b32_e32 v200, 0xffff0000, v182
	v_add_f32_e32 v112, 1.0, v96
	v_add_f32_e32 v110, 1.0, v97
	v_pk_fma_f32 v[118:119], v[136:137], v[136:137], v[94:95]
	v_lshlrev_b32_e32 v216, 16, v166
	v_lshlrev_b32_e32 v217, 16, v164
	v_pk_mul_f32 v[94:95], v[218:219], v[218:219]
	v_lshlrev_b32_e32 v202, 16, v182
	v_lshlrev_b32_e32 v203, 16, v168
	v_pk_mul_f32 v[96:97], v[200:201], v[200:201]
	v_lshlrev_b32_e32 v214, 16, v167
	v_lshlrev_b32_e32 v215, 16, v165
	v_pk_fma_f32 v[94:95], v[216:217], v[216:217], v[94:95]
	v_lshlrev_b32_e32 v198, 16, v183
	v_lshlrev_b32_e32 v199, 16, v169
	v_pk_fma_f32 v[96:97], v[202:203], v[202:203], v[96:97]
	v_and_b32_e32 v213, 0xffff0000, v165
	v_and_b32_e32 v212, 0xffff0000, v167
	v_pk_fma_f32 v[94:95], v[214:215], v[214:215], v[94:95]
	v_and_b32_e32 v197, 0xffff0000, v169
	v_and_b32_e32 v196, 0xffff0000, v183
	v_pk_fma_f32 v[96:97], v[198:199], v[198:199], v[96:97]
	v_pk_fma_f32 v[94:95], v[212:213], v[212:213], v[94:95]
	v_pk_fma_f32 v[96:97], v[196:197], v[196:197], v[96:97]
	v_and_b32_e32 v185, 0xffff0000, v180
	s_waitcnt vmcnt(11)
	v_and_b32_e32 v184, 0xffff0000, v226
	v_pk_add_f32 v[94:95], v[94:95], v[96:97]
	v_lshlrev_b32_e32 v186, 16, v226
	v_lshlrev_b32_e32 v187, 16, v180
	v_pk_mul_f32 v[96:97], v[184:185], v[184:185]
	v_lshlrev_b32_e32 v182, 16, v227
	v_lshlrev_b32_e32 v183, 16, v181
	v_pk_fma_f32 v[96:97], v[186:187], v[186:187], v[96:97]
	v_and_b32_e32 v181, 0xffff0000, v181
	v_and_b32_e32 v180, 0xffff0000, v227
	v_pk_fma_f32 v[96:97], v[182:183], v[182:183], v[96:97]
	v_and_b32_e32 v167, 0xffff0000, v224
	v_pk_fma_f32 v[96:97], v[180:181], v[180:181], v[96:97]
	s_waitcnt vmcnt(10)
	v_and_b32_e32 v166, 0xffff0000, v228
	v_pk_add_f32 v[94:95], v[94:95], v[96:97]
	v_lshlrev_b32_e32 v168, 16, v228
	v_lshlrev_b32_e32 v169, 16, v224
	v_pk_mul_f32 v[96:97], v[166:167], v[166:167]
	v_lshlrev_b32_e32 v164, 16, v229
	v_lshlrev_b32_e32 v165, 16, v225
	v_pk_fma_f32 v[96:97], v[168:169], v[168:169], v[96:97]
	v_and_b32_e32 v163, 0xffff0000, v225
	v_and_b32_e32 v162, 0xffff0000, v229
	v_pk_fma_f32 v[96:97], v[164:165], v[164:165], v[96:97]
	v_add_f32_e32 v126, 1.0, v90
	v_add_f32_e32 v122, 1.0, v92
	v_add_f32_e32 v92, 1.0, v98
	v_add_f32_e32 v90, 1.0, v99
	v_pk_fma_f32 v[96:97], v[162:163], v[162:163], v[96:97]
	v_and_b32_e32 v99, 0xffff0000, v106
	v_and_b32_e32 v98, 0xffff0000, v104
	v_add_f32_e32 v150, 1.0, v86
	v_add_f32_e32 v146, 1.0, v88
	v_add_f32_e32 v88, 1.0, v100
	v_add_f32_e32 v86, 1.0, v101
	v_pk_add_f32 v[94:95], v[94:95], v[96:97]
	v_mov_b32_e32 v96, v118
	v_mov_b32_e32 v97, v230
	v_lshlrev_b32_e32 v101, 16, v106
	v_lshlrev_b32_e32 v100, 16, v104
	v_pk_mul_f32 v[102:103], v[98:99], v[98:99]
	v_pk_add_f32 v[224:225], v[94:95], v[96:97]
	v_lshlrev_b32_e32 v97, 16, v107
	v_lshlrev_b32_e32 v96, 16, v105
	v_pk_fma_f32 v[102:103], v[100:101], v[100:101], v[102:103]
	v_and_b32_e32 v95, 0xffff0000, v107
	v_and_b32_e32 v94, 0xffff0000, v105
	v_pk_fma_f32 v[102:103], v[96:97], v[96:97], v[102:103]
	v_and_b32_e32 v107, 0xffff0000, v222
	v_and_b32_e32 v106, 0xffff0000, v220
	v_pk_fma_f32 v[226:227], v[94:95], v[94:95], v[102:103]
	v_lshlrev_b32_e32 v109, 16, v222
	v_lshlrev_b32_e32 v108, 16, v220
	v_lshlrev_b32_e32 v104, 16, v221
	v_and_b32_e32 v102, 0xffff0000, v221
	v_pk_mul_f32 v[220:221], v[106:107], v[106:107]
	v_lshlrev_b32_e32 v105, 16, v223
	v_pk_fma_f32 v[220:221], v[108:109], v[108:109], v[220:221]
	v_and_b32_e32 v103, 0xffff0000, v223
	v_pk_fma_f32 v[220:221], v[104:105], v[104:105], v[220:221]
	v_add_f32_e32 v148, 1.0, v87
	v_add_f32_e32 v144, 1.0, v89
	v_add_f32_e32 v124, 1.0, v91
	v_add_f32_e32 v120, 1.0, v93
	v_pk_fma_f32 v[220:221], v[102:103], v[102:103], v[220:221]
	v_mov_b32_e32 v230, v119
	v_pk_add_f32 v[118:119], v[224:225], v[230:231]
	v_mov_b32_e32 v222, v220
	v_mov_b32_e32 v223, v226
	v_pk_add_f32 v[118:119], v[118:119], v[222:223]
	v_mov_b32_e32 v226, v221
	v_pk_add_f32 v[118:119], v[118:119], v[226:227]
	ds_bpermute_b32 v221, v1, v119
	ds_bpermute_b32 v220, v1, v118
	v_mov_b32_e32 v205, v216
	v_mov_b32_e32 v207, v218
	v_mov_b32_e32 v209, v214
	v_mov_b32_e32 v211, v212
	s_waitcnt lgkmcnt(0)
	v_pk_add_f32 v[118:119], v[118:119], v[220:221]
	ds_bpermute_b32 v221, v85, v119
	ds_bpermute_b32 v220, v85, v118
	s_add_i32 s28, s20, 1
	s_ashr_i32 s29, s28, 31
	s_lshl_b64 s[28:29], s[28:29], 12
	s_waitcnt lgkmcnt(0)
	v_pk_add_f32 v[118:119], v[118:119], v[220:221]
	ds_bpermute_b32 v221, v159, v119
	ds_bpermute_b32 v220, v159, v118
	s_waitcnt lgkmcnt(0)
	v_pk_add_f32 v[118:119], v[118:119], v[220:221]
	ds_bpermute_b32 v221, v171, v119
	ds_bpermute_b32 v220, v171, v118
	s_waitcnt lgkmcnt(0)
	v_pk_add_f32 v[118:119], v[118:119], v[220:221]
	ds_bpermute_b32 v221, v238, v119
	ds_bpermute_b32 v220, v238, v118
	s_waitcnt lgkmcnt(0)
	v_pk_add_f32 v[220:221], v[118:119], v[220:221]
	ds_bpermute_b32 v223, v239, v221
	ds_bpermute_b32 v222, v239, v220
	v_mov_b32_e32 v118, v62
	s_waitcnt lgkmcnt(0)
	v_pk_add_f32 v[220:221], v[220:221], v[222:223]
	s_nop 0
	v_pk_fma_f32 v[220:221], v[220:221], s[24:25], v[84:85] op_sel_hi:[1,0,0]
	ds_read_b128 v[222:225], v240 offset:24624
	v_mul_f32_e32 v62, 0x4b800000, v221
	v_mul_f32_e32 v83, 0x4b800000, v220
	v_cmp_gt_f32_e32 vcc, s37, v221
	v_cmp_gt_f32_e64 s[14:15], s37, v220
	s_nop 0
	v_cndmask_b32_e32 v62, v221, v62, vcc
	v_cndmask_b32_e64 v83, v220, v83, s[14:15]
	v_rsq_f32_e32 v62, v62
	v_rsq_f32_e32 v87, v83
	v_mul_f32_e32 v83, 0x45800000, v62
	v_mul_f32_e32 v89, 0x45800000, v87
	v_cndmask_b32_e32 v83, v62, v83, vcc
	v_cndmask_b32_e64 v119, v87, v89, s[14:15]
	v_mul_f32_e32 v62, v83, v217
	v_pk_mul_f32 v[216:217], v[118:119], v[204:205]
	v_mov_b32_e32 v118, v63
	v_mul_f32_e32 v87, v83, v219
	s_waitcnt vmcnt(9)
	v_fma_f32 v204, v216, v62, v58
	v_pk_mul_f32 v[62:63], v[118:119], v[206:207]
	v_mov_b32_e32 v118, v64
	v_fma_f32 v205, v216, v217, v58
	v_fma_f32 v206, v62, v87, v59
	v_fma_f32 v207, v62, v63, v59
	v_mul_f32_e32 v62, v83, v215
	v_pk_mul_f32 v[58:59], v[118:119], v[208:209]
	v_mov_b32_e32 v118, v65
	v_fma_f32 v208, v58, v62, v60
	v_fma_f32 v209, v58, v59, v60
	v_mul_f32_e32 v60, v83, v213
	v_pk_mul_f32 v[58:59], v[118:119], v[210:211]
	ds_read_b128 v[210:213], v240
	ds_read_b128 v[214:217], v240 offset:8208
	v_fma_f32 v60, v58, v60, v61
	v_fmac_f32_e32 v61, v58, v59
	v_cvt_pk_bf16_f32 v62, v204, v206
	v_cvt_pk_bf16_f32 v63, v208, v60
	v_lshl_add_u64 v[58:59], v[80:81], 0, s[26:27]
	global_store_dwordx2 v[58:59], v[62:63], off sc1
	v_cvt_pk_bf16_f32 v64, v205, v207
	v_cvt_pk_bf16_f32 v65, v209, v61
	v_lshl_add_u64 v[62:63], v[80:81], 0, s[28:29]
	ds_read_b128 v[218:221], v240 offset:16416
	global_store_dwordx2 v[62:63], v[64:65], off sc1
	s_waitcnt lgkmcnt(2)
	v_pk_fma_f32 v[64:65], v[204:205], v[210:211], 0 op_sel_hi:[1,0,0]
	v_mov_b32_e32 v118, v213
	v_pk_fma_f32 v[64:65], v[206:207], v[210:211], v[64:65] op_sel:[0,1,0]
	s_waitcnt lgkmcnt(1)
	v_pk_fma_f32 v[210:211], v[204:205], v[214:215], 0 op_sel_hi:[1,0,0]
	v_pk_fma_f32 v[64:65], v[208:209], v[212:213], v[64:65] op_sel_hi:[1,0,1]
	v_pk_fma_f32 v[210:211], v[206:207], v[214:215], v[210:211] op_sel:[0,1,0]
	v_pk_fma_f32 v[64:65], v[60:61], v[118:119], v[64:65] op_sel_hi:[1,0,1]
	v_pk_fma_f32 v[210:211], v[208:209], v[216:217], v[210:211] op_sel_hi:[1,0,1]
	v_mov_b32_e32 v118, v217
	v_pk_fma_f32 v[212:213], v[60:61], v[118:119], v[210:211] op_sel_hi:[1,0,1]
	s_waitcnt lgkmcnt(0)
	v_pk_fma_f32 v[210:211], v[204:205], v[218:219], 0 op_sel_hi:[1,0,0]
	v_mov_b32_e32 v118, v221
	v_pk_fma_f32 v[210:211], v[206:207], v[218:219], v[210:211] op_sel:[0,1,0]
	s_nop 0
	v_pk_fma_f32 v[210:211], v[208:209], v[220:221], v[210:211] op_sel_hi:[1,0,1]
	s_nop 0
	v_pk_fma_f32 v[216:217], v[60:61], v[118:119], v[210:211] op_sel_hi:[1,0,1]
	v_pk_fma_f32 v[210:211], v[204:205], v[222:223], 0 op_sel_hi:[1,0,0]
	v_mov_b32_e32 v118, v225
	v_pk_fma_f32 v[210:211], v[206:207], v[222:223], v[210:211] op_sel:[0,1,0]
	s_nop 0
	v_pk_fma_f32 v[210:211], v[208:209], v[224:225], v[210:211] op_sel_hi:[1,0,1]
	s_nop 0
	v_pk_fma_f32 v[222:223], v[60:61], v[118:119], v[210:211] op_sel_hi:[1,0,1]
	ds_read_b128 v[218:221], v240 offset:32832
	ds_read_b128 v[224:227], v240 offset:41040
	s_waitcnt lgkmcnt(1)
	v_pk_fma_f32 v[210:211], v[204:205], v[218:219], 0 op_sel_hi:[1,0,0]
	s_nop 0
	v_pk_fma_f32 v[210:211], v[206:207], v[218:219], v[210:211] op_sel:[0,1,0]
	v_mov_b32_e32 v118, v221
	v_pk_fma_f32 v[210:211], v[208:209], v[220:221], v[210:211] op_sel_hi:[1,0,1]
	ds_read_b128 v[218:221], v240 offset:49248
	s_waitcnt lgkmcnt(1)
	v_pk_fma_f32 v[214:215], v[204:205], v[224:225], 0 op_sel_hi:[1,0,0]
	v_pk_fma_f32 v[230:231], v[60:61], v[118:119], v[210:211] op_sel_hi:[1,0,1]
	v_pk_fma_f32 v[214:215], v[206:207], v[224:225], v[214:215] op_sel:[0,1,0]
	v_mov_b32_e32 v118, v227
	v_pk_fma_f32 v[210:211], v[208:209], v[226:227], v[214:215] op_sel_hi:[1,0,1]
	ds_read_b128 v[224:227], v240 offset:57456
	v_pk_fma_f32 v[234:235], v[60:61], v[118:119], v[210:211] op_sel_hi:[1,0,1]
	s_waitcnt lgkmcnt(1)
	v_pk_fma_f32 v[210:211], v[204:205], v[218:219], 0 op_sel_hi:[1,0,0]
	v_mov_b32_e32 v118, v221
	v_pk_fma_f32 v[210:211], v[206:207], v[218:219], v[210:211] op_sel:[0,1,0]
	s_nop 0
	v_pk_fma_f32 v[210:211], v[208:209], v[220:221], v[210:211] op_sel_hi:[1,0,1]
	s_nop 0
	v_pk_fma_f32 v[218:219], v[60:61], v[118:119], v[210:211] op_sel_hi:[1,0,1]
	s_waitcnt lgkmcnt(0)
	v_pk_fma_f32 v[210:211], v[204:205], v[224:225], 0 op_sel_hi:[1,0,0]
	v_mov_b32_e32 v118, v227
	v_pk_fma_f32 v[210:211], v[206:207], v[224:225], v[210:211] op_sel:[0,1,0]
	s_nop 0
	v_pk_fma_f32 v[210:211], v[208:209], v[226:227], v[210:211] op_sel_hi:[1,0,1]
	s_nop 0
	v_pk_fma_f32 v[224:225], v[60:61], v[118:119], v[210:211] op_sel_hi:[1,0,1]
	v_add_u32_e32 v87, 0x10080, v240
	ds_read_b128 v[226:229], v87
	v_add_u32_e32 v87, 0x12090, v240
	ds_read_b128 v[242:245], v87
	v_add_u32_e32 v87, 0x140a0, v240
	ds_read_b128 v[246:249], v87
	s_waitcnt lgkmcnt(2)
	v_pk_fma_f32 v[210:211], v[204:205], v[226:227], 0 op_sel_hi:[1,0,0]
	v_mov_b32_e32 v118, v229
	v_pk_fma_f32 v[210:211], v[206:207], v[226:227], v[210:211] op_sel:[0,1,0]
	s_waitcnt lgkmcnt(1)
	v_pk_fma_f32 v[214:215], v[204:205], v[242:243], 0 op_sel_hi:[1,0,0]
	v_pk_fma_f32 v[210:211], v[208:209], v[228:229], v[210:211] op_sel_hi:[1,0,1]
	v_add_u32_e32 v87, 0x160b0, v240
	v_pk_fma_f32 v[228:229], v[60:61], v[118:119], v[210:211] op_sel_hi:[1,0,1]
	v_pk_fma_f32 v[210:211], v[206:207], v[242:243], v[214:215] op_sel:[0,1,0]
	v_mov_b32_e32 v118, v245
	v_pk_fma_f32 v[210:211], v[208:209], v[244:245], v[210:211] op_sel_hi:[1,0,1]
	ds_read_b128 v[242:245], v87
	v_pk_fma_f32 v[236:237], v[60:61], v[118:119], v[210:211] op_sel_hi:[1,0,1]
	s_waitcnt lgkmcnt(1)
	v_pk_fma_f32 v[210:211], v[204:205], v[246:247], 0 op_sel_hi:[1,0,0]
	v_mov_b32_e32 v118, v249
	v_pk_fma_f32 v[210:211], v[206:207], v[246:247], v[210:211] op_sel:[0,1,0]
	s_nop 0
	v_pk_fma_f32 v[210:211], v[208:209], v[248:249], v[210:211] op_sel_hi:[1,0,1]
	s_nop 0
	v_pk_fma_f32 v[220:221], v[60:61], v[118:119], v[210:211] op_sel_hi:[1,0,1]
	s_waitcnt lgkmcnt(0)
	v_pk_fma_f32 v[210:211], v[204:205], v[242:243], 0 op_sel_hi:[1,0,0]
	v_mov_b32_e32 v118, v245
	v_pk_fma_f32 v[210:211], v[206:207], v[242:243], v[210:211] op_sel:[0,1,0]
	s_nop 0
	v_pk_fma_f32 v[210:211], v[208:209], v[244:245], v[210:211] op_sel_hi:[1,0,1]
	s_nop 0
	v_pk_fma_f32 v[226:227], v[60:61], v[118:119], v[210:211] op_sel_hi:[1,0,1]
	v_add_u32_e32 v87, 0x180c0, v240
	ds_read_b128 v[242:245], v87
	v_add_u32_e32 v87, 0x1a0d0, v240
	s_waitcnt lgkmcnt(0)
	v_pk_fma_f32 v[210:211], v[204:205], v[242:243], 0 op_sel_hi:[1,0,0]
	s_nop 0
	v_pk_fma_f32 v[210:211], v[206:207], v[242:243], v[210:211] op_sel:[0,1,0]
	v_mov_b32_e32 v118, v245
	v_pk_fma_f32 v[210:211], v[208:209], v[244:245], v[210:211] op_sel_hi:[1,0,1]
	ds_read_b128 v[242:245], v87
	v_pk_fma_f32 v[214:215], v[60:61], v[118:119], v[210:211] op_sel_hi:[1,0,1]
	v_add_u32_e32 v87, 0x1c0e0, v240
	s_waitcnt lgkmcnt(0)
	v_pk_fma_f32 v[210:211], v[204:205], v[242:243], 0 op_sel_hi:[1,0,0]
	s_nop 0
	v_pk_fma_f32 v[210:211], v[206:207], v[242:243], v[210:211] op_sel:[0,1,0]
	v_mov_b32_e32 v118, v245
	v_pk_fma_f32 v[210:211], v[208:209], v[244:245], v[210:211] op_sel_hi:[1,0,1]
	ds_read_b128 v[242:245], v87
	v_pk_fma_f32 v[232:233], v[60:61], v[118:119], v[210:211] op_sel_hi:[1,0,1]
	v_add_u32_e32 v87, 0x1e0f0, v240
	s_waitcnt lgkmcnt(0)
	v_pk_fma_f32 v[210:211], v[204:205], v[242:243], 0 op_sel_hi:[1,0,0]
	s_nop 0
	v_pk_fma_f32 v[210:211], v[206:207], v[242:243], v[210:211] op_sel:[0,1,0]
	v_mov_b32_e32 v118, v245
	v_pk_fma_f32 v[210:211], v[208:209], v[244:245], v[210:211] op_sel_hi:[1,0,1]
	ds_read_b128 v[242:245], v87
	v_pk_fma_f32 v[210:211], v[60:61], v[118:119], v[210:211] op_sel_hi:[1,0,1]
	s_waitcnt lgkmcnt(0)
	v_pk_fma_f32 v[204:205], v[204:205], v[242:243], 0 op_sel_hi:[1,0,0]
	s_nop 0
	v_pk_fma_f32 v[204:205], v[206:207], v[242:243], v[204:205] op_sel:[0,1,0]
	v_mov_b32_e32 v118, v245
	v_pk_fma_f32 v[204:205], v[208:209], v[244:245], v[204:205] op_sel_hi:[1,0,1]
	s_nop 0
	v_pk_fma_f32 v[60:61], v[60:61], v[118:119], v[204:205] op_sel_hi:[1,0,1]
	v_mov_b32_e32 v118, v54
	v_mov_b32_e32 v195, v202
	v_mul_f32_e32 v87, v83, v203
	v_pk_mul_f32 v[202:203], v[118:119], v[194:195]
	v_mov_b32_e32 v118, v55
	v_mov_b32_e32 v193, v200
	s_waitcnt vmcnt(10)
	v_fma_f32 v194, v202, v87, v50
	v_fma_f32 v195, v202, v203, v50
	v_mul_f32_e32 v50, v83, v201
	v_pk_mul_f32 v[54:55], v[118:119], v[192:193]
	v_mov_b32_e32 v118, v56
	v_mov_b32_e32 v191, v198
	v_fma_f32 v192, v54, v50, v51
	v_fma_f32 v193, v54, v55, v51
	v_mul_f32_e32 v54, v83, v199
	v_pk_mul_f32 v[50:51], v[118:119], v[190:191]
	v_mov_b32_e32 v118, v57
	v_fma_f32 v190, v50, v54, v52
	v_mov_b32_e32 v189, v196
	ds_read_b128 v[54:57], v240 offset:1024
	v_fma_f32 v191, v50, v51, v52
	v_mul_f32_e32 v52, v83, v197
	v_pk_mul_f32 v[50:51], v[118:119], v[188:189]
	ds_read_b128 v[196:199], v240 offset:9232
	v_fma_f32 v52, v50, v52, v53
	v_fmac_f32_e32 v53, v50, v51
	v_cvt_pk_bf16_f32 v50, v194, v192
	v_cvt_pk_bf16_f32 v51, v190, v52
	global_store_dwordx2 v[58:59], v[50:51], off offset:512 sc1
	v_cvt_pk_bf16_f32 v50, v195, v193
	v_cvt_pk_bf16_f32 v51, v191, v53
	global_store_dwordx2 v[62:63], v[50:51], off offset:512 sc1
	s_waitcnt lgkmcnt(1)
	v_pk_fma_f32 v[50:51], v[194:195], v[54:55], v[64:65] op_sel_hi:[1,0,1]
	s_waitcnt lgkmcnt(0)
	v_mov_b32_e32 v118, v199
	v_pk_fma_f32 v[50:51], v[192:193], v[54:55], v[50:51] op_sel:[0,1,0]
	v_mov_b32_e32 v54, v57
	v_pk_fma_f32 v[50:51], v[190:191], v[56:57], v[50:51] op_sel_hi:[1,0,1]
	s_nop 0
	v_pk_fma_f32 v[50:51], v[52:53], v[54:55], v[50:51] op_sel_hi:[1,0,1]
	v_pk_fma_f32 v[54:55], v[194:195], v[196:197], v[212:213] op_sel_hi:[1,0,1]
	s_nop 0
	v_pk_fma_f32 v[64:65], v[192:193], v[196:197], v[54:55] op_sel:[0,1,0]
	ds_read_b128 v[54:57], v240 offset:17440
	v_pk_fma_f32 v[64:65], v[190:191], v[198:199], v[64:65] op_sel_hi:[1,0,1]
	ds_read_b128 v[196:199], v240 offset:25648
	v_pk_fma_f32 v[64:65], v[52:53], v[118:119], v[64:65] op_sel_hi:[1,0,1]
	s_waitcnt lgkmcnt(1)
	v_pk_fma_f32 v[188:189], v[194:195], v[54:55], v[216:217] op_sel_hi:[1,0,1]
	s_nop 0
	v_pk_fma_f32 v[54:55], v[192:193], v[54:55], v[188:189] op_sel:[0,1,0]
	s_waitcnt lgkmcnt(0)
	v_mov_b32_e32 v118, v199
	v_pk_fma_f32 v[54:55], v[190:191], v[56:57], v[54:55] op_sel_hi:[1,0,1]
	v_mov_b32_e32 v56, v57
	v_pk_fma_f32 v[54:55], v[52:53], v[56:57], v[54:55] op_sel_hi:[1,0,1]
	v_pk_fma_f32 v[56:57], v[194:195], v[196:197], v[222:223] op_sel_hi:[1,0,1]
	s_nop 0
	v_pk_fma_f32 v[56:57], v[192:193], v[196:197], v[56:57] op_sel:[0,1,0]
	s_nop 0
	v_pk_fma_f32 v[56:57], v[190:191], v[198:199], v[56:57] op_sel_hi:[1,0,1]
	s_nop 0
	v_pk_fma_f32 v[56:57], v[52:53], v[118:119], v[56:57] op_sel_hi:[1,0,1]
	ds_read_b128 v[196:199], v240 offset:33856
	ds_read_b128 v[200:203], v240 offset:42064
	s_waitcnt lgkmcnt(1)
	v_pk_fma_f32 v[188:189], v[194:195], v[196:197], v[230:231] op_sel_hi:[1,0,1]
	s_waitcnt lgkmcnt(0)
	v_pk_fma_f32 v[204:205], v[194:195], v[200:201], v[234:235] op_sel_hi:[1,0,1]
	v_pk_fma_f32 v[188:189], v[192:193], v[196:197], v[188:189] op_sel:[0,1,0]
	v_mov_b32_e32 v118, v199
	v_pk_fma_f32 v[196:197], v[192:193], v[200:201], v[204:205] op_sel:[0,1,0]
	v_pk_fma_f32 v[188:189], v[190:191], v[198:199], v[188:189] op_sel_hi:[1,0,1]
	ds_read_b128 v[198:201], v240 offset:50272
	v_pk_fma_f32 v[188:189], v[52:53], v[118:119], v[188:189] op_sel_hi:[1,0,1]
	v_pk_fma_f32 v[196:197], v[190:191], v[202:203], v[196:197] op_sel_hi:[1,0,1]
	v_mov_b32_e32 v118, v203
	ds_read_b128 v[202:205], v240 offset:58480
	s_waitcnt lgkmcnt(1)
	v_pk_fma_f32 v[206:207], v[194:195], v[198:199], v[218:219] op_sel_hi:[1,0,1]
	v_pk_fma_f32 v[196:197], v[52:53], v[118:119], v[196:197] op_sel_hi:[1,0,1]
	v_pk_fma_f32 v[198:199], v[192:193], v[198:199], v[206:207] op_sel:[0,1,0]
	v_mov_b32_e32 v118, v201
	v_pk_fma_f32 v[198:199], v[190:191], v[200:201], v[198:199] op_sel_hi:[1,0,1]
	s_waitcnt lgkmcnt(0)
	v_pk_fma_f32 v[200:201], v[194:195], v[202:203], v[224:225] op_sel_hi:[1,0,1]
	v_pk_fma_f32 v[198:199], v[52:53], v[118:119], v[198:199] op_sel_hi:[1,0,1]
	v_pk_fma_f32 v[200:201], v[192:193], v[202:203], v[200:201] op_sel:[0,1,0]
	v_mov_b32_e32 v118, v205
	v_pk_fma_f32 v[200:201], v[190:191], v[204:205], v[200:201] op_sel_hi:[1,0,1]
	s_nop 0
	v_pk_fma_f32 v[200:201], v[52:53], v[118:119], v[200:201] op_sel_hi:[1,0,1]
	v_add_u32_e32 v87, 0x10480, v240
	ds_read_b128 v[202:205], v87
	v_add_u32_e32 v87, 0x12490, v240
	ds_read_b128 v[206:209], v87
	v_add_u32_e32 v87, 0x144a0, v240
	s_waitcnt lgkmcnt(1)
	v_pk_fma_f32 v[212:213], v[194:195], v[202:203], v[228:229] op_sel_hi:[1,0,1]
	s_nop 0
	v_pk_fma_f32 v[202:203], v[192:193], v[202:203], v[212:213] op_sel:[0,1,0]
	s_waitcnt lgkmcnt(0)
	v_pk_fma_f32 v[216:217], v[194:195], v[206:207], v[236:237] op_sel_hi:[1,0,1]
	v_mov_b32_e32 v118, v205
	v_pk_fma_f32 v[202:203], v[190:191], v[204:205], v[202:203] op_sel_hi:[1,0,1]
	v_pk_fma_f32 v[204:205], v[192:193], v[206:207], v[216:217] op_sel:[0,1,0]
	ds_read_b128 v[216:219], v87
	v_add_u32_e32 v87, 0x164b0, v240
	ds_read_b128 v[222:225], v87
	v_pk_fma_f32 v[202:203], v[52:53], v[118:119], v[202:203] op_sel_hi:[1,0,1]
	v_pk_fma_f32 v[204:205], v[190:191], v[208:209], v[204:205] op_sel_hi:[1,0,1]
	s_waitcnt lgkmcnt(1)
	v_pk_fma_f32 v[206:207], v[194:195], v[216:217], v[220:221] op_sel_hi:[1,0,1]
	v_mov_b32_e32 v118, v209
	v_pk_fma_f32 v[206:207], v[192:193], v[216:217], v[206:207] op_sel:[0,1,0]
	s_waitcnt lgkmcnt(0)
	v_pk_fma_f32 v[208:209], v[194:195], v[222:223], v[226:227] op_sel_hi:[1,0,1]
	v_pk_fma_f32 v[204:205], v[52:53], v[118:119], v[204:205] op_sel_hi:[1,0,1]
	v_pk_fma_f32 v[206:207], v[190:191], v[218:219], v[206:207] op_sel_hi:[1,0,1]
	v_mov_b32_e32 v118, v219
	v_pk_fma_f32 v[208:209], v[192:193], v[222:223], v[208:209] op_sel:[0,1,0]
	v_pk_fma_f32 v[206:207], v[52:53], v[118:119], v[206:207] op_sel_hi:[1,0,1]
	v_pk_fma_f32 v[208:209], v[190:191], v[224:225], v[208:209] op_sel_hi:[1,0,1]
	v_mov_b32_e32 v118, v225
	v_pk_fma_f32 v[208:209], v[52:53], v[118:119], v[208:209] op_sel_hi:[1,0,1]
	v_add_u32_e32 v87, 0x184c0, v240
	ds_read_b128 v[216:219], v87
	v_add_u32_e32 v87, 0x1a4d0, v240
	ds_read_b128 v[220:223], v87
	v_add_u32_e32 v87, 0x1c4e0, v240
	s_waitcnt lgkmcnt(1)
	v_pk_fma_f32 v[212:213], v[194:195], v[216:217], v[214:215] op_sel_hi:[1,0,1]
	s_nop 0
	v_pk_fma_f32 v[212:213], v[192:193], v[216:217], v[212:213] op_sel:[0,1,0]
	s_waitcnt lgkmcnt(0)
	v_pk_fma_f32 v[214:215], v[194:195], v[220:221], v[232:233] op_sel_hi:[1,0,1]
	v_mov_b32_e32 v118, v219
	v_pk_fma_f32 v[212:213], v[190:191], v[218:219], v[212:213] op_sel_hi:[1,0,1]
	v_pk_fma_f32 v[214:215], v[192:193], v[220:221], v[214:215] op_sel:[0,1,0]
	ds_read_b128 v[216:219], v87
	v_add_u32_e32 v87, 0x1e4f0, v240
	v_pk_fma_f32 v[212:213], v[52:53], v[118:119], v[212:213] op_sel_hi:[1,0,1]
	v_pk_fma_f32 v[214:215], v[190:191], v[222:223], v[214:215] op_sel_hi:[1,0,1]
	v_mov_b32_e32 v118, v223
	ds_read_b128 v[220:223], v87
	s_waitcnt lgkmcnt(1)
	v_pk_fma_f32 v[210:211], v[194:195], v[216:217], v[210:211] op_sel_hi:[1,0,1]
	v_pk_fma_f32 v[214:215], v[52:53], v[118:119], v[214:215] op_sel_hi:[1,0,1]
	v_pk_fma_f32 v[210:211], v[192:193], v[216:217], v[210:211] op_sel:[0,1,0]
	v_mov_b32_e32 v118, v219
	s_waitcnt lgkmcnt(0)
	v_pk_fma_f32 v[60:61], v[194:195], v[220:221], v[60:61] op_sel_hi:[1,0,1]
	v_pk_fma_f32 v[210:211], v[190:191], v[218:219], v[210:211] op_sel_hi:[1,0,1]
	v_pk_fma_f32 v[60:61], v[192:193], v[220:221], v[60:61] op_sel:[0,1,0]
	v_pk_fma_f32 v[210:211], v[52:53], v[118:119], v[210:211] op_sel_hi:[1,0,1]
	v_pk_fma_f32 v[60:61], v[190:191], v[222:223], v[60:61] op_sel_hi:[1,0,1]
	v_mov_b32_e32 v118, v223
	v_pk_fma_f32 v[60:61], v[52:53], v[118:119], v[60:61] op_sel_hi:[1,0,1]
	v_mov_b32_e32 v118, v46
	v_mov_b32_e32 v179, v186
	v_mul_f32_e32 v87, v83, v187
	v_pk_mul_f32 v[52:53], v[118:119], v[178:179]
	v_mov_b32_e32 v118, v47
	v_mov_b32_e32 v177, v184
	s_waitcnt vmcnt(11)
	v_fma_f32 v178, v52, v87, v42
	v_fma_f32 v179, v52, v53, v42
	v_mul_f32_e32 v42, v83, v185
	v_pk_mul_f32 v[46:47], v[118:119], v[176:177]
	v_mov_b32_e32 v118, v48
	v_mov_b32_e32 v175, v182
	v_fma_f32 v42, v46, v42, v43
	v_fma_f32 v43, v46, v47, v43
	v_mul_f32_e32 v52, v83, v183
	v_pk_mul_f32 v[46:47], v[118:119], v[174:175]
	v_mov_b32_e32 v118, v49
	v_mov_b32_e32 v173, v180
	v_fma_f32 v176, v46, v52, v44
	v_fma_f32 v177, v46, v47, v44
	v_mul_f32_e32 v44, v83, v181
	v_pk_mul_f32 v[46:47], v[118:119], v[172:173]
	ds_read_b128 v[172:175], v240 offset:10256
	v_fma_f32 v44, v46, v44, v45
	v_fmac_f32_e32 v45, v46, v47
	v_cvt_pk_bf16_f32 v46, v178, v42
	v_cvt_pk_bf16_f32 v47, v176, v44
	global_store_dwordx2 v[58:59], v[46:47], off offset:1024 sc1
	ds_read_b128 v[46:49], v240 offset:2048
	v_cvt_pk_bf16_f32 v52, v179, v43
	v_cvt_pk_bf16_f32 v53, v177, v45
	global_store_dwordx2 v[62:63], v[52:53], off offset:1024 sc1
	s_waitcnt lgkmcnt(1)
	v_mov_b32_e32 v52, v175
	s_waitcnt lgkmcnt(0)
	v_pk_fma_f32 v[50:51], v[178:179], v[46:47], v[50:51] op_sel_hi:[1,0,1]
	s_nop 0
	v_pk_fma_f32 v[46:47], v[42:43], v[46:47], v[50:51] op_sel:[0,1,0]
	s_nop 0
	v_pk_fma_f32 v[46:47], v[176:177], v[48:49], v[46:47] op_sel_hi:[1,0,1]
	v_mov_b32_e32 v48, v49
	v_pk_fma_f32 v[180:181], v[44:45], v[48:49], v[46:47] op_sel_hi:[1,0,1]
	v_pk_fma_f32 v[46:47], v[178:179], v[172:173], v[64:65] op_sel_hi:[1,0,1]
	s_nop 0
	v_pk_fma_f32 v[50:51], v[42:43], v[172:173], v[46:47] op_sel:[0,1,0]
	ds_read_b128 v[46:49], v240 offset:18464
	v_pk_fma_f32 v[50:51], v[176:177], v[174:175], v[50:51] op_sel_hi:[1,0,1]
	s_nop 0
	v_pk_fma_f32 v[64:65], v[44:45], v[52:53], v[50:51] op_sel_hi:[1,0,1]
	ds_read_b128 v[50:53], v240 offset:26672
	s_waitcnt lgkmcnt(1)
	v_pk_fma_f32 v[54:55], v[178:179], v[46:47], v[54:55] op_sel_hi:[1,0,1]
	s_nop 0
	v_pk_fma_f32 v[46:47], v[42:43], v[46:47], v[54:55] op_sel:[0,1,0]
	s_nop 0
	v_pk_fma_f32 v[46:47], v[176:177], v[48:49], v[46:47] op_sel_hi:[1,0,1]
	v_mov_b32_e32 v48, v49
	v_pk_fma_f32 v[54:55], v[44:45], v[48:49], v[46:47] op_sel_hi:[1,0,1]
	s_waitcnt lgkmcnt(0)
	v_pk_fma_f32 v[46:47], v[178:179], v[50:51], v[56:57] op_sel_hi:[1,0,1]
	v_mov_b32_e32 v48, v53
	v_pk_fma_f32 v[46:47], v[42:43], v[50:51], v[46:47] op_sel:[0,1,0]
	s_nop 0
	v_pk_fma_f32 v[46:47], v[176:177], v[52:53], v[46:47] op_sel_hi:[1,0,1]
	s_nop 0
	v_pk_fma_f32 v[56:57], v[44:45], v[48:49], v[46:47] op_sel_hi:[1,0,1]
	ds_read_b128 v[46:49], v240 offset:34880
	ds_read_b128 v[50:53], v240 offset:43088
	s_waitcnt lgkmcnt(1)
	v_pk_fma_f32 v[172:173], v[178:179], v[46:47], v[188:189] op_sel_hi:[1,0,1]
	s_nop 0
	v_pk_fma_f32 v[46:47], v[42:43], v[46:47], v[172:173] op_sel:[0,1,0]
	v_mov_b32_e32 v118, v49
	v_pk_fma_f32 v[46:47], v[176:177], v[48:49], v[46:47] op_sel_hi:[1,0,1]
	s_waitcnt lgkmcnt(0)
	v_pk_fma_f32 v[174:175], v[178:179], v[50:51], v[196:197] op_sel_hi:[1,0,1]
	v_pk_fma_f32 v[172:173], v[44:45], v[118:119], v[46:47] op_sel_hi:[1,0,1]
	ds_read_b128 v[46:49], v240 offset:51296
	v_pk_fma_f32 v[50:51], v[42:43], v[50:51], v[174:175] op_sel:[0,1,0]
	s_nop 0
	v_pk_fma_f32 v[50:51], v[176:177], v[52:53], v[50:51] op_sel_hi:[1,0,1]
	v_mov_b32_e32 v52, v53
	v_pk_fma_f32 v[174:175], v[44:45], v[52:53], v[50:51] op_sel_hi:[1,0,1]
	ds_read_b128 v[50:53], v240 offset:59504
	s_waitcnt lgkmcnt(1)
	v_pk_fma_f32 v[182:183], v[178:179], v[46:47], v[198:199] op_sel_hi:[1,0,1]
	s_nop 0
	v_pk_fma_f32 v[46:47], v[42:43], v[46:47], v[182:183] op_sel:[0,1,0]
	s_nop 0
	v_pk_fma_f32 v[46:47], v[176:177], v[48:49], v[46:47] op_sel_hi:[1,0,1]
	v_mov_b32_e32 v48, v49
	v_pk_fma_f32 v[182:183], v[44:45], v[48:49], v[46:47] op_sel_hi:[1,0,1]
	s_waitcnt lgkmcnt(0)
	v_pk_fma_f32 v[46:47], v[178:179], v[50:51], v[200:201] op_sel_hi:[1,0,1]
	v_mov_b32_e32 v48, v53
	v_pk_fma_f32 v[46:47], v[42:43], v[50:51], v[46:47] op_sel:[0,1,0]
	s_nop 0
	v_pk_fma_f32 v[46:47], v[176:177], v[52:53], v[46:47] op_sel_hi:[1,0,1]
	s_nop 0
	v_pk_fma_f32 v[184:185], v[44:45], v[48:49], v[46:47] op_sel_hi:[1,0,1]
	v_add_u32_e32 v46, 0x10880, v240
	ds_read_b128 v[46:49], v46
	v_add_u32_e32 v50, 0x12890, v240
	ds_read_b128 v[50:53], v50
	s_waitcnt lgkmcnt(1)
	v_pk_fma_f32 v[186:187], v[178:179], v[46:47], v[202:203] op_sel_hi:[1,0,1]
	s_nop 0
	v_pk_fma_f32 v[46:47], v[42:43], v[46:47], v[186:187] op_sel:[0,1,0]
	v_mov_b32_e32 v118, v49
	v_pk_fma_f32 v[46:47], v[176:177], v[48:49], v[46:47] op_sel_hi:[1,0,1]
	s_waitcnt lgkmcnt(0)
	v_pk_fma_f32 v[188:189], v[178:179], v[50:51], v[204:205] op_sel_hi:[1,0,1]
	v_pk_fma_f32 v[186:187], v[44:45], v[118:119], v[46:47] op_sel_hi:[1,0,1]
	v_add_u32_e32 v46, 0x148a0, v240
	v_pk_fma_f32 v[50:51], v[42:43], v[50:51], v[188:189] op_sel:[0,1,0]
	ds_read_b128 v[46:49], v46
	v_pk_fma_f32 v[50:51], v[176:177], v[52:53], v[50:51] op_sel_hi:[1,0,1]
	v_mov_b32_e32 v52, v53
	v_pk_fma_f32 v[188:189], v[44:45], v[52:53], v[50:51] op_sel_hi:[1,0,1]
	v_add_u32_e32 v50, 0x168b0, v240
	ds_read_b128 v[50:53], v50
	s_waitcnt lgkmcnt(1)
	v_pk_fma_f32 v[190:191], v[178:179], v[46:47], v[206:207] op_sel_hi:[1,0,1]
	s_nop 0
	v_pk_fma_f32 v[46:47], v[42:43], v[46:47], v[190:191] op_sel:[0,1,0]
	s_nop 0
	v_pk_fma_f32 v[46:47], v[176:177], v[48:49], v[46:47] op_sel_hi:[1,0,1]
	v_mov_b32_e32 v48, v49
	v_pk_fma_f32 v[190:191], v[44:45], v[48:49], v[46:47] op_sel_hi:[1,0,1]
	s_waitcnt lgkmcnt(0)
	v_pk_fma_f32 v[46:47], v[178:179], v[50:51], v[208:209] op_sel_hi:[1,0,1]
	v_mov_b32_e32 v48, v53
	v_pk_fma_f32 v[46:47], v[42:43], v[50:51], v[46:47] op_sel:[0,1,0]
	s_nop 0
	v_pk_fma_f32 v[46:47], v[176:177], v[52:53], v[46:47] op_sel_hi:[1,0,1]
	s_nop 0
	v_pk_fma_f32 v[192:193], v[44:45], v[48:49], v[46:47] op_sel_hi:[1,0,1]
	v_add_u32_e32 v46, 0x188c0, v240
	ds_read_b128 v[46:49], v46
	v_add_u32_e32 v50, 0x1a8d0, v240
	ds_read_b128 v[50:53], v50
	s_waitcnt lgkmcnt(1)
	v_pk_fma_f32 v[194:195], v[178:179], v[46:47], v[212:213] op_sel_hi:[1,0,1]
	s_nop 0
	v_pk_fma_f32 v[46:47], v[42:43], v[46:47], v[194:195] op_sel:[0,1,0]
	v_mov_b32_e32 v118, v49
	v_pk_fma_f32 v[46:47], v[176:177], v[48:49], v[46:47] op_sel_hi:[1,0,1]
	s_waitcnt lgkmcnt(0)
	v_pk_fma_f32 v[196:197], v[178:179], v[50:51], v[214:215] op_sel_hi:[1,0,1]
	v_pk_fma_f32 v[194:195], v[44:45], v[118:119], v[46:47] op_sel_hi:[1,0,1]
	v_add_u32_e32 v46, 0x1c8e0, v240
	v_pk_fma_f32 v[50:51], v[42:43], v[50:51], v[196:197] op_sel:[0,1,0]
	ds_read_b128 v[46:49], v46
	v_pk_fma_f32 v[50:51], v[176:177], v[52:53], v[50:51] op_sel_hi:[1,0,1]
	v_mov_b32_e32 v52, v53
	v_pk_fma_f32 v[196:197], v[44:45], v[52:53], v[50:51] op_sel_hi:[1,0,1]
	v_add_u32_e32 v50, 0x1e8f0, v240
	ds_read_b128 v[50:53], v50
	s_waitcnt lgkmcnt(1)
	v_pk_fma_f32 v[198:199], v[178:179], v[46:47], v[210:211] op_sel_hi:[1,0,1]
	s_nop 0
	v_pk_fma_f32 v[46:47], v[42:43], v[46:47], v[198:199] op_sel:[0,1,0]
	s_nop 0
	v_pk_fma_f32 v[46:47], v[176:177], v[48:49], v[46:47] op_sel_hi:[1,0,1]
	v_mov_b32_e32 v48, v49
	v_pk_fma_f32 v[46:47], v[44:45], v[48:49], v[46:47] op_sel_hi:[1,0,1]
	s_waitcnt lgkmcnt(0)
	v_pk_fma_f32 v[48:49], v[178:179], v[50:51], v[60:61] op_sel_hi:[1,0,1]
	s_nop 0
	v_pk_fma_f32 v[42:43], v[42:43], v[50:51], v[48:49] op_sel:[0,1,0]
	v_mov_b32_e32 v48, v53
	v_pk_fma_f32 v[42:43], v[176:177], v[52:53], v[42:43] op_sel_hi:[1,0,1]
	s_nop 0
	v_pk_fma_f32 v[48:49], v[44:45], v[48:49], v[42:43] op_sel_hi:[1,0,1]
	v_mov_b32_e32 v118, v38
	v_mov_b32_e32 v161, v168
	v_mul_f32_e32 v44, v83, v169
	v_pk_mul_f32 v[42:43], v[118:119], v[160:161]
	v_mov_b32_e32 v118, v39
	v_mov_b32_e32 v157, v166
	s_waitcnt vmcnt(12)
	v_fma_f32 v50, v42, v44, v34
	v_fma_f32 v51, v42, v43, v34
	v_mul_f32_e32 v34, v83, v167
	v_pk_mul_f32 v[38:39], v[118:119], v[156:157]
	v_mov_b32_e32 v118, v40
	v_mov_b32_e32 v155, v164
	v_fma_f32 v34, v38, v34, v35
	v_fma_f32 v35, v38, v39, v35
	v_mul_f32_e32 v42, v83, v165
	v_pk_mul_f32 v[38:39], v[118:119], v[154:155]
	v_mov_b32_e32 v118, v41
	v_mov_b32_e32 v153, v162
	v_fma_f32 v52, v38, v42, v36
	v_fma_f32 v53, v38, v39, v36
	v_mul_f32_e32 v36, v83, v163
	v_pk_mul_f32 v[38:39], v[118:119], v[152:153]
	v_cvt_pk_bf16_f32 v42, v51, v35
	v_fma_f32 v36, v38, v36, v37
	v_fmac_f32_e32 v37, v38, v39
	v_cvt_pk_bf16_f32 v38, v50, v34
	v_cvt_pk_bf16_f32 v39, v52, v36
	global_store_dwordx2 v[58:59], v[38:39], off offset:1536 sc1
	ds_read_b128 v[38:41], v240 offset:3072
	v_cvt_pk_bf16_f32 v43, v53, v37
	global_store_dwordx2 v[62:63], v[42:43], off offset:1536 sc1
	ds_read_b128 v[42:45], v240 offset:11280
	s_waitcnt lgkmcnt(1)
	v_pk_fma_f32 v[60:61], v[50:51], v[38:39], v[180:181] op_sel_hi:[1,0,1]
	s_nop 0
	v_pk_fma_f32 v[38:39], v[34:35], v[38:39], v[60:61] op_sel:[0,1,0]
	s_nop 0
	v_pk_fma_f32 v[38:39], v[52:53], v[40:41], v[38:39] op_sel_hi:[1,0,1]
	v_mov_b32_e32 v40, v41
	v_pk_fma_f32 v[60:61], v[36:37], v[40:41], v[38:39] op_sel_hi:[1,0,1]
	s_waitcnt lgkmcnt(0)
	v_pk_fma_f32 v[38:39], v[50:51], v[42:43], v[64:65] op_sel_hi:[1,0,1]
	s_nop 0
	v_pk_fma_f32 v[42:43], v[34:35], v[42:43], v[38:39] op_sel:[0,1,0]
	ds_read_b128 v[38:41], v240 offset:19488
	v_pk_fma_f32 v[42:43], v[52:53], v[44:45], v[42:43] op_sel_hi:[1,0,1]
	v_mov_b32_e32 v44, v45
	v_pk_fma_f32 v[64:65], v[36:37], v[44:45], v[42:43] op_sel_hi:[1,0,1]
	ds_read_b128 v[42:45], v240 offset:27696
	s_waitcnt lgkmcnt(1)
	v_pk_fma_f32 v[54:55], v[50:51], v[38:39], v[54:55] op_sel_hi:[1,0,1]
	s_nop 0
	v_pk_fma_f32 v[38:39], v[34:35], v[38:39], v[54:55] op_sel:[0,1,0]
	s_nop 0
	v_pk_fma_f32 v[38:39], v[52:53], v[40:41], v[38:39] op_sel_hi:[1,0,1]
	v_mov_b32_e32 v40, v41
	v_pk_fma_f32 v[54:55], v[36:37], v[40:41], v[38:39] op_sel_hi:[1,0,1]
	s_waitcnt lgkmcnt(0)
	v_pk_fma_f32 v[38:39], v[50:51], v[42:43], v[56:57] op_sel_hi:[1,0,1]
	v_mov_b32_e32 v40, v45
	v_pk_fma_f32 v[38:39], v[34:35], v[42:43], v[38:39] op_sel:[0,1,0]
	s_nop 0
	v_pk_fma_f32 v[38:39], v[52:53], v[44:45], v[38:39] op_sel_hi:[1,0,1]
	s_nop 0
	v_pk_fma_f32 v[56:57], v[36:37], v[40:41], v[38:39] op_sel_hi:[1,0,1]
	ds_read_b128 v[38:41], v240 offset:35904
	ds_read_b128 v[42:45], v240 offset:44112
	s_waitcnt lgkmcnt(1)
	v_pk_fma_f32 v[152:153], v[50:51], v[38:39], v[172:173] op_sel_hi:[1,0,1]
	s_nop 0
	v_pk_fma_f32 v[38:39], v[34:35], v[38:39], v[152:153] op_sel:[0,1,0]
	v_mov_b32_e32 v118, v41
	v_pk_fma_f32 v[38:39], v[52:53], v[40:41], v[38:39] op_sel_hi:[1,0,1]
	s_waitcnt lgkmcnt(0)
	v_pk_fma_f32 v[154:155], v[50:51], v[42:43], v[174:175] op_sel_hi:[1,0,1]
	v_pk_fma_f32 v[152:153], v[36:37], v[118:119], v[38:39] op_sel_hi:[1,0,1]
	ds_read_b128 v[38:41], v240 offset:52320
	v_pk_fma_f32 v[42:43], v[34:35], v[42:43], v[154:155] op_sel:[0,1,0]
	s_nop 0
	v_pk_fma_f32 v[42:43], v[52:53], v[44:45], v[42:43] op_sel_hi:[1,0,1]
	v_mov_b32_e32 v44, v45
	v_pk_fma_f32 v[154:155], v[36:37], v[44:45], v[42:43] op_sel_hi:[1,0,1]
	ds_read_b128 v[42:45], v240 offset:60528
	s_waitcnt lgkmcnt(1)
	v_pk_fma_f32 v[156:157], v[50:51], v[38:39], v[182:183] op_sel_hi:[1,0,1]
	s_nop 0
	v_pk_fma_f32 v[38:39], v[34:35], v[38:39], v[156:157] op_sel:[0,1,0]
	s_nop 0
	v_pk_fma_f32 v[38:39], v[52:53], v[40:41], v[38:39] op_sel_hi:[1,0,1]
	v_mov_b32_e32 v40, v41
	v_pk_fma_f32 v[156:157], v[36:37], v[40:41], v[38:39] op_sel_hi:[1,0,1]
	s_waitcnt lgkmcnt(0)
	v_pk_fma_f32 v[38:39], v[50:51], v[42:43], v[184:185] op_sel_hi:[1,0,1]
	v_mov_b32_e32 v40, v45
	v_pk_fma_f32 v[38:39], v[34:35], v[42:43], v[38:39] op_sel:[0,1,0]
	s_nop 0
	v_pk_fma_f32 v[38:39], v[52:53], v[44:45], v[38:39] op_sel_hi:[1,0,1]
	s_nop 0
	v_pk_fma_f32 v[160:161], v[36:37], v[40:41], v[38:39] op_sel_hi:[1,0,1]
	v_add_u32_e32 v38, 0x10c80, v240
	ds_read_b128 v[38:41], v38
	v_add_u32_e32 v42, 0x12c90, v240
	ds_read_b128 v[42:45], v42
	s_waitcnt lgkmcnt(1)
	v_pk_fma_f32 v[162:163], v[50:51], v[38:39], v[186:187] op_sel_hi:[1,0,1]
	s_nop 0
	v_pk_fma_f32 v[38:39], v[34:35], v[38:39], v[162:163] op_sel:[0,1,0]
	v_mov_b32_e32 v118, v41
	v_pk_fma_f32 v[38:39], v[52:53], v[40:41], v[38:39] op_sel_hi:[1,0,1]
	s_waitcnt lgkmcnt(0)
	v_pk_fma_f32 v[164:165], v[50:51], v[42:43], v[188:189] op_sel_hi:[1,0,1]
	v_pk_fma_f32 v[162:163], v[36:37], v[118:119], v[38:39] op_sel_hi:[1,0,1]
	v_add_u32_e32 v38, 0x14ca0, v240
	v_pk_fma_f32 v[42:43], v[34:35], v[42:43], v[164:165] op_sel:[0,1,0]
	ds_read_b128 v[38:41], v38
	v_pk_fma_f32 v[42:43], v[52:53], v[44:45], v[42:43] op_sel_hi:[1,0,1]
	v_mov_b32_e32 v44, v45
	v_pk_fma_f32 v[164:165], v[36:37], v[44:45], v[42:43] op_sel_hi:[1,0,1]
	v_add_u32_e32 v42, 0x16cb0, v240
	ds_read_b128 v[42:45], v42
	s_waitcnt lgkmcnt(1)
	v_pk_fma_f32 v[166:167], v[50:51], v[38:39], v[190:191] op_sel_hi:[1,0,1]
	s_nop 0
	v_pk_fma_f32 v[38:39], v[34:35], v[38:39], v[166:167] op_sel:[0,1,0]
	s_nop 0
	v_pk_fma_f32 v[38:39], v[52:53], v[40:41], v[38:39] op_sel_hi:[1,0,1]
	v_mov_b32_e32 v40, v41
	v_pk_fma_f32 v[166:167], v[36:37], v[40:41], v[38:39] op_sel_hi:[1,0,1]
	s_waitcnt lgkmcnt(0)
	v_pk_fma_f32 v[38:39], v[50:51], v[42:43], v[192:193] op_sel_hi:[1,0,1]
	v_mov_b32_e32 v40, v45
	v_pk_fma_f32 v[38:39], v[34:35], v[42:43], v[38:39] op_sel:[0,1,0]
	s_nop 0
	v_pk_fma_f32 v[38:39], v[52:53], v[44:45], v[38:39] op_sel_hi:[1,0,1]
	s_nop 0
	v_pk_fma_f32 v[168:169], v[36:37], v[40:41], v[38:39] op_sel_hi:[1,0,1]
	v_add_u32_e32 v38, 0x18cc0, v240
	ds_read_b128 v[38:41], v38
	v_add_u32_e32 v42, 0x1acd0, v240
	ds_read_b128 v[42:45], v42
	s_waitcnt lgkmcnt(1)
	v_pk_fma_f32 v[172:173], v[50:51], v[38:39], v[194:195] op_sel_hi:[1,0,1]
	s_nop 0
	v_pk_fma_f32 v[38:39], v[34:35], v[38:39], v[172:173] op_sel:[0,1,0]
	v_mov_b32_e32 v118, v41
	v_pk_fma_f32 v[38:39], v[52:53], v[40:41], v[38:39] op_sel_hi:[1,0,1]
	s_waitcnt lgkmcnt(0)
	v_pk_fma_f32 v[174:175], v[50:51], v[42:43], v[196:197] op_sel_hi:[1,0,1]
	v_pk_fma_f32 v[172:173], v[36:37], v[118:119], v[38:39] op_sel_hi:[1,0,1]
	v_add_u32_e32 v38, 0x1cce0, v240
	v_pk_fma_f32 v[42:43], v[34:35], v[42:43], v[174:175] op_sel:[0,1,0]
	ds_read_b128 v[38:41], v38
	v_pk_fma_f32 v[42:43], v[52:53], v[44:45], v[42:43] op_sel_hi:[1,0,1]
	v_mov_b32_e32 v44, v45
	v_pk_fma_f32 v[174:175], v[36:37], v[44:45], v[42:43] op_sel_hi:[1,0,1]
	v_add_u32_e32 v42, 0x1ecf0, v240
	ds_read_b128 v[42:45], v42
	s_waitcnt lgkmcnt(1)
	v_pk_fma_f32 v[46:47], v[50:51], v[38:39], v[46:47] op_sel_hi:[1,0,1]
	s_nop 0
	v_pk_fma_f32 v[38:39], v[34:35], v[38:39], v[46:47] op_sel:[0,1,0]
	s_nop 0
	v_pk_fma_f32 v[38:39], v[52:53], v[40:41], v[38:39] op_sel_hi:[1,0,1]
	v_mov_b32_e32 v40, v41
	v_pk_fma_f32 v[38:39], v[36:37], v[40:41], v[38:39] op_sel_hi:[1,0,1]
	s_waitcnt lgkmcnt(0)
	v_pk_fma_f32 v[40:41], v[50:51], v[42:43], v[48:49] op_sel_hi:[1,0,1]
	s_nop 0
	v_pk_fma_f32 v[34:35], v[34:35], v[42:43], v[40:41] op_sel:[0,1,0]
	v_mov_b32_e32 v40, v45
	v_pk_fma_f32 v[34:35], v[52:53], v[44:45], v[34:35] op_sel_hi:[1,0,1]
	s_nop 0
	v_pk_fma_f32 v[40:41], v[36:37], v[40:41], v[34:35] op_sel_hi:[1,0,1]
	v_mov_b32_e32 v118, v30
	v_mov_b32_e32 v151, v142
	v_mul_f32_e32 v36, v83, v134
	v_pk_mul_f32 v[34:35], v[118:119], v[150:151]
	v_mov_b32_e32 v118, v31
	v_mov_b32_e32 v149, v140
	s_waitcnt vmcnt(13)
	v_fma_f32 v42, v34, v36, v26
	v_fma_f32 v43, v34, v35, v26
	v_mul_f32_e32 v26, v83, v132
	v_pk_mul_f32 v[30:31], v[118:119], v[148:149]
	v_mov_b32_e32 v118, v32
	v_mov_b32_e32 v147, v138
	v_fma_f32 v26, v30, v26, v27
	v_fma_f32 v27, v30, v31, v27
	v_mul_f32_e32 v34, v83, v130
	v_pk_mul_f32 v[30:31], v[118:119], v[146:147]
	v_mov_b32_e32 v118, v33
	v_mov_b32_e32 v145, v136
	v_fma_f32 v44, v30, v34, v28
	v_fma_f32 v45, v30, v31, v28
	v_mul_f32_e32 v28, v83, v128
	v_pk_mul_f32 v[30:31], v[118:119], v[144:145]
	v_cvt_pk_bf16_f32 v34, v43, v27
	v_fma_f32 v28, v30, v28, v29
	v_fmac_f32_e32 v29, v30, v31
	v_cvt_pk_bf16_f32 v30, v42, v26
	v_cvt_pk_bf16_f32 v31, v44, v28
	global_store_dwordx2 v[58:59], v[30:31], off offset:2048 sc1
	ds_read_b128 v[30:33], v240 offset:4096
	v_cvt_pk_bf16_f32 v35, v45, v29
	global_store_dwordx2 v[62:63], v[34:35], off offset:2048 sc1
	ds_read_b128 v[34:37], v240 offset:12304
	s_waitcnt lgkmcnt(1)
	v_pk_fma_f32 v[46:47], v[42:43], v[30:31], v[60:61] op_sel_hi:[1,0,1]
	s_nop 0
	v_pk_fma_f32 v[30:31], v[26:27], v[30:31], v[46:47] op_sel:[0,1,0]
	s_nop 0
	v_pk_fma_f32 v[30:31], v[44:45], v[32:33], v[30:31] op_sel_hi:[1,0,1]
	v_mov_b32_e32 v32, v33
	v_pk_fma_f32 v[46:47], v[28:29], v[32:33], v[30:31] op_sel_hi:[1,0,1]
	s_waitcnt lgkmcnt(0)
	v_pk_fma_f32 v[30:31], v[42:43], v[34:35], v[64:65] op_sel_hi:[1,0,1]
	s_nop 0
	v_pk_fma_f32 v[34:35], v[26:27], v[34:35], v[30:31] op_sel:[0,1,0]
	ds_read_b128 v[30:33], v240 offset:20512
	v_pk_fma_f32 v[34:35], v[44:45], v[36:37], v[34:35] op_sel_hi:[1,0,1]
	v_mov_b32_e32 v36, v37
	v_pk_fma_f32 v[48:49], v[28:29], v[36:37], v[34:35] op_sel_hi:[1,0,1]
	ds_read_b128 v[34:37], v240 offset:28720
	s_waitcnt lgkmcnt(1)
	v_pk_fma_f32 v[50:51], v[42:43], v[30:31], v[54:55] op_sel_hi:[1,0,1]
	s_nop 0
	v_pk_fma_f32 v[30:31], v[26:27], v[30:31], v[50:51] op_sel:[0,1,0]
	s_nop 0
	v_pk_fma_f32 v[30:31], v[44:45], v[32:33], v[30:31] op_sel_hi:[1,0,1]
	v_mov_b32_e32 v32, v33
	v_pk_fma_f32 v[50:51], v[28:29], v[32:33], v[30:31] op_sel_hi:[1,0,1]
	s_waitcnt lgkmcnt(0)
	v_pk_fma_f32 v[30:31], v[42:43], v[34:35], v[56:57] op_sel_hi:[1,0,1]
	v_mov_b32_e32 v32, v37
	v_pk_fma_f32 v[30:31], v[26:27], v[34:35], v[30:31] op_sel:[0,1,0]
	s_nop 0
	v_pk_fma_f32 v[30:31], v[44:45], v[36:37], v[30:31] op_sel_hi:[1,0,1]
	s_nop 0
	v_pk_fma_f32 v[52:53], v[28:29], v[32:33], v[30:31] op_sel_hi:[1,0,1]
	ds_read_b128 v[30:33], v240 offset:36928
	ds_read_b128 v[34:37], v240 offset:45136
	s_waitcnt lgkmcnt(1)
	v_pk_fma_f32 v[54:55], v[42:43], v[30:31], v[152:153] op_sel_hi:[1,0,1]
	s_nop 0
	v_pk_fma_f32 v[30:31], v[26:27], v[30:31], v[54:55] op_sel:[0,1,0]
	v_mov_b32_e32 v56, v33
	v_pk_fma_f32 v[30:31], v[44:45], v[32:33], v[30:31] op_sel_hi:[1,0,1]
	s_waitcnt lgkmcnt(0)
	v_pk_fma_f32 v[60:61], v[42:43], v[34:35], v[154:155] op_sel_hi:[1,0,1]
	v_pk_fma_f32 v[54:55], v[28:29], v[56:57], v[30:31] op_sel_hi:[1,0,1]
	ds_read_b128 v[30:33], v240 offset:53344
	v_pk_fma_f32 v[34:35], v[26:27], v[34:35], v[60:61] op_sel:[0,1,0]
	s_nop 0
	v_pk_fma_f32 v[34:35], v[44:45], v[36:37], v[34:35] op_sel_hi:[1,0,1]
	v_mov_b32_e32 v36, v37
	v_pk_fma_f32 v[56:57], v[28:29], v[36:37], v[34:35] op_sel_hi:[1,0,1]
	ds_read_b128 v[34:37], v240 offset:61552
	s_waitcnt lgkmcnt(1)
	v_pk_fma_f32 v[60:61], v[42:43], v[30:31], v[156:157] op_sel_hi:[1,0,1]
	s_nop 0
	v_pk_fma_f32 v[30:31], v[26:27], v[30:31], v[60:61] op_sel:[0,1,0]
	s_nop 0
	v_pk_fma_f32 v[30:31], v[44:45], v[32:33], v[30:31] op_sel_hi:[1,0,1]
	v_mov_b32_e32 v32, v33
	v_pk_fma_f32 v[60:61], v[28:29], v[32:33], v[30:31] op_sel_hi:[1,0,1]
	s_waitcnt lgkmcnt(0)
	v_pk_fma_f32 v[30:31], v[42:43], v[34:35], v[160:161] op_sel_hi:[1,0,1]
	v_mov_b32_e32 v32, v37
	v_pk_fma_f32 v[30:31], v[26:27], v[34:35], v[30:31] op_sel:[0,1,0]
	s_nop 0
	v_pk_fma_f32 v[30:31], v[44:45], v[36:37], v[30:31] op_sel_hi:[1,0,1]
	s_nop 0
	v_pk_fma_f32 v[64:65], v[28:29], v[32:33], v[30:31] op_sel_hi:[1,0,1]
	v_add_u32_e32 v30, 0x11080, v240
	ds_read_b128 v[30:33], v30
	v_add_u32_e32 v34, 0x13090, v240
	ds_read_b128 v[34:37], v34
	s_waitcnt lgkmcnt(1)
	v_pk_fma_f32 v[144:145], v[42:43], v[30:31], v[162:163] op_sel_hi:[1,0,1]
	s_nop 0
	v_pk_fma_f32 v[30:31], v[26:27], v[30:31], v[144:145] op_sel:[0,1,0]
	v_mov_b32_e32 v118, v33
	v_pk_fma_f32 v[30:31], v[44:45], v[32:33], v[30:31] op_sel_hi:[1,0,1]
	s_waitcnt lgkmcnt(0)
	v_pk_fma_f32 v[146:147], v[42:43], v[34:35], v[164:165] op_sel_hi:[1,0,1]
	v_pk_fma_f32 v[144:145], v[28:29], v[118:119], v[30:31] op_sel_hi:[1,0,1]
	v_add_u32_e32 v30, 0x150a0, v240
	v_pk_fma_f32 v[34:35], v[26:27], v[34:35], v[146:147] op_sel:[0,1,0]
	ds_read_b128 v[30:33], v30
	v_pk_fma_f32 v[34:35], v[44:45], v[36:37], v[34:35] op_sel_hi:[1,0,1]
	v_mov_b32_e32 v36, v37
	v_pk_fma_f32 v[146:147], v[28:29], v[36:37], v[34:35] op_sel_hi:[1,0,1]
	v_add_u32_e32 v34, 0x170b0, v240
	ds_read_b128 v[34:37], v34
	s_waitcnt lgkmcnt(1)
	v_pk_fma_f32 v[148:149], v[42:43], v[30:31], v[166:167] op_sel_hi:[1,0,1]
	s_nop 0
	v_pk_fma_f32 v[30:31], v[26:27], v[30:31], v[148:149] op_sel:[0,1,0]
	s_nop 0
	v_pk_fma_f32 v[30:31], v[44:45], v[32:33], v[30:31] op_sel_hi:[1,0,1]
	v_mov_b32_e32 v32, v33
	v_pk_fma_f32 v[148:149], v[28:29], v[32:33], v[30:31] op_sel_hi:[1,0,1]
	s_waitcnt lgkmcnt(0)
	v_pk_fma_f32 v[30:31], v[42:43], v[34:35], v[168:169] op_sel_hi:[1,0,1]
	v_mov_b32_e32 v32, v37
	v_pk_fma_f32 v[30:31], v[26:27], v[34:35], v[30:31] op_sel:[0,1,0]
	s_nop 0
	v_pk_fma_f32 v[30:31], v[44:45], v[36:37], v[30:31] op_sel_hi:[1,0,1]
	s_nop 0
	v_pk_fma_f32 v[150:151], v[28:29], v[32:33], v[30:31] op_sel_hi:[1,0,1]
	v_add_u32_e32 v30, 0x190c0, v240
	ds_read_b128 v[30:33], v30
	v_add_u32_e32 v34, 0x1b0d0, v240
	ds_read_b128 v[34:37], v34
	s_waitcnt lgkmcnt(1)
	v_pk_fma_f32 v[152:153], v[42:43], v[30:31], v[172:173] op_sel_hi:[1,0,1]
	s_nop 0
	v_pk_fma_f32 v[30:31], v[26:27], v[30:31], v[152:153] op_sel:[0,1,0]
	v_mov_b32_e32 v118, v33
	v_pk_fma_f32 v[30:31], v[44:45], v[32:33], v[30:31] op_sel_hi:[1,0,1]
	s_waitcnt lgkmcnt(0)
	v_pk_fma_f32 v[154:155], v[42:43], v[34:35], v[174:175] op_sel_hi:[1,0,1]
	v_pk_fma_f32 v[152:153], v[28:29], v[118:119], v[30:31] op_sel_hi:[1,0,1]
	v_add_u32_e32 v30, 0x1d0e0, v240
	v_pk_fma_f32 v[34:35], v[26:27], v[34:35], v[154:155] op_sel:[0,1,0]
	ds_read_b128 v[30:33], v30
	v_pk_fma_f32 v[34:35], v[44:45], v[36:37], v[34:35] op_sel_hi:[1,0,1]
	v_mov_b32_e32 v36, v37
	v_pk_fma_f32 v[154:155], v[28:29], v[36:37], v[34:35] op_sel_hi:[1,0,1]
	v_add_u32_e32 v34, 0x1f0f0, v240
	ds_read_b128 v[34:37], v34
	s_waitcnt lgkmcnt(1)
	v_pk_fma_f32 v[38:39], v[42:43], v[30:31], v[38:39] op_sel_hi:[1,0,1]
	s_nop 0
	v_pk_fma_f32 v[30:31], v[26:27], v[30:31], v[38:39] op_sel:[0,1,0]
	s_nop 0
	v_pk_fma_f32 v[30:31], v[44:45], v[32:33], v[30:31] op_sel_hi:[1,0,1]
	v_mov_b32_e32 v32, v33
	v_pk_fma_f32 v[30:31], v[28:29], v[32:33], v[30:31] op_sel_hi:[1,0,1]
	s_waitcnt lgkmcnt(0)
	v_pk_fma_f32 v[32:33], v[42:43], v[34:35], v[40:41] op_sel_hi:[1,0,1]
	s_nop 0
	v_pk_fma_f32 v[26:27], v[26:27], v[34:35], v[32:33] op_sel:[0,1,0]
	v_mov_b32_e32 v32, v37
	v_pk_fma_f32 v[26:27], v[44:45], v[36:37], v[26:27] op_sel_hi:[1,0,1]
	s_nop 0
	v_pk_fma_f32 v[32:33], v[28:29], v[32:33], v[26:27] op_sel_hi:[1,0,1]
	v_mov_b32_e32 v118, v22
	v_mov_b32_e32 v127, v143
	v_mul_f32_e32 v28, v83, v135
	v_pk_mul_f32 v[26:27], v[118:119], v[126:127]
	v_mov_b32_e32 v118, v23
	v_mov_b32_e32 v125, v141
	s_waitcnt vmcnt(14)
	v_fma_f32 v34, v26, v28, v14
	v_fma_f32 v35, v26, v27, v14
	v_mul_f32_e32 v14, v83, v133
	v_pk_mul_f32 v[22:23], v[118:119], v[124:125]
	v_mov_b32_e32 v118, v24
	v_mov_b32_e32 v123, v139
	v_fma_f32 v14, v22, v14, v15
	v_fma_f32 v15, v22, v23, v15
	v_mul_f32_e32 v26, v83, v131
	v_pk_mul_f32 v[22:23], v[118:119], v[122:123]
	v_mov_b32_e32 v118, v25
	v_mov_b32_e32 v121, v137
	v_fma_f32 v36, v22, v26, v16
	v_fma_f32 v37, v22, v23, v16
	v_mul_f32_e32 v16, v83, v129
	v_pk_mul_f32 v[22:23], v[118:119], v[120:121]
	v_cvt_pk_bf16_f32 v26, v35, v15
	v_fma_f32 v16, v22, v16, v17
	v_fmac_f32_e32 v17, v22, v23
	v_cvt_pk_bf16_f32 v22, v34, v14
	v_cvt_pk_bf16_f32 v23, v36, v16
	global_store_dwordx2 v[58:59], v[22:23], off offset:2560 sc1
	ds_read_b128 v[22:25], v240 offset:5120
	v_cvt_pk_bf16_f32 v27, v37, v17
	global_store_dwordx2 v[62:63], v[26:27], off offset:2560 sc1
	ds_read_b128 v[26:29], v240 offset:13328
	s_waitcnt lgkmcnt(1)
	v_pk_fma_f32 v[38:39], v[34:35], v[22:23], v[46:47] op_sel_hi:[1,0,1]
	s_nop 0
	v_pk_fma_f32 v[22:23], v[14:15], v[22:23], v[38:39] op_sel:[0,1,0]
	s_nop 0
	v_pk_fma_f32 v[22:23], v[36:37], v[24:25], v[22:23] op_sel_hi:[1,0,1]
	v_mov_b32_e32 v24, v25
	v_pk_fma_f32 v[38:39], v[16:17], v[24:25], v[22:23] op_sel_hi:[1,0,1]
	s_waitcnt lgkmcnt(0)
	v_pk_fma_f32 v[22:23], v[34:35], v[26:27], v[48:49] op_sel_hi:[1,0,1]
	s_nop 0
	v_pk_fma_f32 v[26:27], v[14:15], v[26:27], v[22:23] op_sel:[0,1,0]
	ds_read_b128 v[22:25], v240 offset:21536
	v_pk_fma_f32 v[26:27], v[36:37], v[28:29], v[26:27] op_sel_hi:[1,0,1]
	v_mov_b32_e32 v28, v29
	v_pk_fma_f32 v[40:41], v[16:17], v[28:29], v[26:27] op_sel_hi:[1,0,1]
	ds_read_b128 v[26:29], v240 offset:29744
	s_waitcnt lgkmcnt(1)
	v_pk_fma_f32 v[42:43], v[34:35], v[22:23], v[50:51] op_sel_hi:[1,0,1]
	s_nop 0
	v_pk_fma_f32 v[22:23], v[14:15], v[22:23], v[42:43] op_sel:[0,1,0]
	s_nop 0
	v_pk_fma_f32 v[22:23], v[36:37], v[24:25], v[22:23] op_sel_hi:[1,0,1]
	v_mov_b32_e32 v24, v25
	v_pk_fma_f32 v[42:43], v[16:17], v[24:25], v[22:23] op_sel_hi:[1,0,1]
	s_waitcnt lgkmcnt(0)
	v_pk_fma_f32 v[22:23], v[34:35], v[26:27], v[52:53] op_sel_hi:[1,0,1]
	v_mov_b32_e32 v24, v29
	v_pk_fma_f32 v[22:23], v[14:15], v[26:27], v[22:23] op_sel:[0,1,0]
	s_nop 0
	v_pk_fma_f32 v[22:23], v[36:37], v[28:29], v[22:23] op_sel_hi:[1,0,1]
	s_nop 0
	v_pk_fma_f32 v[44:45], v[16:17], v[24:25], v[22:23] op_sel_hi:[1,0,1]
	ds_read_b128 v[22:25], v240 offset:37952
	ds_read_b128 v[26:29], v240 offset:46160
	s_waitcnt lgkmcnt(1)
	v_pk_fma_f32 v[46:47], v[34:35], v[22:23], v[54:55] op_sel_hi:[1,0,1]
	s_nop 0
	v_pk_fma_f32 v[22:23], v[14:15], v[22:23], v[46:47] op_sel:[0,1,0]
	v_mov_b32_e32 v48, v25
	v_pk_fma_f32 v[22:23], v[36:37], v[24:25], v[22:23] op_sel_hi:[1,0,1]
	s_waitcnt lgkmcnt(0)
	v_pk_fma_f32 v[50:51], v[34:35], v[26:27], v[56:57] op_sel_hi:[1,0,1]
	v_pk_fma_f32 v[46:47], v[16:17], v[48:49], v[22:23] op_sel_hi:[1,0,1]
	ds_read_b128 v[22:25], v240 offset:54368
	v_pk_fma_f32 v[26:27], v[14:15], v[26:27], v[50:51] op_sel:[0,1,0]
	s_nop 0
	v_pk_fma_f32 v[26:27], v[36:37], v[28:29], v[26:27] op_sel_hi:[1,0,1]
	v_mov_b32_e32 v28, v29
	v_pk_fma_f32 v[48:49], v[16:17], v[28:29], v[26:27] op_sel_hi:[1,0,1]
	ds_read_b128 v[26:29], v240 offset:62576
	s_waitcnt lgkmcnt(1)
	v_pk_fma_f32 v[50:51], v[34:35], v[22:23], v[60:61] op_sel_hi:[1,0,1]
	s_nop 0
	v_pk_fma_f32 v[22:23], v[14:15], v[22:23], v[50:51] op_sel:[0,1,0]
	s_nop 0
	v_pk_fma_f32 v[22:23], v[36:37], v[24:25], v[22:23] op_sel_hi:[1,0,1]
	v_mov_b32_e32 v24, v25
	v_pk_fma_f32 v[50:51], v[16:17], v[24:25], v[22:23] op_sel_hi:[1,0,1]
	s_waitcnt lgkmcnt(0)
	v_pk_fma_f32 v[22:23], v[34:35], v[26:27], v[64:65] op_sel_hi:[1,0,1]
	v_mov_b32_e32 v24, v29
	v_pk_fma_f32 v[22:23], v[14:15], v[26:27], v[22:23] op_sel:[0,1,0]
	s_nop 0
	v_pk_fma_f32 v[22:23], v[36:37], v[28:29], v[22:23] op_sel_hi:[1,0,1]
	s_nop 0
	v_pk_fma_f32 v[52:53], v[16:17], v[24:25], v[22:23] op_sel_hi:[1,0,1]
	v_add_u32_e32 v22, 0x11480, v240
	ds_read_b128 v[22:25], v22
	v_add_u32_e32 v26, 0x13490, v240
	ds_read_b128 v[26:29], v26
	s_waitcnt lgkmcnt(1)
	v_pk_fma_f32 v[54:55], v[34:35], v[22:23], v[144:145] op_sel_hi:[1,0,1]
	s_nop 0
	v_pk_fma_f32 v[22:23], v[14:15], v[22:23], v[54:55] op_sel:[0,1,0]
	v_mov_b32_e32 v56, v25
	v_pk_fma_f32 v[22:23], v[36:37], v[24:25], v[22:23] op_sel_hi:[1,0,1]
	s_waitcnt lgkmcnt(0)
	v_pk_fma_f32 v[60:61], v[34:35], v[26:27], v[146:147] op_sel_hi:[1,0,1]
	v_pk_fma_f32 v[54:55], v[16:17], v[56:57], v[22:23] op_sel_hi:[1,0,1]
	v_add_u32_e32 v22, 0x154a0, v240
	v_pk_fma_f32 v[26:27], v[14:15], v[26:27], v[60:61] op_sel:[0,1,0]
	ds_read_b128 v[22:25], v22
	v_pk_fma_f32 v[26:27], v[36:37], v[28:29], v[26:27] op_sel_hi:[1,0,1]
	v_mov_b32_e32 v28, v29
	v_pk_fma_f32 v[56:57], v[16:17], v[28:29], v[26:27] op_sel_hi:[1,0,1]
	v_add_u32_e32 v26, 0x174b0, v240
	ds_read_b128 v[26:29], v26
	s_waitcnt lgkmcnt(1)
	v_pk_fma_f32 v[60:61], v[34:35], v[22:23], v[148:149] op_sel_hi:[1,0,1]
	s_nop 0
	v_pk_fma_f32 v[22:23], v[14:15], v[22:23], v[60:61] op_sel:[0,1,0]
	s_nop 0
	v_pk_fma_f32 v[22:23], v[36:37], v[24:25], v[22:23] op_sel_hi:[1,0,1]
	v_mov_b32_e32 v24, v25
	v_pk_fma_f32 v[60:61], v[16:17], v[24:25], v[22:23] op_sel_hi:[1,0,1]
	s_waitcnt lgkmcnt(0)
	v_pk_fma_f32 v[22:23], v[34:35], v[26:27], v[150:151] op_sel_hi:[1,0,1]
	v_mov_b32_e32 v24, v29
	v_pk_fma_f32 v[22:23], v[14:15], v[26:27], v[22:23] op_sel:[0,1,0]
	s_nop 0
	v_pk_fma_f32 v[22:23], v[36:37], v[28:29], v[22:23] op_sel_hi:[1,0,1]
	s_nop 0
	v_pk_fma_f32 v[64:65], v[16:17], v[24:25], v[22:23] op_sel_hi:[1,0,1]
	v_add_u32_e32 v22, 0x194c0, v240
	ds_read_b128 v[22:25], v22
	v_add_u32_e32 v26, 0x1b4d0, v240
	ds_read_b128 v[26:29], v26
	s_waitcnt lgkmcnt(1)
	v_pk_fma_f32 v[120:121], v[34:35], v[22:23], v[152:153] op_sel_hi:[1,0,1]
	s_nop 0
	v_pk_fma_f32 v[22:23], v[14:15], v[22:23], v[120:121] op_sel:[0,1,0]
	v_mov_b32_e32 v118, v25
	v_pk_fma_f32 v[22:23], v[36:37], v[24:25], v[22:23] op_sel_hi:[1,0,1]
	s_waitcnt lgkmcnt(0)
	v_pk_fma_f32 v[122:123], v[34:35], v[26:27], v[154:155] op_sel_hi:[1,0,1]
	v_pk_fma_f32 v[120:121], v[16:17], v[118:119], v[22:23] op_sel_hi:[1,0,1]
	v_add_u32_e32 v22, 0x1d4e0, v240
	v_pk_fma_f32 v[26:27], v[14:15], v[26:27], v[122:123] op_sel:[0,1,0]
	ds_read_b128 v[22:25], v22
	v_pk_fma_f32 v[26:27], v[36:37], v[28:29], v[26:27] op_sel_hi:[1,0,1]
	v_mov_b32_e32 v28, v29
	v_pk_fma_f32 v[122:123], v[16:17], v[28:29], v[26:27] op_sel_hi:[1,0,1]
	v_add_u32_e32 v26, 0x1f4f0, v240
	ds_read_b128 v[26:29], v26
	s_waitcnt lgkmcnt(1)
	v_pk_fma_f32 v[30:31], v[34:35], v[22:23], v[30:31] op_sel_hi:[1,0,1]
	s_nop 0
	v_pk_fma_f32 v[22:23], v[14:15], v[22:23], v[30:31] op_sel:[0,1,0]
	s_nop 0
	v_pk_fma_f32 v[22:23], v[36:37], v[24:25], v[22:23] op_sel_hi:[1,0,1]
	v_mov_b32_e32 v24, v25
	v_pk_fma_f32 v[22:23], v[16:17], v[24:25], v[22:23] op_sel_hi:[1,0,1]
	s_waitcnt lgkmcnt(0)
	v_pk_fma_f32 v[24:25], v[34:35], v[26:27], v[32:33] op_sel_hi:[1,0,1]
	s_nop 0
	v_pk_fma_f32 v[14:15], v[14:15], v[26:27], v[24:25] op_sel:[0,1,0]
	v_mov_b32_e32 v24, v29
	v_pk_fma_f32 v[14:15], v[36:37], v[28:29], v[14:15] op_sel_hi:[1,0,1]
	s_nop 0
	v_pk_fma_f32 v[24:25], v[16:17], v[24:25], v[14:15] op_sel_hi:[1,0,1]
	s_waitcnt vmcnt(15)
	v_mov_b32_e32 v118, v18
	v_mov_b32_e32 v117, v108
	v_mul_f32_e32 v16, v83, v100
	v_pk_mul_f32 v[14:15], v[118:119], v[116:117]
	v_mov_b32_e32 v118, v19
	v_mov_b32_e32 v115, v106
	s_waitcnt vmcnt(13)
	v_fma_f32 v26, v14, v16, v10
	v_fma_f32 v27, v14, v15, v10
	v_mul_f32_e32 v10, v83, v98
	v_pk_mul_f32 v[14:15], v[118:119], v[114:115]
	v_mov_b32_e32 v118, v20
	v_mov_b32_e32 v113, v104
	v_fma_f32 v10, v14, v10, v11
	v_fma_f32 v11, v14, v15, v11
	v_mul_f32_e32 v16, v83, v96
	v_pk_mul_f32 v[14:15], v[118:119], v[112:113]
	v_mov_b32_e32 v118, v21
	v_mov_b32_e32 v111, v102
	v_fma_f32 v28, v14, v16, v12
	v_fma_f32 v29, v14, v15, v12
	v_mul_f32_e32 v12, v83, v94
	v_pk_mul_f32 v[14:15], v[118:119], v[110:111]
	v_cvt_pk_bf16_f32 v18, v27, v11
	v_fma_f32 v12, v14, v12, v13
	v_fmac_f32_e32 v13, v14, v15
	v_cvt_pk_bf16_f32 v14, v26, v10
	v_cvt_pk_bf16_f32 v15, v28, v12
	global_store_dwordx2 v[58:59], v[14:15], off offset:3072 sc1
	ds_read_b128 v[14:17], v240 offset:6144
	v_cvt_pk_bf16_f32 v19, v29, v13
	global_store_dwordx2 v[62:63], v[18:19], off offset:3072 sc1
	ds_read_b128 v[18:21], v240 offset:14352
	s_waitcnt lgkmcnt(1)
	v_pk_fma_f32 v[30:31], v[26:27], v[14:15], v[38:39] op_sel_hi:[1,0,1]
	s_nop 0
	v_pk_fma_f32 v[14:15], v[10:11], v[14:15], v[30:31] op_sel:[0,1,0]
	s_nop 0
	v_pk_fma_f32 v[14:15], v[28:29], v[16:17], v[14:15] op_sel_hi:[1,0,1]
	v_mov_b32_e32 v16, v17
	v_pk_fma_f32 v[30:31], v[12:13], v[16:17], v[14:15] op_sel_hi:[1,0,1]
	s_waitcnt lgkmcnt(0)
	v_pk_fma_f32 v[14:15], v[26:27], v[18:19], v[40:41] op_sel_hi:[1,0,1]
	s_nop 0
	v_pk_fma_f32 v[18:19], v[10:11], v[18:19], v[14:15] op_sel:[0,1,0]
	ds_read_b128 v[14:17], v240 offset:22560
	v_pk_fma_f32 v[18:19], v[28:29], v[20:21], v[18:19] op_sel_hi:[1,0,1]
	v_mov_b32_e32 v20, v21
	v_pk_fma_f32 v[32:33], v[12:13], v[20:21], v[18:19] op_sel_hi:[1,0,1]
	ds_read_b128 v[18:21], v240 offset:30768
	s_waitcnt lgkmcnt(1)
	v_pk_fma_f32 v[34:35], v[26:27], v[14:15], v[42:43] op_sel_hi:[1,0,1]
	s_nop 0
	v_pk_fma_f32 v[14:15], v[10:11], v[14:15], v[34:35] op_sel:[0,1,0]
	s_nop 0
	v_pk_fma_f32 v[14:15], v[28:29], v[16:17], v[14:15] op_sel_hi:[1,0,1]
	v_mov_b32_e32 v16, v17
	v_pk_fma_f32 v[34:35], v[12:13], v[16:17], v[14:15] op_sel_hi:[1,0,1]
	s_waitcnt lgkmcnt(0)
	v_pk_fma_f32 v[14:15], v[26:27], v[18:19], v[44:45] op_sel_hi:[1,0,1]
	v_mov_b32_e32 v16, v21
	v_pk_fma_f32 v[14:15], v[10:11], v[18:19], v[14:15] op_sel:[0,1,0]
	s_nop 0
	v_pk_fma_f32 v[14:15], v[28:29], v[20:21], v[14:15] op_sel_hi:[1,0,1]
	s_nop 0
	v_pk_fma_f32 v[36:37], v[12:13], v[16:17], v[14:15] op_sel_hi:[1,0,1]
	ds_read_b128 v[14:17], v240 offset:38976
	ds_read_b128 v[18:21], v240 offset:47184
	s_waitcnt lgkmcnt(1)
	v_pk_fma_f32 v[38:39], v[26:27], v[14:15], v[46:47] op_sel_hi:[1,0,1]
	s_nop 0
	v_pk_fma_f32 v[14:15], v[10:11], v[14:15], v[38:39] op_sel:[0,1,0]
	v_mov_b32_e32 v40, v17
	v_pk_fma_f32 v[14:15], v[28:29], v[16:17], v[14:15] op_sel_hi:[1,0,1]
	s_waitcnt lgkmcnt(0)
	v_pk_fma_f32 v[42:43], v[26:27], v[18:19], v[48:49] op_sel_hi:[1,0,1]
	v_pk_fma_f32 v[38:39], v[12:13], v[40:41], v[14:15] op_sel_hi:[1,0,1]
	ds_read_b128 v[14:17], v240 offset:55392
	v_pk_fma_f32 v[18:19], v[10:11], v[18:19], v[42:43] op_sel:[0,1,0]
	s_nop 0
	v_pk_fma_f32 v[18:19], v[28:29], v[20:21], v[18:19] op_sel_hi:[1,0,1]
	v_mov_b32_e32 v20, v21
	v_pk_fma_f32 v[40:41], v[12:13], v[20:21], v[18:19] op_sel_hi:[1,0,1]
	ds_read_b128 v[18:21], v240 offset:63600
	s_waitcnt lgkmcnt(1)
	v_pk_fma_f32 v[42:43], v[26:27], v[14:15], v[50:51] op_sel_hi:[1,0,1]
	s_nop 0
	v_pk_fma_f32 v[14:15], v[10:11], v[14:15], v[42:43] op_sel:[0,1,0]
	s_nop 0
	v_pk_fma_f32 v[14:15], v[28:29], v[16:17], v[14:15] op_sel_hi:[1,0,1]
	v_mov_b32_e32 v16, v17
	v_pk_fma_f32 v[42:43], v[12:13], v[16:17], v[14:15] op_sel_hi:[1,0,1]
	s_waitcnt lgkmcnt(0)
	v_pk_fma_f32 v[14:15], v[26:27], v[18:19], v[52:53] op_sel_hi:[1,0,1]
	v_mov_b32_e32 v16, v21
	v_pk_fma_f32 v[14:15], v[10:11], v[18:19], v[14:15] op_sel:[0,1,0]
	s_nop 0
	v_pk_fma_f32 v[14:15], v[28:29], v[20:21], v[14:15] op_sel_hi:[1,0,1]
	s_nop 0
	v_pk_fma_f32 v[44:45], v[12:13], v[16:17], v[14:15] op_sel_hi:[1,0,1]
	v_add_u32_e32 v14, 0x11880, v240
	ds_read_b128 v[14:17], v14
	v_add_u32_e32 v18, 0x13890, v240
	ds_read_b128 v[18:21], v18
	s_waitcnt lgkmcnt(1)
	v_pk_fma_f32 v[46:47], v[26:27], v[14:15], v[54:55] op_sel_hi:[1,0,1]
	s_nop 0
	v_pk_fma_f32 v[14:15], v[10:11], v[14:15], v[46:47] op_sel:[0,1,0]
	v_mov_b32_e32 v48, v17
	v_pk_fma_f32 v[14:15], v[28:29], v[16:17], v[14:15] op_sel_hi:[1,0,1]
	s_waitcnt lgkmcnt(0)
	v_pk_fma_f32 v[50:51], v[26:27], v[18:19], v[56:57] op_sel_hi:[1,0,1]
	v_pk_fma_f32 v[46:47], v[12:13], v[48:49], v[14:15] op_sel_hi:[1,0,1]
	v_add_u32_e32 v14, 0x158a0, v240
	v_pk_fma_f32 v[18:19], v[10:11], v[18:19], v[50:51] op_sel:[0,1,0]
	ds_read_b128 v[14:17], v14
	v_pk_fma_f32 v[18:19], v[28:29], v[20:21], v[18:19] op_sel_hi:[1,0,1]
	v_mov_b32_e32 v20, v21
	v_pk_fma_f32 v[48:49], v[12:13], v[20:21], v[18:19] op_sel_hi:[1,0,1]
	v_add_u32_e32 v18, 0x178b0, v240
	ds_read_b128 v[18:21], v18
	s_waitcnt lgkmcnt(1)
	v_pk_fma_f32 v[50:51], v[26:27], v[14:15], v[60:61] op_sel_hi:[1,0,1]
	s_nop 0
	v_pk_fma_f32 v[14:15], v[10:11], v[14:15], v[50:51] op_sel:[0,1,0]
	s_nop 0
	v_pk_fma_f32 v[14:15], v[28:29], v[16:17], v[14:15] op_sel_hi:[1,0,1]
	v_mov_b32_e32 v16, v17
	v_pk_fma_f32 v[50:51], v[12:13], v[16:17], v[14:15] op_sel_hi:[1,0,1]
	s_waitcnt lgkmcnt(0)
	v_pk_fma_f32 v[14:15], v[26:27], v[18:19], v[64:65] op_sel_hi:[1,0,1]
	v_mov_b32_e32 v16, v21
	v_pk_fma_f32 v[14:15], v[10:11], v[18:19], v[14:15] op_sel:[0,1,0]
	s_nop 0
	v_pk_fma_f32 v[14:15], v[28:29], v[20:21], v[14:15] op_sel_hi:[1,0,1]
	s_nop 0
	v_pk_fma_f32 v[52:53], v[12:13], v[16:17], v[14:15] op_sel_hi:[1,0,1]
	v_add_u32_e32 v14, 0x198c0, v240
	ds_read_b128 v[14:17], v14
	v_add_u32_e32 v18, 0x1b8d0, v240
	ds_read_b128 v[18:21], v18
	s_waitcnt lgkmcnt(1)
	v_pk_fma_f32 v[54:55], v[26:27], v[14:15], v[120:121] op_sel_hi:[1,0,1]
	s_nop 0
	v_pk_fma_f32 v[14:15], v[10:11], v[14:15], v[54:55] op_sel:[0,1,0]
	v_mov_b32_e32 v56, v17
	v_pk_fma_f32 v[14:15], v[28:29], v[16:17], v[14:15] op_sel_hi:[1,0,1]
	s_waitcnt lgkmcnt(0)
	v_pk_fma_f32 v[60:61], v[26:27], v[18:19], v[122:123] op_sel_hi:[1,0,1]
	v_pk_fma_f32 v[54:55], v[12:13], v[56:57], v[14:15] op_sel_hi:[1,0,1]
	v_add_u32_e32 v14, 0x1d8e0, v240
	v_pk_fma_f32 v[18:19], v[10:11], v[18:19], v[60:61] op_sel:[0,1,0]
	ds_read_b128 v[14:17], v14
	v_pk_fma_f32 v[18:19], v[28:29], v[20:21], v[18:19] op_sel_hi:[1,0,1]
	v_mov_b32_e32 v20, v21
	v_pk_fma_f32 v[56:57], v[12:13], v[20:21], v[18:19] op_sel_hi:[1,0,1]
	v_add_u32_e32 v18, 0x1f8f0, v240
	ds_read_b128 v[18:21], v18
	s_waitcnt lgkmcnt(1)
	v_pk_fma_f32 v[22:23], v[26:27], v[14:15], v[22:23] op_sel_hi:[1,0,1]
	s_nop 0
	v_pk_fma_f32 v[14:15], v[10:11], v[14:15], v[22:23] op_sel:[0,1,0]
	s_nop 0
	v_pk_fma_f32 v[14:15], v[28:29], v[16:17], v[14:15] op_sel_hi:[1,0,1]
	v_mov_b32_e32 v16, v17
	v_pk_fma_f32 v[14:15], v[12:13], v[16:17], v[14:15] op_sel_hi:[1,0,1]
	s_waitcnt lgkmcnt(0)
	v_pk_fma_f32 v[16:17], v[26:27], v[18:19], v[24:25] op_sel_hi:[1,0,1]
	s_nop 0
	v_pk_fma_f32 v[10:11], v[10:11], v[18:19], v[16:17] op_sel:[0,1,0]
	v_mov_b32_e32 v16, v21
	v_pk_fma_f32 v[10:11], v[28:29], v[20:21], v[10:11] op_sel_hi:[1,0,1]
	s_nop 0
	v_pk_fma_f32 v[16:17], v[12:13], v[16:17], v[10:11] op_sel_hi:[1,0,1]
	v_mov_b32_e32 v118, v6
	v_mov_b32_e32 v93, v109
	v_mul_f32_e32 v12, v83, v101
	v_pk_mul_f32 v[10:11], v[118:119], v[92:93]
	v_mov_b32_e32 v118, v7
	v_mov_b32_e32 v91, v107
	s_waitcnt vmcnt(14)
	v_fma_f32 v18, v10, v12, v2
	v_fma_f32 v19, v10, v11, v2
	v_mul_f32_e32 v2, v83, v99
	v_pk_mul_f32 v[6:7], v[118:119], v[90:91]
	v_mov_b32_e32 v118, v8
	v_mov_b32_e32 v89, v105
	v_fma_f32 v2, v6, v2, v3
	v_fma_f32 v3, v6, v7, v3
	v_mul_f32_e32 v10, v83, v97
	v_pk_mul_f32 v[6:7], v[118:119], v[88:89]
	v_mov_b32_e32 v118, v9
	v_mov_b32_e32 v87, v103
	v_fma_f32 v20, v6, v10, v4
	v_fma_f32 v21, v6, v7, v4
	v_mul_f32_e32 v4, v83, v95
	v_pk_mul_f32 v[6:7], v[118:119], v[86:87]
	v_cvt_pk_bf16_f32 v10, v19, v3
	v_fma_f32 v4, v6, v4, v5
	v_fmac_f32_e32 v5, v6, v7
	v_cvt_pk_bf16_f32 v6, v18, v2
	v_cvt_pk_bf16_f32 v7, v20, v4
	global_store_dwordx2 v[58:59], v[6:7], off offset:3584 sc1
	ds_read_b128 v[6:9], v240 offset:7168
	v_cvt_pk_bf16_f32 v11, v21, v5
	global_store_dwordx2 v[62:63], v[10:11], off offset:3584 sc1
	ds_read_b128 v[10:13], v240 offset:15376
	s_waitcnt lgkmcnt(1)
	v_pk_fma_f32 v[22:23], v[18:19], v[6:7], v[30:31] op_sel_hi:[1,0,1]
	s_nop 0
	v_pk_fma_f32 v[6:7], v[2:3], v[6:7], v[22:23] op_sel:[0,1,0]
	s_nop 0
	v_pk_fma_f32 v[6:7], v[20:21], v[8:9], v[6:7] op_sel_hi:[1,0,1]
	v_mov_b32_e32 v8, v9
	v_pk_fma_f32 v[22:23], v[4:5], v[8:9], v[6:7] op_sel_hi:[1,0,1]
	s_waitcnt lgkmcnt(0)
	v_pk_fma_f32 v[6:7], v[18:19], v[10:11], v[32:33] op_sel_hi:[1,0,1]
	s_nop 0
	v_pk_fma_f32 v[10:11], v[2:3], v[10:11], v[6:7] op_sel:[0,1,0]
	ds_read_b128 v[6:9], v240 offset:23584
	v_pk_fma_f32 v[10:11], v[20:21], v[12:13], v[10:11] op_sel_hi:[1,0,1]
	v_mov_b32_e32 v12, v13
	v_pk_fma_f32 v[24:25], v[4:5], v[12:13], v[10:11] op_sel_hi:[1,0,1]
	ds_read_b128 v[10:13], v240 offset:31792
	s_waitcnt lgkmcnt(1)
	v_pk_fma_f32 v[26:27], v[18:19], v[6:7], v[34:35] op_sel_hi:[1,0,1]
	s_nop 0
	v_pk_fma_f32 v[6:7], v[2:3], v[6:7], v[26:27] op_sel:[0,1,0]
	s_nop 0
	v_pk_fma_f32 v[6:7], v[20:21], v[8:9], v[6:7] op_sel_hi:[1,0,1]
	v_mov_b32_e32 v8, v9
	v_pk_fma_f32 v[26:27], v[4:5], v[8:9], v[6:7] op_sel_hi:[1,0,1]
	s_waitcnt lgkmcnt(0)
	v_pk_fma_f32 v[6:7], v[18:19], v[10:11], v[36:37] op_sel_hi:[1,0,1]
	v_mov_b32_e32 v8, v13
	v_pk_fma_f32 v[6:7], v[2:3], v[10:11], v[6:7] op_sel:[0,1,0]
	s_nop 0
	v_pk_fma_f32 v[6:7], v[20:21], v[12:13], v[6:7] op_sel_hi:[1,0,1]
	s_nop 0
	v_pk_fma_f32 v[28:29], v[4:5], v[8:9], v[6:7] op_sel_hi:[1,0,1]
	ds_read_b128 v[6:9], v240 offset:40000
	ds_read_b128 v[10:13], v240 offset:48208
	s_waitcnt lgkmcnt(1)
	v_pk_fma_f32 v[30:31], v[18:19], v[6:7], v[38:39] op_sel_hi:[1,0,1]
	s_nop 0
	v_pk_fma_f32 v[6:7], v[2:3], v[6:7], v[30:31] op_sel:[0,1,0]
	v_mov_b32_e32 v32, v9
	v_pk_fma_f32 v[6:7], v[20:21], v[8:9], v[6:7] op_sel_hi:[1,0,1]
	s_waitcnt lgkmcnt(0)
	v_pk_fma_f32 v[34:35], v[18:19], v[10:11], v[40:41] op_sel_hi:[1,0,1]
	v_pk_fma_f32 v[30:31], v[4:5], v[32:33], v[6:7] op_sel_hi:[1,0,1]
	ds_read_b128 v[6:9], v240 offset:56416
	v_pk_fma_f32 v[10:11], v[2:3], v[10:11], v[34:35] op_sel:[0,1,0]
	s_nop 0
	v_pk_fma_f32 v[10:11], v[20:21], v[12:13], v[10:11] op_sel_hi:[1,0,1]
	v_mov_b32_e32 v12, v13
	v_pk_fma_f32 v[32:33], v[4:5], v[12:13], v[10:11] op_sel_hi:[1,0,1]
	ds_read_b128 v[10:13], v240 offset:64624
	s_waitcnt lgkmcnt(1)
	v_pk_fma_f32 v[34:35], v[18:19], v[6:7], v[42:43] op_sel_hi:[1,0,1]
	s_nop 0
	v_pk_fma_f32 v[6:7], v[2:3], v[6:7], v[34:35] op_sel:[0,1,0]
	s_nop 0
	v_pk_fma_f32 v[6:7], v[20:21], v[8:9], v[6:7] op_sel_hi:[1,0,1]
	v_mov_b32_e32 v8, v9
	v_pk_fma_f32 v[34:35], v[4:5], v[8:9], v[6:7] op_sel_hi:[1,0,1]
	s_waitcnt lgkmcnt(0)
	v_pk_fma_f32 v[6:7], v[18:19], v[10:11], v[44:45] op_sel_hi:[1,0,1]
	v_mov_b32_e32 v8, v13
	v_pk_fma_f32 v[6:7], v[2:3], v[10:11], v[6:7] op_sel:[0,1,0]
	s_nop 0
	v_pk_fma_f32 v[6:7], v[20:21], v[12:13], v[6:7] op_sel_hi:[1,0,1]
	s_nop 0
	v_pk_fma_f32 v[36:37], v[4:5], v[8:9], v[6:7] op_sel_hi:[1,0,1]
	v_add_u32_e32 v6, 0x11c80, v240
	ds_read_b128 v[6:9], v6
	v_add_u32_e32 v10, 0x13c90, v240
	ds_read_b128 v[10:13], v10
	s_waitcnt lgkmcnt(1)
	v_pk_fma_f32 v[38:39], v[18:19], v[6:7], v[46:47] op_sel_hi:[1,0,1]
	s_nop 0
	v_pk_fma_f32 v[6:7], v[2:3], v[6:7], v[38:39] op_sel:[0,1,0]
	v_mov_b32_e32 v40, v9
	v_pk_fma_f32 v[6:7], v[20:21], v[8:9], v[6:7] op_sel_hi:[1,0,1]
	s_waitcnt lgkmcnt(0)
	v_pk_fma_f32 v[42:43], v[18:19], v[10:11], v[48:49] op_sel_hi:[1,0,1]
	v_pk_fma_f32 v[38:39], v[4:5], v[40:41], v[6:7] op_sel_hi:[1,0,1]
	v_add_u32_e32 v6, 0x15ca0, v240
	ds_read_b128 v[6:9], v6
	v_pk_fma_f32 v[10:11], v[2:3], v[10:11], v[42:43] op_sel:[0,1,0]
	s_nop 0
	v_pk_fma_f32 v[10:11], v[20:21], v[12:13], v[10:11] op_sel_hi:[1,0,1]
	v_mov_b32_e32 v12, v13
	v_pk_fma_f32 v[40:41], v[4:5], v[12:13], v[10:11] op_sel_hi:[1,0,1]
	ds_read_b128 v[10:13], v254
	s_waitcnt lgkmcnt(1)
	v_pk_fma_f32 v[42:43], v[18:19], v[6:7], v[50:51] op_sel_hi:[1,0,1]
	s_nop 0
	v_pk_fma_f32 v[6:7], v[2:3], v[6:7], v[42:43] op_sel:[0,1,0]
	s_nop 0
	v_pk_fma_f32 v[6:7], v[20:21], v[8:9], v[6:7] op_sel_hi:[1,0,1]
	v_mov_b32_e32 v8, v9
	v_pk_fma_f32 v[42:43], v[4:5], v[8:9], v[6:7] op_sel_hi:[1,0,1]
	s_waitcnt lgkmcnt(0)
	v_pk_fma_f32 v[6:7], v[18:19], v[10:11], v[52:53] op_sel_hi:[1,0,1]
	v_mov_b32_e32 v8, v13
	v_pk_fma_f32 v[6:7], v[2:3], v[10:11], v[6:7] op_sel:[0,1,0]
	s_nop 0
	v_pk_fma_f32 v[6:7], v[20:21], v[12:13], v[6:7] op_sel_hi:[1,0,1]
	s_nop 0
	v_pk_fma_f32 v[44:45], v[4:5], v[8:9], v[6:7] op_sel_hi:[1,0,1]
	ds_read_b128 v[6:9], v241
	ds_read_b128 v[10:13], v251
	s_waitcnt lgkmcnt(1)
	v_pk_fma_f32 v[46:47], v[18:19], v[6:7], v[54:55] op_sel_hi:[1,0,1]
	s_nop 0
	v_pk_fma_f32 v[6:7], v[2:3], v[6:7], v[46:47] op_sel:[0,1,0]
	v_mov_b32_e32 v48, v9
	v_pk_fma_f32 v[6:7], v[20:21], v[8:9], v[6:7] op_sel_hi:[1,0,1]
	s_waitcnt lgkmcnt(0)
	v_pk_fma_f32 v[50:51], v[18:19], v[10:11], v[56:57] op_sel_hi:[1,0,1]
	v_pk_fma_f32 v[46:47], v[4:5], v[48:49], v[6:7] op_sel_hi:[1,0,1]
	ds_read_b128 v[6:9], v252
	v_pk_fma_f32 v[10:11], v[2:3], v[10:11], v[50:51] op_sel:[0,1,0]
	s_nop 0
	v_pk_fma_f32 v[10:11], v[20:21], v[12:13], v[10:11] op_sel_hi:[1,0,1]
	v_mov_b32_e32 v12, v13
	v_pk_fma_f32 v[48:49], v[4:5], v[12:13], v[10:11] op_sel_hi:[1,0,1]
	ds_read_b128 v[10:13], v253
	s_waitcnt lgkmcnt(1)
	v_pk_fma_f32 v[14:15], v[18:19], v[6:7], v[14:15] op_sel_hi:[1,0,1]
	s_nop 0
	v_pk_fma_f32 v[6:7], v[2:3], v[6:7], v[14:15] op_sel:[0,1,0]
	s_nop 0
	v_pk_fma_f32 v[6:7], v[20:21], v[8:9], v[6:7] op_sel_hi:[1,0,1]
	v_mov_b32_e32 v8, v9
	v_pk_fma_f32 v[6:7], v[4:5], v[8:9], v[6:7] op_sel_hi:[1,0,1]
	s_waitcnt lgkmcnt(0)
	v_pk_fma_f32 v[8:9], v[18:19], v[10:11], v[16:17] op_sel_hi:[1,0,1]
	s_nop 0
	v_pk_fma_f32 v[2:3], v[2:3], v[10:11], v[8:9] op_sel:[0,1,0]
	v_mov_b32_e32 v8, v13
	v_pk_fma_f32 v[2:3], v[20:21], v[12:13], v[2:3] op_sel_hi:[1,0,1]
	s_nop 0
	v_pk_fma_f32 v[2:3], v[4:5], v[8:9], v[2:3] op_sel_hi:[1,0,1]
	v_mov_b32_e32 v4, v23
	v_mov_b32_e32 v8, v24
	v_cndmask_b32_e64 v5, v22, v4, s[0:1]
	ds_bpermute_b32 v5, v1, v5
	v_cndmask_b32_e64 v4, v4, v22, s[0:1]
	v_cndmask_b32_e64 v9, v25, v8, s[0:1]
	v_mov_b32_e32 v11, v29
	s_waitcnt lgkmcnt(0)
	v_add_f32_e32 v4, v4, v5
	v_cndmask_b32_e64 v5, v8, v25, s[0:1]
	v_mov_b32_e32 v8, v26
	ds_bpermute_b32 v5, v1, v5
	v_cndmask_b32_e64 v10, v8, v27, s[0:1]
	ds_bpermute_b32 v10, v1, v10
	v_cndmask_b32_e64 v8, v27, v8, s[0:1]
	v_cndmask_b32_e64 v12, v28, v11, s[0:1]
	ds_bpermute_b32 v12, v1, v12
	s_waitcnt lgkmcnt(1)
	v_add_f32_e32 v8, v8, v10
	v_mov_b32_e32 v10, v30
	v_add_f32_e32 v5, v9, v5
	v_cndmask_b32_e64 v9, v11, v28, s[0:1]
	s_waitcnt lgkmcnt(0)
	v_add_f32_e32 v9, v9, v12
	v_cndmask_b32_e64 v11, v31, v10, s[0:1]
	v_cndmask_b32_e64 v10, v10, v31, s[0:1]
	v_mov_b32_e32 v12, v32
	ds_bpermute_b32 v10, v1, v10
	v_mov_b32_e32 v14, v35
	v_cndmask_b32_e64 v13, v12, v33, s[0:1]
	ds_bpermute_b32 v13, v1, v13
	s_waitcnt lgkmcnt(1)
	v_add_f32_e32 v10, v11, v10
	v_cndmask_b32_e64 v15, v34, v14, s[0:1]
	ds_bpermute_b32 v15, v1, v15
	v_cndmask_b32_e64 v11, v33, v12, s[0:1]
	s_waitcnt lgkmcnt(1)
	v_add_f32_e32 v11, v11, v13
	v_mov_b32_e32 v13, v36
	v_cndmask_b32_e64 v12, v14, v34, s[0:1]
	s_waitcnt lgkmcnt(0)
	v_add_f32_e32 v12, v12, v15
	v_cndmask_b32_e64 v14, v37, v13, s[0:1]
	v_cndmask_b32_e64 v13, v13, v37, s[0:1]
	v_mov_b32_e32 v15, v38
	ds_bpermute_b32 v13, v1, v13
	v_mov_b32_e32 v17, v41
	v_cndmask_b32_e64 v16, v15, v39, s[0:1]
	ds_bpermute_b32 v16, v1, v16
	s_waitcnt lgkmcnt(1)
	v_add_f32_e32 v13, v14, v13
	v_cndmask_b32_e64 v18, v40, v17, s[0:1]
	ds_bpermute_b32 v18, v1, v18
	v_cndmask_b32_e64 v14, v39, v15, s[0:1]
	s_waitcnt lgkmcnt(1)
	v_add_f32_e32 v14, v14, v16
	v_mov_b32_e32 v16, v43
	v_cndmask_b32_e64 v15, v17, v40, s[0:1]
	s_waitcnt lgkmcnt(0)
	v_add_f32_e32 v15, v15, v18
	v_cndmask_b32_e64 v17, v16, v42, s[0:1]
	v_cndmask_b32_e64 v16, v42, v16, s[0:1]
	v_mov_b32_e32 v18, v44
	ds_bpermute_b32 v16, v1, v16
	v_mov_b32_e32 v20, v47
	v_cndmask_b32_e64 v19, v18, v45, s[0:1]
	ds_bpermute_b32 v19, v1, v19
	s_waitcnt lgkmcnt(1)
	v_add_f32_e32 v16, v17, v16
	v_cndmask_b32_e64 v21, v46, v20, s[0:1]
	ds_bpermute_b32 v21, v1, v21
	v_cndmask_b32_e64 v17, v45, v18, s[0:1]
	s_waitcnt lgkmcnt(1)
	v_add_f32_e32 v17, v17, v19
	v_mov_b32_e32 v19, v49
	v_cndmask_b32_e64 v18, v20, v46, s[0:1]
	v_cndmask_b32_e64 v22, v2, v3, s[0:1]
	v_cndmask_b32_e64 v2, v3, v2, s[0:1]
	v_cndmask_b32_e64 v3, v14, v4, s[4:5]
	v_cndmask_b32_e64 v4, v4, v14, s[4:5]
	s_waitcnt lgkmcnt(0)
	v_add_f32_e32 v18, v18, v21
	v_cndmask_b32_e64 v21, v6, v7, s[0:1]
	v_cndmask_b32_e64 v6, v7, v6, s[0:1]
	ds_bpermute_b32 v4, v85, v4
	v_cndmask_b32_e64 v20, v19, v48, s[0:1]
	v_cndmask_b32_e64 v7, v5, v15, s[4:5]
	ds_bpermute_b32 v7, v85, v7
	v_cndmask_b32_e64 v19, v48, v19, s[0:1]
	ds_bpermute_b32 v19, v1, v19
	ds_bpermute_b32 v21, v1, v21
	v_cndmask_b32_e64 v14, v8, v16, s[4:5]
	s_waitcnt lgkmcnt(3)
	v_add_f32_e32 v3, v3, v4
	v_cndmask_b32_e64 v4, v15, v5, s[4:5]
	v_cndmask_b32_e64 v5, v16, v8, s[4:5]
	ds_bpermute_b32 v22, v1, v22
	v_cndmask_b32_e64 v8, v9, v17, s[4:5]
	ds_bpermute_b32 v14, v85, v14
	s_waitcnt lgkmcnt(4)
	v_add_f32_e32 v4, v4, v7
	v_cndmask_b32_e64 v7, v17, v9, s[4:5]
	ds_bpermute_b32 v8, v85, v8
	s_waitcnt lgkmcnt(4)
	v_add_f32_e32 v19, v20, v19
	v_cndmask_b32_e64 v9, v10, v18, s[4:5]
	ds_bpermute_b32 v9, v85, v9
	s_waitcnt lgkmcnt(4)
	v_add_f32_e32 v6, v6, v21
	s_waitcnt lgkmcnt(3)
	v_add_f32_e32 v2, v2, v22
	s_waitcnt lgkmcnt(2)
	v_add_f32_e32 v5, v5, v14
	s_waitcnt lgkmcnt(1)
	v_add_f32_e32 v7, v7, v8
	v_cndmask_b32_e64 v14, v11, v19, s[4:5]
	v_cndmask_b32_e64 v8, v18, v10, s[4:5]
	ds_bpermute_b32 v14, v85, v14
	s_waitcnt lgkmcnt(1)
	v_add_f32_e32 v8, v8, v9
	v_cndmask_b32_e64 v9, v19, v11, s[4:5]
	v_cndmask_b32_e64 v10, v6, v12, s[4:5]
	v_cndmask_b32_e64 v6, v12, v6, s[4:5]
	ds_bpermute_b32 v6, v85, v6
	v_cndmask_b32_e64 v11, v13, v2, s[4:5]
	ds_bpermute_b32 v11, v85, v11
	s_waitcnt lgkmcnt(2)
	v_add_f32_e32 v9, v9, v14
	v_cndmask_b32_e64 v2, v2, v13, s[4:5]
	s_waitcnt lgkmcnt(1)
	v_add_f32_e32 v6, v10, v6
	s_waitcnt lgkmcnt(0)
	v_add_f32_e32 v2, v2, v11
	v_cndmask_b32_e64 v12, v3, v8, s[6:7]
	v_cndmask_b32_e64 v3, v8, v3, s[6:7]
	v_cndmask_b32_e64 v8, v9, v4, s[6:7]
	v_cndmask_b32_e64 v4, v4, v9, s[6:7]
	ds_bpermute_b32 v12, v159, v12
	v_cndmask_b32_e64 v9, v5, v6, s[6:7]
	v_cndmask_b32_e64 v10, v7, v2, s[6:7]
	ds_bpermute_b32 v4, v159, v4
	ds_bpermute_b32 v9, v159, v9
	ds_bpermute_b32 v10, v159, v10
	v_cndmask_b32_e64 v5, v6, v5, s[6:7]
	v_cndmask_b32_e64 v2, v2, v7, s[6:7]
	s_waitcnt lgkmcnt(3)
	v_add_f32_e32 v3, v3, v12
	s_waitcnt lgkmcnt(2)
	v_add_f32_e32 v4, v8, v4
	s_waitcnt lgkmcnt(1)
	v_add_f32_e32 v5, v5, v9
	s_waitcnt lgkmcnt(0)
	v_add_f32_e32 v2, v2, v10
	s_nop 0
	v_cndmask_b32_e64 v6, v3, v5, s[8:9]
	v_cndmask_b32_e64 v7, v4, v2, s[8:9]
	ds_bpermute_b32 v6, v171, v6
	ds_bpermute_b32 v7, v171, v7
	v_cndmask_b32_e64 v3, v5, v3, s[8:9]
	v_cndmask_b32_e64 v2, v2, v4, s[8:9]
	s_waitcnt lgkmcnt(1)
	v_add_f32_e32 v3, v3, v6
	s_waitcnt lgkmcnt(0)
	v_add_f32_e32 v2, v2, v7
	s_nop 0
	v_cndmask_b32_e64 v4, v3, v2, s[10:11]
	ds_bpermute_b32 v4, v238, v4
	v_cndmask_b32_e64 v2, v2, v3, s[10:11]
	s_waitcnt lgkmcnt(0)
	v_add_f32_e32 v2, v2, v4
	ds_bpermute_b32 v3, v239, v2
	s_waitcnt lgkmcnt(0)
	v_add_f32_e32 v2, v2, v3
	ds_bpermute_b32 v3, v238, v2
	s_waitcnt lgkmcnt(0)
	v_max_f32_e32 v3, v3, v3
	v_max_f32_e32 v3, v2, v3
	ds_bpermute_b32 v4, v171, v3
	s_waitcnt lgkmcnt(0)
	v_max_f32_e32 v4, v4, v4
	v_max_f32_e32 v3, v3, v4
	ds_bpermute_b32 v4, v159, v3
	s_waitcnt lgkmcnt(0)
	v_max_f32_e32 v4, v4, v4
	v_max_f32_e32 v3, v3, v4
	ds_bpermute_b32 v4, v85, v3
	s_waitcnt lgkmcnt(0)
	v_max_f32_e32 v4, v4, v4
	v_max_f32_e32 v3, v3, v4
	v_sub_f32_e32 v2, v2, v3
	v_mul_f32_e32 v3, 0x3fb8aa3b, v2
	v_fma_f32 v4, v2, s38, -v3
	v_rndne_f32_e32 v5, v3
	v_fmac_f32_e32 v4, 0x32a5705f, v2
	v_sub_f32_e32 v3, v3, v5
	v_add_f32_e32 v3, v3, v4
	v_exp_f32_e32 v3, v3
	v_cvt_i32_f32_e32 v4, v5
	v_cmp_ngt_f32_e32 vcc, s39, v2
	v_ldexp_f32 v3, v3, v4
	s_nop 0
	v_cndmask_b32_e32 v3, 0, v3, vcc
	v_cmp_nlt_f32_e32 vcc, s40, v2
	s_nop 1
	v_cndmask_b32_e32 v2, v250, v3, vcc
	ds_bpermute_b32 v3, v238, v2
	s_waitcnt lgkmcnt(0)
	v_add_f32_e32 v3, v2, v3
	ds_bpermute_b32 v4, v171, v3
	s_waitcnt lgkmcnt(0)
	v_add_f32_e32 v3, v3, v4
	ds_bpermute_b32 v4, v159, v3
	s_waitcnt lgkmcnt(0)
	v_add_f32_e32 v3, v3, v4
	ds_bpermute_b32 v4, v85, v3
	s_and_saveexec_b64 s[14:15], s[12:13]
	s_cbranch_execz .LBB0_1200
	s_waitcnt lgkmcnt(0)
	v_add_f32_e32 v3, v3, v4
	v_div_scale_f32 v4, s[26:27], v3, v3, v2
	v_rcp_f32_e32 v5, v4
	s_and_b32 s21, s20, 0x7fe
	v_mov_b32_e32 v83, v67
	v_fma_f32 v6, -v4, v5, 1.0
	v_fmac_f32_e32 v5, v6, v5
	v_div_scale_f32 v6, vcc, v2, v3, v2
	v_mul_f32_e32 v7, v6, v5
	v_fma_f32 v8, -v4, v7, v6
	v_fmac_f32_e32 v7, v8, v5
	v_fma_f32 v4, -v4, v7, v6
	v_div_fmas_f32 v4, v4, v5, v7
	v_div_fixup_f32 v4, v4, v3, v2
	v_bfe_u32 v2, v0, 1, 4
	v_lshl_or_b32 v2, s18, 4, v2
	v_ashrrev_i32_e32 v3, 31, v2
	v_lshlrev_b64 v[2:3], 13, v[2:3]
	v_lshl_add_u64 v[2:3], s[2:3], 0, v[2:3]
	s_lshl_b32 s18, s21, 2
	v_lshl_add_u64 v[2:3], v[2:3], 0, s[18:19]
	v_lshl_add_u64 v[2:3], v[2:3], 0, v[82:83]
	global_store_dword v[2:3], v4, off
	s_branch .LBB0_1200

.LBB0_1235:
	s_ashr_i32 s18, s25, 10
	s_mul_i32 s14, s18, 0x3000
	s_ashr_i32 s21, s20, 31
	s_ashr_i32 s15, s14, 31
	s_lshl_b64 s[26:27], s[20:21], 12
	s_lshl_b64 s[14:15], s[14:15], 2
	s_add_u32 s14, s70, s14
	s_addc_u32 s15, s71, s15
	v_lshl_add_u64 v[14:15], s[14:15], 0, v[66:67]
	v_add_co_u32_e32 v16, vcc, s36, v14
	s_nop 1
	v_addc_co_u32_e32 v17, vcc, 0, v15, vcc
	s_waitcnt lgkmcnt(0)
	global_load_dwordx4 v[2:5], v[16:17], off offset:-4096
	v_add_co_u32_e32 v18, vcc, s35, v14
	s_waitcnt vmcnt(0)
	v_add_f32_e32 v204, 1.0, v2
	v_addc_co_u32_e32 v19, vcc, 0, v15, vcc
	global_load_dwordx4 v[6:9], v[18:19], off offset:1024
	global_load_dwordx4 v[10:13], v[18:19], off offset:2048
	s_nop 0
	global_load_dwordx4 v[18:21], v[18:19], off offset:3072
	s_nop 0
	global_load_dwordx4 v[86:89], v[16:17], off
	global_load_dwordx4 v[90:93], v[16:17], off offset:1024
	global_load_dwordx4 v[94:97], v[16:17], off offset:2048
	global_load_dwordx4 v[98:101], v[16:17], off offset:3072
	v_lshl_add_u64 v[16:17], v[68:69], 0, s[26:27]
	global_load_dwordx2 v[102:103], v[16:17], off offset:2560
	global_load_dwordx2 v[104:105], v[16:17], off offset:3072
	global_load_dwordx2 v[106:107], v[16:17], off offset:3584
	global_load_dwordx2 v[108:109], v[16:17], off offset:2048
	v_add_co_u32_e32 v26, vcc, s33, v16
	v_add_f32_e32 v206, 1.0, v3
	s_nop 0
	v_addc_co_u32_e32 v27, vcc, 0, v17, vcc
	global_load_dwordx2 v[118:119], v[26:27], off offset:2560
	global_load_dwordx2 v[220:221], v[26:27], off offset:3072
	global_load_dwordx2 v[222:223], v[26:27], off offset:3584
	global_load_dwordx2 v[162:163], v[26:27], off offset:2048
	global_load_dwordx4 v[62:65], v[70:71], off
	global_load_dwordx4 v[54:57], v[70:71], off offset:1024
	global_load_dwordx4 v[46:49], v[70:71], off offset:2048
	global_load_dwordx4 v[38:41], v[70:71], off offset:3072
	global_load_dwordx2 v[164:165], v[16:17], off
	global_load_dwordx2 v[166:167], v[26:27], off
	global_load_dwordx4 v[30:33], v[72:73], off
	global_load_dwordx4 v[22:25], v[74:75], off
	global_load_dwordx2 v[168:169], v[16:17], off offset:512
	global_load_dwordx2 v[180:181], v[16:17], off offset:1024
	global_load_dwordx2 v[224:225], v[16:17], off offset:1536
	global_load_dwordx2 v[182:183], v[26:27], off offset:512
	global_load_dwordx2 v[226:227], v[26:27], off offset:1024
	global_load_dwordx2 v[228:229], v[26:27], off offset:1536
	v_add_co_u32_e32 v128, vcc, s37, v14
	v_add_f32_e32 v208, 1.0, v4
	s_nop 0
	v_addc_co_u32_e32 v129, vcc, 0, v15, vcc
	v_lshl_add_u64 v[14:15], v[14:15], 0, s[22:23]
	global_load_dwordx4 v[58:61], v[128:129], off offset:-4096
	global_load_dwordx4 v[50:53], v[14:15], off offset:1024
	global_load_dwordx4 v[42:45], v[14:15], off offset:2048
	global_load_dwordx4 v[34:37], v[14:15], off offset:3072
	global_load_dwordx4 v[26:29], v[128:129], off
	s_nop 0
	global_load_dwordx4 v[14:17], v[128:129], off offset:1024
	v_add_f32_e32 v210, 1.0, v5
	s_waitcnt vmcnt(23)
	v_and_b32_e32 v141, 0xffff0000, v118
	v_lshlrev_b32_e32 v143, 16, v118
	v_lshlrev_b32_e32 v139, 16, v119
	v_add_f32_e32 v194, 1.0, v6
	v_add_f32_e32 v192, 1.0, v7
	v_add_f32_e32 v190, 1.0, v8
	v_add_f32_e32 v188, 1.0, v9
	v_add_f32_e32 v178, 1.0, v10
	v_add_f32_e32 v176, 1.0, v11
	v_add_f32_e32 v174, 1.0, v12
	v_add_f32_e32 v172, 1.0, v13
	v_add_f32_e32 v160, 1.0, v18
	v_add_f32_e32 v156, 1.0, v19
	v_add_f32_e32 v154, 1.0, v20
	v_add_f32_e32 v152, 1.0, v21
	global_load_dwordx4 v[18:21], v[76:77], off
	global_load_dwordx4 v[6:9], v[78:79], off
	global_load_dwordx4 v[10:13], v[128:129], off offset:2048
	global_load_dwordx4 v[2:5], v[128:129], off offset:3072
	v_and_b32_e32 v133, 0xffff0000, v102
	v_and_b32_e32 v132, 0xffff0000, v108
	v_add_f32_e32 v116, 1.0, v94
	v_add_f32_e32 v114, 1.0, v95
	v_lshlrev_b32_e32 v135, 16, v102
	v_lshlrev_b32_e32 v134, 16, v108
	v_pk_mul_f32 v[94:95], v[132:133], v[132:133]
	v_lshlrev_b32_e32 v131, 16, v103
	v_lshlrev_b32_e32 v130, 16, v109
	v_pk_fma_f32 v[94:95], v[134:135], v[134:135], v[94:95]
	v_and_b32_e32 v129, 0xffff0000, v103
	v_and_b32_e32 v128, 0xffff0000, v109
	v_pk_fma_f32 v[94:95], v[130:131], v[130:131], v[94:95]
	s_waitcnt vmcnt(24)
	v_and_b32_e32 v140, 0xffff0000, v162
	v_pk_fma_f32 v[230:231], v[128:129], v[128:129], v[94:95]
	v_lshlrev_b32_e32 v142, 16, v162
	v_pk_mul_f32 v[94:95], v[140:141], v[140:141]
	v_lshlrev_b32_e32 v138, 16, v163
	v_pk_fma_f32 v[94:95], v[142:143], v[142:143], v[94:95]
	v_and_b32_e32 v137, 0xffff0000, v119
	v_and_b32_e32 v136, 0xffff0000, v163
	v_pk_fma_f32 v[94:95], v[138:139], v[138:139], v[94:95]
	s_waitcnt vmcnt(19)
	v_and_b32_e32 v219, 0xffff0000, v164
	s_waitcnt vmcnt(18)
	v_and_b32_e32 v218, 0xffff0000, v166
	s_waitcnt vmcnt(15)
	v_and_b32_e32 v201, 0xffff0000, v168
	s_waitcnt vmcnt(12)
	v_and_b32_e32 v200, 0xffff0000, v182
	v_add_f32_e32 v112, 1.0, v96
	v_add_f32_e32 v110, 1.0, v97
	v_pk_fma_f32 v[118:119], v[136:137], v[136:137], v[94:95]
	v_lshlrev_b32_e32 v216, 16, v166
	v_lshlrev_b32_e32 v217, 16, v164
	v_pk_mul_f32 v[94:95], v[218:219], v[218:219]
	v_lshlrev_b32_e32 v202, 16, v182
	v_lshlrev_b32_e32 v203, 16, v168
	v_pk_mul_f32 v[96:97], v[200:201], v[200:201]
	v_lshlrev_b32_e32 v214, 16, v167
	v_lshlrev_b32_e32 v215, 16, v165
	v_pk_fma_f32 v[94:95], v[216:217], v[216:217], v[94:95]
	v_lshlrev_b32_e32 v198, 16, v183
	v_lshlrev_b32_e32 v199, 16, v169
	v_pk_fma_f32 v[96:97], v[202:203], v[202:203], v[96:97]
	v_and_b32_e32 v213, 0xffff0000, v165
	v_and_b32_e32 v212, 0xffff0000, v167
	v_pk_fma_f32 v[94:95], v[214:215], v[214:215], v[94:95]
	v_and_b32_e32 v197, 0xffff0000, v169
	v_and_b32_e32 v196, 0xffff0000, v183
	v_pk_fma_f32 v[96:97], v[198:199], v[198:199], v[96:97]
	v_pk_fma_f32 v[94:95], v[212:213], v[212:213], v[94:95]
	v_pk_fma_f32 v[96:97], v[196:197], v[196:197], v[96:97]
	v_and_b32_e32 v185, 0xffff0000, v180
	s_waitcnt vmcnt(11)
	v_and_b32_e32 v184, 0xffff0000, v226
	v_pk_add_f32 v[94:95], v[94:95], v[96:97]
	v_lshlrev_b32_e32 v186, 16, v226
	v_lshlrev_b32_e32 v187, 16, v180
	v_pk_mul_f32 v[96:97], v[184:185], v[184:185]
	v_lshlrev_b32_e32 v182, 16, v227
	v_lshlrev_b32_e32 v183, 16, v181
	v_pk_fma_f32 v[96:97], v[186:187], v[186:187], v[96:97]
	v_and_b32_e32 v181, 0xffff0000, v181
	v_and_b32_e32 v180, 0xffff0000, v227
	v_pk_fma_f32 v[96:97], v[182:183], v[182:183], v[96:97]
	v_and_b32_e32 v167, 0xffff0000, v224
	v_pk_fma_f32 v[96:97], v[180:181], v[180:181], v[96:97]
	s_waitcnt vmcnt(10)
	v_and_b32_e32 v166, 0xffff0000, v228
	v_pk_add_f32 v[94:95], v[94:95], v[96:97]
	v_lshlrev_b32_e32 v168, 16, v228
	v_lshlrev_b32_e32 v169, 16, v224
	v_pk_mul_f32 v[96:97], v[166:167], v[166:167]
	v_lshlrev_b32_e32 v164, 16, v229
	v_lshlrev_b32_e32 v165, 16, v225
	v_pk_fma_f32 v[96:97], v[168:169], v[168:169], v[96:97]
	v_and_b32_e32 v163, 0xffff0000, v225
	v_and_b32_e32 v162, 0xffff0000, v229
	v_pk_fma_f32 v[96:97], v[164:165], v[164:165], v[96:97]
	v_add_f32_e32 v126, 1.0, v90
	v_add_f32_e32 v122, 1.0, v92
	v_add_f32_e32 v92, 1.0, v98
	v_add_f32_e32 v90, 1.0, v99
	v_pk_fma_f32 v[96:97], v[162:163], v[162:163], v[96:97]
	v_and_b32_e32 v99, 0xffff0000, v106
	v_and_b32_e32 v98, 0xffff0000, v104
	v_add_f32_e32 v150, 1.0, v86
	v_add_f32_e32 v146, 1.0, v88
	v_add_f32_e32 v88, 1.0, v100
	v_add_f32_e32 v86, 1.0, v101
	v_pk_add_f32 v[94:95], v[94:95], v[96:97]
	v_mov_b32_e32 v96, v118
	v_mov_b32_e32 v97, v230
	v_lshlrev_b32_e32 v101, 16, v106
	v_lshlrev_b32_e32 v100, 16, v104
	v_pk_mul_f32 v[102:103], v[98:99], v[98:99]
	v_pk_add_f32 v[224:225], v[94:95], v[96:97]
	v_lshlrev_b32_e32 v97, 16, v107
	v_lshlrev_b32_e32 v96, 16, v105
	v_pk_fma_f32 v[102:103], v[100:101], v[100:101], v[102:103]
	v_and_b32_e32 v95, 0xffff0000, v107
	v_and_b32_e32 v94, 0xffff0000, v105
	v_pk_fma_f32 v[102:103], v[96:97], v[96:97], v[102:103]
	v_and_b32_e32 v107, 0xffff0000, v222
	v_and_b32_e32 v106, 0xffff0000, v220
	v_pk_fma_f32 v[226:227], v[94:95], v[94:95], v[102:103]
	v_lshlrev_b32_e32 v109, 16, v222
	v_lshlrev_b32_e32 v108, 16, v220
	v_lshlrev_b32_e32 v104, 16, v221
	v_and_b32_e32 v102, 0xffff0000, v221
	v_pk_mul_f32 v[220:221], v[106:107], v[106:107]
	v_lshlrev_b32_e32 v105, 16, v223
	v_pk_fma_f32 v[220:221], v[108:109], v[108:109], v[220:221]
	v_and_b32_e32 v103, 0xffff0000, v223
	v_pk_fma_f32 v[220:221], v[104:105], v[104:105], v[220:221]
	v_add_f32_e32 v148, 1.0, v87
	v_add_f32_e32 v144, 1.0, v89
	v_add_f32_e32 v124, 1.0, v91
	v_add_f32_e32 v120, 1.0, v93
	v_pk_fma_f32 v[220:221], v[102:103], v[102:103], v[220:221]
	v_mov_b32_e32 v230, v119
	v_pk_add_f32 v[118:119], v[224:225], v[230:231]
	v_mov_b32_e32 v222, v220
	v_mov_b32_e32 v223, v226
	v_pk_add_f32 v[118:119], v[118:119], v[222:223]
	v_mov_b32_e32 v226, v221
	v_pk_add_f32 v[118:119], v[118:119], v[226:227]
	ds_bpermute_b32 v221, v1, v119
	ds_bpermute_b32 v220, v1, v118
	v_mov_b32_e32 v205, v216
	v_mov_b32_e32 v207, v218
	v_mov_b32_e32 v209, v214
	v_mov_b32_e32 v211, v212
	s_waitcnt lgkmcnt(0)
	v_pk_add_f32 v[118:119], v[118:119], v[220:221]
	ds_bpermute_b32 v221, v85, v119
	ds_bpermute_b32 v220, v85, v118
	s_add_i32 s28, s20, 1
	s_ashr_i32 s29, s28, 31
	s_lshl_b64 s[28:29], s[28:29], 12
	s_waitcnt lgkmcnt(0)
	v_pk_add_f32 v[118:119], v[118:119], v[220:221]
	ds_bpermute_b32 v221, v159, v119
	ds_bpermute_b32 v220, v159, v118
	s_waitcnt lgkmcnt(0)
	v_pk_add_f32 v[118:119], v[118:119], v[220:221]
	ds_bpermute_b32 v221, v171, v119
	ds_bpermute_b32 v220, v171, v118
	s_waitcnt lgkmcnt(0)
	v_pk_add_f32 v[118:119], v[118:119], v[220:221]
	ds_bpermute_b32 v221, v238, v119
	ds_bpermute_b32 v220, v238, v118
	s_waitcnt lgkmcnt(0)
	v_pk_add_f32 v[220:221], v[118:119], v[220:221]
	ds_bpermute_b32 v223, v239, v221
	ds_bpermute_b32 v222, v239, v220
	v_mov_b32_e32 v118, v62
	s_waitcnt lgkmcnt(0)
	v_pk_add_f32 v[220:221], v[220:221], v[222:223]
	s_nop 0
	v_pk_fma_f32 v[220:221], v[220:221], s[24:25], v[84:85] op_sel_hi:[1,0,0]
	ds_read_b128 v[222:225], v240 offset:24624
	v_mul_f32_e32 v62, 0x4b800000, v221
	v_mul_f32_e32 v83, 0x4b800000, v220
	v_cmp_gt_f32_e32 vcc, s38, v221
	v_cmp_gt_f32_e64 s[14:15], s38, v220
	s_nop 0
	v_cndmask_b32_e32 v62, v221, v62, vcc
	v_cndmask_b32_e64 v83, v220, v83, s[14:15]
	v_rsq_f32_e32 v62, v62
	v_rsq_f32_e32 v87, v83
	v_mul_f32_e32 v83, 0x45800000, v62
	v_mul_f32_e32 v89, 0x45800000, v87
	v_cndmask_b32_e32 v83, v62, v83, vcc
	v_cndmask_b32_e64 v119, v87, v89, s[14:15]
	v_mul_f32_e32 v62, v83, v217
	v_pk_mul_f32 v[216:217], v[118:119], v[204:205]
	v_mov_b32_e32 v118, v63
	v_mul_f32_e32 v87, v83, v219
	s_waitcnt vmcnt(9)
	v_fma_f32 v204, v216, v62, v58
	v_pk_mul_f32 v[62:63], v[118:119], v[206:207]
	v_mov_b32_e32 v118, v64
	v_fma_f32 v205, v216, v217, v58
	v_fma_f32 v206, v62, v87, v59
	v_fma_f32 v207, v62, v63, v59
	v_mul_f32_e32 v62, v83, v215
	v_pk_mul_f32 v[58:59], v[118:119], v[208:209]
	v_mov_b32_e32 v118, v65
	v_fma_f32 v208, v58, v62, v60
	v_fma_f32 v209, v58, v59, v60
	v_mul_f32_e32 v60, v83, v213
	v_pk_mul_f32 v[58:59], v[118:119], v[210:211]
	ds_read_b128 v[210:213], v240
	ds_read_b128 v[214:217], v240 offset:8208
	v_fma_f32 v60, v58, v60, v61
	v_fmac_f32_e32 v61, v58, v59
	v_cvt_pk_bf16_f32 v62, v204, v206
	v_cvt_pk_bf16_f32 v63, v208, v60
	v_lshl_add_u64 v[58:59], v[80:81], 0, s[26:27]
	global_store_dwordx2 v[58:59], v[62:63], off sc1
	v_cvt_pk_bf16_f32 v64, v205, v207
	v_cvt_pk_bf16_f32 v65, v209, v61
	v_lshl_add_u64 v[62:63], v[80:81], 0, s[28:29]
	ds_read_b128 v[218:221], v240 offset:16416
	global_store_dwordx2 v[62:63], v[64:65], off sc1
	s_waitcnt lgkmcnt(2)
	v_pk_fma_f32 v[64:65], v[204:205], v[210:211], 0 op_sel_hi:[1,0,0]
	v_mov_b32_e32 v118, v213
	v_pk_fma_f32 v[64:65], v[206:207], v[210:211], v[64:65] op_sel:[0,1,0]
	s_waitcnt lgkmcnt(1)
	v_pk_fma_f32 v[210:211], v[204:205], v[214:215], 0 op_sel_hi:[1,0,0]
	v_pk_fma_f32 v[64:65], v[208:209], v[212:213], v[64:65] op_sel_hi:[1,0,1]
	v_pk_fma_f32 v[210:211], v[206:207], v[214:215], v[210:211] op_sel:[0,1,0]
	v_pk_fma_f32 v[64:65], v[60:61], v[118:119], v[64:65] op_sel_hi:[1,0,1]
	v_pk_fma_f32 v[210:211], v[208:209], v[216:217], v[210:211] op_sel_hi:[1,0,1]
	v_mov_b32_e32 v118, v217
	v_pk_fma_f32 v[212:213], v[60:61], v[118:119], v[210:211] op_sel_hi:[1,0,1]
	s_waitcnt lgkmcnt(0)
	v_pk_fma_f32 v[210:211], v[204:205], v[218:219], 0 op_sel_hi:[1,0,0]
	v_mov_b32_e32 v118, v221
	v_pk_fma_f32 v[210:211], v[206:207], v[218:219], v[210:211] op_sel:[0,1,0]
	s_nop 0
	v_pk_fma_f32 v[210:211], v[208:209], v[220:221], v[210:211] op_sel_hi:[1,0,1]
	s_nop 0
	v_pk_fma_f32 v[216:217], v[60:61], v[118:119], v[210:211] op_sel_hi:[1,0,1]
	v_pk_fma_f32 v[210:211], v[204:205], v[222:223], 0 op_sel_hi:[1,0,0]
	v_mov_b32_e32 v118, v225
	v_pk_fma_f32 v[210:211], v[206:207], v[222:223], v[210:211] op_sel:[0,1,0]
	s_nop 0
	v_pk_fma_f32 v[210:211], v[208:209], v[224:225], v[210:211] op_sel_hi:[1,0,1]
	s_nop 0
	v_pk_fma_f32 v[222:223], v[60:61], v[118:119], v[210:211] op_sel_hi:[1,0,1]
	ds_read_b128 v[218:221], v240 offset:32832
	ds_read_b128 v[224:227], v240 offset:41040
	s_waitcnt lgkmcnt(1)
	v_pk_fma_f32 v[210:211], v[204:205], v[218:219], 0 op_sel_hi:[1,0,0]
	s_nop 0
	v_pk_fma_f32 v[210:211], v[206:207], v[218:219], v[210:211] op_sel:[0,1,0]
	v_mov_b32_e32 v118, v221
	v_pk_fma_f32 v[210:211], v[208:209], v[220:221], v[210:211] op_sel_hi:[1,0,1]
	ds_read_b128 v[218:221], v240 offset:49248
	s_waitcnt lgkmcnt(1)
	v_pk_fma_f32 v[214:215], v[204:205], v[224:225], 0 op_sel_hi:[1,0,0]
	v_pk_fma_f32 v[230:231], v[60:61], v[118:119], v[210:211] op_sel_hi:[1,0,1]
	v_pk_fma_f32 v[214:215], v[206:207], v[224:225], v[214:215] op_sel:[0,1,0]
	v_mov_b32_e32 v118, v227
	v_pk_fma_f32 v[210:211], v[208:209], v[226:227], v[214:215] op_sel_hi:[1,0,1]
	ds_read_b128 v[224:227], v240 offset:57456
	v_pk_fma_f32 v[234:235], v[60:61], v[118:119], v[210:211] op_sel_hi:[1,0,1]
	s_waitcnt lgkmcnt(1)
	v_pk_fma_f32 v[210:211], v[204:205], v[218:219], 0 op_sel_hi:[1,0,0]
	v_mov_b32_e32 v118, v221
	v_pk_fma_f32 v[210:211], v[206:207], v[218:219], v[210:211] op_sel:[0,1,0]
	s_nop 0
	v_pk_fma_f32 v[210:211], v[208:209], v[220:221], v[210:211] op_sel_hi:[1,0,1]
	s_nop 0
	v_pk_fma_f32 v[218:219], v[60:61], v[118:119], v[210:211] op_sel_hi:[1,0,1]
	s_waitcnt lgkmcnt(0)
	v_pk_fma_f32 v[210:211], v[204:205], v[224:225], 0 op_sel_hi:[1,0,0]
	v_mov_b32_e32 v118, v227
	v_pk_fma_f32 v[210:211], v[206:207], v[224:225], v[210:211] op_sel:[0,1,0]
	s_nop 0
	v_pk_fma_f32 v[210:211], v[208:209], v[226:227], v[210:211] op_sel_hi:[1,0,1]
	s_nop 0
	v_pk_fma_f32 v[224:225], v[60:61], v[118:119], v[210:211] op_sel_hi:[1,0,1]
	v_add_u32_e32 v87, 0x10080, v240
	ds_read_b128 v[226:229], v87
	v_add_u32_e32 v87, 0x12090, v240
	ds_read_b128 v[242:245], v87
	v_add_u32_e32 v87, 0x140a0, v240
	ds_read_b128 v[246:249], v87
	s_waitcnt lgkmcnt(2)
	v_pk_fma_f32 v[210:211], v[204:205], v[226:227], 0 op_sel_hi:[1,0,0]
	v_mov_b32_e32 v118, v229
	v_pk_fma_f32 v[210:211], v[206:207], v[226:227], v[210:211] op_sel:[0,1,0]
	s_waitcnt lgkmcnt(1)
	v_pk_fma_f32 v[214:215], v[204:205], v[242:243], 0 op_sel_hi:[1,0,0]
	v_pk_fma_f32 v[210:211], v[208:209], v[228:229], v[210:211] op_sel_hi:[1,0,1]
	v_add_u32_e32 v87, 0x160b0, v240
	v_pk_fma_f32 v[228:229], v[60:61], v[118:119], v[210:211] op_sel_hi:[1,0,1]
	v_pk_fma_f32 v[210:211], v[206:207], v[242:243], v[214:215] op_sel:[0,1,0]
	v_mov_b32_e32 v118, v245
	v_pk_fma_f32 v[210:211], v[208:209], v[244:245], v[210:211] op_sel_hi:[1,0,1]
	ds_read_b128 v[242:245], v87
	v_pk_fma_f32 v[236:237], v[60:61], v[118:119], v[210:211] op_sel_hi:[1,0,1]
	s_waitcnt lgkmcnt(1)
	v_pk_fma_f32 v[210:211], v[204:205], v[246:247], 0 op_sel_hi:[1,0,0]
	v_mov_b32_e32 v118, v249
	v_pk_fma_f32 v[210:211], v[206:207], v[246:247], v[210:211] op_sel:[0,1,0]
	s_nop 0
	v_pk_fma_f32 v[210:211], v[208:209], v[248:249], v[210:211] op_sel_hi:[1,0,1]
	s_nop 0
	v_pk_fma_f32 v[220:221], v[60:61], v[118:119], v[210:211] op_sel_hi:[1,0,1]
	s_waitcnt lgkmcnt(0)
	v_pk_fma_f32 v[210:211], v[204:205], v[242:243], 0 op_sel_hi:[1,0,0]
	v_mov_b32_e32 v118, v245
	v_pk_fma_f32 v[210:211], v[206:207], v[242:243], v[210:211] op_sel:[0,1,0]
	s_nop 0
	v_pk_fma_f32 v[210:211], v[208:209], v[244:245], v[210:211] op_sel_hi:[1,0,1]
	s_nop 0
	v_pk_fma_f32 v[226:227], v[60:61], v[118:119], v[210:211] op_sel_hi:[1,0,1]
	v_add_u32_e32 v87, 0x180c0, v240
	ds_read_b128 v[242:245], v87
	v_add_u32_e32 v87, 0x1a0d0, v240
	s_waitcnt lgkmcnt(0)
	v_pk_fma_f32 v[210:211], v[204:205], v[242:243], 0 op_sel_hi:[1,0,0]
	s_nop 0
	v_pk_fma_f32 v[210:211], v[206:207], v[242:243], v[210:211] op_sel:[0,1,0]
	v_mov_b32_e32 v118, v245
	v_pk_fma_f32 v[210:211], v[208:209], v[244:245], v[210:211] op_sel_hi:[1,0,1]
	ds_read_b128 v[242:245], v87
	v_pk_fma_f32 v[214:215], v[60:61], v[118:119], v[210:211] op_sel_hi:[1,0,1]
	v_add_u32_e32 v87, 0x1c0e0, v240
	s_waitcnt lgkmcnt(0)
	v_pk_fma_f32 v[210:211], v[204:205], v[242:243], 0 op_sel_hi:[1,0,0]
	s_nop 0
	v_pk_fma_f32 v[210:211], v[206:207], v[242:243], v[210:211] op_sel:[0,1,0]
	v_mov_b32_e32 v118, v245
	v_pk_fma_f32 v[210:211], v[208:209], v[244:245], v[210:211] op_sel_hi:[1,0,1]
	ds_read_b128 v[242:245], v87
	v_pk_fma_f32 v[232:233], v[60:61], v[118:119], v[210:211] op_sel_hi:[1,0,1]
	v_add_u32_e32 v87, 0x1e0f0, v240
	s_waitcnt lgkmcnt(0)
	v_pk_fma_f32 v[210:211], v[204:205], v[242:243], 0 op_sel_hi:[1,0,0]
	s_nop 0
	v_pk_fma_f32 v[210:211], v[206:207], v[242:243], v[210:211] op_sel:[0,1,0]
	v_mov_b32_e32 v118, v245
	v_pk_fma_f32 v[210:211], v[208:209], v[244:245], v[210:211] op_sel_hi:[1,0,1]
	ds_read_b128 v[242:245], v87
	v_pk_fma_f32 v[210:211], v[60:61], v[118:119], v[210:211] op_sel_hi:[1,0,1]
	s_waitcnt lgkmcnt(0)
	v_pk_fma_f32 v[204:205], v[204:205], v[242:243], 0 op_sel_hi:[1,0,0]
	s_nop 0
	v_pk_fma_f32 v[204:205], v[206:207], v[242:243], v[204:205] op_sel:[0,1,0]
	v_mov_b32_e32 v118, v245
	v_pk_fma_f32 v[204:205], v[208:209], v[244:245], v[204:205] op_sel_hi:[1,0,1]
	s_nop 0
	v_pk_fma_f32 v[60:61], v[60:61], v[118:119], v[204:205] op_sel_hi:[1,0,1]
	v_mov_b32_e32 v118, v54
	v_mov_b32_e32 v195, v202
	v_mul_f32_e32 v87, v83, v203
	v_pk_mul_f32 v[202:203], v[118:119], v[194:195]
	v_mov_b32_e32 v118, v55
	v_mov_b32_e32 v193, v200
	s_waitcnt vmcnt(10)
	v_fma_f32 v194, v202, v87, v50
	v_fma_f32 v195, v202, v203, v50
	v_mul_f32_e32 v50, v83, v201
	v_pk_mul_f32 v[54:55], v[118:119], v[192:193]
	v_mov_b32_e32 v118, v56
	v_mov_b32_e32 v191, v198
	v_fma_f32 v192, v54, v50, v51
	v_fma_f32 v193, v54, v55, v51
	v_mul_f32_e32 v54, v83, v199
	v_pk_mul_f32 v[50:51], v[118:119], v[190:191]
	v_mov_b32_e32 v118, v57
	v_fma_f32 v190, v50, v54, v52
	v_mov_b32_e32 v189, v196
	ds_read_b128 v[54:57], v240 offset:1024
	v_fma_f32 v191, v50, v51, v52
	v_mul_f32_e32 v52, v83, v197
	v_pk_mul_f32 v[50:51], v[118:119], v[188:189]
	ds_read_b128 v[196:199], v240 offset:9232
	v_fma_f32 v52, v50, v52, v53
	v_fmac_f32_e32 v53, v50, v51
	v_cvt_pk_bf16_f32 v50, v194, v192
	v_cvt_pk_bf16_f32 v51, v190, v52
	global_store_dwordx2 v[58:59], v[50:51], off offset:512 sc1
	v_cvt_pk_bf16_f32 v50, v195, v193
	v_cvt_pk_bf16_f32 v51, v191, v53
	global_store_dwordx2 v[62:63], v[50:51], off offset:512 sc1
	s_waitcnt lgkmcnt(1)
	v_pk_fma_f32 v[50:51], v[194:195], v[54:55], v[64:65] op_sel_hi:[1,0,1]
	s_waitcnt lgkmcnt(0)
	v_mov_b32_e32 v118, v199
	v_pk_fma_f32 v[50:51], v[192:193], v[54:55], v[50:51] op_sel:[0,1,0]
	v_mov_b32_e32 v54, v57
	v_pk_fma_f32 v[50:51], v[190:191], v[56:57], v[50:51] op_sel_hi:[1,0,1]
	s_nop 0
	v_pk_fma_f32 v[50:51], v[52:53], v[54:55], v[50:51] op_sel_hi:[1,0,1]
	v_pk_fma_f32 v[54:55], v[194:195], v[196:197], v[212:213] op_sel_hi:[1,0,1]
	s_nop 0
	v_pk_fma_f32 v[64:65], v[192:193], v[196:197], v[54:55] op_sel:[0,1,0]
	ds_read_b128 v[54:57], v240 offset:17440
	v_pk_fma_f32 v[64:65], v[190:191], v[198:199], v[64:65] op_sel_hi:[1,0,1]
	ds_read_b128 v[196:199], v240 offset:25648
	v_pk_fma_f32 v[64:65], v[52:53], v[118:119], v[64:65] op_sel_hi:[1,0,1]
	s_waitcnt lgkmcnt(1)
	v_pk_fma_f32 v[188:189], v[194:195], v[54:55], v[216:217] op_sel_hi:[1,0,1]
	s_nop 0
	v_pk_fma_f32 v[54:55], v[192:193], v[54:55], v[188:189] op_sel:[0,1,0]
	s_waitcnt lgkmcnt(0)
	v_mov_b32_e32 v118, v199
	v_pk_fma_f32 v[54:55], v[190:191], v[56:57], v[54:55] op_sel_hi:[1,0,1]
	v_mov_b32_e32 v56, v57
	v_pk_fma_f32 v[54:55], v[52:53], v[56:57], v[54:55] op_sel_hi:[1,0,1]
	v_pk_fma_f32 v[56:57], v[194:195], v[196:197], v[222:223] op_sel_hi:[1,0,1]
	s_nop 0
	v_pk_fma_f32 v[56:57], v[192:193], v[196:197], v[56:57] op_sel:[0,1,0]
	s_nop 0
	v_pk_fma_f32 v[56:57], v[190:191], v[198:199], v[56:57] op_sel_hi:[1,0,1]
	s_nop 0
	v_pk_fma_f32 v[56:57], v[52:53], v[118:119], v[56:57] op_sel_hi:[1,0,1]
	ds_read_b128 v[196:199], v240 offset:33856
	ds_read_b128 v[200:203], v240 offset:42064
	s_waitcnt lgkmcnt(1)
	v_pk_fma_f32 v[188:189], v[194:195], v[196:197], v[230:231] op_sel_hi:[1,0,1]
	s_waitcnt lgkmcnt(0)
	v_pk_fma_f32 v[204:205], v[194:195], v[200:201], v[234:235] op_sel_hi:[1,0,1]
	v_pk_fma_f32 v[188:189], v[192:193], v[196:197], v[188:189] op_sel:[0,1,0]
	v_mov_b32_e32 v118, v199
	v_pk_fma_f32 v[196:197], v[192:193], v[200:201], v[204:205] op_sel:[0,1,0]
	v_pk_fma_f32 v[188:189], v[190:191], v[198:199], v[188:189] op_sel_hi:[1,0,1]
	ds_read_b128 v[198:201], v240 offset:50272
	v_pk_fma_f32 v[188:189], v[52:53], v[118:119], v[188:189] op_sel_hi:[1,0,1]
	v_pk_fma_f32 v[196:197], v[190:191], v[202:203], v[196:197] op_sel_hi:[1,0,1]
	v_mov_b32_e32 v118, v203
	ds_read_b128 v[202:205], v240 offset:58480
	s_waitcnt lgkmcnt(1)
	v_pk_fma_f32 v[206:207], v[194:195], v[198:199], v[218:219] op_sel_hi:[1,0,1]
	v_pk_fma_f32 v[196:197], v[52:53], v[118:119], v[196:197] op_sel_hi:[1,0,1]
	v_pk_fma_f32 v[198:199], v[192:193], v[198:199], v[206:207] op_sel:[0,1,0]
	v_mov_b32_e32 v118, v201
	v_pk_fma_f32 v[198:199], v[190:191], v[200:201], v[198:199] op_sel_hi:[1,0,1]
	s_waitcnt lgkmcnt(0)
	v_pk_fma_f32 v[200:201], v[194:195], v[202:203], v[224:225] op_sel_hi:[1,0,1]
	v_pk_fma_f32 v[198:199], v[52:53], v[118:119], v[198:199] op_sel_hi:[1,0,1]
	v_pk_fma_f32 v[200:201], v[192:193], v[202:203], v[200:201] op_sel:[0,1,0]
	v_mov_b32_e32 v118, v205
	v_pk_fma_f32 v[200:201], v[190:191], v[204:205], v[200:201] op_sel_hi:[1,0,1]
	s_nop 0
	v_pk_fma_f32 v[200:201], v[52:53], v[118:119], v[200:201] op_sel_hi:[1,0,1]
	v_add_u32_e32 v87, 0x10480, v240
	ds_read_b128 v[202:205], v87
	v_add_u32_e32 v87, 0x12490, v240
	ds_read_b128 v[206:209], v87
	v_add_u32_e32 v87, 0x144a0, v240
	s_waitcnt lgkmcnt(1)
	v_pk_fma_f32 v[212:213], v[194:195], v[202:203], v[228:229] op_sel_hi:[1,0,1]
	s_nop 0
	v_pk_fma_f32 v[202:203], v[192:193], v[202:203], v[212:213] op_sel:[0,1,0]
	s_waitcnt lgkmcnt(0)
	v_pk_fma_f32 v[216:217], v[194:195], v[206:207], v[236:237] op_sel_hi:[1,0,1]
	v_mov_b32_e32 v118, v205
	v_pk_fma_f32 v[202:203], v[190:191], v[204:205], v[202:203] op_sel_hi:[1,0,1]
	v_pk_fma_f32 v[204:205], v[192:193], v[206:207], v[216:217] op_sel:[0,1,0]
	ds_read_b128 v[216:219], v87
	v_add_u32_e32 v87, 0x164b0, v240
	ds_read_b128 v[222:225], v87
	v_pk_fma_f32 v[202:203], v[52:53], v[118:119], v[202:203] op_sel_hi:[1,0,1]
	v_pk_fma_f32 v[204:205], v[190:191], v[208:209], v[204:205] op_sel_hi:[1,0,1]
	s_waitcnt lgkmcnt(1)
	v_pk_fma_f32 v[206:207], v[194:195], v[216:217], v[220:221] op_sel_hi:[1,0,1]
	v_mov_b32_e32 v118, v209
	v_pk_fma_f32 v[206:207], v[192:193], v[216:217], v[206:207] op_sel:[0,1,0]
	s_waitcnt lgkmcnt(0)
	v_pk_fma_f32 v[208:209], v[194:195], v[222:223], v[226:227] op_sel_hi:[1,0,1]
	v_pk_fma_f32 v[204:205], v[52:53], v[118:119], v[204:205] op_sel_hi:[1,0,1]
	v_pk_fma_f32 v[206:207], v[190:191], v[218:219], v[206:207] op_sel_hi:[1,0,1]
	v_mov_b32_e32 v118, v219
	v_pk_fma_f32 v[208:209], v[192:193], v[222:223], v[208:209] op_sel:[0,1,0]
	v_pk_fma_f32 v[206:207], v[52:53], v[118:119], v[206:207] op_sel_hi:[1,0,1]
	v_pk_fma_f32 v[208:209], v[190:191], v[224:225], v[208:209] op_sel_hi:[1,0,1]
	v_mov_b32_e32 v118, v225
	v_pk_fma_f32 v[208:209], v[52:53], v[118:119], v[208:209] op_sel_hi:[1,0,1]
	v_add_u32_e32 v87, 0x184c0, v240
	ds_read_b128 v[216:219], v87
	v_add_u32_e32 v87, 0x1a4d0, v240
	ds_read_b128 v[220:223], v87
	v_add_u32_e32 v87, 0x1c4e0, v240
	s_waitcnt lgkmcnt(1)
	v_pk_fma_f32 v[212:213], v[194:195], v[216:217], v[214:215] op_sel_hi:[1,0,1]
	s_nop 0
	v_pk_fma_f32 v[212:213], v[192:193], v[216:217], v[212:213] op_sel:[0,1,0]
	s_waitcnt lgkmcnt(0)
	v_pk_fma_f32 v[214:215], v[194:195], v[220:221], v[232:233] op_sel_hi:[1,0,1]
	v_mov_b32_e32 v118, v219
	v_pk_fma_f32 v[212:213], v[190:191], v[218:219], v[212:213] op_sel_hi:[1,0,1]
	v_pk_fma_f32 v[214:215], v[192:193], v[220:221], v[214:215] op_sel:[0,1,0]
	ds_read_b128 v[216:219], v87
	v_add_u32_e32 v87, 0x1e4f0, v240
	v_pk_fma_f32 v[212:213], v[52:53], v[118:119], v[212:213] op_sel_hi:[1,0,1]
	v_pk_fma_f32 v[214:215], v[190:191], v[222:223], v[214:215] op_sel_hi:[1,0,1]
	v_mov_b32_e32 v118, v223
	ds_read_b128 v[220:223], v87
	s_waitcnt lgkmcnt(1)
	v_pk_fma_f32 v[210:211], v[194:195], v[216:217], v[210:211] op_sel_hi:[1,0,1]
	v_pk_fma_f32 v[214:215], v[52:53], v[118:119], v[214:215] op_sel_hi:[1,0,1]
	v_pk_fma_f32 v[210:211], v[192:193], v[216:217], v[210:211] op_sel:[0,1,0]
	v_mov_b32_e32 v118, v219
	s_waitcnt lgkmcnt(0)
	v_pk_fma_f32 v[60:61], v[194:195], v[220:221], v[60:61] op_sel_hi:[1,0,1]
	v_pk_fma_f32 v[210:211], v[190:191], v[218:219], v[210:211] op_sel_hi:[1,0,1]
	v_pk_fma_f32 v[60:61], v[192:193], v[220:221], v[60:61] op_sel:[0,1,0]
	v_pk_fma_f32 v[210:211], v[52:53], v[118:119], v[210:211] op_sel_hi:[1,0,1]
	v_pk_fma_f32 v[60:61], v[190:191], v[222:223], v[60:61] op_sel_hi:[1,0,1]
	v_mov_b32_e32 v118, v223
	v_pk_fma_f32 v[60:61], v[52:53], v[118:119], v[60:61] op_sel_hi:[1,0,1]
	v_mov_b32_e32 v118, v46
	v_mov_b32_e32 v179, v186
	v_mul_f32_e32 v87, v83, v187
	v_pk_mul_f32 v[52:53], v[118:119], v[178:179]
	v_mov_b32_e32 v118, v47
	v_mov_b32_e32 v177, v184
	s_waitcnt vmcnt(11)
	v_fma_f32 v178, v52, v87, v42
	v_fma_f32 v179, v52, v53, v42
	v_mul_f32_e32 v42, v83, v185
	v_pk_mul_f32 v[46:47], v[118:119], v[176:177]
	v_mov_b32_e32 v118, v48
	v_mov_b32_e32 v175, v182
	v_fma_f32 v42, v46, v42, v43
	v_fma_f32 v43, v46, v47, v43
	v_mul_f32_e32 v52, v83, v183
	v_pk_mul_f32 v[46:47], v[118:119], v[174:175]
	v_mov_b32_e32 v118, v49
	v_mov_b32_e32 v173, v180
	v_fma_f32 v176, v46, v52, v44
	v_fma_f32 v177, v46, v47, v44
	v_mul_f32_e32 v44, v83, v181
	v_pk_mul_f32 v[46:47], v[118:119], v[172:173]
	ds_read_b128 v[172:175], v240 offset:10256
	v_fma_f32 v44, v46, v44, v45
	v_fmac_f32_e32 v45, v46, v47
	v_cvt_pk_bf16_f32 v46, v178, v42
	v_cvt_pk_bf16_f32 v47, v176, v44
	global_store_dwordx2 v[58:59], v[46:47], off offset:1024 sc1
	ds_read_b128 v[46:49], v240 offset:2048
	v_cvt_pk_bf16_f32 v52, v179, v43
	v_cvt_pk_bf16_f32 v53, v177, v45
	global_store_dwordx2 v[62:63], v[52:53], off offset:1024 sc1
	s_waitcnt lgkmcnt(1)
	v_mov_b32_e32 v52, v175
	s_waitcnt lgkmcnt(0)
	v_pk_fma_f32 v[50:51], v[178:179], v[46:47], v[50:51] op_sel_hi:[1,0,1]
	s_nop 0
	v_pk_fma_f32 v[46:47], v[42:43], v[46:47], v[50:51] op_sel:[0,1,0]
	s_nop 0
	v_pk_fma_f32 v[46:47], v[176:177], v[48:49], v[46:47] op_sel_hi:[1,0,1]
	v_mov_b32_e32 v48, v49
	v_pk_fma_f32 v[180:181], v[44:45], v[48:49], v[46:47] op_sel_hi:[1,0,1]
	v_pk_fma_f32 v[46:47], v[178:179], v[172:173], v[64:65] op_sel_hi:[1,0,1]
	s_nop 0
	v_pk_fma_f32 v[50:51], v[42:43], v[172:173], v[46:47] op_sel:[0,1,0]
	ds_read_b128 v[46:49], v240 offset:18464
	v_pk_fma_f32 v[50:51], v[176:177], v[174:175], v[50:51] op_sel_hi:[1,0,1]
	s_nop 0
	v_pk_fma_f32 v[64:65], v[44:45], v[52:53], v[50:51] op_sel_hi:[1,0,1]
	ds_read_b128 v[50:53], v240 offset:26672
	s_waitcnt lgkmcnt(1)
	v_pk_fma_f32 v[54:55], v[178:179], v[46:47], v[54:55] op_sel_hi:[1,0,1]
	s_nop 0
	v_pk_fma_f32 v[46:47], v[42:43], v[46:47], v[54:55] op_sel:[0,1,0]
	s_nop 0
	v_pk_fma_f32 v[46:47], v[176:177], v[48:49], v[46:47] op_sel_hi:[1,0,1]
	v_mov_b32_e32 v48, v49
	v_pk_fma_f32 v[54:55], v[44:45], v[48:49], v[46:47] op_sel_hi:[1,0,1]
	s_waitcnt lgkmcnt(0)
	v_pk_fma_f32 v[46:47], v[178:179], v[50:51], v[56:57] op_sel_hi:[1,0,1]
	v_mov_b32_e32 v48, v53
	v_pk_fma_f32 v[46:47], v[42:43], v[50:51], v[46:47] op_sel:[0,1,0]
	s_nop 0
	v_pk_fma_f32 v[46:47], v[176:177], v[52:53], v[46:47] op_sel_hi:[1,0,1]
	s_nop 0
	v_pk_fma_f32 v[56:57], v[44:45], v[48:49], v[46:47] op_sel_hi:[1,0,1]
	ds_read_b128 v[46:49], v240 offset:34880
	ds_read_b128 v[50:53], v240 offset:43088
	s_waitcnt lgkmcnt(1)
	v_pk_fma_f32 v[172:173], v[178:179], v[46:47], v[188:189] op_sel_hi:[1,0,1]
	s_nop 0
	v_pk_fma_f32 v[46:47], v[42:43], v[46:47], v[172:173] op_sel:[0,1,0]
	v_mov_b32_e32 v118, v49
	v_pk_fma_f32 v[46:47], v[176:177], v[48:49], v[46:47] op_sel_hi:[1,0,1]
	s_waitcnt lgkmcnt(0)
	v_pk_fma_f32 v[174:175], v[178:179], v[50:51], v[196:197] op_sel_hi:[1,0,1]
	v_pk_fma_f32 v[172:173], v[44:45], v[118:119], v[46:47] op_sel_hi:[1,0,1]
	ds_read_b128 v[46:49], v240 offset:51296
	v_pk_fma_f32 v[50:51], v[42:43], v[50:51], v[174:175] op_sel:[0,1,0]
	s_nop 0
	v_pk_fma_f32 v[50:51], v[176:177], v[52:53], v[50:51] op_sel_hi:[1,0,1]
	v_mov_b32_e32 v52, v53
	v_pk_fma_f32 v[174:175], v[44:45], v[52:53], v[50:51] op_sel_hi:[1,0,1]
	ds_read_b128 v[50:53], v240 offset:59504
	s_waitcnt lgkmcnt(1)
	v_pk_fma_f32 v[182:183], v[178:179], v[46:47], v[198:199] op_sel_hi:[1,0,1]
	s_nop 0
	v_pk_fma_f32 v[46:47], v[42:43], v[46:47], v[182:183] op_sel:[0,1,0]
	s_nop 0
	v_pk_fma_f32 v[46:47], v[176:177], v[48:49], v[46:47] op_sel_hi:[1,0,1]
	v_mov_b32_e32 v48, v49
	v_pk_fma_f32 v[182:183], v[44:45], v[48:49], v[46:47] op_sel_hi:[1,0,1]
	s_waitcnt lgkmcnt(0)
	v_pk_fma_f32 v[46:47], v[178:179], v[50:51], v[200:201] op_sel_hi:[1,0,1]
	v_mov_b32_e32 v48, v53
	v_pk_fma_f32 v[46:47], v[42:43], v[50:51], v[46:47] op_sel:[0,1,0]
	s_nop 0
	v_pk_fma_f32 v[46:47], v[176:177], v[52:53], v[46:47] op_sel_hi:[1,0,1]
	s_nop 0
	v_pk_fma_f32 v[184:185], v[44:45], v[48:49], v[46:47] op_sel_hi:[1,0,1]
	v_add_u32_e32 v46, 0x10880, v240
	ds_read_b128 v[46:49], v46
	v_add_u32_e32 v50, 0x12890, v240
	ds_read_b128 v[50:53], v50
	s_waitcnt lgkmcnt(1)
	v_pk_fma_f32 v[186:187], v[178:179], v[46:47], v[202:203] op_sel_hi:[1,0,1]
	s_nop 0
	v_pk_fma_f32 v[46:47], v[42:43], v[46:47], v[186:187] op_sel:[0,1,0]
	v_mov_b32_e32 v118, v49
	v_pk_fma_f32 v[46:47], v[176:177], v[48:49], v[46:47] op_sel_hi:[1,0,1]
	s_waitcnt lgkmcnt(0)
	v_pk_fma_f32 v[188:189], v[178:179], v[50:51], v[204:205] op_sel_hi:[1,0,1]
	v_pk_fma_f32 v[186:187], v[44:45], v[118:119], v[46:47] op_sel_hi:[1,0,1]
	v_add_u32_e32 v46, 0x148a0, v240
	v_pk_fma_f32 v[50:51], v[42:43], v[50:51], v[188:189] op_sel:[0,1,0]
	ds_read_b128 v[46:49], v46
	v_pk_fma_f32 v[50:51], v[176:177], v[52:53], v[50:51] op_sel_hi:[1,0,1]
	v_mov_b32_e32 v52, v53
	v_pk_fma_f32 v[188:189], v[44:45], v[52:53], v[50:51] op_sel_hi:[1,0,1]
	v_add_u32_e32 v50, 0x168b0, v240
	ds_read_b128 v[50:53], v50
	s_waitcnt lgkmcnt(1)
	v_pk_fma_f32 v[190:191], v[178:179], v[46:47], v[206:207] op_sel_hi:[1,0,1]
	s_nop 0
	v_pk_fma_f32 v[46:47], v[42:43], v[46:47], v[190:191] op_sel:[0,1,0]
	s_nop 0
	v_pk_fma_f32 v[46:47], v[176:177], v[48:49], v[46:47] op_sel_hi:[1,0,1]
	v_mov_b32_e32 v48, v49
	v_pk_fma_f32 v[190:191], v[44:45], v[48:49], v[46:47] op_sel_hi:[1,0,1]
	s_waitcnt lgkmcnt(0)
	v_pk_fma_f32 v[46:47], v[178:179], v[50:51], v[208:209] op_sel_hi:[1,0,1]
	v_mov_b32_e32 v48, v53
	v_pk_fma_f32 v[46:47], v[42:43], v[50:51], v[46:47] op_sel:[0,1,0]
	s_nop 0
	v_pk_fma_f32 v[46:47], v[176:177], v[52:53], v[46:47] op_sel_hi:[1,0,1]
	s_nop 0
	v_pk_fma_f32 v[192:193], v[44:45], v[48:49], v[46:47] op_sel_hi:[1,0,1]
	v_add_u32_e32 v46, 0x188c0, v240
	ds_read_b128 v[46:49], v46
	v_add_u32_e32 v50, 0x1a8d0, v240
	ds_read_b128 v[50:53], v50
	s_waitcnt lgkmcnt(1)
	v_pk_fma_f32 v[194:195], v[178:179], v[46:47], v[212:213] op_sel_hi:[1,0,1]
	s_nop 0
	v_pk_fma_f32 v[46:47], v[42:43], v[46:47], v[194:195] op_sel:[0,1,0]
	v_mov_b32_e32 v118, v49
	v_pk_fma_f32 v[46:47], v[176:177], v[48:49], v[46:47] op_sel_hi:[1,0,1]
	s_waitcnt lgkmcnt(0)
	v_pk_fma_f32 v[196:197], v[178:179], v[50:51], v[214:215] op_sel_hi:[1,0,1]
	v_pk_fma_f32 v[194:195], v[44:45], v[118:119], v[46:47] op_sel_hi:[1,0,1]
	v_add_u32_e32 v46, 0x1c8e0, v240
	v_pk_fma_f32 v[50:51], v[42:43], v[50:51], v[196:197] op_sel:[0,1,0]
	ds_read_b128 v[46:49], v46
	v_pk_fma_f32 v[50:51], v[176:177], v[52:53], v[50:51] op_sel_hi:[1,0,1]
	v_mov_b32_e32 v52, v53
	v_pk_fma_f32 v[196:197], v[44:45], v[52:53], v[50:51] op_sel_hi:[1,0,1]
	v_add_u32_e32 v50, 0x1e8f0, v240
	ds_read_b128 v[50:53], v50
	s_waitcnt lgkmcnt(1)
	v_pk_fma_f32 v[198:199], v[178:179], v[46:47], v[210:211] op_sel_hi:[1,0,1]
	s_nop 0
	v_pk_fma_f32 v[46:47], v[42:43], v[46:47], v[198:199] op_sel:[0,1,0]
	s_nop 0
	v_pk_fma_f32 v[46:47], v[176:177], v[48:49], v[46:47] op_sel_hi:[1,0,1]
	v_mov_b32_e32 v48, v49
	v_pk_fma_f32 v[46:47], v[44:45], v[48:49], v[46:47] op_sel_hi:[1,0,1]
	s_waitcnt lgkmcnt(0)
	v_pk_fma_f32 v[48:49], v[178:179], v[50:51], v[60:61] op_sel_hi:[1,0,1]
	s_nop 0
	v_pk_fma_f32 v[42:43], v[42:43], v[50:51], v[48:49] op_sel:[0,1,0]
	v_mov_b32_e32 v48, v53
	v_pk_fma_f32 v[42:43], v[176:177], v[52:53], v[42:43] op_sel_hi:[1,0,1]
	s_nop 0
	v_pk_fma_f32 v[48:49], v[44:45], v[48:49], v[42:43] op_sel_hi:[1,0,1]
	v_mov_b32_e32 v118, v38
	v_mov_b32_e32 v161, v168
	v_mul_f32_e32 v44, v83, v169
	v_pk_mul_f32 v[42:43], v[118:119], v[160:161]
	v_mov_b32_e32 v118, v39
	v_mov_b32_e32 v157, v166
	s_waitcnt vmcnt(12)
	v_fma_f32 v50, v42, v44, v34
	v_fma_f32 v51, v42, v43, v34
	v_mul_f32_e32 v34, v83, v167
	v_pk_mul_f32 v[38:39], v[118:119], v[156:157]
	v_mov_b32_e32 v118, v40
	v_mov_b32_e32 v155, v164
	v_fma_f32 v34, v38, v34, v35
	v_fma_f32 v35, v38, v39, v35
	v_mul_f32_e32 v42, v83, v165
	v_pk_mul_f32 v[38:39], v[118:119], v[154:155]
	v_mov_b32_e32 v118, v41
	v_mov_b32_e32 v153, v162
	v_fma_f32 v52, v38, v42, v36
	v_fma_f32 v53, v38, v39, v36
	v_mul_f32_e32 v36, v83, v163
	v_pk_mul_f32 v[38:39], v[118:119], v[152:153]
	v_cvt_pk_bf16_f32 v42, v51, v35
	v_fma_f32 v36, v38, v36, v37
	v_fmac_f32_e32 v37, v38, v39
	v_cvt_pk_bf16_f32 v38, v50, v34
	v_cvt_pk_bf16_f32 v39, v52, v36
	global_store_dwordx2 v[58:59], v[38:39], off offset:1536 sc1
	ds_read_b128 v[38:41], v240 offset:3072
	v_cvt_pk_bf16_f32 v43, v53, v37
	global_store_dwordx2 v[62:63], v[42:43], off offset:1536 sc1
	ds_read_b128 v[42:45], v240 offset:11280
	s_waitcnt lgkmcnt(1)
	v_pk_fma_f32 v[60:61], v[50:51], v[38:39], v[180:181] op_sel_hi:[1,0,1]
	s_nop 0
	v_pk_fma_f32 v[38:39], v[34:35], v[38:39], v[60:61] op_sel:[0,1,0]
	s_nop 0
	v_pk_fma_f32 v[38:39], v[52:53], v[40:41], v[38:39] op_sel_hi:[1,0,1]
	v_mov_b32_e32 v40, v41
	v_pk_fma_f32 v[60:61], v[36:37], v[40:41], v[38:39] op_sel_hi:[1,0,1]
	s_waitcnt lgkmcnt(0)
	v_pk_fma_f32 v[38:39], v[50:51], v[42:43], v[64:65] op_sel_hi:[1,0,1]
	s_nop 0
	v_pk_fma_f32 v[42:43], v[34:35], v[42:43], v[38:39] op_sel:[0,1,0]
	ds_read_b128 v[38:41], v240 offset:19488
	v_pk_fma_f32 v[42:43], v[52:53], v[44:45], v[42:43] op_sel_hi:[1,0,1]
	v_mov_b32_e32 v44, v45
	v_pk_fma_f32 v[64:65], v[36:37], v[44:45], v[42:43] op_sel_hi:[1,0,1]
	ds_read_b128 v[42:45], v240 offset:27696
	s_waitcnt lgkmcnt(1)
	v_pk_fma_f32 v[54:55], v[50:51], v[38:39], v[54:55] op_sel_hi:[1,0,1]
	s_nop 0
	v_pk_fma_f32 v[38:39], v[34:35], v[38:39], v[54:55] op_sel:[0,1,0]
	s_nop 0
	v_pk_fma_f32 v[38:39], v[52:53], v[40:41], v[38:39] op_sel_hi:[1,0,1]
	v_mov_b32_e32 v40, v41
	v_pk_fma_f32 v[54:55], v[36:37], v[40:41], v[38:39] op_sel_hi:[1,0,1]
	s_waitcnt lgkmcnt(0)
	v_pk_fma_f32 v[38:39], v[50:51], v[42:43], v[56:57] op_sel_hi:[1,0,1]
	v_mov_b32_e32 v40, v45
	v_pk_fma_f32 v[38:39], v[34:35], v[42:43], v[38:39] op_sel:[0,1,0]
	s_nop 0
	v_pk_fma_f32 v[38:39], v[52:53], v[44:45], v[38:39] op_sel_hi:[1,0,1]
	s_nop 0
	v_pk_fma_f32 v[56:57], v[36:37], v[40:41], v[38:39] op_sel_hi:[1,0,1]
	ds_read_b128 v[38:41], v240 offset:35904
	ds_read_b128 v[42:45], v240 offset:44112
	s_waitcnt lgkmcnt(1)
	v_pk_fma_f32 v[152:153], v[50:51], v[38:39], v[172:173] op_sel_hi:[1,0,1]
	s_nop 0
	v_pk_fma_f32 v[38:39], v[34:35], v[38:39], v[152:153] op_sel:[0,1,0]
	v_mov_b32_e32 v118, v41
	v_pk_fma_f32 v[38:39], v[52:53], v[40:41], v[38:39] op_sel_hi:[1,0,1]
	s_waitcnt lgkmcnt(0)
	v_pk_fma_f32 v[154:155], v[50:51], v[42:43], v[174:175] op_sel_hi:[1,0,1]
	v_pk_fma_f32 v[152:153], v[36:37], v[118:119], v[38:39] op_sel_hi:[1,0,1]
	ds_read_b128 v[38:41], v240 offset:52320
	v_pk_fma_f32 v[42:43], v[34:35], v[42:43], v[154:155] op_sel:[0,1,0]
	s_nop 0
	v_pk_fma_f32 v[42:43], v[52:53], v[44:45], v[42:43] op_sel_hi:[1,0,1]
	v_mov_b32_e32 v44, v45
	v_pk_fma_f32 v[154:155], v[36:37], v[44:45], v[42:43] op_sel_hi:[1,0,1]
	ds_read_b128 v[42:45], v240 offset:60528
	s_waitcnt lgkmcnt(1)
	v_pk_fma_f32 v[156:157], v[50:51], v[38:39], v[182:183] op_sel_hi:[1,0,1]
	s_nop 0
	v_pk_fma_f32 v[38:39], v[34:35], v[38:39], v[156:157] op_sel:[0,1,0]
	s_nop 0
	v_pk_fma_f32 v[38:39], v[52:53], v[40:41], v[38:39] op_sel_hi:[1,0,1]
	v_mov_b32_e32 v40, v41
	v_pk_fma_f32 v[156:157], v[36:37], v[40:41], v[38:39] op_sel_hi:[1,0,1]
	s_waitcnt lgkmcnt(0)
	v_pk_fma_f32 v[38:39], v[50:51], v[42:43], v[184:185] op_sel_hi:[1,0,1]
	v_mov_b32_e32 v40, v45
	v_pk_fma_f32 v[38:39], v[34:35], v[42:43], v[38:39] op_sel:[0,1,0]
	s_nop 0
	v_pk_fma_f32 v[38:39], v[52:53], v[44:45], v[38:39] op_sel_hi:[1,0,1]
	s_nop 0
	v_pk_fma_f32 v[160:161], v[36:37], v[40:41], v[38:39] op_sel_hi:[1,0,1]
	v_add_u32_e32 v38, 0x10c80, v240
	ds_read_b128 v[38:41], v38
	v_add_u32_e32 v42, 0x12c90, v240
	ds_read_b128 v[42:45], v42
	s_waitcnt lgkmcnt(1)
	v_pk_fma_f32 v[162:163], v[50:51], v[38:39], v[186:187] op_sel_hi:[1,0,1]
	s_nop 0
	v_pk_fma_f32 v[38:39], v[34:35], v[38:39], v[162:163] op_sel:[0,1,0]
	v_mov_b32_e32 v118, v41
	v_pk_fma_f32 v[38:39], v[52:53], v[40:41], v[38:39] op_sel_hi:[1,0,1]
	s_waitcnt lgkmcnt(0)
	v_pk_fma_f32 v[164:165], v[50:51], v[42:43], v[188:189] op_sel_hi:[1,0,1]
	v_pk_fma_f32 v[162:163], v[36:37], v[118:119], v[38:39] op_sel_hi:[1,0,1]
	v_add_u32_e32 v38, 0x14ca0, v240
	v_pk_fma_f32 v[42:43], v[34:35], v[42:43], v[164:165] op_sel:[0,1,0]
	ds_read_b128 v[38:41], v38
	v_pk_fma_f32 v[42:43], v[52:53], v[44:45], v[42:43] op_sel_hi:[1,0,1]
	v_mov_b32_e32 v44, v45
	v_pk_fma_f32 v[164:165], v[36:37], v[44:45], v[42:43] op_sel_hi:[1,0,1]
	v_add_u32_e32 v42, 0x16cb0, v240
	ds_read_b128 v[42:45], v42
	s_waitcnt lgkmcnt(1)
	v_pk_fma_f32 v[166:167], v[50:51], v[38:39], v[190:191] op_sel_hi:[1,0,1]
	s_nop 0
	v_pk_fma_f32 v[38:39], v[34:35], v[38:39], v[166:167] op_sel:[0,1,0]
	s_nop 0
	v_pk_fma_f32 v[38:39], v[52:53], v[40:41], v[38:39] op_sel_hi:[1,0,1]
	v_mov_b32_e32 v40, v41
	v_pk_fma_f32 v[166:167], v[36:37], v[40:41], v[38:39] op_sel_hi:[1,0,1]
	s_waitcnt lgkmcnt(0)
	v_pk_fma_f32 v[38:39], v[50:51], v[42:43], v[192:193] op_sel_hi:[1,0,1]
	v_mov_b32_e32 v40, v45
	v_pk_fma_f32 v[38:39], v[34:35], v[42:43], v[38:39] op_sel:[0,1,0]
	s_nop 0
	v_pk_fma_f32 v[38:39], v[52:53], v[44:45], v[38:39] op_sel_hi:[1,0,1]
	s_nop 0
	v_pk_fma_f32 v[168:169], v[36:37], v[40:41], v[38:39] op_sel_hi:[1,0,1]
	v_add_u32_e32 v38, 0x18cc0, v240
	ds_read_b128 v[38:41], v38
	v_add_u32_e32 v42, 0x1acd0, v240
	ds_read_b128 v[42:45], v42
	s_waitcnt lgkmcnt(1)
	v_pk_fma_f32 v[172:173], v[50:51], v[38:39], v[194:195] op_sel_hi:[1,0,1]
	s_nop 0
	v_pk_fma_f32 v[38:39], v[34:35], v[38:39], v[172:173] op_sel:[0,1,0]
	v_mov_b32_e32 v118, v41
	v_pk_fma_f32 v[38:39], v[52:53], v[40:41], v[38:39] op_sel_hi:[1,0,1]
	s_waitcnt lgkmcnt(0)
	v_pk_fma_f32 v[174:175], v[50:51], v[42:43], v[196:197] op_sel_hi:[1,0,1]
	v_pk_fma_f32 v[172:173], v[36:37], v[118:119], v[38:39] op_sel_hi:[1,0,1]
	v_add_u32_e32 v38, 0x1cce0, v240
	v_pk_fma_f32 v[42:43], v[34:35], v[42:43], v[174:175] op_sel:[0,1,0]
	ds_read_b128 v[38:41], v38
	v_pk_fma_f32 v[42:43], v[52:53], v[44:45], v[42:43] op_sel_hi:[1,0,1]
	v_mov_b32_e32 v44, v45
	v_pk_fma_f32 v[174:175], v[36:37], v[44:45], v[42:43] op_sel_hi:[1,0,1]
	v_add_u32_e32 v42, 0x1ecf0, v240
	ds_read_b128 v[42:45], v42
	s_waitcnt lgkmcnt(1)
	v_pk_fma_f32 v[46:47], v[50:51], v[38:39], v[46:47] op_sel_hi:[1,0,1]
	s_nop 0
	v_pk_fma_f32 v[38:39], v[34:35], v[38:39], v[46:47] op_sel:[0,1,0]
	s_nop 0
	v_pk_fma_f32 v[38:39], v[52:53], v[40:41], v[38:39] op_sel_hi:[1,0,1]
	v_mov_b32_e32 v40, v41
	v_pk_fma_f32 v[38:39], v[36:37], v[40:41], v[38:39] op_sel_hi:[1,0,1]
	s_waitcnt lgkmcnt(0)
	v_pk_fma_f32 v[40:41], v[50:51], v[42:43], v[48:49] op_sel_hi:[1,0,1]
	s_nop 0
	v_pk_fma_f32 v[34:35], v[34:35], v[42:43], v[40:41] op_sel:[0,1,0]
	v_mov_b32_e32 v40, v45
	v_pk_fma_f32 v[34:35], v[52:53], v[44:45], v[34:35] op_sel_hi:[1,0,1]
	s_nop 0
	v_pk_fma_f32 v[40:41], v[36:37], v[40:41], v[34:35] op_sel_hi:[1,0,1]
	v_mov_b32_e32 v118, v30
	v_mov_b32_e32 v151, v142
	v_mul_f32_e32 v36, v83, v134
	v_pk_mul_f32 v[34:35], v[118:119], v[150:151]
	v_mov_b32_e32 v118, v31
	v_mov_b32_e32 v149, v140
	s_waitcnt vmcnt(13)
	v_fma_f32 v42, v34, v36, v26
	v_fma_f32 v43, v34, v35, v26
	v_mul_f32_e32 v26, v83, v132
	v_pk_mul_f32 v[30:31], v[118:119], v[148:149]
	v_mov_b32_e32 v118, v32
	v_mov_b32_e32 v147, v138
	v_fma_f32 v26, v30, v26, v27
	v_fma_f32 v27, v30, v31, v27
	v_mul_f32_e32 v34, v83, v130
	v_pk_mul_f32 v[30:31], v[118:119], v[146:147]
	v_mov_b32_e32 v118, v33
	v_mov_b32_e32 v145, v136
	v_fma_f32 v44, v30, v34, v28
	v_fma_f32 v45, v30, v31, v28
	v_mul_f32_e32 v28, v83, v128
	v_pk_mul_f32 v[30:31], v[118:119], v[144:145]
	v_cvt_pk_bf16_f32 v34, v43, v27
	v_fma_f32 v28, v30, v28, v29
	v_fmac_f32_e32 v29, v30, v31
	v_cvt_pk_bf16_f32 v30, v42, v26
	v_cvt_pk_bf16_f32 v31, v44, v28
	global_store_dwordx2 v[58:59], v[30:31], off offset:2048 sc1
	ds_read_b128 v[30:33], v240 offset:4096
	v_cvt_pk_bf16_f32 v35, v45, v29
	global_store_dwordx2 v[62:63], v[34:35], off offset:2048 sc1
	ds_read_b128 v[34:37], v240 offset:12304
	s_waitcnt lgkmcnt(1)
	v_pk_fma_f32 v[46:47], v[42:43], v[30:31], v[60:61] op_sel_hi:[1,0,1]
	s_nop 0
	v_pk_fma_f32 v[30:31], v[26:27], v[30:31], v[46:47] op_sel:[0,1,0]
	s_nop 0
	v_pk_fma_f32 v[30:31], v[44:45], v[32:33], v[30:31] op_sel_hi:[1,0,1]
	v_mov_b32_e32 v32, v33
	v_pk_fma_f32 v[46:47], v[28:29], v[32:33], v[30:31] op_sel_hi:[1,0,1]
	s_waitcnt lgkmcnt(0)
	v_pk_fma_f32 v[30:31], v[42:43], v[34:35], v[64:65] op_sel_hi:[1,0,1]
	s_nop 0
	v_pk_fma_f32 v[34:35], v[26:27], v[34:35], v[30:31] op_sel:[0,1,0]
	ds_read_b128 v[30:33], v240 offset:20512
	v_pk_fma_f32 v[34:35], v[44:45], v[36:37], v[34:35] op_sel_hi:[1,0,1]
	v_mov_b32_e32 v36, v37
	v_pk_fma_f32 v[48:49], v[28:29], v[36:37], v[34:35] op_sel_hi:[1,0,1]
	ds_read_b128 v[34:37], v240 offset:28720
	s_waitcnt lgkmcnt(1)
	v_pk_fma_f32 v[50:51], v[42:43], v[30:31], v[54:55] op_sel_hi:[1,0,1]
	s_nop 0
	v_pk_fma_f32 v[30:31], v[26:27], v[30:31], v[50:51] op_sel:[0,1,0]
	s_nop 0
	v_pk_fma_f32 v[30:31], v[44:45], v[32:33], v[30:31] op_sel_hi:[1,0,1]
	v_mov_b32_e32 v32, v33
	v_pk_fma_f32 v[50:51], v[28:29], v[32:33], v[30:31] op_sel_hi:[1,0,1]
	s_waitcnt lgkmcnt(0)
	v_pk_fma_f32 v[30:31], v[42:43], v[34:35], v[56:57] op_sel_hi:[1,0,1]
	v_mov_b32_e32 v32, v37
	v_pk_fma_f32 v[30:31], v[26:27], v[34:35], v[30:31] op_sel:[0,1,0]
	s_nop 0
	v_pk_fma_f32 v[30:31], v[44:45], v[36:37], v[30:31] op_sel_hi:[1,0,1]
	s_nop 0
	v_pk_fma_f32 v[52:53], v[28:29], v[32:33], v[30:31] op_sel_hi:[1,0,1]
	ds_read_b128 v[30:33], v240 offset:36928
	ds_read_b128 v[34:37], v240 offset:45136
	s_waitcnt lgkmcnt(1)
	v_pk_fma_f32 v[54:55], v[42:43], v[30:31], v[152:153] op_sel_hi:[1,0,1]
	s_nop 0
	v_pk_fma_f32 v[30:31], v[26:27], v[30:31], v[54:55] op_sel:[0,1,0]
	v_mov_b32_e32 v56, v33
	v_pk_fma_f32 v[30:31], v[44:45], v[32:33], v[30:31] op_sel_hi:[1,0,1]
	s_waitcnt lgkmcnt(0)
	v_pk_fma_f32 v[60:61], v[42:43], v[34:35], v[154:155] op_sel_hi:[1,0,1]
	v_pk_fma_f32 v[54:55], v[28:29], v[56:57], v[30:31] op_sel_hi:[1,0,1]
	ds_read_b128 v[30:33], v240 offset:53344
	v_pk_fma_f32 v[34:35], v[26:27], v[34:35], v[60:61] op_sel:[0,1,0]
	s_nop 0
	v_pk_fma_f32 v[34:35], v[44:45], v[36:37], v[34:35] op_sel_hi:[1,0,1]
	v_mov_b32_e32 v36, v37
	v_pk_fma_f32 v[56:57], v[28:29], v[36:37], v[34:35] op_sel_hi:[1,0,1]
	ds_read_b128 v[34:37], v240 offset:61552
	s_waitcnt lgkmcnt(1)
	v_pk_fma_f32 v[60:61], v[42:43], v[30:31], v[156:157] op_sel_hi:[1,0,1]
	s_nop 0
	v_pk_fma_f32 v[30:31], v[26:27], v[30:31], v[60:61] op_sel:[0,1,0]
	s_nop 0
	v_pk_fma_f32 v[30:31], v[44:45], v[32:33], v[30:31] op_sel_hi:[1,0,1]
	v_mov_b32_e32 v32, v33
	v_pk_fma_f32 v[60:61], v[28:29], v[32:33], v[30:31] op_sel_hi:[1,0,1]
	s_waitcnt lgkmcnt(0)
	v_pk_fma_f32 v[30:31], v[42:43], v[34:35], v[160:161] op_sel_hi:[1,0,1]
	v_mov_b32_e32 v32, v37
	v_pk_fma_f32 v[30:31], v[26:27], v[34:35], v[30:31] op_sel:[0,1,0]
	s_nop 0
	v_pk_fma_f32 v[30:31], v[44:45], v[36:37], v[30:31] op_sel_hi:[1,0,1]
	s_nop 0
	v_pk_fma_f32 v[64:65], v[28:29], v[32:33], v[30:31] op_sel_hi:[1,0,1]
	v_add_u32_e32 v30, 0x11080, v240
	ds_read_b128 v[30:33], v30
	v_add_u32_e32 v34, 0x13090, v240
	ds_read_b128 v[34:37], v34
	s_waitcnt lgkmcnt(1)
	v_pk_fma_f32 v[144:145], v[42:43], v[30:31], v[162:163] op_sel_hi:[1,0,1]
	s_nop 0
	v_pk_fma_f32 v[30:31], v[26:27], v[30:31], v[144:145] op_sel:[0,1,0]
	v_mov_b32_e32 v118, v33
	v_pk_fma_f32 v[30:31], v[44:45], v[32:33], v[30:31] op_sel_hi:[1,0,1]
	s_waitcnt lgkmcnt(0)
	v_pk_fma_f32 v[146:147], v[42:43], v[34:35], v[164:165] op_sel_hi:[1,0,1]
	v_pk_fma_f32 v[144:145], v[28:29], v[118:119], v[30:31] op_sel_hi:[1,0,1]
	v_add_u32_e32 v30, 0x150a0, v240
	v_pk_fma_f32 v[34:35], v[26:27], v[34:35], v[146:147] op_sel:[0,1,0]
	ds_read_b128 v[30:33], v30
	v_pk_fma_f32 v[34:35], v[44:45], v[36:37], v[34:35] op_sel_hi:[1,0,1]
	v_mov_b32_e32 v36, v37
	v_pk_fma_f32 v[146:147], v[28:29], v[36:37], v[34:35] op_sel_hi:[1,0,1]
	v_add_u32_e32 v34, 0x170b0, v240
	ds_read_b128 v[34:37], v34
	s_waitcnt lgkmcnt(1)
	v_pk_fma_f32 v[148:149], v[42:43], v[30:31], v[166:167] op_sel_hi:[1,0,1]
	s_nop 0
	v_pk_fma_f32 v[30:31], v[26:27], v[30:31], v[148:149] op_sel:[0,1,0]
	s_nop 0
	v_pk_fma_f32 v[30:31], v[44:45], v[32:33], v[30:31] op_sel_hi:[1,0,1]
	v_mov_b32_e32 v32, v33
	v_pk_fma_f32 v[148:149], v[28:29], v[32:33], v[30:31] op_sel_hi:[1,0,1]
	s_waitcnt lgkmcnt(0)
	v_pk_fma_f32 v[30:31], v[42:43], v[34:35], v[168:169] op_sel_hi:[1,0,1]
	v_mov_b32_e32 v32, v37
	v_pk_fma_f32 v[30:31], v[26:27], v[34:35], v[30:31] op_sel:[0,1,0]
	s_nop 0
	v_pk_fma_f32 v[30:31], v[44:45], v[36:37], v[30:31] op_sel_hi:[1,0,1]
	s_nop 0
	v_pk_fma_f32 v[150:151], v[28:29], v[32:33], v[30:31] op_sel_hi:[1,0,1]
	v_add_u32_e32 v30, 0x190c0, v240
	ds_read_b128 v[30:33], v30
	v_add_u32_e32 v34, 0x1b0d0, v240
	ds_read_b128 v[34:37], v34
	s_waitcnt lgkmcnt(1)
	v_pk_fma_f32 v[152:153], v[42:43], v[30:31], v[172:173] op_sel_hi:[1,0,1]
	s_nop 0
	v_pk_fma_f32 v[30:31], v[26:27], v[30:31], v[152:153] op_sel:[0,1,0]
	v_mov_b32_e32 v118, v33
	v_pk_fma_f32 v[30:31], v[44:45], v[32:33], v[30:31] op_sel_hi:[1,0,1]
	s_waitcnt lgkmcnt(0)
	v_pk_fma_f32 v[154:155], v[42:43], v[34:35], v[174:175] op_sel_hi:[1,0,1]
	v_pk_fma_f32 v[152:153], v[28:29], v[118:119], v[30:31] op_sel_hi:[1,0,1]
	v_add_u32_e32 v30, 0x1d0e0, v240
	v_pk_fma_f32 v[34:35], v[26:27], v[34:35], v[154:155] op_sel:[0,1,0]
	ds_read_b128 v[30:33], v30
	v_pk_fma_f32 v[34:35], v[44:45], v[36:37], v[34:35] op_sel_hi:[1,0,1]
	v_mov_b32_e32 v36, v37
	v_pk_fma_f32 v[154:155], v[28:29], v[36:37], v[34:35] op_sel_hi:[1,0,1]
	v_add_u32_e32 v34, 0x1f0f0, v240
	ds_read_b128 v[34:37], v34
	s_waitcnt lgkmcnt(1)
	v_pk_fma_f32 v[38:39], v[42:43], v[30:31], v[38:39] op_sel_hi:[1,0,1]
	s_nop 0
	v_pk_fma_f32 v[30:31], v[26:27], v[30:31], v[38:39] op_sel:[0,1,0]
	s_nop 0
	v_pk_fma_f32 v[30:31], v[44:45], v[32:33], v[30:31] op_sel_hi:[1,0,1]
	v_mov_b32_e32 v32, v33
	v_pk_fma_f32 v[30:31], v[28:29], v[32:33], v[30:31] op_sel_hi:[1,0,1]
	s_waitcnt lgkmcnt(0)
	v_pk_fma_f32 v[32:33], v[42:43], v[34:35], v[40:41] op_sel_hi:[1,0,1]
	s_nop 0
	v_pk_fma_f32 v[26:27], v[26:27], v[34:35], v[32:33] op_sel:[0,1,0]
	v_mov_b32_e32 v32, v37
	v_pk_fma_f32 v[26:27], v[44:45], v[36:37], v[26:27] op_sel_hi:[1,0,1]
	s_nop 0
	v_pk_fma_f32 v[32:33], v[28:29], v[32:33], v[26:27] op_sel_hi:[1,0,1]
	v_mov_b32_e32 v118, v22
	v_mov_b32_e32 v127, v143
	v_mul_f32_e32 v28, v83, v135
	v_pk_mul_f32 v[26:27], v[118:119], v[126:127]
	v_mov_b32_e32 v118, v23
	v_mov_b32_e32 v125, v141
	s_waitcnt vmcnt(14)
	v_fma_f32 v34, v26, v28, v14
	v_fma_f32 v35, v26, v27, v14
	v_mul_f32_e32 v14, v83, v133
	v_pk_mul_f32 v[22:23], v[118:119], v[124:125]
	v_mov_b32_e32 v118, v24
	v_mov_b32_e32 v123, v139
	v_fma_f32 v14, v22, v14, v15
	v_fma_f32 v15, v22, v23, v15
	v_mul_f32_e32 v26, v83, v131
	v_pk_mul_f32 v[22:23], v[118:119], v[122:123]
	v_mov_b32_e32 v118, v25
	v_mov_b32_e32 v121, v137
	v_fma_f32 v36, v22, v26, v16
	v_fma_f32 v37, v22, v23, v16
	v_mul_f32_e32 v16, v83, v129
	v_pk_mul_f32 v[22:23], v[118:119], v[120:121]
	v_cvt_pk_bf16_f32 v26, v35, v15
	v_fma_f32 v16, v22, v16, v17
	v_fmac_f32_e32 v17, v22, v23
	v_cvt_pk_bf16_f32 v22, v34, v14
	v_cvt_pk_bf16_f32 v23, v36, v16
	global_store_dwordx2 v[58:59], v[22:23], off offset:2560 sc1
	ds_read_b128 v[22:25], v240 offset:5120
	v_cvt_pk_bf16_f32 v27, v37, v17
	global_store_dwordx2 v[62:63], v[26:27], off offset:2560 sc1
	ds_read_b128 v[26:29], v240 offset:13328
	s_waitcnt lgkmcnt(1)
	v_pk_fma_f32 v[38:39], v[34:35], v[22:23], v[46:47] op_sel_hi:[1,0,1]
	s_nop 0
	v_pk_fma_f32 v[22:23], v[14:15], v[22:23], v[38:39] op_sel:[0,1,0]
	s_nop 0
	v_pk_fma_f32 v[22:23], v[36:37], v[24:25], v[22:23] op_sel_hi:[1,0,1]
	v_mov_b32_e32 v24, v25
	v_pk_fma_f32 v[38:39], v[16:17], v[24:25], v[22:23] op_sel_hi:[1,0,1]
	s_waitcnt lgkmcnt(0)
	v_pk_fma_f32 v[22:23], v[34:35], v[26:27], v[48:49] op_sel_hi:[1,0,1]
	s_nop 0
	v_pk_fma_f32 v[26:27], v[14:15], v[26:27], v[22:23] op_sel:[0,1,0]
	ds_read_b128 v[22:25], v240 offset:21536
	v_pk_fma_f32 v[26:27], v[36:37], v[28:29], v[26:27] op_sel_hi:[1,0,1]
	v_mov_b32_e32 v28, v29
	v_pk_fma_f32 v[40:41], v[16:17], v[28:29], v[26:27] op_sel_hi:[1,0,1]
	ds_read_b128 v[26:29], v240 offset:29744
	s_waitcnt lgkmcnt(1)
	v_pk_fma_f32 v[42:43], v[34:35], v[22:23], v[50:51] op_sel_hi:[1,0,1]
	s_nop 0
	v_pk_fma_f32 v[22:23], v[14:15], v[22:23], v[42:43] op_sel:[0,1,0]
	s_nop 0
	v_pk_fma_f32 v[22:23], v[36:37], v[24:25], v[22:23] op_sel_hi:[1,0,1]
	v_mov_b32_e32 v24, v25
	v_pk_fma_f32 v[42:43], v[16:17], v[24:25], v[22:23] op_sel_hi:[1,0,1]
	s_waitcnt lgkmcnt(0)
	v_pk_fma_f32 v[22:23], v[34:35], v[26:27], v[52:53] op_sel_hi:[1,0,1]
	v_mov_b32_e32 v24, v29
	v_pk_fma_f32 v[22:23], v[14:15], v[26:27], v[22:23] op_sel:[0,1,0]
	s_nop 0
	v_pk_fma_f32 v[22:23], v[36:37], v[28:29], v[22:23] op_sel_hi:[1,0,1]
	s_nop 0
	v_pk_fma_f32 v[44:45], v[16:17], v[24:25], v[22:23] op_sel_hi:[1,0,1]
	ds_read_b128 v[22:25], v240 offset:37952
	ds_read_b128 v[26:29], v240 offset:46160
	s_waitcnt lgkmcnt(1)
	v_pk_fma_f32 v[46:47], v[34:35], v[22:23], v[54:55] op_sel_hi:[1,0,1]
	s_nop 0
	v_pk_fma_f32 v[22:23], v[14:15], v[22:23], v[46:47] op_sel:[0,1,0]
	v_mov_b32_e32 v48, v25
	v_pk_fma_f32 v[22:23], v[36:37], v[24:25], v[22:23] op_sel_hi:[1,0,1]
	s_waitcnt lgkmcnt(0)
	v_pk_fma_f32 v[50:51], v[34:35], v[26:27], v[56:57] op_sel_hi:[1,0,1]
	v_pk_fma_f32 v[46:47], v[16:17], v[48:49], v[22:23] op_sel_hi:[1,0,1]
	ds_read_b128 v[22:25], v240 offset:54368
	v_pk_fma_f32 v[26:27], v[14:15], v[26:27], v[50:51] op_sel:[0,1,0]
	s_nop 0
	v_pk_fma_f32 v[26:27], v[36:37], v[28:29], v[26:27] op_sel_hi:[1,0,1]
	v_mov_b32_e32 v28, v29
	v_pk_fma_f32 v[48:49], v[16:17], v[28:29], v[26:27] op_sel_hi:[1,0,1]
	ds_read_b128 v[26:29], v240 offset:62576
	s_waitcnt lgkmcnt(1)
	v_pk_fma_f32 v[50:51], v[34:35], v[22:23], v[60:61] op_sel_hi:[1,0,1]
	s_nop 0
	v_pk_fma_f32 v[22:23], v[14:15], v[22:23], v[50:51] op_sel:[0,1,0]
	s_nop 0
	v_pk_fma_f32 v[22:23], v[36:37], v[24:25], v[22:23] op_sel_hi:[1,0,1]
	v_mov_b32_e32 v24, v25
	v_pk_fma_f32 v[50:51], v[16:17], v[24:25], v[22:23] op_sel_hi:[1,0,1]
	s_waitcnt lgkmcnt(0)
	v_pk_fma_f32 v[22:23], v[34:35], v[26:27], v[64:65] op_sel_hi:[1,0,1]
	v_mov_b32_e32 v24, v29
	v_pk_fma_f32 v[22:23], v[14:15], v[26:27], v[22:23] op_sel:[0,1,0]
	s_nop 0
	v_pk_fma_f32 v[22:23], v[36:37], v[28:29], v[22:23] op_sel_hi:[1,0,1]
	s_nop 0
	v_pk_fma_f32 v[52:53], v[16:17], v[24:25], v[22:23] op_sel_hi:[1,0,1]
	v_add_u32_e32 v22, 0x11480, v240
	ds_read_b128 v[22:25], v22
	v_add_u32_e32 v26, 0x13490, v240
	ds_read_b128 v[26:29], v26
	s_waitcnt lgkmcnt(1)
	v_pk_fma_f32 v[54:55], v[34:35], v[22:23], v[144:145] op_sel_hi:[1,0,1]
	s_nop 0
	v_pk_fma_f32 v[22:23], v[14:15], v[22:23], v[54:55] op_sel:[0,1,0]
	v_mov_b32_e32 v56, v25
	v_pk_fma_f32 v[22:23], v[36:37], v[24:25], v[22:23] op_sel_hi:[1,0,1]
	s_waitcnt lgkmcnt(0)
	v_pk_fma_f32 v[60:61], v[34:35], v[26:27], v[146:147] op_sel_hi:[1,0,1]
	v_pk_fma_f32 v[54:55], v[16:17], v[56:57], v[22:23] op_sel_hi:[1,0,1]
	v_add_u32_e32 v22, 0x154a0, v240
	v_pk_fma_f32 v[26:27], v[14:15], v[26:27], v[60:61] op_sel:[0,1,0]
	ds_read_b128 v[22:25], v22
	v_pk_fma_f32 v[26:27], v[36:37], v[28:29], v[26:27] op_sel_hi:[1,0,1]
	v_mov_b32_e32 v28, v29
	v_pk_fma_f32 v[56:57], v[16:17], v[28:29], v[26:27] op_sel_hi:[1,0,1]
	v_add_u32_e32 v26, 0x174b0, v240
	ds_read_b128 v[26:29], v26
	s_waitcnt lgkmcnt(1)
	v_pk_fma_f32 v[60:61], v[34:35], v[22:23], v[148:149] op_sel_hi:[1,0,1]
	s_nop 0
	v_pk_fma_f32 v[22:23], v[14:15], v[22:23], v[60:61] op_sel:[0,1,0]
	s_nop 0
	v_pk_fma_f32 v[22:23], v[36:37], v[24:25], v[22:23] op_sel_hi:[1,0,1]
	v_mov_b32_e32 v24, v25
	v_pk_fma_f32 v[60:61], v[16:17], v[24:25], v[22:23] op_sel_hi:[1,0,1]
	s_waitcnt lgkmcnt(0)
	v_pk_fma_f32 v[22:23], v[34:35], v[26:27], v[150:151] op_sel_hi:[1,0,1]
	v_mov_b32_e32 v24, v29
	v_pk_fma_f32 v[22:23], v[14:15], v[26:27], v[22:23] op_sel:[0,1,0]
	s_nop 0
	v_pk_fma_f32 v[22:23], v[36:37], v[28:29], v[22:23] op_sel_hi:[1,0,1]
	s_nop 0
	v_pk_fma_f32 v[64:65], v[16:17], v[24:25], v[22:23] op_sel_hi:[1,0,1]
	v_add_u32_e32 v22, 0x194c0, v240
	ds_read_b128 v[22:25], v22
	v_add_u32_e32 v26, 0x1b4d0, v240
	ds_read_b128 v[26:29], v26
	s_waitcnt lgkmcnt(1)
	v_pk_fma_f32 v[120:121], v[34:35], v[22:23], v[152:153] op_sel_hi:[1,0,1]
	s_nop 0
	v_pk_fma_f32 v[22:23], v[14:15], v[22:23], v[120:121] op_sel:[0,1,0]
	v_mov_b32_e32 v118, v25
	v_pk_fma_f32 v[22:23], v[36:37], v[24:25], v[22:23] op_sel_hi:[1,0,1]
	s_waitcnt lgkmcnt(0)
	v_pk_fma_f32 v[122:123], v[34:35], v[26:27], v[154:155] op_sel_hi:[1,0,1]
	v_pk_fma_f32 v[120:121], v[16:17], v[118:119], v[22:23] op_sel_hi:[1,0,1]
	v_add_u32_e32 v22, 0x1d4e0, v240
	v_pk_fma_f32 v[26:27], v[14:15], v[26:27], v[122:123] op_sel:[0,1,0]
	ds_read_b128 v[22:25], v22
	v_pk_fma_f32 v[26:27], v[36:37], v[28:29], v[26:27] op_sel_hi:[1,0,1]
	v_mov_b32_e32 v28, v29
	v_pk_fma_f32 v[122:123], v[16:17], v[28:29], v[26:27] op_sel_hi:[1,0,1]
	v_add_u32_e32 v26, 0x1f4f0, v240
	ds_read_b128 v[26:29], v26
	s_waitcnt lgkmcnt(1)
	v_pk_fma_f32 v[30:31], v[34:35], v[22:23], v[30:31] op_sel_hi:[1,0,1]
	s_nop 0
	v_pk_fma_f32 v[22:23], v[14:15], v[22:23], v[30:31] op_sel:[0,1,0]
	s_nop 0
	v_pk_fma_f32 v[22:23], v[36:37], v[24:25], v[22:23] op_sel_hi:[1,0,1]
	v_mov_b32_e32 v24, v25
	v_pk_fma_f32 v[22:23], v[16:17], v[24:25], v[22:23] op_sel_hi:[1,0,1]
	s_waitcnt lgkmcnt(0)
	v_pk_fma_f32 v[24:25], v[34:35], v[26:27], v[32:33] op_sel_hi:[1,0,1]
	s_nop 0
	v_pk_fma_f32 v[14:15], v[14:15], v[26:27], v[24:25] op_sel:[0,1,0]
	v_mov_b32_e32 v24, v29
	v_pk_fma_f32 v[14:15], v[36:37], v[28:29], v[14:15] op_sel_hi:[1,0,1]
	s_nop 0
	v_pk_fma_f32 v[24:25], v[16:17], v[24:25], v[14:15] op_sel_hi:[1,0,1]
	s_waitcnt vmcnt(15)
	v_mov_b32_e32 v118, v18
	v_mov_b32_e32 v117, v108
	v_mul_f32_e32 v16, v83, v100
	v_pk_mul_f32 v[14:15], v[118:119], v[116:117]
	v_mov_b32_e32 v118, v19
	v_mov_b32_e32 v115, v106
	s_waitcnt vmcnt(13)
	v_fma_f32 v26, v14, v16, v10
	v_fma_f32 v27, v14, v15, v10
	v_mul_f32_e32 v10, v83, v98
	v_pk_mul_f32 v[14:15], v[118:119], v[114:115]
	v_mov_b32_e32 v118, v20
	v_mov_b32_e32 v113, v104
	v_fma_f32 v10, v14, v10, v11
	v_fma_f32 v11, v14, v15, v11
	v_mul_f32_e32 v16, v83, v96
	v_pk_mul_f32 v[14:15], v[118:119], v[112:113]
	v_mov_b32_e32 v118, v21
	v_mov_b32_e32 v111, v102
	v_fma_f32 v28, v14, v16, v12
	v_fma_f32 v29, v14, v15, v12
	v_mul_f32_e32 v12, v83, v94
	v_pk_mul_f32 v[14:15], v[118:119], v[110:111]
	v_cvt_pk_bf16_f32 v18, v27, v11
	v_fma_f32 v12, v14, v12, v13
	v_fmac_f32_e32 v13, v14, v15
	v_cvt_pk_bf16_f32 v14, v26, v10
	v_cvt_pk_bf16_f32 v15, v28, v12
	global_store_dwordx2 v[58:59], v[14:15], off offset:3072 sc1
	ds_read_b128 v[14:17], v240 offset:6144
	v_cvt_pk_bf16_f32 v19, v29, v13
	global_store_dwordx2 v[62:63], v[18:19], off offset:3072 sc1
	ds_read_b128 v[18:21], v240 offset:14352
	s_waitcnt lgkmcnt(1)
	v_pk_fma_f32 v[30:31], v[26:27], v[14:15], v[38:39] op_sel_hi:[1,0,1]
	s_nop 0
	v_pk_fma_f32 v[14:15], v[10:11], v[14:15], v[30:31] op_sel:[0,1,0]
	s_nop 0
	v_pk_fma_f32 v[14:15], v[28:29], v[16:17], v[14:15] op_sel_hi:[1,0,1]
	v_mov_b32_e32 v16, v17
	v_pk_fma_f32 v[30:31], v[12:13], v[16:17], v[14:15] op_sel_hi:[1,0,1]
	s_waitcnt lgkmcnt(0)
	v_pk_fma_f32 v[14:15], v[26:27], v[18:19], v[40:41] op_sel_hi:[1,0,1]
	s_nop 0
	v_pk_fma_f32 v[18:19], v[10:11], v[18:19], v[14:15] op_sel:[0,1,0]
	ds_read_b128 v[14:17], v240 offset:22560
	v_pk_fma_f32 v[18:19], v[28:29], v[20:21], v[18:19] op_sel_hi:[1,0,1]
	v_mov_b32_e32 v20, v21
	v_pk_fma_f32 v[32:33], v[12:13], v[20:21], v[18:19] op_sel_hi:[1,0,1]
	ds_read_b128 v[18:21], v240 offset:30768
	s_waitcnt lgkmcnt(1)
	v_pk_fma_f32 v[34:35], v[26:27], v[14:15], v[42:43] op_sel_hi:[1,0,1]
	s_nop 0
	v_pk_fma_f32 v[14:15], v[10:11], v[14:15], v[34:35] op_sel:[0,1,0]
	s_nop 0
	v_pk_fma_f32 v[14:15], v[28:29], v[16:17], v[14:15] op_sel_hi:[1,0,1]
	v_mov_b32_e32 v16, v17
	v_pk_fma_f32 v[34:35], v[12:13], v[16:17], v[14:15] op_sel_hi:[1,0,1]
	s_waitcnt lgkmcnt(0)
	v_pk_fma_f32 v[14:15], v[26:27], v[18:19], v[44:45] op_sel_hi:[1,0,1]
	v_mov_b32_e32 v16, v21
	v_pk_fma_f32 v[14:15], v[10:11], v[18:19], v[14:15] op_sel:[0,1,0]
	s_nop 0
	v_pk_fma_f32 v[14:15], v[28:29], v[20:21], v[14:15] op_sel_hi:[1,0,1]
	s_nop 0
	v_pk_fma_f32 v[36:37], v[12:13], v[16:17], v[14:15] op_sel_hi:[1,0,1]
	ds_read_b128 v[14:17], v240 offset:38976
	ds_read_b128 v[18:21], v240 offset:47184
	s_waitcnt lgkmcnt(1)
	v_pk_fma_f32 v[38:39], v[26:27], v[14:15], v[46:47] op_sel_hi:[1,0,1]
	s_nop 0
	v_pk_fma_f32 v[14:15], v[10:11], v[14:15], v[38:39] op_sel:[0,1,0]
	v_mov_b32_e32 v40, v17
	v_pk_fma_f32 v[14:15], v[28:29], v[16:17], v[14:15] op_sel_hi:[1,0,1]
	s_waitcnt lgkmcnt(0)
	v_pk_fma_f32 v[42:43], v[26:27], v[18:19], v[48:49] op_sel_hi:[1,0,1]
	v_pk_fma_f32 v[38:39], v[12:13], v[40:41], v[14:15] op_sel_hi:[1,0,1]
	ds_read_b128 v[14:17], v240 offset:55392
	v_pk_fma_f32 v[18:19], v[10:11], v[18:19], v[42:43] op_sel:[0,1,0]
	s_nop 0
	v_pk_fma_f32 v[18:19], v[28:29], v[20:21], v[18:19] op_sel_hi:[1,0,1]
	v_mov_b32_e32 v20, v21
	v_pk_fma_f32 v[40:41], v[12:13], v[20:21], v[18:19] op_sel_hi:[1,0,1]
	ds_read_b128 v[18:21], v240 offset:63600
	s_waitcnt lgkmcnt(1)
	v_pk_fma_f32 v[42:43], v[26:27], v[14:15], v[50:51] op_sel_hi:[1,0,1]
	s_nop 0
	v_pk_fma_f32 v[14:15], v[10:11], v[14:15], v[42:43] op_sel:[0,1,0]
	s_nop 0
	v_pk_fma_f32 v[14:15], v[28:29], v[16:17], v[14:15] op_sel_hi:[1,0,1]
	v_mov_b32_e32 v16, v17
	v_pk_fma_f32 v[42:43], v[12:13], v[16:17], v[14:15] op_sel_hi:[1,0,1]
	s_waitcnt lgkmcnt(0)
	v_pk_fma_f32 v[14:15], v[26:27], v[18:19], v[52:53] op_sel_hi:[1,0,1]
	v_mov_b32_e32 v16, v21
	v_pk_fma_f32 v[14:15], v[10:11], v[18:19], v[14:15] op_sel:[0,1,0]
	s_nop 0
	v_pk_fma_f32 v[14:15], v[28:29], v[20:21], v[14:15] op_sel_hi:[1,0,1]
	s_nop 0
	v_pk_fma_f32 v[44:45], v[12:13], v[16:17], v[14:15] op_sel_hi:[1,0,1]
	v_add_u32_e32 v14, 0x11880, v240
	ds_read_b128 v[14:17], v14
	v_add_u32_e32 v18, 0x13890, v240
	ds_read_b128 v[18:21], v18
	s_waitcnt lgkmcnt(1)
	v_pk_fma_f32 v[46:47], v[26:27], v[14:15], v[54:55] op_sel_hi:[1,0,1]
	s_nop 0
	v_pk_fma_f32 v[14:15], v[10:11], v[14:15], v[46:47] op_sel:[0,1,0]
	v_mov_b32_e32 v48, v17
	v_pk_fma_f32 v[14:15], v[28:29], v[16:17], v[14:15] op_sel_hi:[1,0,1]
	s_waitcnt lgkmcnt(0)
	v_pk_fma_f32 v[50:51], v[26:27], v[18:19], v[56:57] op_sel_hi:[1,0,1]
	v_pk_fma_f32 v[46:47], v[12:13], v[48:49], v[14:15] op_sel_hi:[1,0,1]
	v_add_u32_e32 v14, 0x158a0, v240
	v_pk_fma_f32 v[18:19], v[10:11], v[18:19], v[50:51] op_sel:[0,1,0]
	ds_read_b128 v[14:17], v14
	v_pk_fma_f32 v[18:19], v[28:29], v[20:21], v[18:19] op_sel_hi:[1,0,1]
	v_mov_b32_e32 v20, v21
	v_pk_fma_f32 v[48:49], v[12:13], v[20:21], v[18:19] op_sel_hi:[1,0,1]
	v_add_u32_e32 v18, 0x178b0, v240
	ds_read_b128 v[18:21], v18
	s_waitcnt lgkmcnt(1)
	v_pk_fma_f32 v[50:51], v[26:27], v[14:15], v[60:61] op_sel_hi:[1,0,1]
	s_nop 0
	v_pk_fma_f32 v[14:15], v[10:11], v[14:15], v[50:51] op_sel:[0,1,0]
	s_nop 0
	v_pk_fma_f32 v[14:15], v[28:29], v[16:17], v[14:15] op_sel_hi:[1,0,1]
	v_mov_b32_e32 v16, v17
	v_pk_fma_f32 v[50:51], v[12:13], v[16:17], v[14:15] op_sel_hi:[1,0,1]
	s_waitcnt lgkmcnt(0)
	v_pk_fma_f32 v[14:15], v[26:27], v[18:19], v[64:65] op_sel_hi:[1,0,1]
	v_mov_b32_e32 v16, v21
	v_pk_fma_f32 v[14:15], v[10:11], v[18:19], v[14:15] op_sel:[0,1,0]
	s_nop 0
	v_pk_fma_f32 v[14:15], v[28:29], v[20:21], v[14:15] op_sel_hi:[1,0,1]
	s_nop 0
	v_pk_fma_f32 v[52:53], v[12:13], v[16:17], v[14:15] op_sel_hi:[1,0,1]
	v_add_u32_e32 v14, 0x198c0, v240
	ds_read_b128 v[14:17], v14
	v_add_u32_e32 v18, 0x1b8d0, v240
	ds_read_b128 v[18:21], v18
	s_waitcnt lgkmcnt(1)
	v_pk_fma_f32 v[54:55], v[26:27], v[14:15], v[120:121] op_sel_hi:[1,0,1]
	s_nop 0
	v_pk_fma_f32 v[14:15], v[10:11], v[14:15], v[54:55] op_sel:[0,1,0]
	v_mov_b32_e32 v56, v17
	v_pk_fma_f32 v[14:15], v[28:29], v[16:17], v[14:15] op_sel_hi:[1,0,1]
	s_waitcnt lgkmcnt(0)
	v_pk_fma_f32 v[60:61], v[26:27], v[18:19], v[122:123] op_sel_hi:[1,0,1]
	v_pk_fma_f32 v[54:55], v[12:13], v[56:57], v[14:15] op_sel_hi:[1,0,1]
	v_add_u32_e32 v14, 0x1d8e0, v240
	v_pk_fma_f32 v[18:19], v[10:11], v[18:19], v[60:61] op_sel:[0,1,0]
	ds_read_b128 v[14:17], v14
	v_pk_fma_f32 v[18:19], v[28:29], v[20:21], v[18:19] op_sel_hi:[1,0,1]
	v_mov_b32_e32 v20, v21
	v_pk_fma_f32 v[56:57], v[12:13], v[20:21], v[18:19] op_sel_hi:[1,0,1]
	v_add_u32_e32 v18, 0x1f8f0, v240
	ds_read_b128 v[18:21], v18
	s_waitcnt lgkmcnt(1)
	v_pk_fma_f32 v[22:23], v[26:27], v[14:15], v[22:23] op_sel_hi:[1,0,1]
	s_nop 0
	v_pk_fma_f32 v[14:15], v[10:11], v[14:15], v[22:23] op_sel:[0,1,0]
	s_nop 0
	v_pk_fma_f32 v[14:15], v[28:29], v[16:17], v[14:15] op_sel_hi:[1,0,1]
	v_mov_b32_e32 v16, v17
	v_pk_fma_f32 v[14:15], v[12:13], v[16:17], v[14:15] op_sel_hi:[1,0,1]
	s_waitcnt lgkmcnt(0)
	v_pk_fma_f32 v[16:17], v[26:27], v[18:19], v[24:25] op_sel_hi:[1,0,1]
	s_nop 0
	v_pk_fma_f32 v[10:11], v[10:11], v[18:19], v[16:17] op_sel:[0,1,0]
	v_mov_b32_e32 v16, v21
	v_pk_fma_f32 v[10:11], v[28:29], v[20:21], v[10:11] op_sel_hi:[1,0,1]
	s_nop 0
	v_pk_fma_f32 v[16:17], v[12:13], v[16:17], v[10:11] op_sel_hi:[1,0,1]
	v_mov_b32_e32 v118, v6
	v_mov_b32_e32 v93, v109
	v_mul_f32_e32 v12, v83, v101
	v_pk_mul_f32 v[10:11], v[118:119], v[92:93]
	v_mov_b32_e32 v118, v7
	v_mov_b32_e32 v91, v107
	s_waitcnt vmcnt(14)
	v_fma_f32 v18, v10, v12, v2
	v_fma_f32 v19, v10, v11, v2
	v_mul_f32_e32 v2, v83, v99
	v_pk_mul_f32 v[6:7], v[118:119], v[90:91]
	v_mov_b32_e32 v118, v8
	v_mov_b32_e32 v89, v105
	v_fma_f32 v2, v6, v2, v3
	v_fma_f32 v3, v6, v7, v3
	v_mul_f32_e32 v10, v83, v97
	v_pk_mul_f32 v[6:7], v[118:119], v[88:89]
	v_mov_b32_e32 v118, v9
	v_mov_b32_e32 v87, v103
	v_fma_f32 v20, v6, v10, v4
	v_fma_f32 v21, v6, v7, v4
	v_mul_f32_e32 v4, v83, v95
	v_pk_mul_f32 v[6:7], v[118:119], v[86:87]
	v_cvt_pk_bf16_f32 v10, v19, v3
	v_fma_f32 v4, v6, v4, v5
	v_fmac_f32_e32 v5, v6, v7
	v_cvt_pk_bf16_f32 v6, v18, v2
	v_cvt_pk_bf16_f32 v7, v20, v4
	global_store_dwordx2 v[58:59], v[6:7], off offset:3584 sc1
	ds_read_b128 v[6:9], v240 offset:7168
	v_cvt_pk_bf16_f32 v11, v21, v5
	global_store_dwordx2 v[62:63], v[10:11], off offset:3584 sc1
	ds_read_b128 v[10:13], v240 offset:15376
	s_waitcnt lgkmcnt(1)
	v_pk_fma_f32 v[22:23], v[18:19], v[6:7], v[30:31] op_sel_hi:[1,0,1]
	s_nop 0
	v_pk_fma_f32 v[6:7], v[2:3], v[6:7], v[22:23] op_sel:[0,1,0]
	s_nop 0
	v_pk_fma_f32 v[6:7], v[20:21], v[8:9], v[6:7] op_sel_hi:[1,0,1]
	v_mov_b32_e32 v8, v9
	v_pk_fma_f32 v[22:23], v[4:5], v[8:9], v[6:7] op_sel_hi:[1,0,1]
	s_waitcnt lgkmcnt(0)
	v_pk_fma_f32 v[6:7], v[18:19], v[10:11], v[32:33] op_sel_hi:[1,0,1]
	s_nop 0
	v_pk_fma_f32 v[10:11], v[2:3], v[10:11], v[6:7] op_sel:[0,1,0]
	ds_read_b128 v[6:9], v240 offset:23584
	v_pk_fma_f32 v[10:11], v[20:21], v[12:13], v[10:11] op_sel_hi:[1,0,1]
	v_mov_b32_e32 v12, v13
	v_pk_fma_f32 v[24:25], v[4:5], v[12:13], v[10:11] op_sel_hi:[1,0,1]
	ds_read_b128 v[10:13], v240 offset:31792
	s_waitcnt lgkmcnt(1)
	v_pk_fma_f32 v[26:27], v[18:19], v[6:7], v[34:35] op_sel_hi:[1,0,1]
	s_nop 0
	v_pk_fma_f32 v[6:7], v[2:3], v[6:7], v[26:27] op_sel:[0,1,0]
	s_nop 0
	v_pk_fma_f32 v[6:7], v[20:21], v[8:9], v[6:7] op_sel_hi:[1,0,1]
	v_mov_b32_e32 v8, v9
	v_pk_fma_f32 v[26:27], v[4:5], v[8:9], v[6:7] op_sel_hi:[1,0,1]
	s_waitcnt lgkmcnt(0)
	v_pk_fma_f32 v[6:7], v[18:19], v[10:11], v[36:37] op_sel_hi:[1,0,1]
	v_mov_b32_e32 v8, v13
	v_pk_fma_f32 v[6:7], v[2:3], v[10:11], v[6:7] op_sel:[0,1,0]
	s_nop 0
	v_pk_fma_f32 v[6:7], v[20:21], v[12:13], v[6:7] op_sel_hi:[1,0,1]
	s_nop 0
	v_pk_fma_f32 v[28:29], v[4:5], v[8:9], v[6:7] op_sel_hi:[1,0,1]
	ds_read_b128 v[6:9], v240 offset:40000
	ds_read_b128 v[10:13], v240 offset:48208
	s_waitcnt lgkmcnt(1)
	v_pk_fma_f32 v[30:31], v[18:19], v[6:7], v[38:39] op_sel_hi:[1,0,1]
	s_nop 0
	v_pk_fma_f32 v[6:7], v[2:3], v[6:7], v[30:31] op_sel:[0,1,0]
	v_mov_b32_e32 v32, v9
	v_pk_fma_f32 v[6:7], v[20:21], v[8:9], v[6:7] op_sel_hi:[1,0,1]
	s_waitcnt lgkmcnt(0)
	v_pk_fma_f32 v[34:35], v[18:19], v[10:11], v[40:41] op_sel_hi:[1,0,1]
	v_pk_fma_f32 v[30:31], v[4:5], v[32:33], v[6:7] op_sel_hi:[1,0,1]
	ds_read_b128 v[6:9], v240 offset:56416
	v_pk_fma_f32 v[10:11], v[2:3], v[10:11], v[34:35] op_sel:[0,1,0]
	s_nop 0
	v_pk_fma_f32 v[10:11], v[20:21], v[12:13], v[10:11] op_sel_hi:[1,0,1]
	v_mov_b32_e32 v12, v13
	v_pk_fma_f32 v[32:33], v[4:5], v[12:13], v[10:11] op_sel_hi:[1,0,1]
	ds_read_b128 v[10:13], v240 offset:64624
	s_waitcnt lgkmcnt(1)
	v_pk_fma_f32 v[34:35], v[18:19], v[6:7], v[42:43] op_sel_hi:[1,0,1]
	s_nop 0
	v_pk_fma_f32 v[6:7], v[2:3], v[6:7], v[34:35] op_sel:[0,1,0]
	s_nop 0
	v_pk_fma_f32 v[6:7], v[20:21], v[8:9], v[6:7] op_sel_hi:[1,0,1]
	v_mov_b32_e32 v8, v9
	v_pk_fma_f32 v[34:35], v[4:5], v[8:9], v[6:7] op_sel_hi:[1,0,1]
	s_waitcnt lgkmcnt(0)
	v_pk_fma_f32 v[6:7], v[18:19], v[10:11], v[44:45] op_sel_hi:[1,0,1]
	v_mov_b32_e32 v8, v13
	v_pk_fma_f32 v[6:7], v[2:3], v[10:11], v[6:7] op_sel:[0,1,0]
	s_nop 0
	v_pk_fma_f32 v[6:7], v[20:21], v[12:13], v[6:7] op_sel_hi:[1,0,1]
	s_nop 0
	v_pk_fma_f32 v[36:37], v[4:5], v[8:9], v[6:7] op_sel_hi:[1,0,1]
	v_add_u32_e32 v6, 0x11c80, v240
	ds_read_b128 v[6:9], v6
	v_add_u32_e32 v10, 0x13c90, v240
	ds_read_b128 v[10:13], v10
	s_waitcnt lgkmcnt(1)
	v_pk_fma_f32 v[38:39], v[18:19], v[6:7], v[46:47] op_sel_hi:[1,0,1]
	s_nop 0
	v_pk_fma_f32 v[6:7], v[2:3], v[6:7], v[38:39] op_sel:[0,1,0]
	v_mov_b32_e32 v40, v9
	v_pk_fma_f32 v[6:7], v[20:21], v[8:9], v[6:7] op_sel_hi:[1,0,1]
	s_waitcnt lgkmcnt(0)
	v_pk_fma_f32 v[42:43], v[18:19], v[10:11], v[48:49] op_sel_hi:[1,0,1]
	v_pk_fma_f32 v[38:39], v[4:5], v[40:41], v[6:7] op_sel_hi:[1,0,1]
	v_add_u32_e32 v6, 0x15ca0, v240
	ds_read_b128 v[6:9], v6
	v_pk_fma_f32 v[10:11], v[2:3], v[10:11], v[42:43] op_sel:[0,1,0]
	s_nop 0
	v_pk_fma_f32 v[10:11], v[20:21], v[12:13], v[10:11] op_sel_hi:[1,0,1]
	v_mov_b32_e32 v12, v13
	v_pk_fma_f32 v[40:41], v[4:5], v[12:13], v[10:11] op_sel_hi:[1,0,1]
	ds_read_b128 v[10:13], v254
	s_waitcnt lgkmcnt(1)
	v_pk_fma_f32 v[42:43], v[18:19], v[6:7], v[50:51] op_sel_hi:[1,0,1]
	s_nop 0
	v_pk_fma_f32 v[6:7], v[2:3], v[6:7], v[42:43] op_sel:[0,1,0]
	s_nop 0
	v_pk_fma_f32 v[6:7], v[20:21], v[8:9], v[6:7] op_sel_hi:[1,0,1]
	v_mov_b32_e32 v8, v9
	v_pk_fma_f32 v[42:43], v[4:5], v[8:9], v[6:7] op_sel_hi:[1,0,1]
	s_waitcnt lgkmcnt(0)
	v_pk_fma_f32 v[6:7], v[18:19], v[10:11], v[52:53] op_sel_hi:[1,0,1]
	v_mov_b32_e32 v8, v13
	v_pk_fma_f32 v[6:7], v[2:3], v[10:11], v[6:7] op_sel:[0,1,0]
	s_nop 0
	v_pk_fma_f32 v[6:7], v[20:21], v[12:13], v[6:7] op_sel_hi:[1,0,1]
	s_nop 0
	v_pk_fma_f32 v[44:45], v[4:5], v[8:9], v[6:7] op_sel_hi:[1,0,1]
	ds_read_b128 v[6:9], v241
	ds_read_b128 v[10:13], v251
	s_waitcnt lgkmcnt(1)
	v_pk_fma_f32 v[46:47], v[18:19], v[6:7], v[54:55] op_sel_hi:[1,0,1]
	s_nop 0
	v_pk_fma_f32 v[6:7], v[2:3], v[6:7], v[46:47] op_sel:[0,1,0]
	v_mov_b32_e32 v48, v9
	v_pk_fma_f32 v[6:7], v[20:21], v[8:9], v[6:7] op_sel_hi:[1,0,1]
	s_waitcnt lgkmcnt(0)
	v_pk_fma_f32 v[50:51], v[18:19], v[10:11], v[56:57] op_sel_hi:[1,0,1]
	v_pk_fma_f32 v[46:47], v[4:5], v[48:49], v[6:7] op_sel_hi:[1,0,1]
	ds_read_b128 v[6:9], v252
	v_pk_fma_f32 v[10:11], v[2:3], v[10:11], v[50:51] op_sel:[0,1,0]
	s_nop 0
	v_pk_fma_f32 v[10:11], v[20:21], v[12:13], v[10:11] op_sel_hi:[1,0,1]
	v_mov_b32_e32 v12, v13
	v_pk_fma_f32 v[48:49], v[4:5], v[12:13], v[10:11] op_sel_hi:[1,0,1]
	ds_read_b128 v[10:13], v253
	s_waitcnt lgkmcnt(1)
	v_pk_fma_f32 v[14:15], v[18:19], v[6:7], v[14:15] op_sel_hi:[1,0,1]
	s_nop 0
	v_pk_fma_f32 v[6:7], v[2:3], v[6:7], v[14:15] op_sel:[0,1,0]
	s_nop 0
	v_pk_fma_f32 v[6:7], v[20:21], v[8:9], v[6:7] op_sel_hi:[1,0,1]
	v_mov_b32_e32 v8, v9
	v_pk_fma_f32 v[6:7], v[4:5], v[8:9], v[6:7] op_sel_hi:[1,0,1]
	s_waitcnt lgkmcnt(0)
	v_pk_fma_f32 v[8:9], v[18:19], v[10:11], v[16:17] op_sel_hi:[1,0,1]
	s_nop 0
	v_pk_fma_f32 v[2:3], v[2:3], v[10:11], v[8:9] op_sel:[0,1,0]
	v_mov_b32_e32 v8, v13
	v_pk_fma_f32 v[2:3], v[20:21], v[12:13], v[2:3] op_sel_hi:[1,0,1]
	s_nop 0
	v_pk_fma_f32 v[2:3], v[4:5], v[8:9], v[2:3] op_sel_hi:[1,0,1]
	v_mov_b32_e32 v4, v23
	v_mov_b32_e32 v8, v24
	v_cndmask_b32_e64 v5, v22, v4, s[0:1]
	ds_bpermute_b32 v5, v1, v5
	v_cndmask_b32_e64 v4, v4, v22, s[0:1]
	v_cndmask_b32_e64 v9, v25, v8, s[0:1]
	v_mov_b32_e32 v11, v29
	s_waitcnt lgkmcnt(0)
	v_add_f32_e32 v4, v4, v5
	v_cndmask_b32_e64 v5, v8, v25, s[0:1]
	v_mov_b32_e32 v8, v26
	ds_bpermute_b32 v5, v1, v5
	v_cndmask_b32_e64 v10, v8, v27, s[0:1]
	ds_bpermute_b32 v10, v1, v10
	v_cndmask_b32_e64 v8, v27, v8, s[0:1]
	v_cndmask_b32_e64 v12, v28, v11, s[0:1]
	ds_bpermute_b32 v12, v1, v12
	s_waitcnt lgkmcnt(1)
	v_add_f32_e32 v8, v8, v10
	v_mov_b32_e32 v10, v31
	v_add_f32_e32 v5, v9, v5
	v_cndmask_b32_e64 v9, v11, v28, s[0:1]
	s_waitcnt lgkmcnt(0)
	v_add_f32_e32 v9, v9, v12
	v_cndmask_b32_e64 v11, v10, v30, s[0:1]
	v_cndmask_b32_e64 v10, v30, v10, s[0:1]
	v_mov_b32_e32 v12, v32
	ds_bpermute_b32 v10, v1, v10
	v_mov_b32_e32 v14, v35
	v_cndmask_b32_e64 v13, v12, v33, s[0:1]
	ds_bpermute_b32 v13, v1, v13
	s_waitcnt lgkmcnt(1)
	v_add_f32_e32 v10, v11, v10
	v_cndmask_b32_e64 v15, v34, v14, s[0:1]
	ds_bpermute_b32 v15, v1, v15
	v_cndmask_b32_e64 v11, v33, v12, s[0:1]
	s_waitcnt lgkmcnt(1)
	v_add_f32_e32 v11, v11, v13
	v_mov_b32_e32 v13, v37
	v_cndmask_b32_e64 v12, v14, v34, s[0:1]
	s_waitcnt lgkmcnt(0)
	v_add_f32_e32 v12, v12, v15
	v_cndmask_b32_e64 v14, v13, v36, s[0:1]
	v_cndmask_b32_e64 v13, v36, v13, s[0:1]
	v_mov_b32_e32 v15, v38
	ds_bpermute_b32 v13, v1, v13
	v_mov_b32_e32 v17, v40
	v_cndmask_b32_e64 v16, v15, v39, s[0:1]
	ds_bpermute_b32 v16, v1, v16
	s_waitcnt lgkmcnt(1)
	v_add_f32_e32 v13, v14, v13
	v_cndmask_b32_e64 v18, v17, v41, s[0:1]
	ds_bpermute_b32 v18, v1, v18
	v_cndmask_b32_e64 v14, v39, v15, s[0:1]
	s_waitcnt lgkmcnt(1)
	v_add_f32_e32 v14, v14, v16
	v_mov_b32_e32 v16, v43
	v_cndmask_b32_e64 v15, v41, v17, s[0:1]
	s_waitcnt lgkmcnt(0)
	v_add_f32_e32 v15, v15, v18
	v_cndmask_b32_e64 v17, v16, v42, s[0:1]
	v_cndmask_b32_e64 v16, v42, v16, s[0:1]
	v_mov_b32_e32 v18, v44
	ds_bpermute_b32 v16, v1, v16
	v_mov_b32_e32 v20, v46
	v_cndmask_b32_e64 v19, v18, v45, s[0:1]
	ds_bpermute_b32 v19, v1, v19
	s_waitcnt lgkmcnt(1)
	v_add_f32_e32 v16, v17, v16
	v_cndmask_b32_e64 v21, v20, v47, s[0:1]
	ds_bpermute_b32 v21, v1, v21
	v_cndmask_b32_e64 v17, v45, v18, s[0:1]
	s_waitcnt lgkmcnt(1)
	v_add_f32_e32 v17, v17, v19
	v_mov_b32_e32 v19, v49
	v_cndmask_b32_e64 v18, v47, v20, s[0:1]
	v_cndmask_b32_e64 v22, v2, v3, s[0:1]
	v_cndmask_b32_e64 v2, v3, v2, s[0:1]
	v_cndmask_b32_e64 v3, v14, v4, s[4:5]
	v_cndmask_b32_e64 v4, v4, v14, s[4:5]
	s_waitcnt lgkmcnt(0)
	v_add_f32_e32 v18, v18, v21
	v_cndmask_b32_e64 v21, v6, v7, s[0:1]
	v_cndmask_b32_e64 v6, v7, v6, s[0:1]
	ds_bpermute_b32 v4, v85, v4
	v_cndmask_b32_e64 v20, v19, v48, s[0:1]
	v_cndmask_b32_e64 v7, v5, v15, s[4:5]
	ds_bpermute_b32 v7, v85, v7
	v_cndmask_b32_e64 v19, v48, v19, s[0:1]
	ds_bpermute_b32 v19, v1, v19
	ds_bpermute_b32 v21, v1, v21
	v_cndmask_b32_e64 v14, v8, v16, s[4:5]
	s_waitcnt lgkmcnt(3)
	v_add_f32_e32 v3, v3, v4
	v_cndmask_b32_e64 v4, v15, v5, s[4:5]
	v_cndmask_b32_e64 v5, v16, v8, s[4:5]
	ds_bpermute_b32 v22, v1, v22
	v_cndmask_b32_e64 v8, v9, v17, s[4:5]
	ds_bpermute_b32 v14, v85, v14
	s_waitcnt lgkmcnt(4)
	v_add_f32_e32 v4, v4, v7
	v_cndmask_b32_e64 v7, v17, v9, s[4:5]
	ds_bpermute_b32 v8, v85, v8
	s_waitcnt lgkmcnt(4)
	v_add_f32_e32 v19, v20, v19
	v_cndmask_b32_e64 v9, v10, v18, s[4:5]
	ds_bpermute_b32 v9, v85, v9
	s_waitcnt lgkmcnt(4)
	v_add_f32_e32 v6, v6, v21
	s_waitcnt lgkmcnt(3)
	v_add_f32_e32 v2, v2, v22
	s_waitcnt lgkmcnt(2)
	v_add_f32_e32 v5, v5, v14
	s_waitcnt lgkmcnt(1)
	v_add_f32_e32 v7, v7, v8
	v_cndmask_b32_e64 v14, v11, v19, s[4:5]
	v_cndmask_b32_e64 v8, v18, v10, s[4:5]
	ds_bpermute_b32 v14, v85, v14
	s_waitcnt lgkmcnt(1)
	v_add_f32_e32 v8, v8, v9
	v_cndmask_b32_e64 v9, v19, v11, s[4:5]
	v_cndmask_b32_e64 v10, v6, v12, s[4:5]
	v_cndmask_b32_e64 v6, v12, v6, s[4:5]
	ds_bpermute_b32 v6, v85, v6
	v_cndmask_b32_e64 v11, v13, v2, s[4:5]
	ds_bpermute_b32 v11, v85, v11
	s_waitcnt lgkmcnt(2)
	v_add_f32_e32 v9, v9, v14
	v_cndmask_b32_e64 v2, v2, v13, s[4:5]
	s_waitcnt lgkmcnt(1)
	v_add_f32_e32 v6, v10, v6
	s_waitcnt lgkmcnt(0)
	v_add_f32_e32 v2, v2, v11
	v_cndmask_b32_e64 v12, v3, v8, s[6:7]
	v_cndmask_b32_e64 v3, v8, v3, s[6:7]
	v_cndmask_b32_e64 v8, v9, v4, s[6:7]
	v_cndmask_b32_e64 v4, v4, v9, s[6:7]
	ds_bpermute_b32 v12, v159, v12
	v_cndmask_b32_e64 v9, v5, v6, s[6:7]
	v_cndmask_b32_e64 v10, v7, v2, s[6:7]
	ds_bpermute_b32 v4, v159, v4
	ds_bpermute_b32 v9, v159, v9
	ds_bpermute_b32 v10, v159, v10
	v_cndmask_b32_e64 v5, v6, v5, s[6:7]
	v_cndmask_b32_e64 v2, v2, v7, s[6:7]
	s_waitcnt lgkmcnt(3)
	v_add_f32_e32 v3, v3, v12
	s_waitcnt lgkmcnt(2)
	v_add_f32_e32 v4, v8, v4
	s_waitcnt lgkmcnt(1)
	v_add_f32_e32 v5, v5, v9
	s_waitcnt lgkmcnt(0)
	v_add_f32_e32 v2, v2, v10
	s_nop 0
	v_cndmask_b32_e64 v6, v3, v5, s[8:9]
	v_cndmask_b32_e64 v7, v4, v2, s[8:9]
	ds_bpermute_b32 v6, v171, v6
	ds_bpermute_b32 v7, v171, v7
	v_cndmask_b32_e64 v3, v5, v3, s[8:9]
	v_cndmask_b32_e64 v2, v2, v4, s[8:9]
	s_waitcnt lgkmcnt(1)
	v_add_f32_e32 v3, v3, v6
	s_waitcnt lgkmcnt(0)
	v_add_f32_e32 v2, v2, v7
	s_nop 0
	v_cndmask_b32_e64 v4, v3, v2, s[10:11]
	ds_bpermute_b32 v4, v238, v4
	v_cndmask_b32_e64 v2, v2, v3, s[10:11]
	s_waitcnt lgkmcnt(0)
	v_add_f32_e32 v2, v2, v4
	ds_bpermute_b32 v3, v239, v2
	s_waitcnt lgkmcnt(0)
	v_add_f32_e32 v2, v2, v3
	ds_bpermute_b32 v3, v238, v2
	s_waitcnt lgkmcnt(0)
	v_max_f32_e32 v3, v3, v3
	v_max_f32_e32 v3, v2, v3
	ds_bpermute_b32 v4, v171, v3
	s_waitcnt lgkmcnt(0)
	v_max_f32_e32 v4, v4, v4
	v_max_f32_e32 v3, v3, v4
	ds_bpermute_b32 v4, v159, v3
	s_waitcnt lgkmcnt(0)
	v_max_f32_e32 v4, v4, v4
	v_max_f32_e32 v3, v3, v4
	ds_bpermute_b32 v4, v85, v3
	s_waitcnt lgkmcnt(0)
	v_max_f32_e32 v4, v4, v4
	v_max_f32_e32 v3, v3, v4
	v_sub_f32_e32 v2, v2, v3
	v_mul_f32_e32 v3, 0x3fb8aa3b, v2
	v_fma_f32 v4, v2, s39, -v3
	v_rndne_f32_e32 v5, v3
	v_fmac_f32_e32 v4, 0x32a5705f, v2
	v_sub_f32_e32 v3, v3, v5
	v_add_f32_e32 v3, v3, v4
	v_exp_f32_e32 v3, v3
	v_cvt_i32_f32_e32 v4, v5
	v_cmp_ngt_f32_e32 vcc, s40, v2
	v_ldexp_f32 v3, v3, v4
	s_nop 0
	v_cndmask_b32_e32 v3, 0, v3, vcc
	v_cmp_nlt_f32_e32 vcc, s41, v2
	s_nop 1
	v_cndmask_b32_e32 v2, v250, v3, vcc
	ds_bpermute_b32 v3, v238, v2
	s_waitcnt lgkmcnt(0)
	v_add_f32_e32 v3, v2, v3
	ds_bpermute_b32 v4, v171, v3
	s_waitcnt lgkmcnt(0)
	v_add_f32_e32 v3, v3, v4
	ds_bpermute_b32 v4, v159, v3
	s_waitcnt lgkmcnt(0)
	v_add_f32_e32 v3, v3, v4
	ds_bpermute_b32 v4, v85, v3
	s_and_saveexec_b64 s[14:15], s[12:13]
	s_cbranch_execz .LBB0_1234
	s_waitcnt lgkmcnt(0)
	v_add_f32_e32 v3, v3, v4
	v_div_scale_f32 v4, s[26:27], v3, v3, v2
	v_rcp_f32_e32 v5, v4
	s_and_b32 s21, s20, 0x7fe
	v_mov_b32_e32 v83, v67
	v_fma_f32 v6, -v4, v5, 1.0
	v_fmac_f32_e32 v5, v6, v5
	v_div_scale_f32 v6, vcc, v2, v3, v2
	v_mul_f32_e32 v7, v6, v5
	v_fma_f32 v8, -v4, v7, v6
	v_fmac_f32_e32 v7, v8, v5
	v_fma_f32 v4, -v4, v7, v6
	v_div_fmas_f32 v4, v4, v5, v7
	v_div_fixup_f32 v4, v4, v3, v2
	v_bfe_u32 v2, v0, 1, 4
	v_lshl_or_b32 v2, s18, 4, v2
	v_ashrrev_i32_e32 v3, 31, v2
	v_lshlrev_b64 v[2:3], 13, v[2:3]
	v_lshl_add_u64 v[2:3], s[2:3], 0, v[2:3]
	s_lshl_b32 s18, s21, 2
	v_lshl_add_u64 v[2:3], v[2:3], 0, s[18:19]
	v_lshl_add_u64 v[2:3], v[2:3], 0, v[82:83]
	global_store_dword v[2:3], v4, off
	s_branch .LBB0_1234

.LBB0_1599:
	s_waitcnt vmcnt(13)
	v_lshlrev_b32_e32 v168, 16, v150
	v_and_b32_e32 v169, 0xffff0000, v150
	v_lshlrev_b32_e32 v150, 16, v151
	v_and_b32_e32 v151, 0xffff0000, v151
	s_waitcnt vmcnt(9)
	v_pk_fma_f32 v[62:63], v[62:63], v[166:167], v[150:151]
	v_lshlrev_b32_e32 v150, 16, v144
	v_and_b32_e32 v151, 0xffff0000, v144
	v_pk_fma_f32 v[60:61], v[60:61], v[160:161], v[168:169]
	v_lshlrev_b32_e32 v144, 16, v145
	v_and_b32_e32 v145, 0xffff0000, v145
	v_pk_fma_f32 v[56:57], v[56:57], v[162:163], v[150:151]
	v_mul_f32_e32 v160, v61, v61
	v_pk_fma_f32 v[58:59], v[58:59], v[164:165], v[144:145]
	v_mul_f32_e32 v144, v57, v57
	v_fmac_f32_e32 v160, v60, v60
	v_fmac_f32_e32 v144, v56, v56
	v_fmac_f32_e32 v160, v62, v62
	v_fmac_f32_e32 v144, v58, v58
	v_fmac_f32_e32 v160, v63, v63
	v_fmac_f32_e32 v144, v59, v59
	v_add_f32_e32 v150, v160, v144
	v_lshlrev_b32_e32 v144, 16, v138
	v_and_b32_e32 v145, 0xffff0000, v138
	v_lshlrev_b32_e32 v138, 16, v139
	v_and_b32_e32 v139, 0xffff0000, v139
	v_pk_fma_f32 v[52:53], v[52:53], v[156:157], v[144:145]
	v_pk_fma_f32 v[54:55], v[54:55], v[158:159], v[138:139]
	v_mul_f32_e32 v138, v53, v53
	v_fmac_f32_e32 v138, v52, v52
	v_fmac_f32_e32 v138, v54, v54
	v_fmac_f32_e32 v138, v55, v55
	v_add_f32_e32 v144, v138, v150
	v_lshlrev_b32_e32 v138, 16, v132
	v_and_b32_e32 v139, 0xffff0000, v132
	v_lshlrev_b32_e32 v132, 16, v133
	v_and_b32_e32 v133, 0xffff0000, v133
	s_waitcnt vmcnt(8)
	v_pk_fma_f32 v[48:49], v[48:49], v[152:153], v[138:139]
	v_pk_fma_f32 v[50:51], v[50:51], v[154:155], v[132:133]
	v_mul_f32_e32 v132, v49, v49
	v_fmac_f32_e32 v132, v48, v48
	v_fmac_f32_e32 v132, v50, v50
	v_fmac_f32_e32 v132, v51, v51
	v_add_f32_e32 v138, v132, v144
	s_waitcnt vmcnt(5)
	v_lshlrev_b32_e32 v132, 16, v128
	v_and_b32_e32 v133, 0xffff0000, v128
	v_lshlrev_b32_e32 v128, 16, v129
	v_and_b32_e32 v129, 0xffff0000, v129
	v_pk_fma_f32 v[46:47], v[46:47], v[148:149], v[128:129]
	s_waitcnt vmcnt(4)
	v_lshlrev_b32_e32 v128, 16, v124
	v_and_b32_e32 v129, 0xffff0000, v124
	v_pk_fma_f32 v[44:45], v[44:45], v[146:147], v[132:133]
	v_pk_fma_f32 v[40:41], v[40:41], v[140:141], v[128:129]
	v_lshlrev_b32_e32 v124, 16, v125
	v_and_b32_e32 v125, 0xffff0000, v125
	v_mov_b32_e32 v128, v41
	v_mov_b32_e32 v129, v45
	v_pk_fma_f32 v[42:43], v[42:43], v[142:143], v[124:125]
	v_mov_b32_e32 v124, v40
	v_mov_b32_e32 v125, v44
	v_pk_mul_f32 v[128:129], v[128:129], v[128:129]
	s_lshl_b64 s[14:15], s[14:15], 13
	v_pk_fma_f32 v[124:125], v[124:125], v[124:125], v[128:129]
	v_mov_b32_e32 v128, v42
	v_mov_b32_e32 v129, v46
	v_pk_fma_f32 v[124:125], v[128:129], v[128:129], v[124:125]
	v_mov_b32_e32 v128, v43
	v_mov_b32_e32 v129, v47
	v_pk_fma_f32 v[124:125], v[128:129], v[128:129], v[124:125]
	s_add_u32 s14, s68, s14
	v_add_f32_e32 v125, v125, v138
	v_add_f32_e32 v128, v124, v125
	s_waitcnt vmcnt(3)
	v_lshlrev_b32_e32 v124, 16, v122
	v_and_b32_e32 v125, 0xffff0000, v122
	v_lshlrev_b32_e32 v122, 16, v123
	v_and_b32_e32 v123, 0xffff0000, v123
	s_waitcnt vmcnt(1)
	v_pk_fma_f32 v[38:39], v[38:39], v[136:137], v[122:123]
	v_lshlrev_b32_e32 v122, 16, v120
	v_and_b32_e32 v123, 0xffff0000, v120
	v_pk_fma_f32 v[36:37], v[36:37], v[134:135], v[124:125]
	v_lshlrev_b32_e32 v120, 16, v121
	v_and_b32_e32 v121, 0xffff0000, v121
	s_waitcnt vmcnt(0)
	v_pk_fma_f32 v[122:123], v[32:33], v[126:127], v[122:123]
	v_pk_fma_f32 v[120:121], v[34:35], v[130:131], v[120:121]
	v_mov_b32_e32 v34, v123
	v_mov_b32_e32 v35, v37
	v_mov_b32_e32 v32, v122
	v_mov_b32_e32 v33, v36
	v_pk_mul_f32 v[34:35], v[34:35], v[34:35]
	s_addc_u32 s15, s69, s15
	v_pk_fma_f32 v[32:33], v[32:33], v[32:33], v[34:35]
	v_mov_b32_e32 v34, v120
	v_mov_b32_e32 v35, v38
	v_pk_fma_f32 v[32:33], v[34:35], v[34:35], v[32:33]
	v_mov_b32_e32 v34, v121
	v_mov_b32_e32 v35, v39
	v_pk_fma_f32 v[32:33], v[34:35], v[34:35], v[32:33]
	s_nop 0
	v_add_f32_e32 v33, v33, v128
	v_add_f32_e32 v32, v32, v33
	ds_bpermute_b32 v33, v67, v32
	s_waitcnt lgkmcnt(0)
	v_add_f32_e32 v32, v32, v33
	ds_bpermute_b32 v33, v171, v32
	s_waitcnt lgkmcnt(0)
	v_add_f32_e32 v32, v32, v33
	ds_bpermute_b32 v33, v186, v32
	s_waitcnt lgkmcnt(0)
	v_add_f32_e32 v32, v32, v33
	ds_bpermute_b32 v33, v187, v32
	s_waitcnt lgkmcnt(0)
	v_add_f32_e32 v32, v32, v33
	ds_bpermute_b32 v33, v188, v32
	s_waitcnt lgkmcnt(0)
	v_add_f32_e32 v32, v32, v33
	ds_bpermute_b32 v33, v189, v32
	s_waitcnt lgkmcnt(0)
	v_add_f32_e32 v32, v32, v33
	v_fmamk_f32 v32, v32, 0x3a000000, v190
	v_mul_f32_e32 v33, 0x4b800000, v32
	v_cmp_gt_f32_e32 vcc, s33, v32
	s_nop 1
	v_cndmask_b32_e32 v32, v32, v33, vcc
	v_rsq_f32_e32 v32, v32
	s_nop 0
	v_mul_f32_e32 v33, 0x45800000, v32
	v_cndmask_b32_e32 v124, v32, v33, vcc
	v_pk_mul_f32 v[32:33], v[60:61], v[124:125] op_sel_hi:[1,0]
	v_pk_mul_f32 v[34:35], v[62:63], v[124:125] op_sel_hi:[1,0]
	v_pk_mul_f32 v[32:33], v[0:1], v[32:33]
	v_pk_mul_f32 v[34:35], v[2:3], v[34:35]
	global_store_dwordx4 v64, v[32:35], s[14:15] sc1
	v_lshl_add_u64 v[60:61], s[14:15], 0, v[64:65]
	s_nop 0
	v_pk_mul_f32 v[32:33], v[56:57], v[124:125] op_sel_hi:[1,0]
	v_pk_mul_f32 v[34:35], v[58:59], v[124:125] op_sel_hi:[1,0]
	v_pk_mul_f32 v[32:33], v[4:5], v[32:33]
	v_pk_mul_f32 v[34:35], v[6:7], v[34:35]
	global_store_dwordx4 v64, v[32:35], s[14:15] offset:1024 sc1
	s_nop 1
	v_pk_mul_f32 v[32:33], v[52:53], v[124:125] op_sel_hi:[1,0]
	v_pk_mul_f32 v[34:35], v[54:55], v[124:125] op_sel_hi:[1,0]
	v_pk_mul_f32 v[32:33], v[8:9], v[32:33]
	v_pk_mul_f32 v[34:35], v[10:11], v[34:35]
	global_store_dwordx4 v64, v[32:35], s[14:15] offset:2048 sc1
	s_nop 1
	v_pk_mul_f32 v[32:33], v[48:49], v[124:125] op_sel_hi:[1,0]
	v_pk_mul_f32 v[34:35], v[50:51], v[124:125] op_sel_hi:[1,0]
	v_pk_mul_f32 v[32:33], v[12:13], v[32:33]
	v_pk_mul_f32 v[34:35], v[14:15], v[34:35]
	global_store_dwordx4 v64, v[32:35], s[14:15] offset:3072 sc1
	s_nop 1
	v_pk_mul_f32 v[32:33], v[44:45], v[124:125] op_sel_hi:[1,0]
	v_pk_mul_f32 v[34:35], v[46:47], v[124:125] op_sel_hi:[1,0]
	v_add_co_u32_e32 v44, vcc, s28, v60
	v_pk_mul_f32 v[34:35], v[18:19], v[34:35]
	v_pk_mul_f32 v[32:33], v[16:17], v[32:33]
	v_addc_co_u32_e32 v45, vcc, 0, v61, vcc
	global_store_dwordx4 v[44:45], v[32:35], off sc1
	s_nop 1
	v_pk_mul_f32 v[32:33], v[40:41], v[124:125] op_sel_hi:[1,0]
	v_pk_mul_f32 v[34:35], v[42:43], v[124:125] op_sel_hi:[1,0]
	v_pk_mul_f32 v[32:33], v[20:21], v[32:33]
	v_pk_mul_f32 v[34:35], v[22:23], v[34:35]
	global_store_dwordx4 v[44:45], v[32:35], off offset:1024 sc1
	s_nop 1
	v_pk_mul_f32 v[32:33], v[36:37], v[124:125] op_sel_hi:[1,0]
	v_pk_mul_f32 v[34:35], v[38:39], v[124:125] op_sel_hi:[1,0]
	v_pk_mul_f32 v[32:33], v[24:25], v[32:33]
	v_pk_mul_f32 v[34:35], v[26:27], v[34:35]
	global_store_dwordx4 v[44:45], v[32:35], off offset:2048 sc1
	s_nop 1
	v_pk_mul_f32 v[32:33], v[122:123], v[124:125] op_sel_hi:[1,0]
	v_pk_mul_f32 v[34:35], v[120:121], v[124:125] op_sel_hi:[1,0]
	v_pk_mul_f32 v[32:33], v[28:29], v[32:33]
	v_pk_mul_f32 v[34:35], v[30:31], v[34:35]
	global_store_dwordx4 v[44:45], v[32:35], off offset:3072 sc1

.LBB0_1631:
	s_waitcnt vmcnt(13)
	v_lshlrev_b32_e32 v168, 16, v150
	v_and_b32_e32 v169, 0xffff0000, v150
	v_lshlrev_b32_e32 v150, 16, v151
	v_and_b32_e32 v151, 0xffff0000, v151
	s_waitcnt vmcnt(9)
	v_pk_fma_f32 v[62:63], v[62:63], v[166:167], v[150:151]
	v_lshlrev_b32_e32 v150, 16, v144
	v_and_b32_e32 v151, 0xffff0000, v144
	v_pk_fma_f32 v[60:61], v[60:61], v[160:161], v[168:169]
	v_lshlrev_b32_e32 v144, 16, v145
	v_and_b32_e32 v145, 0xffff0000, v145
	v_pk_fma_f32 v[56:57], v[56:57], v[162:163], v[150:151]
	v_mul_f32_e32 v160, v61, v61
	v_pk_fma_f32 v[58:59], v[58:59], v[164:165], v[144:145]
	v_mul_f32_e32 v144, v57, v57
	v_fmac_f32_e32 v160, v60, v60
	v_fmac_f32_e32 v144, v56, v56
	v_fmac_f32_e32 v160, v62, v62
	v_fmac_f32_e32 v144, v58, v58
	v_fmac_f32_e32 v160, v63, v63
	v_fmac_f32_e32 v144, v59, v59
	v_add_f32_e32 v150, v160, v144
	v_lshlrev_b32_e32 v144, 16, v138
	v_and_b32_e32 v145, 0xffff0000, v138
	v_lshlrev_b32_e32 v138, 16, v139
	v_and_b32_e32 v139, 0xffff0000, v139
	v_pk_fma_f32 v[52:53], v[52:53], v[156:157], v[144:145]
	v_pk_fma_f32 v[54:55], v[54:55], v[158:159], v[138:139]
	v_mul_f32_e32 v138, v53, v53
	v_fmac_f32_e32 v138, v52, v52
	v_fmac_f32_e32 v138, v54, v54
	v_fmac_f32_e32 v138, v55, v55
	v_add_f32_e32 v144, v138, v150
	v_lshlrev_b32_e32 v138, 16, v132
	v_and_b32_e32 v139, 0xffff0000, v132
	v_lshlrev_b32_e32 v132, 16, v133
	v_and_b32_e32 v133, 0xffff0000, v133
	s_waitcnt vmcnt(8)
	v_pk_fma_f32 v[48:49], v[48:49], v[152:153], v[138:139]
	v_pk_fma_f32 v[50:51], v[50:51], v[154:155], v[132:133]
	v_mul_f32_e32 v132, v49, v49
	v_fmac_f32_e32 v132, v48, v48
	v_fmac_f32_e32 v132, v50, v50
	v_fmac_f32_e32 v132, v51, v51
	v_add_f32_e32 v138, v132, v144
	s_waitcnt vmcnt(5)
	v_lshlrev_b32_e32 v132, 16, v128
	v_and_b32_e32 v133, 0xffff0000, v128
	v_lshlrev_b32_e32 v128, 16, v129
	v_and_b32_e32 v129, 0xffff0000, v129
	v_pk_fma_f32 v[46:47], v[46:47], v[148:149], v[128:129]
	s_waitcnt vmcnt(4)
	v_lshlrev_b32_e32 v128, 16, v124
	v_and_b32_e32 v129, 0xffff0000, v124
	v_pk_fma_f32 v[44:45], v[44:45], v[146:147], v[132:133]
	v_pk_fma_f32 v[40:41], v[40:41], v[140:141], v[128:129]
	v_lshlrev_b32_e32 v124, 16, v125
	v_and_b32_e32 v125, 0xffff0000, v125
	v_mov_b32_e32 v128, v41
	v_mov_b32_e32 v129, v45
	v_pk_fma_f32 v[42:43], v[42:43], v[142:143], v[124:125]
	v_mov_b32_e32 v124, v40
	v_mov_b32_e32 v125, v44
	v_pk_mul_f32 v[128:129], v[128:129], v[128:129]
	s_lshl_b64 s[20:21], s[2:3], 13
	v_pk_fma_f32 v[124:125], v[124:125], v[124:125], v[128:129]
	v_mov_b32_e32 v128, v42
	v_mov_b32_e32 v129, v46
	v_pk_fma_f32 v[124:125], v[128:129], v[128:129], v[124:125]
	v_mov_b32_e32 v128, v43
	v_mov_b32_e32 v129, v47
	v_pk_fma_f32 v[124:125], v[128:129], v[128:129], v[124:125]
	s_add_u32 s20, s68, s20
	v_add_f32_e32 v125, v125, v138
	v_add_f32_e32 v128, v124, v125
	s_waitcnt vmcnt(3)
	v_lshlrev_b32_e32 v124, 16, v122
	v_and_b32_e32 v125, 0xffff0000, v122
	v_lshlrev_b32_e32 v122, 16, v123
	v_and_b32_e32 v123, 0xffff0000, v123
	s_waitcnt vmcnt(1)
	v_pk_fma_f32 v[38:39], v[38:39], v[136:137], v[122:123]
	v_lshlrev_b32_e32 v122, 16, v120
	v_and_b32_e32 v123, 0xffff0000, v120
	v_pk_fma_f32 v[36:37], v[36:37], v[134:135], v[124:125]
	v_lshlrev_b32_e32 v120, 16, v121
	v_and_b32_e32 v121, 0xffff0000, v121
	s_waitcnt vmcnt(0)
	v_pk_fma_f32 v[122:123], v[32:33], v[126:127], v[122:123]
	v_pk_fma_f32 v[120:121], v[34:35], v[130:131], v[120:121]
	v_mov_b32_e32 v34, v123
	v_mov_b32_e32 v35, v37
	v_mov_b32_e32 v32, v122
	v_mov_b32_e32 v33, v36
	v_pk_mul_f32 v[34:35], v[34:35], v[34:35]
	s_addc_u32 s21, s69, s21
	v_pk_fma_f32 v[32:33], v[32:33], v[32:33], v[34:35]
	v_mov_b32_e32 v34, v120
	v_mov_b32_e32 v35, v38
	v_pk_fma_f32 v[32:33], v[34:35], v[34:35], v[32:33]
	v_mov_b32_e32 v34, v121
	v_mov_b32_e32 v35, v39
	v_pk_fma_f32 v[32:33], v[34:35], v[34:35], v[32:33]
	s_cmpk_gt_i32 s18, 0x1fff
	v_add_f32_e32 v33, v33, v128
	v_add_f32_e32 v32, v32, v33
	ds_bpermute_b32 v33, v67, v32
	s_waitcnt lgkmcnt(0)
	v_add_f32_e32 v32, v32, v33
	ds_bpermute_b32 v33, v171, v32
	s_waitcnt lgkmcnt(0)
	v_add_f32_e32 v32, v32, v33
	ds_bpermute_b32 v33, v186, v32
	s_waitcnt lgkmcnt(0)
	v_add_f32_e32 v32, v32, v33
	ds_bpermute_b32 v33, v187, v32
	s_waitcnt lgkmcnt(0)
	v_add_f32_e32 v32, v32, v33
	ds_bpermute_b32 v33, v188, v32
	s_waitcnt lgkmcnt(0)
	v_add_f32_e32 v32, v32, v33
	ds_bpermute_b32 v33, v189, v32
	s_waitcnt lgkmcnt(0)
	v_add_f32_e32 v32, v32, v33
	v_fmamk_f32 v32, v32, 0x3a000000, v190
	v_mul_f32_e32 v33, 0x4b800000, v32
	v_cmp_gt_f32_e32 vcc, s33, v32
	s_nop 1
	v_cndmask_b32_e32 v32, v32, v33, vcc
	v_rsq_f32_e32 v32, v32
	s_nop 0
	v_mul_f32_e32 v33, 0x45800000, v32
	v_cndmask_b32_e32 v124, v32, v33, vcc
	v_pk_mul_f32 v[32:33], v[60:61], v[124:125] op_sel_hi:[1,0]
	v_pk_mul_f32 v[34:35], v[62:63], v[124:125] op_sel_hi:[1,0]
	v_pk_mul_f32 v[32:33], v[0:1], v[32:33]
	v_pk_mul_f32 v[34:35], v[2:3], v[34:35]
	global_store_dwordx4 v64, v[32:35], s[20:21] sc1
	v_lshl_add_u64 v[60:61], s[20:21], 0, v[64:65]
	s_nop 0
	v_pk_mul_f32 v[32:33], v[56:57], v[124:125] op_sel_hi:[1,0]
	v_pk_mul_f32 v[34:35], v[58:59], v[124:125] op_sel_hi:[1,0]
	v_pk_mul_f32 v[32:33], v[4:5], v[32:33]
	v_pk_mul_f32 v[34:35], v[6:7], v[34:35]
	global_store_dwordx4 v64, v[32:35], s[20:21] offset:1024 sc1
	s_nop 1
	v_pk_mul_f32 v[32:33], v[52:53], v[124:125] op_sel_hi:[1,0]
	v_pk_mul_f32 v[34:35], v[54:55], v[124:125] op_sel_hi:[1,0]
	v_pk_mul_f32 v[32:33], v[8:9], v[32:33]
	v_pk_mul_f32 v[34:35], v[10:11], v[34:35]
	global_store_dwordx4 v64, v[32:35], s[20:21] offset:2048 sc1
	s_nop 1
	v_pk_mul_f32 v[32:33], v[48:49], v[124:125] op_sel_hi:[1,0]
	v_pk_mul_f32 v[34:35], v[50:51], v[124:125] op_sel_hi:[1,0]
	v_pk_mul_f32 v[32:33], v[12:13], v[32:33]
	v_pk_mul_f32 v[34:35], v[14:15], v[34:35]
	global_store_dwordx4 v64, v[32:35], s[20:21] offset:3072 sc1
	s_nop 1
	v_pk_mul_f32 v[32:33], v[44:45], v[124:125] op_sel_hi:[1,0]
	v_pk_mul_f32 v[34:35], v[46:47], v[124:125] op_sel_hi:[1,0]
	v_add_co_u32_e32 v44, vcc, s28, v60
	v_pk_mul_f32 v[34:35], v[18:19], v[34:35]
	v_pk_mul_f32 v[32:33], v[16:17], v[32:33]
	v_addc_co_u32_e32 v45, vcc, 0, v61, vcc
	global_store_dwordx4 v[44:45], v[32:35], off sc1
	s_nop 1
	v_pk_mul_f32 v[32:33], v[40:41], v[124:125] op_sel_hi:[1,0]
	v_pk_mul_f32 v[34:35], v[42:43], v[124:125] op_sel_hi:[1,0]
	v_pk_mul_f32 v[32:33], v[20:21], v[32:33]
	v_pk_mul_f32 v[34:35], v[22:23], v[34:35]
	global_store_dwordx4 v[44:45], v[32:35], off offset:1024 sc1
	s_nop 1
	v_pk_mul_f32 v[32:33], v[36:37], v[124:125] op_sel_hi:[1,0]
	v_pk_mul_f32 v[34:35], v[38:39], v[124:125] op_sel_hi:[1,0]
	v_pk_mul_f32 v[32:33], v[24:25], v[32:33]
	v_pk_mul_f32 v[34:35], v[26:27], v[34:35]
	global_store_dwordx4 v[44:45], v[32:35], off offset:2048 sc1
	s_nop 1
	v_pk_mul_f32 v[32:33], v[122:123], v[124:125] op_sel_hi:[1,0]
	v_pk_mul_f32 v[34:35], v[120:121], v[124:125] op_sel_hi:[1,0]
	v_pk_mul_f32 v[32:33], v[28:29], v[32:33]
	v_pk_mul_f32 v[34:35], v[30:31], v[34:35]
	global_store_dwordx4 v[44:45], v[32:35], off offset:3072 sc1
	s_cbranch_scc1 .LBB0_1600
	s_ashr_i32 s19, s18, 31
	s_ashr_i32 s3, s18, 11
	s_lshl_b64 s[20:21], s[18:19], 12
	v_lshl_add_u64 v[32:33], v[68:69], 0, s[20:21]
	s_mul_i32 s20, s3, 0x3000
	s_ashr_i32 s21, s20, 31
	s_lshl_b64 s[20:21], s[20:21], 2
	s_add_u32 s20, s70, s20
	s_addc_u32 s21, s71, s21
	v_lshl_add_u64 v[34:35], s[20:21], 0, v[64:65]
	v_add_co_u32_e32 v38, vcc, s31, v34
	v_lshl_add_u64 v[36:37], v[34:35], 0, s[12:13]
	s_nop 0
	v_addc_co_u32_e32 v39, vcc, 0, v35, vcc
	v_add_co_u32_e32 v34, vcc, 0x13000, v34
	global_load_dwordx4 v[56:59], v[36:37], off offset:1024
	global_load_dwordx4 v[52:55], v[36:37], off offset:2048
	global_load_dwordx2 v[150:151], v[32:33], off nt
	global_load_dwordx2 v[144:145], v[32:33], off offset:512 nt
	global_load_dwordx2 v[138:139], v[32:33], off offset:1024 nt
	global_load_dwordx2 v[132:133], v[32:33], off offset:1536 nt
	global_load_dwordx4 v[60:63], v[38:39], off
	global_load_dwordx4 v[48:51], v[36:37], off offset:3072
	v_addc_co_u32_e32 v35, vcc, 0, v35, vcc
	global_load_dwordx4 v[44:47], v[34:35], off
	global_load_dwordx4 v[40:43], v[34:35], off offset:1024
	global_load_dwordx2 v[128:129], v[32:33], off offset:2048 nt
	global_load_dwordx2 v[124:125], v[32:33], off offset:2560 nt
	global_load_dwordx2 v[122:123], v[32:33], off offset:3072 nt
	global_load_dwordx2 v[120:121], v[32:33], off offset:3584 nt
	global_load_dwordx4 v[36:39], v[34:35], off offset:2048
	s_nop 0
	global_load_dwordx4 v[32:35], v[34:35], off offset:3072
	v_cmp_lt_i32_e32 vcc, -1, v193
	s_and_b32 s15, vcc_lo, 0xffff
	s_cmp_eq_u32 s15, 0
	s_cbranch_scc1 .LBB0_1653
	s_lshl_b32 s3, s3, 8
	v_mov_b32_e32 v160, 0
	s_ashr_i32 s6, s3, 31
	v_mov_b32_e32 v161, v160
	v_mov_b32_e32 v166, v160
	v_mov_b32_e32 v167, v160
	v_mov_b32_e32 v162, v160
	v_mov_b32_e32 v163, v160
	v_mov_b32_e32 v164, v160
	v_mov_b32_e32 v165, v160
	v_mov_b32_e32 v156, v160
	v_mov_b32_e32 v157, v160
	v_mov_b32_e32 v158, v160
	v_mov_b32_e32 v159, v160
	v_mov_b32_e32 v152, v160
	v_mov_b32_e32 v153, v160
	v_mov_b32_e32 v154, v160
	v_mov_b32_e32 v155, v160
	v_mov_b32_e32 v146, v160
	v_mov_b32_e32 v147, v160
	v_mov_b32_e32 v148, v160
	v_mov_b32_e32 v149, v160
	v_mov_b32_e32 v140, v160
	v_mov_b32_e32 v141, v160
	v_mov_b32_e32 v142, v160
	v_mov_b32_e32 v143, v160
	v_mov_b32_e32 v134, v160
	v_mov_b32_e32 v135, v160
	v_mov_b32_e32 v136, v160
	v_mov_b32_e32 v137, v160
	v_mov_b32_e32 v126, v160
	v_mov_b32_e32 v127, v160
	v_mov_b32_e32 v130, v160
	v_mov_b32_e32 v131, v160
	s_branch .LBB0_1635

.LBB0_1654:
	s_waitcnt vmcnt(13)
	v_lshlrev_b32_e32 v168, 16, v150
	v_and_b32_e32 v169, 0xffff0000, v150
	v_lshlrev_b32_e32 v150, 16, v151
	v_and_b32_e32 v151, 0xffff0000, v151
	s_waitcnt vmcnt(9)
	v_pk_fma_f32 v[62:63], v[62:63], v[166:167], v[150:151]
	v_lshlrev_b32_e32 v150, 16, v144
	v_and_b32_e32 v151, 0xffff0000, v144
	v_pk_fma_f32 v[60:61], v[60:61], v[160:161], v[168:169]
	v_lshlrev_b32_e32 v144, 16, v145
	v_and_b32_e32 v145, 0xffff0000, v145
	v_pk_fma_f32 v[56:57], v[56:57], v[162:163], v[150:151]
	v_mul_f32_e32 v160, v61, v61
	v_pk_fma_f32 v[58:59], v[58:59], v[164:165], v[144:145]
	v_mul_f32_e32 v144, v57, v57
	v_fmac_f32_e32 v160, v60, v60
	v_fmac_f32_e32 v144, v56, v56
	v_fmac_f32_e32 v160, v62, v62
	v_fmac_f32_e32 v144, v58, v58
	v_fmac_f32_e32 v160, v63, v63
	v_fmac_f32_e32 v144, v59, v59
	v_add_f32_e32 v150, v160, v144
	v_lshlrev_b32_e32 v144, 16, v138
	v_and_b32_e32 v145, 0xffff0000, v138
	v_lshlrev_b32_e32 v138, 16, v139
	v_and_b32_e32 v139, 0xffff0000, v139
	v_pk_fma_f32 v[52:53], v[52:53], v[156:157], v[144:145]
	v_pk_fma_f32 v[54:55], v[54:55], v[158:159], v[138:139]
	v_mul_f32_e32 v138, v53, v53
	v_fmac_f32_e32 v138, v52, v52
	v_fmac_f32_e32 v138, v54, v54
	v_fmac_f32_e32 v138, v55, v55
	v_add_f32_e32 v144, v138, v150
	v_lshlrev_b32_e32 v138, 16, v132
	v_and_b32_e32 v139, 0xffff0000, v132
	v_lshlrev_b32_e32 v132, 16, v133
	v_and_b32_e32 v133, 0xffff0000, v133
	s_waitcnt vmcnt(8)
	v_pk_fma_f32 v[48:49], v[48:49], v[152:153], v[138:139]
	v_pk_fma_f32 v[50:51], v[50:51], v[154:155], v[132:133]
	v_mul_f32_e32 v132, v49, v49
	v_fmac_f32_e32 v132, v48, v48
	v_fmac_f32_e32 v132, v50, v50
	v_fmac_f32_e32 v132, v51, v51
	v_add_f32_e32 v138, v132, v144
	s_waitcnt vmcnt(5)
	v_lshlrev_b32_e32 v132, 16, v128
	v_and_b32_e32 v133, 0xffff0000, v128
	v_lshlrev_b32_e32 v128, 16, v129
	v_and_b32_e32 v129, 0xffff0000, v129
	v_pk_fma_f32 v[46:47], v[46:47], v[148:149], v[128:129]
	s_waitcnt vmcnt(4)
	v_lshlrev_b32_e32 v128, 16, v124
	v_and_b32_e32 v129, 0xffff0000, v124
	v_pk_fma_f32 v[44:45], v[44:45], v[146:147], v[132:133]
	v_pk_fma_f32 v[40:41], v[40:41], v[140:141], v[128:129]
	v_lshlrev_b32_e32 v124, 16, v125
	v_and_b32_e32 v125, 0xffff0000, v125
	v_mov_b32_e32 v128, v41
	v_mov_b32_e32 v129, v45
	v_pk_fma_f32 v[42:43], v[42:43], v[142:143], v[124:125]
	v_mov_b32_e32 v124, v40
	v_mov_b32_e32 v125, v44
	v_pk_mul_f32 v[128:129], v[128:129], v[128:129]
	s_lshl_b64 s[18:19], s[18:19], 13
	v_pk_fma_f32 v[124:125], v[124:125], v[124:125], v[128:129]
	v_mov_b32_e32 v128, v42
	v_mov_b32_e32 v129, v46
	v_pk_fma_f32 v[124:125], v[128:129], v[128:129], v[124:125]
	v_mov_b32_e32 v128, v43
	v_mov_b32_e32 v129, v47
	v_pk_fma_f32 v[124:125], v[128:129], v[128:129], v[124:125]
	s_add_u32 s18, s68, s18
	v_add_f32_e32 v125, v125, v138
	v_add_f32_e32 v128, v124, v125
	s_waitcnt vmcnt(3)
	v_lshlrev_b32_e32 v124, 16, v122
	v_and_b32_e32 v125, 0xffff0000, v122
	v_lshlrev_b32_e32 v122, 16, v123
	v_and_b32_e32 v123, 0xffff0000, v123
	s_waitcnt vmcnt(1)
	v_pk_fma_f32 v[38:39], v[38:39], v[136:137], v[122:123]
	v_lshlrev_b32_e32 v122, 16, v120
	v_and_b32_e32 v123, 0xffff0000, v120
	v_pk_fma_f32 v[36:37], v[36:37], v[134:135], v[124:125]
	v_lshlrev_b32_e32 v120, 16, v121
	v_and_b32_e32 v121, 0xffff0000, v121
	s_waitcnt vmcnt(0)
	v_pk_fma_f32 v[122:123], v[32:33], v[126:127], v[122:123]
	v_pk_fma_f32 v[120:121], v[34:35], v[130:131], v[120:121]
	v_mov_b32_e32 v34, v123
	v_mov_b32_e32 v35, v37
	v_mov_b32_e32 v32, v122
	v_mov_b32_e32 v33, v36
	v_pk_mul_f32 v[34:35], v[34:35], v[34:35]
	s_addc_u32 s19, s69, s19
	v_pk_fma_f32 v[32:33], v[32:33], v[32:33], v[34:35]
	v_mov_b32_e32 v34, v120
	v_mov_b32_e32 v35, v38
	v_pk_fma_f32 v[32:33], v[34:35], v[34:35], v[32:33]
	v_mov_b32_e32 v34, v121
	v_mov_b32_e32 v35, v39
	v_pk_fma_f32 v[32:33], v[34:35], v[34:35], v[32:33]
	s_cmpk_gt_i32 s16, 0x1fff
	v_add_f32_e32 v33, v33, v128
	v_add_f32_e32 v32, v32, v33
	ds_bpermute_b32 v33, v67, v32
	s_waitcnt lgkmcnt(0)
	v_add_f32_e32 v32, v32, v33
	ds_bpermute_b32 v33, v171, v32
	s_waitcnt lgkmcnt(0)
	v_add_f32_e32 v32, v32, v33
	ds_bpermute_b32 v33, v186, v32
	s_waitcnt lgkmcnt(0)
	v_add_f32_e32 v32, v32, v33
	ds_bpermute_b32 v33, v187, v32
	s_waitcnt lgkmcnt(0)
	v_add_f32_e32 v32, v32, v33
	ds_bpermute_b32 v33, v188, v32
	s_waitcnt lgkmcnt(0)
	v_add_f32_e32 v32, v32, v33
	ds_bpermute_b32 v33, v189, v32
	s_waitcnt lgkmcnt(0)
	v_add_f32_e32 v32, v32, v33
	v_fmamk_f32 v32, v32, 0x3a000000, v190
	v_mul_f32_e32 v33, 0x4b800000, v32
	v_cmp_gt_f32_e32 vcc, s33, v32
	s_nop 1
	v_cndmask_b32_e32 v32, v32, v33, vcc
	v_rsq_f32_e32 v32, v32
	s_nop 0
	v_mul_f32_e32 v33, 0x45800000, v32
	v_cndmask_b32_e32 v124, v32, v33, vcc
	v_pk_mul_f32 v[32:33], v[60:61], v[124:125] op_sel_hi:[1,0]
	v_pk_mul_f32 v[34:35], v[62:63], v[124:125] op_sel_hi:[1,0]
	v_pk_mul_f32 v[32:33], v[0:1], v[32:33]
	v_pk_mul_f32 v[34:35], v[2:3], v[34:35]
	global_store_dwordx4 v64, v[32:35], s[18:19] sc1
	v_lshl_add_u64 v[60:61], s[18:19], 0, v[64:65]
	s_nop 0
	v_pk_mul_f32 v[32:33], v[56:57], v[124:125] op_sel_hi:[1,0]
	v_pk_mul_f32 v[34:35], v[58:59], v[124:125] op_sel_hi:[1,0]
	v_pk_mul_f32 v[32:33], v[4:5], v[32:33]
	v_pk_mul_f32 v[34:35], v[6:7], v[34:35]
	global_store_dwordx4 v64, v[32:35], s[18:19] offset:1024 sc1
	s_nop 1
	v_pk_mul_f32 v[32:33], v[52:53], v[124:125] op_sel_hi:[1,0]
	v_pk_mul_f32 v[34:35], v[54:55], v[124:125] op_sel_hi:[1,0]
	v_pk_mul_f32 v[32:33], v[8:9], v[32:33]
	v_pk_mul_f32 v[34:35], v[10:11], v[34:35]
	global_store_dwordx4 v64, v[32:35], s[18:19] offset:2048 sc1
	s_nop 1
	v_pk_mul_f32 v[32:33], v[48:49], v[124:125] op_sel_hi:[1,0]
	v_pk_mul_f32 v[34:35], v[50:51], v[124:125] op_sel_hi:[1,0]
	v_pk_mul_f32 v[32:33], v[12:13], v[32:33]
	v_pk_mul_f32 v[34:35], v[14:15], v[34:35]
	global_store_dwordx4 v64, v[32:35], s[18:19] offset:3072 sc1
	s_nop 1
	v_pk_mul_f32 v[32:33], v[44:45], v[124:125] op_sel_hi:[1,0]
	v_pk_mul_f32 v[34:35], v[46:47], v[124:125] op_sel_hi:[1,0]
	v_add_co_u32_e32 v44, vcc, s28, v60
	v_pk_mul_f32 v[34:35], v[18:19], v[34:35]
	v_pk_mul_f32 v[32:33], v[16:17], v[32:33]
	v_addc_co_u32_e32 v45, vcc, 0, v61, vcc
	global_store_dwordx4 v[44:45], v[32:35], off sc1
	s_nop 1
	v_pk_mul_f32 v[32:33], v[40:41], v[124:125] op_sel_hi:[1,0]
	v_pk_mul_f32 v[34:35], v[42:43], v[124:125] op_sel_hi:[1,0]
	v_pk_mul_f32 v[32:33], v[20:21], v[32:33]
	v_pk_mul_f32 v[34:35], v[22:23], v[34:35]
	global_store_dwordx4 v[44:45], v[32:35], off offset:1024 sc1
	s_nop 1
	v_pk_mul_f32 v[32:33], v[36:37], v[124:125] op_sel_hi:[1,0]
	v_pk_mul_f32 v[34:35], v[38:39], v[124:125] op_sel_hi:[1,0]
	v_pk_mul_f32 v[32:33], v[24:25], v[32:33]
	v_pk_mul_f32 v[34:35], v[26:27], v[34:35]
	global_store_dwordx4 v[44:45], v[32:35], off offset:2048 sc1
	s_nop 1
	v_pk_mul_f32 v[32:33], v[122:123], v[124:125] op_sel_hi:[1,0]
	v_pk_mul_f32 v[34:35], v[120:121], v[124:125] op_sel_hi:[1,0]
	v_pk_mul_f32 v[32:33], v[28:29], v[32:33]
	v_pk_mul_f32 v[34:35], v[30:31], v[34:35]
	global_store_dwordx4 v[44:45], v[32:35], off offset:3072 sc1
	s_cbranch_scc1 .LBB0_1600
	s_ashr_i32 s17, s16, 31
	s_ashr_i32 s3, s16, 11
	s_lshl_b64 s[18:19], s[16:17], 12
	v_lshl_add_u64 v[32:33], v[68:69], 0, s[18:19]
	s_mul_i32 s18, s3, 0x3000
	s_ashr_i32 s19, s18, 31
	s_lshl_b64 s[18:19], s[18:19], 2
	s_add_u32 s18, s70, s18
	s_addc_u32 s19, s71, s19
	v_lshl_add_u64 v[34:35], s[18:19], 0, v[64:65]
	v_add_co_u32_e32 v38, vcc, s31, v34
	v_lshl_add_u64 v[36:37], v[34:35], 0, s[12:13]
	s_nop 0
	v_addc_co_u32_e32 v39, vcc, 0, v35, vcc
	v_add_co_u32_e32 v34, vcc, 0x13000, v34
	global_load_dwordx4 v[56:59], v[36:37], off offset:1024
	global_load_dwordx4 v[52:55], v[36:37], off offset:2048
	global_load_dwordx2 v[150:151], v[32:33], off nt
	global_load_dwordx2 v[144:145], v[32:33], off offset:512 nt
	global_load_dwordx2 v[138:139], v[32:33], off offset:1024 nt
	global_load_dwordx2 v[132:133], v[32:33], off offset:1536 nt
	global_load_dwordx4 v[60:63], v[38:39], off
	global_load_dwordx4 v[48:51], v[36:37], off offset:3072
	v_addc_co_u32_e32 v35, vcc, 0, v35, vcc
	global_load_dwordx4 v[44:47], v[34:35], off
	global_load_dwordx4 v[40:43], v[34:35], off offset:1024
	global_load_dwordx2 v[128:129], v[32:33], off offset:2048 nt
	global_load_dwordx2 v[124:125], v[32:33], off offset:2560 nt
	global_load_dwordx2 v[122:123], v[32:33], off offset:3072 nt
	global_load_dwordx2 v[120:121], v[32:33], off offset:3584 nt
	global_load_dwordx4 v[36:39], v[34:35], off offset:2048
	s_nop 0
	global_load_dwordx4 v[32:35], v[34:35], off offset:3072
	v_cmp_lt_i32_e32 vcc, -1, v192
	s_and_b32 s15, vcc_lo, 0xffff
	s_cmp_eq_u32 s15, 0
	s_cbranch_scc1 .LBB0_1676
	s_lshl_b32 s3, s3, 8
	v_mov_b32_e32 v160, 0
	s_ashr_i32 s6, s3, 31
	v_mov_b32_e32 v161, v160
	v_mov_b32_e32 v166, v160
	v_mov_b32_e32 v167, v160
	v_mov_b32_e32 v162, v160
	v_mov_b32_e32 v163, v160
	v_mov_b32_e32 v164, v160
	v_mov_b32_e32 v165, v160
	v_mov_b32_e32 v156, v160
	v_mov_b32_e32 v157, v160
	v_mov_b32_e32 v158, v160
	v_mov_b32_e32 v159, v160
	v_mov_b32_e32 v152, v160
	v_mov_b32_e32 v153, v160
	v_mov_b32_e32 v154, v160
	v_mov_b32_e32 v155, v160
	v_mov_b32_e32 v146, v160
	v_mov_b32_e32 v147, v160
	v_mov_b32_e32 v148, v160
	v_mov_b32_e32 v149, v160
	v_mov_b32_e32 v140, v160
	v_mov_b32_e32 v141, v160
	v_mov_b32_e32 v142, v160
	v_mov_b32_e32 v143, v160
	v_mov_b32_e32 v134, v160
	v_mov_b32_e32 v135, v160
	v_mov_b32_e32 v136, v160
	v_mov_b32_e32 v137, v160
	v_mov_b32_e32 v126, v160
	v_mov_b32_e32 v127, v160
	v_mov_b32_e32 v130, v160
	v_mov_b32_e32 v131, v160
	s_branch .LBB0_1658

.LBB0_1677:
	s_waitcnt vmcnt(13)
	v_lshlrev_b32_e32 v168, 16, v150
	v_and_b32_e32 v169, 0xffff0000, v150
	v_lshlrev_b32_e32 v150, 16, v151
	v_and_b32_e32 v151, 0xffff0000, v151
	s_waitcnt vmcnt(9)
	v_pk_fma_f32 v[62:63], v[62:63], v[166:167], v[150:151]
	v_lshlrev_b32_e32 v150, 16, v144
	v_and_b32_e32 v151, 0xffff0000, v144
	v_pk_fma_f32 v[60:61], v[60:61], v[160:161], v[168:169]
	v_lshlrev_b32_e32 v144, 16, v145
	v_and_b32_e32 v145, 0xffff0000, v145
	v_pk_fma_f32 v[56:57], v[56:57], v[162:163], v[150:151]
	v_mul_f32_e32 v160, v61, v61
	v_pk_fma_f32 v[58:59], v[58:59], v[164:165], v[144:145]
	v_mul_f32_e32 v144, v57, v57
	v_fmac_f32_e32 v160, v60, v60
	v_fmac_f32_e32 v144, v56, v56
	v_fmac_f32_e32 v160, v62, v62
	v_fmac_f32_e32 v144, v58, v58
	v_fmac_f32_e32 v160, v63, v63
	v_fmac_f32_e32 v144, v59, v59
	v_add_f32_e32 v150, v160, v144
	v_lshlrev_b32_e32 v144, 16, v138
	v_and_b32_e32 v145, 0xffff0000, v138
	v_lshlrev_b32_e32 v138, 16, v139
	v_and_b32_e32 v139, 0xffff0000, v139
	v_pk_fma_f32 v[52:53], v[52:53], v[156:157], v[144:145]
	v_pk_fma_f32 v[54:55], v[54:55], v[158:159], v[138:139]
	v_mul_f32_e32 v138, v53, v53
	v_fmac_f32_e32 v138, v52, v52
	v_fmac_f32_e32 v138, v54, v54
	v_fmac_f32_e32 v138, v55, v55
	v_add_f32_e32 v144, v138, v150
	v_lshlrev_b32_e32 v138, 16, v132
	v_and_b32_e32 v139, 0xffff0000, v132
	v_lshlrev_b32_e32 v132, 16, v133
	v_and_b32_e32 v133, 0xffff0000, v133
	s_waitcnt vmcnt(8)
	v_pk_fma_f32 v[48:49], v[48:49], v[152:153], v[138:139]
	v_pk_fma_f32 v[50:51], v[50:51], v[154:155], v[132:133]
	v_mul_f32_e32 v132, v49, v49
	v_fmac_f32_e32 v132, v48, v48
	v_fmac_f32_e32 v132, v50, v50
	v_fmac_f32_e32 v132, v51, v51
	v_add_f32_e32 v138, v132, v144
	s_waitcnt vmcnt(5)
	v_lshlrev_b32_e32 v132, 16, v128
	v_and_b32_e32 v133, 0xffff0000, v128
	v_lshlrev_b32_e32 v128, 16, v129
	v_and_b32_e32 v129, 0xffff0000, v129
	v_pk_fma_f32 v[46:47], v[46:47], v[148:149], v[128:129]
	s_waitcnt vmcnt(4)
	v_lshlrev_b32_e32 v128, 16, v124
	v_and_b32_e32 v129, 0xffff0000, v124
	v_pk_fma_f32 v[44:45], v[44:45], v[146:147], v[132:133]
	v_pk_fma_f32 v[40:41], v[40:41], v[140:141], v[128:129]
	v_lshlrev_b32_e32 v124, 16, v125
	v_and_b32_e32 v125, 0xffff0000, v125
	v_mov_b32_e32 v128, v41
	v_mov_b32_e32 v129, v45
	v_pk_fma_f32 v[42:43], v[42:43], v[142:143], v[124:125]
	v_mov_b32_e32 v124, v40
	v_mov_b32_e32 v125, v44
	v_pk_mul_f32 v[128:129], v[128:129], v[128:129]
	s_lshl_b64 s[16:17], s[16:17], 13
	v_pk_fma_f32 v[124:125], v[124:125], v[124:125], v[128:129]
	v_mov_b32_e32 v128, v42
	v_mov_b32_e32 v129, v46
	v_pk_fma_f32 v[124:125], v[128:129], v[128:129], v[124:125]
	v_mov_b32_e32 v128, v43
	v_mov_b32_e32 v129, v47
	v_pk_fma_f32 v[124:125], v[128:129], v[128:129], v[124:125]
	s_add_u32 s16, s68, s16
	v_add_f32_e32 v125, v125, v138
	v_add_f32_e32 v128, v124, v125
	s_waitcnt vmcnt(3)
	v_lshlrev_b32_e32 v124, 16, v122
	v_and_b32_e32 v125, 0xffff0000, v122
	v_lshlrev_b32_e32 v122, 16, v123
	v_and_b32_e32 v123, 0xffff0000, v123
	s_waitcnt vmcnt(1)
	v_pk_fma_f32 v[38:39], v[38:39], v[136:137], v[122:123]
	v_lshlrev_b32_e32 v122, 16, v120
	v_and_b32_e32 v123, 0xffff0000, v120
	v_pk_fma_f32 v[36:37], v[36:37], v[134:135], v[124:125]
	v_lshlrev_b32_e32 v120, 16, v121
	v_and_b32_e32 v121, 0xffff0000, v121
	s_waitcnt vmcnt(0)
	v_pk_fma_f32 v[122:123], v[32:33], v[126:127], v[122:123]
	v_pk_fma_f32 v[120:121], v[34:35], v[130:131], v[120:121]
	v_mov_b32_e32 v34, v123
	v_mov_b32_e32 v35, v37
	v_mov_b32_e32 v32, v122
	v_mov_b32_e32 v33, v36
	v_pk_mul_f32 v[34:35], v[34:35], v[34:35]
	s_addc_u32 s17, s69, s17
	v_pk_fma_f32 v[32:33], v[32:33], v[32:33], v[34:35]
	v_mov_b32_e32 v34, v120
	v_mov_b32_e32 v35, v38
	v_pk_fma_f32 v[32:33], v[34:35], v[34:35], v[32:33]
	v_mov_b32_e32 v34, v121
	v_mov_b32_e32 v35, v39
	v_pk_fma_f32 v[32:33], v[34:35], v[34:35], v[32:33]
	s_cmpk_gt_i32 s14, 0x1fff
	v_add_f32_e32 v33, v33, v128
	v_add_f32_e32 v32, v32, v33
	ds_bpermute_b32 v33, v67, v32
	s_waitcnt lgkmcnt(0)
	v_add_f32_e32 v32, v32, v33
	ds_bpermute_b32 v33, v171, v32
	s_waitcnt lgkmcnt(0)
	v_add_f32_e32 v32, v32, v33
	ds_bpermute_b32 v33, v186, v32
	s_waitcnt lgkmcnt(0)
	v_add_f32_e32 v32, v32, v33
	ds_bpermute_b32 v33, v187, v32
	s_waitcnt lgkmcnt(0)
	v_add_f32_e32 v32, v32, v33
	ds_bpermute_b32 v33, v188, v32
	s_waitcnt lgkmcnt(0)
	v_add_f32_e32 v32, v32, v33
	ds_bpermute_b32 v33, v189, v32
	s_waitcnt lgkmcnt(0)
	v_add_f32_e32 v32, v32, v33
	v_fmamk_f32 v32, v32, 0x3a000000, v190
	v_mul_f32_e32 v33, 0x4b800000, v32
	v_cmp_gt_f32_e32 vcc, s33, v32
	s_nop 1
	v_cndmask_b32_e32 v32, v32, v33, vcc
	v_rsq_f32_e32 v32, v32
	s_nop 0
	v_mul_f32_e32 v33, 0x45800000, v32
	v_cndmask_b32_e32 v124, v32, v33, vcc
	v_pk_mul_f32 v[32:33], v[60:61], v[124:125] op_sel_hi:[1,0]
	v_pk_mul_f32 v[34:35], v[62:63], v[124:125] op_sel_hi:[1,0]
	v_pk_mul_f32 v[32:33], v[0:1], v[32:33]
	v_pk_mul_f32 v[34:35], v[2:3], v[34:35]
	global_store_dwordx4 v64, v[32:35], s[16:17] sc1
	v_lshl_add_u64 v[60:61], s[16:17], 0, v[64:65]
	s_nop 0
	v_pk_mul_f32 v[32:33], v[56:57], v[124:125] op_sel_hi:[1,0]
	v_pk_mul_f32 v[34:35], v[58:59], v[124:125] op_sel_hi:[1,0]
	v_pk_mul_f32 v[32:33], v[4:5], v[32:33]
	v_pk_mul_f32 v[34:35], v[6:7], v[34:35]
	global_store_dwordx4 v64, v[32:35], s[16:17] offset:1024 sc1
	s_nop 1
	v_pk_mul_f32 v[32:33], v[52:53], v[124:125] op_sel_hi:[1,0]
	v_pk_mul_f32 v[34:35], v[54:55], v[124:125] op_sel_hi:[1,0]
	v_pk_mul_f32 v[32:33], v[8:9], v[32:33]
	v_pk_mul_f32 v[34:35], v[10:11], v[34:35]
	global_store_dwordx4 v64, v[32:35], s[16:17] offset:2048 sc1
	s_nop 1
	v_pk_mul_f32 v[32:33], v[48:49], v[124:125] op_sel_hi:[1,0]
	v_pk_mul_f32 v[34:35], v[50:51], v[124:125] op_sel_hi:[1,0]
	v_pk_mul_f32 v[32:33], v[12:13], v[32:33]
	v_pk_mul_f32 v[34:35], v[14:15], v[34:35]
	global_store_dwordx4 v64, v[32:35], s[16:17] offset:3072 sc1
	s_nop 1
	v_pk_mul_f32 v[32:33], v[44:45], v[124:125] op_sel_hi:[1,0]
	v_pk_mul_f32 v[34:35], v[46:47], v[124:125] op_sel_hi:[1,0]
	v_add_co_u32_e32 v44, vcc, s28, v60
	v_pk_mul_f32 v[34:35], v[18:19], v[34:35]
	v_pk_mul_f32 v[32:33], v[16:17], v[32:33]
	v_addc_co_u32_e32 v45, vcc, 0, v61, vcc
	global_store_dwordx4 v[44:45], v[32:35], off sc1
	s_nop 1
	v_pk_mul_f32 v[32:33], v[40:41], v[124:125] op_sel_hi:[1,0]
	v_pk_mul_f32 v[34:35], v[42:43], v[124:125] op_sel_hi:[1,0]
	v_pk_mul_f32 v[32:33], v[20:21], v[32:33]
	v_pk_mul_f32 v[34:35], v[22:23], v[34:35]
	global_store_dwordx4 v[44:45], v[32:35], off offset:1024 sc1
	s_nop 1
	v_pk_mul_f32 v[32:33], v[36:37], v[124:125] op_sel_hi:[1,0]
	v_pk_mul_f32 v[34:35], v[38:39], v[124:125] op_sel_hi:[1,0]
	v_pk_mul_f32 v[32:33], v[24:25], v[32:33]
	v_pk_mul_f32 v[34:35], v[26:27], v[34:35]
	global_store_dwordx4 v[44:45], v[32:35], off offset:2048 sc1
	s_nop 1
	v_pk_mul_f32 v[32:33], v[122:123], v[124:125] op_sel_hi:[1,0]
	v_pk_mul_f32 v[34:35], v[120:121], v[124:125] op_sel_hi:[1,0]
	v_pk_mul_f32 v[32:33], v[28:29], v[32:33]
	v_pk_mul_f32 v[34:35], v[30:31], v[34:35]
	global_store_dwordx4 v[44:45], v[32:35], off offset:3072 sc1
	s_cbranch_scc1 .LBB0_1600
	s_ashr_i32 s15, s14, 31
	s_ashr_i32 s3, s14, 11
	s_lshl_b64 s[16:17], s[14:15], 12
	v_lshl_add_u64 v[32:33], v[68:69], 0, s[16:17]
	s_mul_i32 s16, s3, 0x3000
	s_ashr_i32 s17, s16, 31
	s_lshl_b64 s[16:17], s[16:17], 2
	s_add_u32 s16, s70, s16
	s_addc_u32 s17, s71, s17
	v_lshl_add_u64 v[34:35], s[16:17], 0, v[64:65]
	v_add_co_u32_e32 v38, vcc, s31, v34
	v_lshl_add_u64 v[36:37], v[34:35], 0, s[12:13]
	s_nop 0
	v_addc_co_u32_e32 v39, vcc, 0, v35, vcc
	v_add_co_u32_e32 v34, vcc, 0x13000, v34
	global_load_dwordx4 v[56:59], v[36:37], off offset:1024
	global_load_dwordx4 v[52:55], v[36:37], off offset:2048
	global_load_dwordx2 v[150:151], v[32:33], off nt
	global_load_dwordx2 v[144:145], v[32:33], off offset:512 nt
	global_load_dwordx2 v[138:139], v[32:33], off offset:1024 nt
	global_load_dwordx2 v[132:133], v[32:33], off offset:1536 nt
	global_load_dwordx4 v[60:63], v[38:39], off
	global_load_dwordx4 v[48:51], v[36:37], off offset:3072
	v_addc_co_u32_e32 v35, vcc, 0, v35, vcc
	global_load_dwordx4 v[44:47], v[34:35], off
	global_load_dwordx4 v[40:43], v[34:35], off offset:1024
	global_load_dwordx2 v[128:129], v[32:33], off offset:2048 nt
	global_load_dwordx2 v[124:125], v[32:33], off offset:2560 nt
	global_load_dwordx2 v[122:123], v[32:33], off offset:3072 nt
	global_load_dwordx2 v[120:121], v[32:33], off offset:3584 nt
	global_load_dwordx4 v[36:39], v[34:35], off offset:2048
	s_nop 0
	global_load_dwordx4 v[32:35], v[34:35], off offset:3072
	v_cmp_lt_i32_e32 vcc, -1, v191
	s_and_b32 s24, vcc_lo, 0xffff
	s_cmp_eq_u32 s24, 0
	s_cbranch_scc1 .LBB0_1598
	s_lshl_b32 s3, s3, 8
	v_mov_b32_e32 v160, 0
	s_ashr_i32 s6, s3, 31
	v_mov_b32_e32 v161, v160
	v_mov_b32_e32 v166, v160
	v_mov_b32_e32 v167, v160
	v_mov_b32_e32 v162, v160
	v_mov_b32_e32 v163, v160
	v_mov_b32_e32 v164, v160
	v_mov_b32_e32 v165, v160
	v_mov_b32_e32 v156, v160
	v_mov_b32_e32 v157, v160
	v_mov_b32_e32 v158, v160
	v_mov_b32_e32 v159, v160
	v_mov_b32_e32 v152, v160
	v_mov_b32_e32 v153, v160
	v_mov_b32_e32 v154, v160
	v_mov_b32_e32 v155, v160
	v_mov_b32_e32 v146, v160
	v_mov_b32_e32 v147, v160
	v_mov_b32_e32 v148, v160
	v_mov_b32_e32 v149, v160
	v_mov_b32_e32 v140, v160
	v_mov_b32_e32 v141, v160
	v_mov_b32_e32 v142, v160
	v_mov_b32_e32 v143, v160
	v_mov_b32_e32 v134, v160
	v_mov_b32_e32 v135, v160
	v_mov_b32_e32 v136, v160
	v_mov_b32_e32 v137, v160
	v_mov_b32_e32 v126, v160
	v_mov_b32_e32 v127, v160
	v_mov_b32_e32 v130, v160
	v_mov_b32_e32 v131, v160
	s_branch .LBB0_1681
